# bf16 bit-trick packs replaced by v_cvt_pk_bf16_f32 in all epilogues (1278 packs), on top of gates epilogue rewrite
# speedup vs baseline: 1.0167x; 1.0095x over previous
; __device__ __forceinline__ unsigned pk2(float lo, float hi) { return f2bf(lo) | (f2bf(hi) << 16); }
; __device__ __forceinline__ float dot4(f32x4 a, f32x4 b) { return (a.x * b.x + a.y * b.y) + (a.z * b.z + a.w * b.w); }
;     __device__ __forceinline__ void epi(const f32x4 (&acc)[2][2][4][2], const Unit& u, int wr, int wc, int fr, int fq) const {
;     ...
;         if (pn < 11) {
;             bf16* dst; int ld;
;             if (pn < 4) { dst = XR + rowt * 1024 + pn * 256; ld = 1024; } else if (pn < 8) { dst = GR + rowt * 1024 + (pn - 4) * 256; ld = 1024; }
;             else if (pn < 10) { dst = CQ + rowt * 512 + (pn - 8) * 256; ld = 512; } else { dst = CKV + rowt * 256; ld = 256; }
;             const unsigned loff = (lrow * (unsigned)ld + lcol) * 2u;
; #pragma unroll
;             for (int ai = 0; ai < 2; ++ai)
; #pragma unroll
;                 for (int m = 0; m < 4; ++m) {
; #pragma unroll
;                     for (int bj = 0; bj < 2; ++bj) { const f32x4 v0 = acc[ai][bj][m][0], v1 = acc[ai][bj][m][1];
;                         u32x4 w; w.x = pk2(v0[0], v0[1]); w.y = pk2(v0[2], v0[3]); w.z = pk2(v1[0], v1[1]); w.w = pk2(v1[2], v1[3]);
;                         *(u32x4*)((char*)dst + ((size_t)(ai * 128 + m * 16) * ld + bj * 128) * 2 + loff) = w; } }
;             if (pn >= 8) {
;                 float* sq = SSQ + rowt * 16 + (pn < 10 ? (pn - 8) * 4 : 8) + wc;
; #pragma unroll
;                 for (int ai = 0; ai < 2; ++ai)
; #pragma unroll
;                     for (int m = 0; m < 4; ++m) { float ss = 0.f;
; #pragma unroll
;                         for (int bj = 0; bj < 2; ++bj)
; #pragma unroll
;                             for (int n = 0; n < 2; ++n) ss += dot4(acc[ai][bj][m][n], acc[ai][bj][m][n]);
;                         ss += __shfl_xor(ss, 16); ss += __shfl_xor(ss, 32);
;                         if (fq == 0) *(float*)((char*)sq + ((size_t)(ai * 128 + m * 16) * 16 + lrow * 16u) * 4) = ss; } }
.LBB0_299:
	v_cvt_pk_bf16_f32 v148, v126, v127
	v_cvt_pk_bf16_f32 v149, v128, v129
	v_cvt_pk_bf16_f32 v150, v122, v123
	v_cvt_pk_bf16_f32 v151, v124, v125
	v_mul_lo_u32 v143, s15, v156
	s_waitcnt lgkmcnt(0)
	v_add_lshl_u32 v146, v143, v142, 1
	global_store_dwordx4 v146, v[148:151], s[26:27]
	v_lshl_add_u64 v[142:143], s[26:27], 0, v[146:147]
	s_lshl_b32 s12, s15, 5
	v_cvt_pk_bf16_f32 v148, v118, v119
	v_cvt_pk_bf16_f32 v149, v120, v121
	v_cvt_pk_bf16_f32 v150, v114, v115
	v_cvt_pk_bf16_f32 v151, v116, v117
	global_store_dwordx4 v146, v[148:151], s[26:27] offset:256
	s_nop 1
	v_cvt_pk_bf16_f32 v148, v110, v111
	v_cvt_pk_bf16_f32 v149, v112, v113
	v_cvt_pk_bf16_f32 v150, v106, v107
	v_cvt_pk_bf16_f32 v151, v108, v109
	v_lshl_add_u64 v[144:145], v[142:143], 0, s[12:13]
	global_store_dwordx4 v[144:145], v[148:151], off
	s_lshl_b32 s12, s15, 6
	s_nop 0
	v_cvt_pk_bf16_f32 v148, v102, v103
	v_cvt_pk_bf16_f32 v149, v104, v105
	v_cvt_pk_bf16_f32 v150, v98, v99
	v_cvt_pk_bf16_f32 v151, v100, v101
	global_store_dwordx4 v[144:145], v[148:151], off offset:256
	s_nop 1
	v_cvt_pk_bf16_f32 v148, v94, v95
	v_cvt_pk_bf16_f32 v149, v96, v97
	v_cvt_pk_bf16_f32 v150, v90, v91
	v_cvt_pk_bf16_f32 v151, v92, v93
	v_lshl_add_u64 v[144:145], v[142:143], 0, s[12:13]
	global_store_dwordx4 v[144:145], v[148:151], off
	s_nop 1
	v_cvt_pk_bf16_f32 v148, v86, v87
	v_cvt_pk_bf16_f32 v149, v88, v89
	v_cvt_pk_bf16_f32 v150, v82, v83
	v_cvt_pk_bf16_f32 v151, v84, v85
	global_store_dwordx4 v[144:145], v[148:151], off offset:256
	s_nop 1
	v_cvt_pk_bf16_f32 v148, v78, v79
	v_cvt_pk_bf16_f32 v149, v80, v81
	v_cvt_pk_bf16_f32 v150, v74, v75
	s_mul_i32 s12, s15, 0x60
	v_cvt_pk_bf16_f32 v151, v76, v77
	v_lshl_add_u64 v[144:145], v[142:143], 0, s[12:13]
	global_store_dwordx4 v[144:145], v[148:151], off
	s_nop 1
	v_cvt_pk_bf16_f32 v148, v70, v71
	v_cvt_pk_bf16_f32 v149, v72, v73
	v_cvt_pk_bf16_f32 v150, v66, v67
	v_cvt_pk_bf16_f32 v151, v68, v69
	global_store_dwordx4 v[144:145], v[148:151], off offset:256
	s_nop 1
	v_cvt_pk_bf16_f32 v148, v62, v63
	v_cvt_pk_bf16_f32 v149, v64, v65
	v_cvt_pk_bf16_f32 v150, v58, v59
	s_lshl_b32 s12, s15, 8
	v_cvt_pk_bf16_f32 v151, v60, v61
	v_lshl_add_u64 v[144:145], v[142:143], 0, s[12:13]
	global_store_dwordx4 v[144:145], v[148:151], off
	s_nop 1
	v_cvt_pk_bf16_f32 v148, v54, v55
	v_cvt_pk_bf16_f32 v149, v56, v57
	v_cvt_pk_bf16_f32 v150, v50, v51
	v_cvt_pk_bf16_f32 v151, v52, v53
	global_store_dwordx4 v[144:145], v[148:151], off offset:256
	s_nop 1
	v_cvt_pk_bf16_f32 v148, v46, v47
	v_cvt_pk_bf16_f32 v149, v48, v49
	v_cvt_pk_bf16_f32 v150, v42, v43
	s_mul_i32 s12, s15, 0x120
	v_cvt_pk_bf16_f32 v151, v44, v45
	v_lshl_add_u64 v[144:145], v[142:143], 0, s[12:13]
	global_store_dwordx4 v[144:145], v[148:151], off
	s_nop 1
	v_cvt_pk_bf16_f32 v148, v38, v39
	v_cvt_pk_bf16_f32 v149, v40, v41
	v_cvt_pk_bf16_f32 v150, v34, v35
	v_cvt_pk_bf16_f32 v151, v36, v37
	global_store_dwordx4 v[144:145], v[148:151], off offset:256
	s_nop 1
	v_cvt_pk_bf16_f32 v148, v30, v31
	v_cvt_pk_bf16_f32 v149, v32, v33
	v_cvt_pk_bf16_f32 v150, v26, v27
	s_mul_i32 s12, s15, 0x140
	v_cvt_pk_bf16_f32 v151, v28, v29
	v_lshl_add_u64 v[144:145], v[142:143], 0, s[12:13]
	global_store_dwordx4 v[144:145], v[148:151], off
	s_nop 1
	v_cvt_pk_bf16_f32 v148, v22, v23
	v_cvt_pk_bf16_f32 v149, v24, v25
	v_cvt_pk_bf16_f32 v150, v18, v19
	v_cvt_pk_bf16_f32 v151, v20, v21
	global_store_dwordx4 v[144:145], v[148:151], off offset:256
	s_nop 1
	v_cvt_pk_bf16_f32 v148, v14, v15
	v_cvt_pk_bf16_f32 v149, v16, v17
	s_mul_i32 s12, s15, 0x160
	v_lshl_add_u64 v[158:159], v[142:143], 0, s[12:13]
	v_cvt_pk_bf16_f32 v150, v10, v11
	v_cvt_pk_bf16_f32 v142, v6, v7
	v_cvt_pk_bf16_f32 v151, v12, v13
	v_cvt_pk_bf16_f32 v143, v8, v9
	v_cvt_pk_bf16_f32 v144, v2, v3
	v_cvt_pk_bf16_f32 v145, v4, v5
	s_cmp_lt_i32 s22, 8
	global_store_dwordx4 v[158:159], v[148:151], off
	global_store_dwordx4 v[158:159], v[142:145], off offset:256
	s_cbranch_scc1 .LBB0_317
	v_mul_f32_e32 v127, v127, v127
	v_mul_f32_e32 v123, v123, v123
	v_fmac_f32_e32 v127, v126, v126
	v_mul_f32_e32 v126, v129, v129
	v_fmac_f32_e32 v123, v122, v122
	v_mul_f32_e32 v122, v125, v125
	v_mul_f32_e32 v119, v119, v119
	v_fmac_f32_e32 v126, v128, v128
	v_fmac_f32_e32 v122, v124, v124
	v_fmac_f32_e32 v119, v118, v118
	v_mul_f32_e32 v118, v121, v121
	v_mul_f32_e32 v115, v115, v115
	v_add_f32_e32 v126, v127, v126
	v_add_f32_e32 v122, v123, v122
	v_fmac_f32_e32 v118, v120, v120
	v_fmac_f32_e32 v115, v114, v114
	v_mul_f32_e32 v114, v117, v117
	v_cmp_lt_i32_e32 vcc, v220, v215
	v_add_f32_e32 v122, v122, v126
	v_add_f32_e32 v118, v119, v118
	v_fmac_f32_e32 v114, v116, v116
	v_cndmask_b32_e32 v142, v210, v220, vcc
	v_add_f32_e32 v118, v118, v122
	v_add_f32_e32 v114, v115, v114
	v_lshlrev_b32_e32 v142, 2, v142
	v_add_f32_e32 v114, v114, v118
	ds_bpermute_b32 v115, v142, v114
	s_lshl_b64 s[24:25], s[24:25], 14
	s_add_u32 s15, s60, s24
	v_cmp_lt_i32_e32 vcc, v221, v215
	s_addc_u32 s17, s61, s25
	s_lshl_b32 s12, s22, 2
	v_cndmask_b32_e32 v116, v210, v221, vcc
	s_lshl_b64 s[22:23], s[12:13], 2
	v_lshlrev_b32_e32 v116, 2, v116
	s_waitcnt lgkmcnt(0)
	v_add_f32_e32 v117, v114, v115
	s_add_u32 s12, s15, s22
	ds_bpermute_b32 v118, v116, v117
	s_addc_u32 s15, s17, s23
	s_add_u32 s22, s12, s68
	s_addc_u32 s23, s15, 0
	v_lshlrev_b32_e32 v146, 4, v156
	v_lshl_add_u64 v[114:115], v[146:147], 2, s[22:23]
	s_and_saveexec_b64 s[22:23], s[38:39]
	s_cbranch_execz .LBB0_302
	s_waitcnt lgkmcnt(0)
	v_add_f32_e32 v117, v117, v118
	global_store_dword v[114:115], v117, off offset:-128

; __device__ __forceinline__ unsigned pk2(float lo, float hi) { return f2bf(lo) | (f2bf(hi) << 16); }
;     __device__ __forceinline__ void epi(const f32x4 (&acc)[2][2][4][2], const Unit& u, int wr, int wc, int fr, int fq) const {
;         unsigned loff = (unsigned)((wr * 64 + fr) * 1536 + wc * 32 + 8 * fq) * 2u; asm volatile("" : "+v"(loff));
;         char* base = (char*)(O + (size_t)u.pm * 256 * 1536 + (size_t)u.pn * 256);
; #pragma unroll
;         for (int ai = 0; ai < 2; ++ai)
; #pragma unroll
;             for (int m = 0; m < 4; ++m)
; #pragma unroll
;                 for (int bj = 0; bj < 2; ++bj) { const f32x4 v0 = acc[ai][bj][m][0], v1 = acc[ai][bj][m][1];
;                     u32x4 w; w.x = pk2(v0[0], v0[1]); w.y = pk2(v0[2], v0[3]); w.z = pk2(v1[0], v1[1]); w.w = pk2(v1[2], v1[3]);
;                     *(u32x4*)(base + ((size_t)(ai * 128 + m * 16) * 1536 + bj * 128) * 2 + loff) = w; }
.LBB0_484:
	v_bfe_u32 v149, v126, 16, 1
	v_add3_u32 v126, v126, v149, s37
	v_bfe_u32 v149, v127, 16, 1
	v_lshrrev_b32_e32 v126, 16, v126
	v_add3_u32 v127, v127, v149, s37
	v_and_or_b32 v126, v127, s33, v126
	v_bfe_u32 v127, v128, 16, 1
	v_add3_u32 v127, v128, v127, s37
	v_bfe_u32 v128, v129, 16, 1
	v_lshrrev_b32_e32 v127, 16, v127
	v_add3_u32 v128, v129, v128, s37
	v_and_or_b32 v127, v128, s33, v127
	v_bfe_u32 v128, v122, 16, 1
	v_add3_u32 v122, v122, v128, s37
	v_bfe_u32 v128, v123, 16, 1
	v_lshrrev_b32_e32 v122, 16, v122
	v_add3_u32 v123, v123, v128, s37
	v_and_or_b32 v128, v123, s33, v122
	v_cvt_pk_bf16_f32 v129, v124, v125
	v_bfe_u32 v122, v118, 16, 1
	v_add3_u32 v118, v118, v122, s37
	v_bfe_u32 v122, v119, 16, 1
	v_lshrrev_b32_e32 v118, 16, v118
	v_add3_u32 v119, v119, v122, s37
	v_and_or_b32 v118, v119, s33, v118
	v_bfe_u32 v119, v120, 16, 1
	v_add3_u32 v119, v120, v119, s37
	v_bfe_u32 v120, v121, 16, 1
	v_lshrrev_b32_e32 v119, 16, v119
	v_add3_u32 v120, v121, v120, s37
	v_and_or_b32 v119, v120, s33, v119
	v_bfe_u32 v120, v114, 16, 1
	v_add3_u32 v114, v114, v120, s37
	v_bfe_u32 v120, v115, 16, 1
	v_lshrrev_b32_e32 v114, 16, v114
	v_add3_u32 v115, v115, v120, s37
	v_and_or_b32 v120, v115, s33, v114
	v_cvt_pk_bf16_f32 v121, v116, v117
	v_bfe_u32 v114, v110, 16, 1
	v_add3_u32 v110, v110, v114, s37
	v_bfe_u32 v114, v111, 16, 1
	v_lshrrev_b32_e32 v110, 16, v110
	v_add3_u32 v111, v111, v114, s37
	v_and_or_b32 v110, v111, s33, v110
	v_bfe_u32 v111, v112, 16, 1
	v_add3_u32 v111, v112, v111, s37
	v_bfe_u32 v112, v113, 16, 1
	v_lshrrev_b32_e32 v111, 16, v111
	v_add3_u32 v112, v113, v112, s37
	v_and_or_b32 v111, v112, s33, v111
	v_bfe_u32 v112, v106, 16, 1
	v_add3_u32 v106, v106, v112, s37
	v_bfe_u32 v112, v107, 16, 1
	v_lshrrev_b32_e32 v106, 16, v106
	v_add3_u32 v107, v107, v112, s37
	v_and_or_b32 v112, v107, s33, v106
	v_bfe_u32 v106, v108, 16, 1
	v_add3_u32 v106, v108, v106, s37
	v_bfe_u32 v108, v102, 16, 1
	v_add3_u32 v102, v102, v108, s37
	v_bfe_u32 v108, v103, 16, 1
	v_lshrrev_b32_e32 v102, 16, v102
	v_add3_u32 v103, v103, v108, s37
	v_and_or_b32 v102, v103, s33, v102
	v_bfe_u32 v103, v104, 16, 1
	v_add3_u32 v103, v104, v103, s37
	v_bfe_u32 v104, v105, 16, 1
	v_lshrrev_b32_e32 v103, 16, v103
	v_add3_u32 v104, v105, v104, s37
	v_and_or_b32 v103, v104, s33, v103
	v_bfe_u32 v104, v98, 16, 1
	v_add3_u32 v98, v98, v104, s37
	v_bfe_u32 v104, v99, 16, 1
	v_lshrrev_b32_e32 v98, 16, v98
	v_add3_u32 v99, v99, v104, s37
	v_and_or_b32 v104, v99, s33, v98
	v_cvt_pk_bf16_f32 v105, v100, v101
	v_bfe_u32 v98, v94, 16, 1
	v_add3_u32 v94, v94, v98, s37
	v_bfe_u32 v98, v95, 16, 1
	v_lshrrev_b32_e32 v94, 16, v94
	v_add3_u32 v95, v95, v98, s37
	v_and_or_b32 v94, v95, s33, v94
	v_bfe_u32 v95, v96, 16, 1
	v_add3_u32 v95, v96, v95, s37
	v_bfe_u32 v96, v97, 16, 1
	v_lshrrev_b32_e32 v95, 16, v95
	v_add3_u32 v96, v97, v96, s37
	v_and_or_b32 v95, v96, s33, v95
	v_bfe_u32 v96, v90, 16, 1
	v_add3_u32 v90, v90, v96, s37
	v_bfe_u32 v96, v91, 16, 1
	v_lshrrev_b32_e32 v90, 16, v90
	v_add3_u32 v91, v91, v96, s37
	v_and_or_b32 v96, v91, s33, v90
	v_bfe_u32 v90, v92, 16, 1
	v_add3_u32 v90, v92, v90, s37
	v_bfe_u32 v92, v86, 16, 1
	v_add3_u32 v86, v86, v92, s37
	v_bfe_u32 v92, v87, 16, 1
	v_lshrrev_b32_e32 v86, 16, v86
	v_add3_u32 v87, v87, v92, s37
	v_and_or_b32 v86, v87, s33, v86
	v_bfe_u32 v87, v88, 16, 1
	v_add3_u32 v87, v88, v87, s37
	v_bfe_u32 v88, v89, 16, 1
	v_lshrrev_b32_e32 v87, 16, v87
	v_add3_u32 v88, v89, v88, s37
	v_and_or_b32 v87, v88, s33, v87
	v_bfe_u32 v88, v82, 16, 1
	v_add3_u32 v82, v82, v88, s37
	v_bfe_u32 v88, v83, 16, 1
	v_lshrrev_b32_e32 v82, 16, v82
	v_add3_u32 v83, v83, v88, s37
	v_and_or_b32 v88, v83, s33, v82
	v_cvt_pk_bf16_f32 v89, v84, v85
	v_bfe_u32 v82, v78, 16, 1
	v_add3_u32 v78, v78, v82, s37
	v_bfe_u32 v82, v79, 16, 1
	v_lshrrev_b32_e32 v78, 16, v78
	v_add3_u32 v79, v79, v82, s37
	v_and_or_b32 v78, v79, s33, v78
	v_bfe_u32 v79, v80, 16, 1
	v_add3_u32 v79, v80, v79, s37
	v_bfe_u32 v80, v81, 16, 1
	v_lshrrev_b32_e32 v79, 16, v79
	v_add3_u32 v80, v81, v80, s37
	v_and_or_b32 v79, v80, s33, v79
	v_bfe_u32 v80, v74, 16, 1
	v_add3_u32 v74, v74, v80, s37
	v_bfe_u32 v80, v75, 16, 1
	v_lshrrev_b32_e32 v74, 16, v74
	v_add3_u32 v75, v75, v80, s37
	v_and_or_b32 v80, v75, s33, v74
	v_bfe_u32 v74, v76, 16, 1
	v_add3_u32 v74, v76, v74, s37
	v_bfe_u32 v76, v70, 16, 1
	v_add3_u32 v70, v70, v76, s37
	v_bfe_u32 v76, v71, 16, 1
	v_lshrrev_b32_e32 v70, 16, v70
	v_add3_u32 v71, v71, v76, s37
	v_and_or_b32 v70, v71, s33, v70
	v_bfe_u32 v71, v72, 16, 1
	v_add3_u32 v71, v72, v71, s37
	v_bfe_u32 v72, v73, 16, 1
	v_lshrrev_b32_e32 v71, 16, v71
	v_add3_u32 v72, v73, v72, s37
	v_and_or_b32 v71, v72, s33, v71
	v_bfe_u32 v72, v66, 16, 1
	v_add3_u32 v66, v66, v72, s37
	v_bfe_u32 v72, v67, 16, 1
	v_lshrrev_b32_e32 v66, 16, v66
	v_add3_u32 v67, v67, v72, s37
	v_and_or_b32 v72, v67, s33, v66
	v_cvt_pk_bf16_f32 v73, v68, v69
	v_bfe_u32 v66, v62, 16, 1
	v_add3_u32 v62, v62, v66, s37
	v_bfe_u32 v66, v63, 16, 1
	v_lshrrev_b32_e32 v62, 16, v62
	v_add3_u32 v63, v63, v66, s37
	v_and_or_b32 v62, v63, s33, v62
	v_bfe_u32 v63, v64, 16, 1
	v_add3_u32 v63, v64, v63, s37
	v_bfe_u32 v64, v65, 16, 1
	v_lshrrev_b32_e32 v63, 16, v63
	v_add3_u32 v64, v65, v64, s37
	v_and_or_b32 v63, v64, s33, v63
	v_bfe_u32 v64, v58, 16, 1
	v_add3_u32 v58, v58, v64, s37
	v_bfe_u32 v64, v59, 16, 1
	v_lshrrev_b32_e32 v58, 16, v58
	v_add3_u32 v59, v59, v64, s37
	v_and_or_b32 v64, v59, s33, v58
	v_bfe_u32 v58, v60, 16, 1
	v_add3_u32 v58, v60, v58, s37
	v_bfe_u32 v60, v54, 16, 1
	v_add3_u32 v54, v54, v60, s37
	v_bfe_u32 v60, v55, 16, 1
	v_lshrrev_b32_e32 v54, 16, v54
	v_add3_u32 v55, v55, v60, s37
; __device__ __forceinline__ unsigned pk2(float lo, float hi) { return f2bf(lo) | (f2bf(hi) << 16); }
; #define PG8_BAR __builtin_amdgcn_s_barrier()
; template <class P>
; __device__ __forceinline__ void gemm_phase(LAS unsigned char* lds, const P& p) {
;     ...
;         if (wr == 0) PG8_BAR;
;         p.epi(acc, cur, wr, wc, fr, fq);
;         if (!has_next) break;
; #pragma unroll
;         for (int a = 0; a < 2; ++a)
; #pragma unroll
;             for (int b = 0; b < 2; ++b)
; #pragma unroll
;                 for (int m = 0; m < 4; ++m)
; #pragma unroll
;                     for (int n = 0; n < 2; ++n) acc[a][b][m][n] = (f32x4){0.f, 0.f, 0.f, 0.f};
;         cur = nxt; cA = nA; cB = nB; ++ui;
;         if (wr == 1) PG8_BAR;
;     __device__ __forceinline__ void epi(const f32x4 (&acc)[2][2][4][2], const Unit& u, int wr, int wc, int fr, int fq) const {
;     ...
;         char* base = (char*)(O + (size_t)u.pm * 256 * 1536 + (size_t)u.pn * 256);
; #pragma unroll
;         for (int ai = 0; ai < 2; ++ai)
; #pragma unroll
;             for (int m = 0; m < 4; ++m)
; #pragma unroll
;                 for (int bj = 0; bj < 2; ++bj) { const f32x4 v0 = acc[ai][bj][m][0], v1 = acc[ai][bj][m][1];
;                     u32x4 w; w.x = pk2(v0[0], v0[1]); w.y = pk2(v0[2], v0[3]); w.z = pk2(v1[0], v1[1]); w.w = pk2(v1[2], v1[3]);
;                     *(u32x4*)(base + ((size_t)(ai * 128 + m * 16) * 1536 + bj * 128) * 2 + loff) = w; }
	v_and_or_b32 v54, v55, s33, v54
	v_bfe_u32 v55, v56, 16, 1
	v_add3_u32 v55, v56, v55, s37
	v_bfe_u32 v56, v57, 16, 1
	v_lshrrev_b32_e32 v55, 16, v55
	v_add3_u32 v56, v57, v56, s37
	v_and_or_b32 v55, v56, s33, v55
	v_bfe_u32 v56, v50, 16, 1
	v_add3_u32 v50, v50, v56, s37
	v_bfe_u32 v56, v51, 16, 1
	v_lshrrev_b32_e32 v50, 16, v50
	v_add3_u32 v51, v51, v56, s37
	v_and_or_b32 v56, v51, s33, v50
	v_cvt_pk_bf16_f32 v57, v52, v53
	v_bfe_u32 v50, v46, 16, 1
	v_add3_u32 v46, v46, v50, s37
	v_bfe_u32 v50, v47, 16, 1
	v_lshrrev_b32_e32 v46, 16, v46
	v_add3_u32 v47, v47, v50, s37
	v_and_or_b32 v46, v47, s33, v46
	v_bfe_u32 v47, v48, 16, 1
	v_add3_u32 v47, v48, v47, s37
	v_bfe_u32 v48, v49, 16, 1
	v_lshrrev_b32_e32 v47, 16, v47
	v_add3_u32 v48, v49, v48, s37
	v_and_or_b32 v47, v48, s33, v47
	v_bfe_u32 v48, v42, 16, 1
	v_add3_u32 v42, v42, v48, s37
	v_bfe_u32 v48, v43, 16, 1
	v_lshrrev_b32_e32 v42, 16, v42
	v_add3_u32 v43, v43, v48, s37
	v_and_or_b32 v48, v43, s33, v42
	v_bfe_u32 v42, v44, 16, 1
	v_add3_u32 v42, v44, v42, s37
	v_bfe_u32 v44, v38, 16, 1
	v_add3_u32 v38, v38, v44, s37
	v_bfe_u32 v44, v39, 16, 1
	v_lshrrev_b32_e32 v38, 16, v38
	v_add3_u32 v39, v39, v44, s37
	v_and_or_b32 v38, v39, s33, v38
	v_bfe_u32 v39, v40, 16, 1
	v_add3_u32 v39, v40, v39, s37
	v_bfe_u32 v40, v41, 16, 1
	v_lshrrev_b32_e32 v39, 16, v39
	v_add3_u32 v40, v41, v40, s37
	v_and_or_b32 v39, v40, s33, v39
	v_bfe_u32 v40, v34, 16, 1
	v_add3_u32 v34, v34, v40, s37
	v_bfe_u32 v40, v35, 16, 1
	v_lshrrev_b32_e32 v34, 16, v34
	v_add3_u32 v35, v35, v40, s37
	v_and_or_b32 v40, v35, s33, v34
	v_cvt_pk_bf16_f32 v41, v36, v37
	v_bfe_u32 v34, v30, 16, 1
	v_add3_u32 v30, v30, v34, s37
	v_bfe_u32 v34, v31, 16, 1
	v_lshrrev_b32_e32 v30, 16, v30
	v_add3_u32 v31, v31, v34, s37
	v_and_or_b32 v30, v31, s33, v30
	v_bfe_u32 v31, v32, 16, 1
	v_add3_u32 v31, v32, v31, s37
	v_bfe_u32 v32, v33, 16, 1
	v_lshrrev_b32_e32 v31, 16, v31
	v_add3_u32 v32, v33, v32, s37
	v_and_or_b32 v31, v32, s33, v31
	v_bfe_u32 v32, v26, 16, 1
	v_add3_u32 v26, v26, v32, s37
	v_bfe_u32 v32, v27, 16, 1
	v_lshrrev_b32_e32 v26, 16, v26
	v_add3_u32 v27, v27, v32, s37
	v_and_or_b32 v32, v27, s33, v26
	v_bfe_u32 v26, v28, 16, 1
	v_add3_u32 v26, v28, v26, s37
	v_bfe_u32 v28, v22, 16, 1
	v_add3_u32 v22, v22, v28, s37
	v_bfe_u32 v28, v23, 16, 1
	v_lshrrev_b32_e32 v22, 16, v22
	v_add3_u32 v23, v23, v28, s37
	v_and_or_b32 v22, v23, s33, v22
	v_bfe_u32 v23, v24, 16, 1
	v_add3_u32 v23, v24, v23, s37
	v_bfe_u32 v24, v25, 16, 1
	v_lshrrev_b32_e32 v23, 16, v23
	v_add3_u32 v24, v25, v24, s37
	v_and_or_b32 v23, v24, s33, v23
	v_bfe_u32 v24, v18, 16, 1
	v_add3_u32 v18, v18, v24, s37
	v_bfe_u32 v24, v19, 16, 1
	v_lshrrev_b32_e32 v18, 16, v18
	v_add3_u32 v19, v19, v24, s37
	v_and_or_b32 v24, v19, s33, v18
	v_cvt_pk_bf16_f32 v25, v20, v21
	v_bfe_u32 v18, v14, 16, 1
	s_mul_i32 s11, s20, 0xc0000
	v_add3_u32 v14, v14, v18, s37
	v_bfe_u32 v18, v15, 16, 1
	s_mul_hi_i32 s9, s20, 0xc0000
	s_add_u32 s11, s57, s11
	v_lshrrev_b32_e32 v14, 16, v14
	v_add3_u32 v15, v15, v18, s37
	s_addc_u32 s9, s58, s9
	s_ashr_i32 s23, s22, 31
	v_and_or_b32 v14, v15, s33, v14
	v_bfe_u32 v15, v16, 16, 1
	s_lshl_b64 s[20:21], s[22:23], 9
	v_add3_u32 v15, v16, v15, s37
	v_bfe_u32 v16, v17, 16, 1
	s_add_u32 s20, s11, s20
	v_lshrrev_b32_e32 v15, 16, v15
	v_add3_u32 v16, v17, v16, s37
	v_mov_b32_e32 v146, v145
	s_addc_u32 s21, s9, s21
	v_bfe_u32 v107, v109, 16, 1
	v_and_or_b32 v15, v16, s33, v15
	v_bfe_u32 v16, v10, 16, 1
	v_lshrrev_b32_e32 v106, 16, v106
	v_lshl_add_u64 v[142:143], s[20:21], 0, v[146:147]
	v_add3_u32 v107, v109, v107, s37
	v_add3_u32 v10, v10, v16, s37
	v_bfe_u32 v16, v11, 16, 1
	v_and_or_b32 v113, v107, s33, v106
	v_add_co_u32_e32 v106, vcc, s86, v142
	v_bfe_u32 v91, v93, 16, 1
	v_lshrrev_b32_e32 v10, 16, v10
	v_add3_u32 v11, v11, v16, s37
	v_addc_co_u32_e32 v107, vcc, 0, v143, vcc
	v_lshrrev_b32_e32 v90, 16, v90
	v_add3_u32 v91, v93, v91, s37
	v_and_or_b32 v16, v11, s33, v10
	v_bfe_u32 v10, v12, 16, 1
	v_and_or_b32 v97, v91, s33, v90
	v_add_co_u32_e32 v90, vcc, s82, v142
	v_bfe_u32 v75, v77, 16, 1
	v_add3_u32 v10, v12, v10, s37
	v_bfe_u32 v12, v6, 16, 1
	v_addc_co_u32_e32 v91, vcc, 0, v143, vcc
	v_lshrrev_b32_e32 v74, 16, v74
	v_add3_u32 v75, v77, v75, s37
	s_mov_b32 s9, 0x24000
	v_add3_u32 v6, v6, v12, s37
	v_bfe_u32 v12, v7, 16, 1
	v_and_or_b32 v81, v75, s33, v74
	v_add_co_u32_e32 v74, vcc, s9, v142
	v_bfe_u32 v59, v61, 16, 1
	v_lshrrev_b32_e32 v6, 16, v6
	v_add3_u32 v7, v7, v12, s37
	v_addc_co_u32_e32 v75, vcc, 0, v143, vcc
	v_lshrrev_b32_e32 v58, 16, v58
	v_add3_u32 v59, v61, v59, s37
	s_mov_b32 s9, 0x60000
	v_and_or_b32 v6, v7, s33, v6
	v_bfe_u32 v7, v8, 16, 1
	v_and_or_b32 v65, v59, s33, v58
	v_add_co_u32_e32 v58, vcc, s9, v142
	v_bfe_u32 v43, v45, 16, 1
	v_add3_u32 v7, v8, v7, s37
	v_bfe_u32 v8, v9, 16, 1
	v_addc_co_u32_e32 v59, vcc, 0, v143, vcc
	v_lshrrev_b32_e32 v42, 16, v42
	v_add3_u32 v43, v45, v43, s37
	s_mov_b32 s9, 0x6c000
	v_lshrrev_b32_e32 v7, 16, v7
	v_add3_u32 v8, v9, v8, s37
	v_and_or_b32 v49, v43, s33, v42
	v_add_co_u32_e32 v42, vcc, s9, v142
	v_bfe_u32 v27, v29, 16, 1
	v_and_or_b32 v7, v8, s33, v7
	v_bfe_u32 v8, v2, 16, 1
	v_addc_co_u32_e32 v43, vcc, 0, v143, vcc
	v_lshrrev_b32_e32 v26, 16, v26
	v_add3_u32 v27, v29, v27, s37
	s_mov_b32 s9, 0x78000
	v_add3_u32 v2, v2, v8, s37
	v_bfe_u32 v8, v3, 16, 1
	v_and_or_b32 v33, v27, s33, v26
	v_add_co_u32_e32 v26, vcc, s9, v142
	v_bfe_u32 v11, v13, 16, 1
	v_lshrrev_b32_e32 v2, 16, v2
	v_add3_u32 v3, v3, v8, s37
	v_addc_co_u32_e32 v27, vcc, 0, v143, vcc
	v_lshrrev_b32_e32 v10, 16, v10
	v_add3_u32 v11, v13, v11, s37
	s_mov_b32 s9, 0x84000
	v_and_or_b32 v8, v3, s33, v2
	v_and_or_b32 v17, v11, s33, v10
	v_add_co_u32_e32 v10, vcc, s9, v142
	v_addc_co_u32_e32 v11, vcc, 0, v143, vcc
	global_store_dwordx4 v146, v[126:129], s[20:21]
	global_store_dwordx4 v146, v[118:121], s[20:21] offset:256
	v_cvt_pk_bf16_f32 v9, v4, v5
	s_andn2_b64 vcc, exec, s[40:41]
	s_mov_b64 s[20:21], -1
	global_store_dwordx4 v[106:107], v[110:113], off
	global_store_dwordx4 v[106:107], v[102:105], off offset:256
	global_store_dwordx4 v[90:91], v[94:97], off
	global_store_dwordx4 v[90:91], v[86:89], off offset:256
	global_store_dwordx4 v[74:75], v[78:81], off
	global_store_dwordx4 v[74:75], v[70:73], off offset:256
	global_store_dwordx4 v[58:59], v[62:65], off
	global_store_dwordx4 v[58:59], v[54:57], off offset:256
	global_store_dwordx4 v[42:43], v[46:49], off
	global_store_dwordx4 v[42:43], v[38:41], off offset:256
	global_store_dwordx4 v[26:27], v[30:33], off
	global_store_dwordx4 v[26:27], v[22:25], off offset:256
	global_store_dwordx4 v[10:11], v[14:17], off
	global_store_dwordx4 v[10:11], v[6:9], off offset:256
	s_cbranch_vccnz .LBB0_476
	s_andn2_b64 vcc, exec, s[2:3]
	s_cbranch_vccnz .LBB0_475
	s_barrier
	s_branch .LBB0_475

; #define LAS __attribute__((address_space(3)))
; __device__ __forceinline__ unsigned pk2(float lo, float hi) { return f2bf(lo) | (f2bf(hi) << 16); }
;     __device__ __forceinline__ void epi(const f32x4 (&acc)[2][2][4][2], const Unit& u, int wr, int wc, int fr, int fq) const {
;     ...
;         asm volatile("s_waitcnt lgkmcnt(0)" ::: "memory"); __builtin_amdgcn_s_barrier(); asm volatile("" ::: "memory");
;         const f32x4 g0 = *(const f32x4*)((const char*)kn + lcol * 4), g1 = *(const f32x4*)((const char*)kn + lcol * 4 + 16);
;         const unsigned koff = (lrow * (unsigned)DQK + lcol) * 2u, voff = (lrow * (unsigned)DVH + lcol) * 2u;
;         char* kb = (char*)(Ko + hrow0 * DQK); char* vb = (char*)(Vo + hrow0 * DVH);
; #pragma unroll
;         for (int ai = 0; ai < 2; ++ai)
; #pragma unroll
;             for (int m = 0; m < 4; ++m) { const f32x4 pt = *(const LAS f32x4*)(part + (ai * 128 + m * 16 + lrow) * 4);
;                 const float tot = ((pt.x + pt.y) + (pt.z + pt.w)) + kr2[ai][m]; const float rk = rsqrtf(tot * (1.f / DQK) + EPS); const float f = sc[ai][m] * rk;
;                 const f32x4 k0 = acc[ai][0][m][0] * f * g0, k1 = acc[ai][0][m][1] * f * g1, v0 = acc[ai][1][m][0] * sc[ai][m], v1 = acc[ai][1][m][1] * sc[ai][m];
;                 u32x4 w; w.x = pk2(k0[0], k0[1]); w.y = pk2(k0[2], k0[3]); w.z = pk2(k1[0], k1[1]); w.w = pk2(k1[2], k1[3]);
;                 *(u32x4*)(kb + (size_t)(ai * 128 + m * 16) * DQK * 2 + koff) = w;
;                 w.x = pk2(v0[0], v0[1]); w.y = pk2(v0[2], v0[3]); w.z = pk2(v1[0], v1[1]); w.w = pk2(v1[2], v1[3]);
;                 *(u32x4*)(vb + (size_t)(ai * 128 + m * 16) * DVH * 2 + voff) = w;
;                 if (wc == 0 && fq == 0) RSTDK[(size_t)(rowt + ai * 128 + m * 16 + lrow) * 8 + h] = rk; }
.LBB0_520:
	s_or_b64 exec, exec, s[48:49]
	s_waitcnt lgkmcnt(0)
	s_barrier
	v_lshlrev_b32_e32 v130, 2, v155
	global_load_dwordx4 v[134:137], v130, s[8:9]
	s_waitcnt lgkmcnt(0)
	global_load_dwordx4 v[130:133], v130, s[8:9] offset:16
	s_movk_i32 s27, 0xc0
	v_lshlrev_b32_e32 v163, 1, v155
	v_add_u32_e32 v167, 0, v146
	v_mov_b32_e32 v183, v182
	v_mul_lo_u32 v159, v153, s27
	v_add_u32_e32 v186, s46, v153
	v_add_f32_e32 v173, v184, v185
	v_mov_b32_e32 v194, v182
	v_mov_b32_e32 v195, v182
	v_lshl_add_u32 v184, v153, 8, v163
	v_add_u32_e32 v153, 0x20000, v167
	v_pk_mul_f32 v[128:129], v[128:129], v[194:195]
	v_pk_mul_f32 v[194:195], v[124:125], v[194:195]
	v_pk_mul_f32 v[196:197], v[122:123], v[182:183]
	ds_read_b128 v[122:125], v153
	s_add_i32 s19, s46, 0xffffc000
	s_and_b32 s21, s46, 0xf00
	s_ashr_i32 s5, s26, 4
	s_lshr_b32 s19, s19, 8
	s_waitcnt lgkmcnt(0)
	v_mov_b32_e32 v198, v123
	v_mov_b32_e32 v199, v124
	v_mov_b32_e32 v123, v125
	v_pk_add_f32 v[122:123], v[198:199], v[122:123]
	s_addk_i32 s21, 0x100
	v_add_f32_e32 v122, v122, v123
	v_add_f32_e32 v122, v173, v122
	v_fmamk_f32 v122, v122, 0x3baaaaab, v180
	v_mul_f32_e32 v123, 0x4b800000, v122
	v_cmp_gt_f32_e32 vcc, s79, v122
	s_cmp_lt_i32 s26, 64
	s_cselect_b32 s5, s5, s19
	v_cndmask_b32_e32 v122, v122, v123, vcc
	v_rsq_f32_e32 v122, v122
	s_cselect_b32 s19, s21, 0
	s_lshl_b32 s5, s5, 3
	s_add_i32 s5, s5, s4
	v_mul_f32_e32 v123, 0x45800000, v122
	v_cndmask_b32_e32 v122, v122, v123, vcc
	v_mul_f32_e32 v124, v182, v122
	v_pk_mul_f32 v[118:119], v[118:119], v[124:125] op_sel_hi:[1,0]
	v_pk_mul_f32 v[120:121], v[120:121], v[124:125] op_sel_hi:[1,0]
	v_pk_mul_f32 v[114:115], v[114:115], v[124:125] op_sel_hi:[1,0]
	v_pk_mul_f32 v[116:117], v[116:117], v[124:125] op_sel_hi:[1,0]
	s_mul_hi_i32 s21, s5, 0x1100
	s_mulk_i32 s5, 0x1100
	v_add_lshl_u32 v188, v159, v155, 1
	s_add_u32 s46, s5, s19
	s_addc_u32 s47, s21, 0
	s_mul_hi_u32 s5, s46, 0x180
	s_mul_i32 s21, s47, 0x180
	s_mul_i32 s19, s46, 0x180
	s_add_i32 s5, s5, s21
	s_add_u32 s26, s63, s19
	v_pk_mul_f32 v[126:127], v[126:127], v[182:183]
	s_addc_u32 s27, s64, s5
	s_lshl_b64 s[46:47], s[46:47], 8
	s_add_u32 s46, s65, s46
	s_addc_u32 s47, s66, s47
	s_ashr_i32 s5, s4, 31
	s_waitcnt vmcnt(1)
	v_pk_mul_f32 v[118:119], v[134:135], v[118:119]
	v_pk_mul_f32 v[120:121], v[136:137], v[120:121]
	s_waitcnt vmcnt(0)
	v_pk_mul_f32 v[124:125], v[132:133], v[116:117]
	v_pk_mul_f32 v[114:115], v[130:131], v[114:115]
	v_bfe_u32 v116, v118, 16, 1
	v_bfe_u32 v117, v119, 16, 1
	v_bfe_u32 v123, v120, 16, 1
	v_bfe_u32 v155, v114, 16, 1
	v_bfe_u32 v159, v115, 16, 1
	v_add3_u32 v116, v118, v116, s37
	v_bfe_u32 v153, v121, 16, 1
	v_add3_u32 v117, v119, v117, s37
	v_add3_u32 v118, v120, v123, s37
	v_add3_u32 v114, v114, v155, s37
	v_add3_u32 v120, v115, v159, s37
	v_lshrrev_b32_e32 v115, 16, v116
	v_add3_u32 v119, v121, v153, s37
	v_lshrrev_b32_e32 v116, 16, v118
	v_lshrrev_b32_e32 v118, 16, v114
	v_and_or_b32 v114, v117, s33, v115
	v_and_or_b32 v115, v119, s33, v116
	v_and_or_b32 v116, v120, s33, v118
	v_cvt_pk_bf16_f32 v117, v124, v125
	global_store_dwordx4 v188, v[114:117], s[26:27]
	s_nop 1
	v_cvt_pk_bf16_f32 v114, v126, v127
	v_cvt_pk_bf16_f32 v115, v128, v129
	v_cvt_pk_bf16_f32 v116, v196, v197
	v_cvt_pk_bf16_f32 v117, v194, v195
	global_store_dwordx4 v184, v[114:117], s[46:47]
	s_and_saveexec_b64 s[48:49], s[42:43]
	s_cbranch_execz .LBB0_522
	v_mov_b32_e32 v187, v147
	v_lshlrev_b64 v[114:115], 5, v[186:187]
	v_lshl_add_u64 v[114:115], s[6:7], 0, v[114:115]
	v_lshl_add_u64 v[114:115], s[4:5], 2, v[114:115]
	global_store_dword v[114:115], v122, off
.LBB0_522:
	s_or_b64 exec, exec, s[48:49]
	s_add_i32 s19, 0, 0x20000
	v_add_u32_e32 v118, s19, v146
	ds_read_b128 v[120:123], v118 offset:256
	v_mov_b32_e32 v177, v176
	v_mov_b32_e32 v189, v147
	v_lshl_add_u64 v[116:117], s[26:27], 0, v[188:189]
	v_pk_mul_f32 v[102:103], v[102:103], v[176:177]
	s_waitcnt lgkmcnt(0)
	v_mov_b32_e32 v124, v121
	v_mov_b32_e32 v125, v122
	v_mov_b32_e32 v121, v123
	v_pk_add_f32 v[120:121], v[124:125], v[120:121]
	v_pk_mul_f32 v[122:123], v[98:99], v[176:177]
	v_add_f32_e32 v119, v120, v121
	v_add_f32_e32 v120, v178, v179
	v_add_f32_e32 v119, v120, v119
	v_fmamk_f32 v119, v119, 0x3baaaaab, v180
	v_cmp_gt_f32_e32 vcc, s79, v119
	v_mul_f32_e32 v120, 0x4b800000, v119
	v_mov_b32_e32 v185, v147
	v_cndmask_b32_e32 v119, v119, v120, vcc
	v_rsq_f32_e32 v119, v119
	v_lshl_add_u64 v[114:115], s[46:47], 0, v[184:185]
	v_mul_f32_e32 v120, 0x45800000, v119
	v_cndmask_b32_e32 v119, v119, v120, vcc
	v_mul_f32_e32 v120, v176, v119
	v_pk_mul_f32 v[110:111], v[110:111], v[120:121] op_sel_hi:[1,0]
	v_pk_mul_f32 v[112:113], v[112:113], v[120:121] op_sel_hi:[1,0]
	v_pk_mul_f32 v[110:111], v[134:135], v[110:111]
	v_pk_mul_f32 v[112:113], v[136:137], v[112:113]
	v_pk_mul_f32 v[106:107], v[106:107], v[120:121] op_sel_hi:[1,0]
	v_pk_mul_f32 v[108:109], v[108:109], v[120:121] op_sel_hi:[1,0]
	v_mov_b32_e32 v120, v176
	v_mov_b32_e32 v121, v176
	v_cvt_pk_bf16_f32 v98, v110, v111
	v_pk_mul_f32 v[104:105], v[104:105], v[120:121]
	v_pk_mul_f32 v[120:121], v[100:101], v[120:121]
	v_pk_mul_f32 v[106:107], v[130:131], v[106:107]
	v_cvt_pk_bf16_f32 v99, v112, v113
	v_pk_mul_f32 v[108:109], v[132:133], v[108:109]
	v_cvt_pk_bf16_f32 v100, v106, v107
	v_cvt_pk_bf16_f32 v101, v108, v109
	v_add_co_u32_e32 v106, vcc, s87, v116
	s_nop 1
	v_addc_co_u32_e32 v107, vcc, 0, v117, vcc
	global_store_dwordx4 v[106:107], v[98:101], off offset:2048
	s_nop 1
	v_cvt_pk_bf16_f32 v98, v102, v103
	v_cvt_pk_bf16_f32 v99, v104, v105
	v_cvt_pk_bf16_f32 v100, v122, v123
	v_cvt_pk_bf16_f32 v101, v120, v121
	v_add_co_u32_e32 v102, vcc, 0x1000, v114
	s_nop 1
	v_addc_co_u32_e32 v103, vcc, 0, v115, vcc
	global_store_dwordx4 v[102:103], v[98:101], off
	s_and_saveexec_b64 s[26:27], s[42:43]
	s_cbranch_execz .LBB0_524
	v_add_u32_e32 v146, 16, v186
	v_lshlrev_b64 v[98:99], 5, v[146:147]
	v_lshl_add_u64 v[98:99], s[6:7], 0, v[98:99]
	v_lshl_add_u64 v[98:99], s[4:5], 2, v[98:99]
	global_store_dword v[98:99], v119, off
; #define LAS __attribute__((address_space(3)))
; __device__ __forceinline__ unsigned pk2(float lo, float hi) { return f2bf(lo) | (f2bf(hi) << 16); }
;     __device__ __forceinline__ void epi(const f32x4 (&acc)[2][2][4][2], const Unit& u, int wr, int wc, int fr, int fq) const {
;     ...
;             for (int m = 0; m < 4; ++m) { const f32x4 pt = *(const LAS f32x4*)(part + (ai * 128 + m * 16 + lrow) * 4);
;                 const float tot = ((pt.x + pt.y) + (pt.z + pt.w)) + kr2[ai][m]; const float rk = rsqrtf(tot * (1.f / DQK) + EPS); const float f = sc[ai][m] * rk;
;                 const f32x4 k0 = acc[ai][0][m][0] * f * g0, k1 = acc[ai][0][m][1] * f * g1, v0 = acc[ai][1][m][0] * sc[ai][m], v1 = acc[ai][1][m][1] * sc[ai][m];
;                 u32x4 w; w.x = pk2(k0[0], k0[1]); w.y = pk2(k0[2], k0[3]); w.z = pk2(k1[0], k1[1]); w.w = pk2(k1[2], k1[3]);
;                 *(u32x4*)(kb + (size_t)(ai * 128 + m * 16) * DQK * 2 + koff) = w;
;                 w.x = pk2(v0[0], v0[1]); w.y = pk2(v0[2], v0[3]); w.z = pk2(v1[0], v1[1]); w.w = pk2(v1[2], v1[3]);
;                 *(u32x4*)(vb + (size_t)(ai * 128 + m * 16) * DVH * 2 + voff) = w;
;                 if (wc == 0 && fq == 0) RSTDK[(size_t)(rowt + ai * 128 + m * 16 + lrow) * 8 + h] = rk; }
.LBB0_524:
	s_or_b64 exec, exec, s[26:27]
	ds_read_b128 v[98:101], v118 offset:512
	v_add_f32_e32 v104, v174, v175
	v_mov_b32_e32 v173, v172
	s_movk_i32 s19, 0x3000
	v_pk_mul_f32 v[86:87], v[86:87], v[172:173]
	s_waitcnt lgkmcnt(0)
	v_mov_b32_e32 v102, v99
	v_mov_b32_e32 v103, v100
	v_mov_b32_e32 v99, v101
	v_pk_add_f32 v[98:99], v[102:103], v[98:99]
	v_pk_mul_f32 v[102:103], v[82:83], v[172:173]
	v_add_f32_e32 v98, v98, v99
	v_add_f32_e32 v98, v104, v98
	v_fmamk_f32 v98, v98, 0x3baaaaab, v180
	v_mul_f32_e32 v99, 0x4b800000, v98
	v_cmp_gt_f32_e32 vcc, s79, v98
	s_nop 1
	v_cndmask_b32_e32 v98, v98, v99, vcc
	v_rsq_f32_e32 v98, v98
	s_nop 0
	v_mul_f32_e32 v99, 0x45800000, v98
	v_cndmask_b32_e32 v98, v98, v99, vcc
	v_mul_f32_e32 v100, v172, v98
	v_pk_mul_f32 v[94:95], v[94:95], v[100:101] op_sel_hi:[1,0]
	v_pk_mul_f32 v[96:97], v[96:97], v[100:101] op_sel_hi:[1,0]
	v_pk_mul_f32 v[94:95], v[134:135], v[94:95]
	v_pk_mul_f32 v[96:97], v[136:137], v[96:97]
	v_pk_mul_f32 v[90:91], v[90:91], v[100:101] op_sel_hi:[1,0]
	v_pk_mul_f32 v[92:93], v[92:93], v[100:101] op_sel_hi:[1,0]
	v_mov_b32_e32 v100, v172
	v_mov_b32_e32 v101, v172
	v_cvt_pk_bf16_f32 v82, v94, v95
	v_pk_mul_f32 v[88:89], v[88:89], v[100:101]
	v_pk_mul_f32 v[100:101], v[84:85], v[100:101]
	v_pk_mul_f32 v[90:91], v[130:131], v[90:91]
	v_cvt_pk_bf16_f32 v83, v96, v97
	v_pk_mul_f32 v[92:93], v[132:133], v[92:93]
	v_cvt_pk_bf16_f32 v84, v90, v91
	v_cvt_pk_bf16_f32 v85, v92, v93
	v_add_co_u32_e32 v90, vcc, s19, v116
	s_nop 1
	v_addc_co_u32_e32 v91, vcc, 0, v117, vcc
	global_store_dwordx4 v[90:91], v[82:85], off
	s_nop 1
	v_cvt_pk_bf16_f32 v82, v86, v87
	v_cvt_pk_bf16_f32 v83, v88, v89
	v_cvt_pk_bf16_f32 v84, v102, v103
	v_cvt_pk_bf16_f32 v85, v100, v101
	v_add_co_u32_e32 v86, vcc, 0x2000, v114
	s_nop 1
	v_addc_co_u32_e32 v87, vcc, 0, v115, vcc
	global_store_dwordx4 v[86:87], v[82:85], off
	s_and_saveexec_b64 s[26:27], s[42:43]
	s_cbranch_execz .LBB0_526
	v_add_u32_e32 v146, 32, v186
	v_lshlrev_b64 v[82:83], 5, v[146:147]
	v_lshl_add_u64 v[82:83], s[6:7], 0, v[82:83]
	v_lshl_add_u64 v[82:83], s[4:5], 2, v[82:83]
	global_store_dword v[82:83], v98, off
.LBB0_526:
	s_or_b64 exec, exec, s[26:27]
	ds_read_b128 v[82:85], v118 offset:768
	v_add_f32_e32 v88, v170, v171
	v_mov_b32_e32 v167, v166
	s_movk_i32 s19, 0x4000
	v_pk_mul_f32 v[70:71], v[70:71], v[166:167]
	s_waitcnt lgkmcnt(0)
	v_mov_b32_e32 v86, v83
	v_mov_b32_e32 v87, v84
	v_mov_b32_e32 v83, v85
	v_pk_add_f32 v[82:83], v[86:87], v[82:83]
	v_pk_mul_f32 v[86:87], v[66:67], v[166:167]
	v_add_f32_e32 v82, v82, v83
	v_add_f32_e32 v82, v88, v82
	v_fmamk_f32 v82, v82, 0x3baaaaab, v180
	v_mul_f32_e32 v83, 0x4b800000, v82
	v_cmp_gt_f32_e32 vcc, s79, v82
	s_nop 1
	v_cndmask_b32_e32 v82, v82, v83, vcc
	v_rsq_f32_e32 v82, v82
	s_nop 0
	v_mul_f32_e32 v83, 0x45800000, v82
	v_cndmask_b32_e32 v82, v82, v83, vcc
	v_mul_f32_e32 v84, v166, v82
	v_pk_mul_f32 v[78:79], v[78:79], v[84:85] op_sel_hi:[1,0]
	v_pk_mul_f32 v[80:81], v[80:81], v[84:85] op_sel_hi:[1,0]
	v_pk_mul_f32 v[78:79], v[134:135], v[78:79]
	v_pk_mul_f32 v[80:81], v[136:137], v[80:81]
	v_pk_mul_f32 v[74:75], v[74:75], v[84:85] op_sel_hi:[1,0]
	v_pk_mul_f32 v[76:77], v[76:77], v[84:85] op_sel_hi:[1,0]
	v_mov_b32_e32 v84, v166
	v_mov_b32_e32 v85, v166
	v_cvt_pk_bf16_f32 v66, v78, v79
	v_pk_mul_f32 v[72:73], v[72:73], v[84:85]
	v_pk_mul_f32 v[84:85], v[68:69], v[84:85]
	v_pk_mul_f32 v[74:75], v[130:131], v[74:75]
	v_cvt_pk_bf16_f32 v67, v80, v81
	v_pk_mul_f32 v[76:77], v[132:133], v[76:77]
	v_cvt_pk_bf16_f32 v68, v74, v75
	v_cvt_pk_bf16_f32 v69, v76, v77
	v_add_co_u32_e32 v74, vcc, s19, v116
	s_nop 1
	v_addc_co_u32_e32 v75, vcc, 0, v117, vcc
	global_store_dwordx4 v[74:75], v[66:69], off offset:2048
	s_nop 1
	v_cvt_pk_bf16_f32 v66, v70, v71
	v_cvt_pk_bf16_f32 v67, v72, v73
	v_cvt_pk_bf16_f32 v68, v86, v87
	v_cvt_pk_bf16_f32 v69, v84, v85
	v_add_co_u32_e32 v70, vcc, 0x3000, v114
	s_nop 1
	v_addc_co_u32_e32 v71, vcc, 0, v115, vcc
	global_store_dwordx4 v[70:71], v[66:69], off
	s_and_saveexec_b64 s[26:27], s[42:43]
	s_cbranch_execz .LBB0_528
	v_add_u32_e32 v146, 48, v186
	v_lshlrev_b64 v[66:67], 5, v[146:147]
	v_lshl_add_u64 v[66:67], s[6:7], 0, v[66:67]
	v_lshl_add_u64 v[66:67], s[4:5], 2, v[66:67]
	global_store_dword v[66:67], v82, off
.LBB0_528:
	s_or_b64 exec, exec, s[26:27]
	ds_read_b128 v[66:69], v118 offset:2048
	v_add_f32_e32 v72, v168, v169
	v_mov_b32_e32 v163, v162
	v_pk_mul_f32 v[54:55], v[54:55], v[162:163]
	v_add_u32_e32 v146, 0x80, v186
	s_waitcnt lgkmcnt(0)
	v_mov_b32_e32 v70, v67
	v_mov_b32_e32 v71, v68
	v_mov_b32_e32 v67, v69
	v_pk_add_f32 v[66:67], v[70:71], v[66:67]
	v_pk_mul_f32 v[70:71], v[50:51], v[162:163]
	v_add_f32_e32 v66, v66, v67
	v_add_f32_e32 v66, v72, v66
	v_fmamk_f32 v66, v66, 0x3baaaaab, v180
	v_mul_f32_e32 v67, 0x4b800000, v66
	v_cmp_gt_f32_e32 vcc, s79, v66
	s_nop 1
	v_cndmask_b32_e32 v66, v66, v67, vcc
	v_rsq_f32_e32 v66, v66
	s_nop 0
	v_mul_f32_e32 v67, 0x45800000, v66
	v_cndmask_b32_e32 v66, v66, v67, vcc
	v_mul_f32_e32 v68, v162, v66
	v_pk_mul_f32 v[62:63], v[62:63], v[68:69] op_sel_hi:[1,0]
	v_pk_mul_f32 v[64:65], v[64:65], v[68:69] op_sel_hi:[1,0]
	v_pk_mul_f32 v[62:63], v[134:135], v[62:63]
	v_pk_mul_f32 v[64:65], v[136:137], v[64:65]
	v_pk_mul_f32 v[58:59], v[58:59], v[68:69] op_sel_hi:[1,0]
	v_pk_mul_f32 v[60:61], v[60:61], v[68:69] op_sel_hi:[1,0]
	v_mov_b32_e32 v68, v162
	v_mov_b32_e32 v69, v162
	v_cvt_pk_bf16_f32 v50, v62, v63
	v_pk_mul_f32 v[56:57], v[56:57], v[68:69]
	v_pk_mul_f32 v[68:69], v[52:53], v[68:69]
	v_pk_mul_f32 v[58:59], v[130:131], v[58:59]
	v_cvt_pk_bf16_f32 v51, v64, v65
	v_pk_mul_f32 v[60:61], v[132:133], v[60:61]
	v_cvt_pk_bf16_f32 v52, v58, v59
	v_cvt_pk_bf16_f32 v53, v60, v61
	v_add_co_u32_e32 v58, vcc, s86, v116
	s_nop 1
	v_addc_co_u32_e32 v59, vcc, 0, v117, vcc
	global_store_dwordx4 v[58:59], v[50:53], off
	s_nop 1
	v_cvt_pk_bf16_f32 v50, v54, v55
	v_cvt_pk_bf16_f32 v51, v56, v57
	v_cvt_pk_bf16_f32 v52, v70, v71
	v_cvt_pk_bf16_f32 v53, v68, v69
	v_add_co_u32_e32 v54, vcc, 0x8000, v114
	s_nop 1
	v_addc_co_u32_e32 v55, vcc, 0, v115, vcc
	global_store_dwordx4 v[54:55], v[50:53], off
	s_and_saveexec_b64 s[26:27], s[42:43]
	s_cbranch_execz .LBB0_530
	v_lshlrev_b64 v[50:51], 5, v[146:147]
	v_lshl_add_u64 v[50:51], s[6:7], 0, v[50:51]
	v_lshl_add_u64 v[50:51], s[4:5], 2, v[50:51]
	global_store_dword v[50:51], v66, off
; #define LAS __attribute__((address_space(3)))
; __device__ __forceinline__ unsigned pk2(float lo, float hi) { return f2bf(lo) | (f2bf(hi) << 16); }
;     __device__ __forceinline__ void epi(const f32x4 (&acc)[2][2][4][2], const Unit& u, int wr, int wc, int fr, int fq) const {
;     ...
;             for (int m = 0; m < 4; ++m) { const f32x4 pt = *(const LAS f32x4*)(part + (ai * 128 + m * 16 + lrow) * 4);
;                 const float tot = ((pt.x + pt.y) + (pt.z + pt.w)) + kr2[ai][m]; const float rk = rsqrtf(tot * (1.f / DQK) + EPS); const float f = sc[ai][m] * rk;
;                 const f32x4 k0 = acc[ai][0][m][0] * f * g0, k1 = acc[ai][0][m][1] * f * g1, v0 = acc[ai][1][m][0] * sc[ai][m], v1 = acc[ai][1][m][1] * sc[ai][m];
;                 u32x4 w; w.x = pk2(k0[0], k0[1]); w.y = pk2(k0[2], k0[3]); w.z = pk2(k1[0], k1[1]); w.w = pk2(k1[2], k1[3]);
;                 *(u32x4*)(kb + (size_t)(ai * 128 + m * 16) * DQK * 2 + koff) = w;
;                 w.x = pk2(v0[0], v0[1]); w.y = pk2(v0[2], v0[3]); w.z = pk2(v1[0], v1[1]); w.w = pk2(v1[2], v1[3]);
;                 *(u32x4*)(vb + (size_t)(ai * 128 + m * 16) * DVH * 2 + voff) = w;
;                 if (wc == 0 && fq == 0) RSTDK[(size_t)(rowt + ai * 128 + m * 16 + lrow) * 8 + h] = rk; }
.LBB0_530:
	s_or_b64 exec, exec, s[26:27]
	ds_read_b128 v[50:53], v118 offset:2304
	v_add_f32_e32 v56, v164, v165
	v_mov_b32_e32 v159, v158
	s_mov_b32 s19, 0xd000
	v_pk_mul_f32 v[38:39], v[38:39], v[158:159]
	s_waitcnt lgkmcnt(0)
	v_mov_b32_e32 v54, v51
	v_mov_b32_e32 v55, v52
	v_mov_b32_e32 v51, v53
	v_pk_add_f32 v[50:51], v[54:55], v[50:51]
	v_pk_mul_f32 v[54:55], v[34:35], v[158:159]
	v_add_f32_e32 v50, v50, v51
	v_add_f32_e32 v50, v56, v50
	v_fmamk_f32 v50, v50, 0x3baaaaab, v180
	v_mul_f32_e32 v51, 0x4b800000, v50
	v_cmp_gt_f32_e32 vcc, s79, v50
	s_nop 1
	v_cndmask_b32_e32 v50, v50, v51, vcc
	v_rsq_f32_e32 v50, v50
	s_nop 0
	v_mul_f32_e32 v51, 0x45800000, v50
	v_cndmask_b32_e32 v50, v50, v51, vcc
	v_mul_f32_e32 v52, v158, v50
	v_pk_mul_f32 v[46:47], v[46:47], v[52:53] op_sel_hi:[1,0]
	v_pk_mul_f32 v[48:49], v[48:49], v[52:53] op_sel_hi:[1,0]
	v_pk_mul_f32 v[46:47], v[134:135], v[46:47]
	v_pk_mul_f32 v[48:49], v[136:137], v[48:49]
	v_pk_mul_f32 v[42:43], v[42:43], v[52:53] op_sel_hi:[1,0]
	v_pk_mul_f32 v[44:45], v[44:45], v[52:53] op_sel_hi:[1,0]
	v_mov_b32_e32 v52, v158
	v_mov_b32_e32 v53, v158
	v_cvt_pk_bf16_f32 v34, v46, v47
	v_pk_mul_f32 v[40:41], v[40:41], v[52:53]
	v_pk_mul_f32 v[52:53], v[36:37], v[52:53]
	v_pk_mul_f32 v[42:43], v[130:131], v[42:43]
	v_cvt_pk_bf16_f32 v35, v48, v49
	v_pk_mul_f32 v[44:45], v[132:133], v[44:45]
	v_cvt_pk_bf16_f32 v36, v42, v43
	v_cvt_pk_bf16_f32 v37, v44, v45
	v_add_co_u32_e32 v42, vcc, s19, v116
	s_nop 1
	v_addc_co_u32_e32 v43, vcc, 0, v117, vcc
	global_store_dwordx4 v[42:43], v[34:37], off offset:2048
	s_nop 1
	v_cvt_pk_bf16_f32 v34, v38, v39
	v_cvt_pk_bf16_f32 v35, v40, v41
	v_cvt_pk_bf16_f32 v36, v54, v55
	v_cvt_pk_bf16_f32 v37, v52, v53
	v_add_co_u32_e32 v38, vcc, 0x9000, v114
	s_nop 1
	v_addc_co_u32_e32 v39, vcc, 0, v115, vcc
	global_store_dwordx4 v[38:39], v[34:37], off
	s_and_saveexec_b64 s[26:27], s[42:43]
	s_cbranch_execz .LBB0_532
	v_add_u32_e32 v34, 16, v146
	v_mov_b32_e32 v35, v147
	v_lshlrev_b64 v[34:35], 5, v[34:35]
	v_lshl_add_u64 v[34:35], s[6:7], 0, v[34:35]
	v_lshl_add_u64 v[34:35], s[4:5], 2, v[34:35]
	global_store_dword v[34:35], v50, off
.LBB0_532:
	s_or_b64 exec, exec, s[26:27]
	ds_read_b128 v[34:37], v118 offset:2560
	v_add_f32_e32 v40, v160, v161
	v_mov_b32_e32 v155, v154
	s_mov_b32 s19, 0xf000
	v_pk_mul_f32 v[22:23], v[22:23], v[154:155]
	s_waitcnt lgkmcnt(0)
	v_mov_b32_e32 v38, v35
	v_mov_b32_e32 v39, v36
	v_mov_b32_e32 v35, v37
	v_pk_add_f32 v[34:35], v[38:39], v[34:35]
	v_pk_mul_f32 v[38:39], v[18:19], v[154:155]
	v_add_f32_e32 v34, v34, v35
	v_add_f32_e32 v34, v40, v34
	v_fmamk_f32 v34, v34, 0x3baaaaab, v180
	v_mul_f32_e32 v35, 0x4b800000, v34
	v_cmp_gt_f32_e32 vcc, s79, v34
	s_nop 1
	v_cndmask_b32_e32 v34, v34, v35, vcc
	v_rsq_f32_e32 v34, v34
	s_nop 0
	v_mul_f32_e32 v35, 0x45800000, v34
	v_cndmask_b32_e32 v34, v34, v35, vcc
	v_mul_f32_e32 v36, v154, v34
	v_pk_mul_f32 v[30:31], v[30:31], v[36:37] op_sel_hi:[1,0]
	v_pk_mul_f32 v[32:33], v[32:33], v[36:37] op_sel_hi:[1,0]
	v_pk_mul_f32 v[30:31], v[134:135], v[30:31]
	v_pk_mul_f32 v[32:33], v[136:137], v[32:33]
	v_pk_mul_f32 v[26:27], v[26:27], v[36:37] op_sel_hi:[1,0]
	v_pk_mul_f32 v[28:29], v[28:29], v[36:37] op_sel_hi:[1,0]
	v_mov_b32_e32 v36, v154
	v_mov_b32_e32 v37, v154
	v_cvt_pk_bf16_f32 v18, v30, v31
	v_pk_mul_f32 v[24:25], v[24:25], v[36:37]
	v_pk_mul_f32 v[36:37], v[20:21], v[36:37]
	v_pk_mul_f32 v[26:27], v[130:131], v[26:27]
	v_cvt_pk_bf16_f32 v19, v32, v33
	v_pk_mul_f32 v[28:29], v[132:133], v[28:29]
	v_cvt_pk_bf16_f32 v20, v26, v27
	v_cvt_pk_bf16_f32 v21, v28, v29
	v_add_co_u32_e32 v26, vcc, s19, v116
	s_nop 1
	v_addc_co_u32_e32 v27, vcc, 0, v117, vcc
	global_store_dwordx4 v[26:27], v[18:21], off
	s_nop 1
	v_cvt_pk_bf16_f32 v18, v22, v23
	v_cvt_pk_bf16_f32 v19, v24, v25
	v_cvt_pk_bf16_f32 v20, v38, v39
	v_cvt_pk_bf16_f32 v21, v36, v37
	v_add_co_u32_e32 v22, vcc, 0xa000, v114
	s_nop 1
	v_addc_co_u32_e32 v23, vcc, 0, v115, vcc
	global_store_dwordx4 v[22:23], v[18:21], off
	s_and_saveexec_b64 s[26:27], s[42:43]
	s_cbranch_execz .LBB0_534
	v_add_u32_e32 v18, 32, v146
	v_mov_b32_e32 v19, v147
	v_lshlrev_b64 v[18:19], 5, v[18:19]
	v_lshl_add_u64 v[18:19], s[6:7], 0, v[18:19]
	v_lshl_add_u64 v[18:19], s[4:5], 2, v[18:19]
	global_store_dword v[18:19], v34, off
.LBB0_534:
	s_or_b64 exec, exec, s[26:27]
	ds_read_b128 v[18:21], v118 offset:2816
	v_add_f32_e32 v24, v156, v157
	v_mov_b32_e32 v153, v152
	v_pk_mul_f32 v[6:7], v[6:7], v[152:153]
	s_waitcnt lgkmcnt(0)
	v_mov_b32_e32 v22, v19
	v_mov_b32_e32 v23, v20
	v_mov_b32_e32 v19, v21
	v_pk_add_f32 v[18:19], v[22:23], v[18:19]
	v_pk_mul_f32 v[22:23], v[2:3], v[152:153]
	v_add_f32_e32 v18, v18, v19
	v_add_f32_e32 v18, v24, v18
	v_fmamk_f32 v18, v18, 0x3baaaaab, v180
	v_mul_f32_e32 v19, 0x4b800000, v18
	v_cmp_gt_f32_e32 vcc, s79, v18
	s_nop 1
	v_cndmask_b32_e32 v18, v18, v19, vcc
	v_rsq_f32_e32 v18, v18
	s_nop 0
	v_mul_f32_e32 v19, 0x45800000, v18
	v_cndmask_b32_e32 v18, v18, v19, vcc
	v_mul_f32_e32 v20, v152, v18
	v_pk_mul_f32 v[14:15], v[14:15], v[20:21] op_sel_hi:[1,0]
	v_pk_mul_f32 v[16:17], v[16:17], v[20:21] op_sel_hi:[1,0]
	v_pk_mul_f32 v[14:15], v[134:135], v[14:15]
	v_pk_mul_f32 v[16:17], v[136:137], v[16:17]
	v_pk_mul_f32 v[10:11], v[10:11], v[20:21] op_sel_hi:[1,0]
	v_pk_mul_f32 v[12:13], v[12:13], v[20:21] op_sel_hi:[1,0]
	v_mov_b32_e32 v20, v152
	v_mov_b32_e32 v21, v152
	v_cvt_pk_bf16_f32 v2, v14, v15
	v_pk_mul_f32 v[8:9], v[8:9], v[20:21]
	v_pk_mul_f32 v[20:21], v[4:5], v[20:21]
	v_pk_mul_f32 v[10:11], v[130:131], v[10:11]
	v_cvt_pk_bf16_f32 v3, v16, v17
	v_pk_mul_f32 v[12:13], v[132:133], v[12:13]
	v_cvt_pk_bf16_f32 v4, v10, v11
	v_cvt_pk_bf16_f32 v5, v12, v13
	v_add_co_u32_e32 v10, vcc, s81, v116
	s_nop 1
	v_addc_co_u32_e32 v11, vcc, 0, v117, vcc
	global_store_dwordx4 v[10:11], v[2:5], off offset:2048
	s_nop 1
	v_cvt_pk_bf16_f32 v2, v6, v7
	v_cvt_pk_bf16_f32 v3, v8, v9
	v_cvt_pk_bf16_f32 v4, v22, v23
	v_cvt_pk_bf16_f32 v5, v20, v21
	v_add_co_u32_e32 v6, vcc, 0xb000, v114
	s_nop 1
	v_addc_co_u32_e32 v7, vcc, 0, v115, vcc
	global_store_dwordx4 v[6:7], v[2:5], off
	s_and_saveexec_b64 s[26:27], s[42:43]
	s_cbranch_execz .LBB0_536
	v_add_u32_e32 v146, 48, v146
	v_lshlrev_b64 v[2:3], 5, v[146:147]
	v_lshl_add_u64 v[2:3], s[6:7], 0, v[2:3]
	v_lshl_add_u64 v[2:3], s[4:5], 2, v[2:3]
	global_store_dword v[2:3], v18, off

; #define LAS __attribute__((address_space(3)))
; #define WSW(T, off, l) WSP(T, WS_WSET + (size_t)(l) * WSET_STRIDE + (off))
; __device__ __forceinline__ void tr_item(const float* W, int ldw, int k0, int n0, bf16* WT, int ldt, int drow0, LAS float* scr, int lane, const float* kscale = nullptr) {
;     const float* src = W + (size_t)(k0 + (lane >> 4)) * ldw + n0 + (lane & 15) * 4;
;     f32x4 v[16];
; #pragma unroll
;     for (int i = 0; i < 16; ++i) v[i] = __builtin_nontemporal_load((const f32x4*)(src + (size_t)(4 * i) * ldw));
;     LAS float* wp = scr + (lane >> 4) * 65 + (lane & 15) * 4;
; #pragma unroll
;     for (int i = 0; i < 16; ++i) { LAS float* q = wp + (4 * i) * 65; const float ks = kscale ? kscale[k0 + 4 * i + (lane >> 4)] : 1.f; q[0] = v[i].x * ks; q[1] = v[i].y * ks; q[2] = v[i].z * ks; q[3] = v[i].w * ks; }
;     asm volatile("s_waitcnt lgkmcnt(0)" ::: "memory");
; __device__ __forceinline__ void convert_tile(const Args& a, GAS unsigned char* wsb, int l, int t, LAS float* scr, int lane) {
;     ...
;     if (r < I_OUT) { const int kb = r / 32, nb = r - kb * 32; tr_item(INP(21) + (size_t)l * DM * DM, DM, kb * 64, nb * 64, WSW(bf16, W_OUT, l), DM, nb * 64, scr, lane); return; }
.LBB0_1275:
	s_andn2_b64 vcc, exec, s[6:7]
	s_cbranch_vccnz .LBB0_1277
	s_lshl_b32 s6, s17, 1
	s_and_b32 s6, s6, 0x1fc0
	s_addk_i32 s6, 0xf240
	s_lshl_b32 s7, s17, 6
	v_or_b32_e32 v146, s6, v67
	v_readlane_b32 s10, v252, 60
	s_and_b32 s8, s7, 0x7c0
	v_lshlrev_b64 v[2:3], 13, v[146:147]
	v_readlane_b32 s11, v252, 61
	s_lshl_b32 s12, s8, 2
	v_lshlrev_b32_e32 v146, 2, v66
	v_lshl_add_u64 v[2:3], s[10:11], 0, v[2:3]
	v_lshl_add_u64 v[2:3], v[2:3], 0, s[12:13]
	v_lshl_add_u64 v[62:63], v[2:3], 0, v[146:147]
	v_add_co_u32_e32 v6, vcc, s83, v62
	s_mov_b32 s7, 0x20000
	s_nop 0
	v_addc_co_u32_e32 v7, vcc, 0, v63, vcc
	v_add_co_u32_e32 v10, vcc, s81, v62
	global_load_dwordx4 v[2:5], v[62:63], off nt
	s_nop 0
	global_load_dwordx4 v[6:9], v[6:7], off nt
	v_addc_co_u32_e32 v11, vcc, 0, v63, vcc
	v_add_co_u32_e32 v14, vcc, s82, v62
	s_nop 1
	v_addc_co_u32_e32 v15, vcc, 0, v63, vcc
	global_load_dwordx4 v[10:13], v[10:11], off nt
	s_nop 0
	global_load_dwordx4 v[14:17], v[14:15], off nt
	v_add_co_u32_e32 v18, vcc, s7, v62
	s_mov_b32 s7, 0x28000
	s_nop 0
	v_addc_co_u32_e32 v19, vcc, 0, v63, vcc
	v_add_co_u32_e32 v22, vcc, s7, v62
	s_mov_b32 s7, 0x30000
	s_nop 0
	v_addc_co_u32_e32 v23, vcc, 0, v63, vcc
	global_load_dwordx4 v[18:21], v[18:19], off nt
	s_nop 0
	global_load_dwordx4 v[22:25], v[22:23], off nt
	v_add_co_u32_e32 v26, vcc, s7, v62
	s_mov_b32 s7, 0x38000
	s_nop 0
	v_addc_co_u32_e32 v27, vcc, 0, v63, vcc
	v_add_co_u32_e32 v30, vcc, s7, v62
	s_mov_b32 s7, 0x40000
	s_nop 0
	v_addc_co_u32_e32 v31, vcc, 0, v63, vcc
	global_load_dwordx4 v[26:29], v[26:27], off nt
	s_nop 0
	global_load_dwordx4 v[30:33], v[30:31], off nt
	v_add_co_u32_e32 v34, vcc, s7, v62
	s_mov_b32 s7, 0x48000
	s_nop 0
	v_addc_co_u32_e32 v35, vcc, 0, v63, vcc
	v_add_co_u32_e32 v38, vcc, s7, v62
	s_mov_b32 s7, 0x50000
	s_nop 0
	v_addc_co_u32_e32 v39, vcc, 0, v63, vcc
	global_load_dwordx4 v[34:37], v[34:35], off nt
	s_nop 0
	global_load_dwordx4 v[38:41], v[38:39], off nt
	v_add_co_u32_e32 v42, vcc, s7, v62
	s_mov_b32 s7, 0x58000
	s_nop 0
	v_addc_co_u32_e32 v43, vcc, 0, v63, vcc
	v_add_co_u32_e32 v46, vcc, s7, v62
	s_mov_b32 s7, 0x60000
	s_nop 0
	v_addc_co_u32_e32 v47, vcc, 0, v63, vcc
	global_load_dwordx4 v[42:45], v[42:43], off nt
	s_nop 0
	global_load_dwordx4 v[46:49], v[46:47], off nt
	v_add_co_u32_e32 v50, vcc, s7, v62
	s_mov_b32 s7, 0x68000
	s_nop 0
	v_addc_co_u32_e32 v51, vcc, 0, v63, vcc
	v_add_co_u32_e32 v54, vcc, s7, v62
	s_mov_b32 s7, 0x70000
	s_nop 0
	v_addc_co_u32_e32 v55, vcc, 0, v63, vcc
	global_load_dwordx4 v[50:53], v[50:51], off nt
	s_nop 0
	global_load_dwordx4 v[54:57], v[54:55], off nt
	v_add_co_u32_e32 v58, vcc, s7, v62
	s_mov_b32 s7, 0x78000
	s_nop 0
	v_addc_co_u32_e32 v59, vcc, 0, v63, vcc
	global_load_dwordx4 v[58:61], v[58:59], off nt
	v_add_co_u32_e32 v62, vcc, s7, v62
	s_mov_b32 s7, s13
	s_nop 0
	v_addc_co_u32_e32 v63, vcc, 0, v63, vcc
	global_load_dwordx4 v[62:65], v[62:63], off nt
	s_waitcnt vmcnt(15)
	ds_write2_b32 v95, v2, v3 offset1:1
	ds_write2_b32 v95, v4, v5 offset0:2 offset1:3
	v_add_u32_e32 v2, 0x410, v95
	s_waitcnt vmcnt(14)
	ds_write2_b32 v2, v6, v7 offset1:1
	v_add_u32_e32 v2, 0x418, v95
	ds_write2_b32 v2, v8, v9 offset1:1
	v_add_u32_e32 v2, 0x820, v95
	s_waitcnt vmcnt(13)
	ds_write2_b32 v2, v10, v11 offset1:1
	v_add_u32_e32 v2, 0x828, v95
	ds_write2_b32 v2, v12, v13 offset1:1
	v_add_u32_e32 v2, 0xc30, v95
	s_waitcnt vmcnt(12)
	ds_write2_b32 v2, v14, v15 offset1:1
	v_add_u32_e32 v2, 0xc38, v95
	ds_write2_b32 v2, v16, v17 offset1:1
	v_add_u32_e32 v2, 0x1040, v95
	s_waitcnt vmcnt(11)
	ds_write2_b32 v2, v18, v19 offset1:1
	v_add_u32_e32 v2, 0x1048, v95
	ds_write2_b32 v2, v20, v21 offset1:1
	v_add_u32_e32 v2, 0x1450, v95
	s_waitcnt vmcnt(10)
	ds_write2_b32 v2, v22, v23 offset1:1
	v_add_u32_e32 v2, 0x1458, v95
	ds_write2_b32 v2, v24, v25 offset1:1
	v_add_u32_e32 v2, 0x1860, v95
	s_waitcnt vmcnt(9)
	ds_write2_b32 v2, v26, v27 offset1:1
	v_add_u32_e32 v2, 0x1868, v95
	ds_write2_b32 v2, v28, v29 offset1:1
	v_add_u32_e32 v2, 0x1c70, v95
	s_waitcnt vmcnt(8)
	ds_write2_b32 v2, v30, v31 offset1:1
	v_add_u32_e32 v2, 0x1c78, v95
	ds_write2_b32 v2, v32, v33 offset1:1
	v_add_u32_e32 v2, 0x2080, v95
	v_add_u32_e32 v26, 0x400, v97
	s_waitcnt vmcnt(7)
	ds_write2_b32 v2, v34, v35 offset1:1
	v_add_u32_e32 v2, 0x2088, v95
	ds_write2_b32 v2, v36, v37 offset1:1
	v_add_u32_e32 v2, 0x2490, v95
	s_waitcnt vmcnt(6)
	ds_write2_b32 v2, v38, v39 offset1:1
	v_add_u32_e32 v2, 0x2498, v95
	ds_write2_b32 v2, v40, v41 offset1:1
	v_add_u32_e32 v2, 0x28a0, v95
	s_waitcnt vmcnt(5)
	ds_write2_b32 v2, v42, v43 offset1:1
	v_add_u32_e32 v2, 0x28a8, v95
	ds_write2_b32 v2, v44, v45 offset1:1
	v_add_u32_e32 v2, 0x2cb0, v95
	s_waitcnt vmcnt(4)
	ds_write2_b32 v2, v46, v47 offset1:1
	v_add_u32_e32 v2, 0x2cb8, v95
	ds_write2_b32 v2, v48, v49 offset1:1
	v_add_u32_e32 v2, 0x30c0, v95
	s_waitcnt vmcnt(3)
	ds_write2_b32 v2, v50, v51 offset1:1
	v_add_u32_e32 v2, 0x30c8, v95
	ds_write2_b32 v2, v52, v53 offset1:1
	v_add_u32_e32 v2, 0x34d0, v95
	s_waitcnt vmcnt(2)
; #define LAS __attribute__((address_space(3)))
; __device__ __forceinline__ unsigned pk2(float lo, float hi) { return f2bf(lo) | (f2bf(hi) << 16); }
; __device__ __forceinline__ void tr_item(const float* W, int ldw, int k0, int n0, bf16* WT, int ldt, int drow0, LAS float* scr, int lane, const float* kscale = nullptr) {
;     ...
;     const int kc = lane & 7;
; #pragma unroll
;     for (int j = 0; j < 8; ++j) { const int n = (lane >> 3) + 8 * j; const LAS float* sp = scr + (8 * kc) * 65 + n;
;         u32x4 o; o.x = pk2(sp[0 * 65], sp[1 * 65]); o.y = pk2(sp[2 * 65], sp[3 * 65]); o.z = pk2(sp[4 * 65], sp[5 * 65]); o.w = pk2(sp[6 * 65], sp[7 * 65]);
;         __builtin_nontemporal_store(o, (u32x4*)(WT + (size_t)(drow0 + n) * ldt + k0 + 8 * kc)); }
;     asm volatile("s_waitcnt lgkmcnt(0)" ::: "memory");
	ds_write2_b32 v2, v54, v55 offset1:1
	v_add_u32_e32 v2, 0x34d8, v95
	ds_write2_b32 v2, v56, v57 offset1:1
	v_add_u32_e32 v2, 0x38e0, v95
	s_waitcnt vmcnt(1)
	ds_write2_b32 v2, v58, v59 offset1:1
	v_add_u32_e32 v2, 0x38e8, v95
	ds_write2_b32 v2, v60, v61 offset1:1
	v_add_u32_e32 v2, 0x3cf0, v95
	s_waitcnt vmcnt(0)
	ds_write2_b32 v2, v62, v63 offset1:1
	v_add_u32_e32 v2, 0x3cf8, v95
	ds_write2_b32 v2, v64, v65 offset1:1
	s_waitcnt lgkmcnt(0)
	ds_read2_b32 v[8:9], v97 offset1:8
	ds_read2_b32 v[10:11], v97 offset0:65 offset1:73
	ds_read2_b32 v[12:13], v97 offset0:130 offset1:138
	ds_read2_b32 v[14:15], v97 offset0:195 offset1:203
	ds_read2_b32 v[16:17], v26 offset0:4 offset1:12
	s_waitcnt lgkmcnt(4)
	s_waitcnt lgkmcnt(3)
	ds_read2_b32 v[18:19], v26 offset0:69 offset1:77
	v_cvt_pk_bf16_f32 v4, v8, v10
	s_waitcnt lgkmcnt(3)
	s_waitcnt lgkmcnt(2)
	ds_read2_b32 v[20:21], v26 offset0:134 offset1:142
	ds_read2_b32 v[22:23], v26 offset0:199 offset1:207
	v_cvt_pk_bf16_f32 v5, v12, v14
	s_waitcnt lgkmcnt(3)
	s_waitcnt lgkmcnt(2)
	v_cvt_pk_bf16_f32 v6, v16, v18
	s_waitcnt lgkmcnt(1)
	s_waitcnt lgkmcnt(0)
	v_cvt_pk_bf16_f32 v7, v20, v22
	v_or_b32_e32 v8, s8, v96
	v_lshl_add_u64 v[2:3], s[6:7], 1, v[72:73]
	v_lshlrev_b32_e32 v146, 12, v8
	v_lshl_add_u64 v[24:25], v[2:3], 0, v[146:147]
	global_store_dwordx4 v[24:25], v[4:7], off nt
	v_or_b32_e32 v10, s8, v98
	s_nop 0
	v_cvt_pk_bf16_f32 v4, v9, v11
	v_cvt_pk_bf16_f32 v5, v13, v15
	v_cvt_pk_bf16_f32 v6, v17, v19
	v_lshlrev_b32_e32 v146, 12, v10
	v_cvt_pk_bf16_f32 v7, v21, v23
	ds_read2_b32 v[8:9], v97 offset0:16 offset1:24
	v_lshl_add_u64 v[10:11], v[2:3], 0, v[146:147]
	global_store_dwordx4 v[10:11], v[4:7], off nt
	ds_read2_b32 v[10:11], v97 offset0:81 offset1:89
	ds_read2_b32 v[12:13], v97 offset0:146 offset1:154
	ds_read2_b32 v[14:15], v97 offset0:211 offset1:219
	s_waitcnt lgkmcnt(3)
	s_waitcnt lgkmcnt(2)
	ds_read2_b32 v[16:17], v26 offset0:20 offset1:28
	ds_read2_b32 v[18:19], v26 offset0:85 offset1:93
	v_cvt_pk_bf16_f32 v4, v8, v10
	s_waitcnt lgkmcnt(3)
	s_waitcnt lgkmcnt(2)
	ds_read2_b32 v[20:21], v26 offset0:150 offset1:158
	ds_read2_b32 v[22:23], v26 offset0:215 offset1:223
	v_cvt_pk_bf16_f32 v5, v12, v14
	s_waitcnt lgkmcnt(3)
	s_waitcnt lgkmcnt(2)
	v_cvt_pk_bf16_f32 v6, v16, v18
	s_waitcnt lgkmcnt(1)
	s_waitcnt lgkmcnt(0)
	v_cvt_pk_bf16_f32 v7, v20, v22
	v_or_b32_e32 v8, s8, v99
	v_lshlrev_b32_e32 v146, 12, v8
	v_lshl_add_u64 v[24:25], v[2:3], 0, v[146:147]
	global_store_dwordx4 v[24:25], v[4:7], off nt
	v_or_b32_e32 v10, s8, v100
	s_nop 0
	v_cvt_pk_bf16_f32 v4, v9, v11
	v_cvt_pk_bf16_f32 v5, v13, v15
	v_cvt_pk_bf16_f32 v6, v17, v19
	v_lshlrev_b32_e32 v146, 12, v10
	v_cvt_pk_bf16_f32 v7, v21, v23
	ds_read2_b32 v[8:9], v97 offset0:32 offset1:40
	v_lshl_add_u64 v[10:11], v[2:3], 0, v[146:147]
	global_store_dwordx4 v[10:11], v[4:7], off nt
	ds_read2_b32 v[10:11], v97 offset0:97 offset1:105
	ds_read2_b32 v[12:13], v97 offset0:162 offset1:170
	ds_read2_b32 v[14:15], v97 offset0:227 offset1:235
	s_waitcnt lgkmcnt(3)
	s_waitcnt lgkmcnt(2)
	ds_read2_b32 v[16:17], v26 offset0:36 offset1:44
	ds_read2_b32 v[18:19], v26 offset0:101 offset1:109
	v_cvt_pk_bf16_f32 v4, v8, v10
	s_waitcnt lgkmcnt(3)
	s_waitcnt lgkmcnt(2)
	ds_read2_b32 v[20:21], v26 offset0:166 offset1:174
	ds_read2_b32 v[22:23], v26 offset0:231 offset1:239
	v_cvt_pk_bf16_f32 v5, v12, v14
	s_waitcnt lgkmcnt(3)
	s_waitcnt lgkmcnt(2)
	v_cvt_pk_bf16_f32 v6, v16, v18
	s_waitcnt lgkmcnt(1)
	s_waitcnt lgkmcnt(0)
	v_cvt_pk_bf16_f32 v7, v20, v22
	v_or_b32_e32 v8, s8, v101
	v_lshlrev_b32_e32 v146, 12, v8
	v_lshl_add_u64 v[24:25], v[2:3], 0, v[146:147]
	global_store_dwordx4 v[24:25], v[4:7], off nt
	v_or_b32_e32 v10, s8, v102
	s_nop 0
	v_cvt_pk_bf16_f32 v4, v9, v11
	v_cvt_pk_bf16_f32 v5, v13, v15
	v_cvt_pk_bf16_f32 v6, v17, v19
	v_lshlrev_b32_e32 v146, 12, v10
	v_cvt_pk_bf16_f32 v7, v21, v23
	ds_read2_b32 v[8:9], v97 offset0:48 offset1:56
	v_lshl_add_u64 v[10:11], v[2:3], 0, v[146:147]
	global_store_dwordx4 v[10:11], v[4:7], off nt
	ds_read2_b32 v[10:11], v97 offset0:113 offset1:121
	ds_read2_b32 v[12:13], v97 offset0:178 offset1:186
	ds_read2_b32 v[14:15], v97 offset0:243 offset1:251
	s_waitcnt lgkmcnt(3)
	s_waitcnt lgkmcnt(2)
	ds_read2_b32 v[16:17], v26 offset0:52 offset1:60
	ds_read2_b32 v[18:19], v26 offset0:117 offset1:125
	v_cvt_pk_bf16_f32 v4, v8, v10
	s_waitcnt lgkmcnt(3)
	s_waitcnt lgkmcnt(2)
	ds_read2_b32 v[20:21], v26 offset0:182 offset1:190
	ds_read2_b32 v[22:23], v26 offset0:247 offset1:255
	v_cvt_pk_bf16_f32 v5, v12, v14
	s_waitcnt lgkmcnt(3)
	s_waitcnt lgkmcnt(2)
	v_cvt_pk_bf16_f32 v6, v16, v18
	s_waitcnt lgkmcnt(1)
	s_waitcnt lgkmcnt(0)
	v_cvt_pk_bf16_f32 v7, v20, v22
	v_or_b32_e32 v8, s8, v103
	v_lshlrev_b32_e32 v146, 12, v8
	v_lshl_add_u64 v[24:25], v[2:3], 0, v[146:147]
	global_store_dwordx4 v[24:25], v[4:7], off nt
	s_nop 1
	v_cvt_pk_bf16_f32 v4, v9, v11
	v_cvt_pk_bf16_f32 v5, v13, v15
	v_cvt_pk_bf16_f32 v6, v17, v19
	v_cvt_pk_bf16_f32 v7, v21, v23
	v_or_b32_e32 v8, s8, v104
	v_lshlrev_b32_e32 v146, 12, v8
	v_lshl_add_u64 v[2:3], v[2:3], 0, v[146:147]
	global_store_dwordx4 v[2:3], v[4:7], off nt
	s_waitcnt lgkmcnt(0)

; #define LAS __attribute__((address_space(3)))
; __device__ __forceinline__ unsigned pk2(float lo, float hi) { return f2bf(lo) | (f2bf(hi) << 16); }
; __device__ __forceinline__ void tr_item(const float* W, int ldw, int k0, int n0, bf16* WT, int ldt, int drow0, LAS float* scr, int lane, const float* kscale = nullptr) {
;     ...
;     for (int i = 0; i < 16; ++i) { LAS float* q = wp + (4 * i) * 65; const float ks = kscale ? kscale[k0 + 4 * i + (lane >> 4)] : 1.f; q[0] = v[i].x * ks; q[1] = v[i].y * ks; q[2] = v[i].z * ks; q[3] = v[i].w * ks; }
;     asm volatile("s_waitcnt lgkmcnt(0)" ::: "memory");
;     const int kc = lane & 7;
; #pragma unroll
;     for (int j = 0; j < 8; ++j) { const int n = (lane >> 3) + 8 * j; const LAS float* sp = scr + (8 * kc) * 65 + n;
;         u32x4 o; o.x = pk2(sp[0 * 65], sp[1 * 65]); o.y = pk2(sp[2 * 65], sp[3 * 65]); o.z = pk2(sp[4 * 65], sp[5 * 65]); o.w = pk2(sp[6 * 65], sp[7 * 65]);
;         __builtin_nontemporal_store(o, (u32x4*)(WT + (size_t)(drow0 + n) * ldt + k0 + 8 * kc)); }
;     asm volatile("s_waitcnt lgkmcnt(0)" ::: "memory");
.LBB0_1303:
	s_waitcnt vmcnt(0)
	v_pk_mul_f32 v[2:3], v[2:3], v[10:11] op_sel_hi:[1,0]
	v_add_u32_e32 v6, 0x3cf0, v95
	ds_write2_b32 v6, v2, v3 offset1:1
	v_pk_mul_f32 v[2:3], v[4:5], v[10:11] op_sel_hi:[1,0]
	v_add_u32_e32 v4, 0x3cf8, v95
	ds_write2_b32 v4, v2, v3 offset1:1
	s_waitcnt lgkmcnt(0)
	ds_read2_b32 v[8:9], v97 offset1:8
	ds_read2_b32 v[10:11], v97 offset0:65 offset1:73
	ds_read2_b32 v[12:13], v97 offset0:130 offset1:138
	ds_read2_b32 v[14:15], v97 offset0:195 offset1:203
	v_add_u32_e32 v26, 0x400, v97
	s_waitcnt lgkmcnt(3)
	s_waitcnt lgkmcnt(2)
	ds_read2_b32 v[16:17], v26 offset0:4 offset1:12
	ds_read2_b32 v[18:19], v26 offset0:69 offset1:77
	v_cvt_pk_bf16_f32 v4, v8, v10
	s_waitcnt lgkmcnt(3)
	s_waitcnt lgkmcnt(2)
	ds_read2_b32 v[20:21], v26 offset0:134 offset1:142
	ds_read2_b32 v[22:23], v26 offset0:199 offset1:207
	v_cvt_pk_bf16_f32 v5, v12, v14
	s_waitcnt lgkmcnt(3)
	s_waitcnt lgkmcnt(2)
	v_cvt_pk_bf16_f32 v6, v16, v18
	s_waitcnt lgkmcnt(1)
	s_waitcnt lgkmcnt(0)
	s_mov_b32 s7, s13
	v_cvt_pk_bf16_f32 v7, v20, v22
	v_or_b32_e32 v8, s10, v96
	v_lshl_add_u64 v[2:3], s[6:7], 1, v[74:75]
	v_lshlrev_b32_e32 v146, 9, v8
	v_lshl_add_u64 v[24:25], v[2:3], 0, v[146:147]
	global_store_dwordx4 v[24:25], v[4:7], off nt
	v_or_b32_e32 v10, s10, v98
	s_nop 0
	v_cvt_pk_bf16_f32 v4, v9, v11
	v_cvt_pk_bf16_f32 v5, v13, v15
	v_cvt_pk_bf16_f32 v6, v17, v19
	v_lshlrev_b32_e32 v146, 9, v10
	v_cvt_pk_bf16_f32 v7, v21, v23
	ds_read2_b32 v[8:9], v97 offset0:16 offset1:24
	v_lshl_add_u64 v[10:11], v[2:3], 0, v[146:147]
	global_store_dwordx4 v[10:11], v[4:7], off nt
	ds_read2_b32 v[10:11], v97 offset0:81 offset1:89
	ds_read2_b32 v[12:13], v97 offset0:146 offset1:154
	ds_read2_b32 v[14:15], v97 offset0:211 offset1:219
	s_waitcnt lgkmcnt(3)
	s_waitcnt lgkmcnt(2)
	ds_read2_b32 v[16:17], v26 offset0:20 offset1:28
	ds_read2_b32 v[18:19], v26 offset0:85 offset1:93
	v_cvt_pk_bf16_f32 v4, v8, v10
	s_waitcnt lgkmcnt(3)
	s_waitcnt lgkmcnt(2)
	ds_read2_b32 v[20:21], v26 offset0:150 offset1:158
	ds_read2_b32 v[22:23], v26 offset0:215 offset1:223
	v_cvt_pk_bf16_f32 v5, v12, v14
	s_waitcnt lgkmcnt(3)
	s_waitcnt lgkmcnt(2)
	v_cvt_pk_bf16_f32 v6, v16, v18
	s_waitcnt lgkmcnt(1)
	s_waitcnt lgkmcnt(0)
	v_cvt_pk_bf16_f32 v7, v20, v22
	v_or_b32_e32 v8, s10, v99
	v_lshlrev_b32_e32 v146, 9, v8
	v_lshl_add_u64 v[24:25], v[2:3], 0, v[146:147]
	global_store_dwordx4 v[24:25], v[4:7], off nt
	v_or_b32_e32 v10, s10, v100
	s_nop 0
	v_cvt_pk_bf16_f32 v4, v9, v11
	v_cvt_pk_bf16_f32 v5, v13, v15
	v_cvt_pk_bf16_f32 v6, v17, v19
	v_lshlrev_b32_e32 v146, 9, v10
	v_cvt_pk_bf16_f32 v7, v21, v23
	ds_read2_b32 v[8:9], v97 offset0:32 offset1:40
	v_lshl_add_u64 v[10:11], v[2:3], 0, v[146:147]
	global_store_dwordx4 v[10:11], v[4:7], off nt
	ds_read2_b32 v[10:11], v97 offset0:97 offset1:105
	ds_read2_b32 v[12:13], v97 offset0:162 offset1:170
	ds_read2_b32 v[14:15], v97 offset0:227 offset1:235
	s_waitcnt lgkmcnt(3)
	s_waitcnt lgkmcnt(2)
	ds_read2_b32 v[16:17], v26 offset0:36 offset1:44
	ds_read2_b32 v[18:19], v26 offset0:101 offset1:109
	v_cvt_pk_bf16_f32 v4, v8, v10
	s_waitcnt lgkmcnt(3)
	s_waitcnt lgkmcnt(2)
	ds_read2_b32 v[20:21], v26 offset0:166 offset1:174
	ds_read2_b32 v[22:23], v26 offset0:231 offset1:239
	v_cvt_pk_bf16_f32 v5, v12, v14
	s_waitcnt lgkmcnt(3)
	s_waitcnt lgkmcnt(2)
	v_cvt_pk_bf16_f32 v6, v16, v18
	s_waitcnt lgkmcnt(1)
	s_waitcnt lgkmcnt(0)
	v_cvt_pk_bf16_f32 v7, v20, v22
	v_or_b32_e32 v8, s10, v101
	v_lshlrev_b32_e32 v146, 9, v8
	v_lshl_add_u64 v[24:25], v[2:3], 0, v[146:147]
	global_store_dwordx4 v[24:25], v[4:7], off nt
	v_or_b32_e32 v10, s10, v102
	s_nop 0
	v_cvt_pk_bf16_f32 v4, v9, v11
	v_cvt_pk_bf16_f32 v5, v13, v15
	v_cvt_pk_bf16_f32 v6, v17, v19
	v_lshlrev_b32_e32 v146, 9, v10
	v_cvt_pk_bf16_f32 v7, v21, v23
	ds_read2_b32 v[8:9], v97 offset0:48 offset1:56
	v_lshl_add_u64 v[10:11], v[2:3], 0, v[146:147]
	global_store_dwordx4 v[10:11], v[4:7], off nt
	ds_read2_b32 v[10:11], v97 offset0:113 offset1:121
	ds_read2_b32 v[12:13], v97 offset0:178 offset1:186
	ds_read2_b32 v[14:15], v97 offset0:243 offset1:251
	s_waitcnt lgkmcnt(3)
	s_waitcnt lgkmcnt(2)
	ds_read2_b32 v[16:17], v26 offset0:52 offset1:60
	ds_read2_b32 v[18:19], v26 offset0:117 offset1:125
	v_cvt_pk_bf16_f32 v4, v8, v10
	s_waitcnt lgkmcnt(3)
	s_waitcnt lgkmcnt(2)
	ds_read2_b32 v[20:21], v26 offset0:182 offset1:190
	ds_read2_b32 v[22:23], v26 offset0:247 offset1:255
	v_cvt_pk_bf16_f32 v5, v12, v14
	s_waitcnt lgkmcnt(3)
	s_waitcnt lgkmcnt(2)
	v_cvt_pk_bf16_f32 v6, v16, v18
	s_waitcnt lgkmcnt(1)
	s_waitcnt lgkmcnt(0)
	v_cvt_pk_bf16_f32 v7, v20, v22
	v_or_b32_e32 v8, s10, v103
	v_lshlrev_b32_e32 v146, 9, v8
	v_lshl_add_u64 v[24:25], v[2:3], 0, v[146:147]
	global_store_dwordx4 v[24:25], v[4:7], off nt
	s_nop 1
	v_cvt_pk_bf16_f32 v4, v9, v11
	v_cvt_pk_bf16_f32 v5, v13, v15
	v_cvt_pk_bf16_f32 v6, v17, v19
	v_cvt_pk_bf16_f32 v7, v21, v23
	v_or_b32_e32 v8, s10, v104
	v_lshlrev_b32_e32 v146, 9, v8
	v_lshl_add_u64 v[2:3], v[2:3], 0, v[146:147]
	global_store_dwordx4 v[2:3], v[4:7], off nt
	s_waitcnt lgkmcnt(0)

; #define LAS __attribute__((address_space(3)))
; __device__ __forceinline__ unsigned pk2(float lo, float hi) { return f2bf(lo) | (f2bf(hi) << 16); }
; __device__ __forceinline__ void tr_item(const float* W, int ldw, int k0, int n0, bf16* WT, int ldt, int drow0, LAS float* scr, int lane, const float* kscale = nullptr) {
;     ...
;     for (int i = 0; i < 16; ++i) { LAS float* q = wp + (4 * i) * 65; const float ks = kscale ? kscale[k0 + 4 * i + (lane >> 4)] : 1.f; q[0] = v[i].x * ks; q[1] = v[i].y * ks; q[2] = v[i].z * ks; q[3] = v[i].w * ks; }
;     asm volatile("s_waitcnt lgkmcnt(0)" ::: "memory");
;     const int kc = lane & 7;
; #pragma unroll
;     for (int j = 0; j < 8; ++j) { const int n = (lane >> 3) + 8 * j; const LAS float* sp = scr + (8 * kc) * 65 + n;
;         u32x4 o; o.x = pk2(sp[0 * 65], sp[1 * 65]); o.y = pk2(sp[2 * 65], sp[3 * 65]); o.z = pk2(sp[4 * 65], sp[5 * 65]); o.w = pk2(sp[6 * 65], sp[7 * 65]);
;         __builtin_nontemporal_store(o, (u32x4*)(WT + (size_t)(drow0 + n) * ldt + k0 + 8 * kc)); }
;     asm volatile("s_waitcnt lgkmcnt(0)" ::: "memory");
.LBB0_1330:
	s_waitcnt vmcnt(0)
	v_pk_mul_f32 v[2:3], v[2:3], v[10:11] op_sel_hi:[1,0]
	v_add_u32_e32 v6, 0x3cf0, v95
	ds_write2_b32 v6, v2, v3 offset1:1
	v_pk_mul_f32 v[2:3], v[4:5], v[10:11] op_sel_hi:[1,0]
	v_add_u32_e32 v4, 0x3cf8, v95
	ds_write2_b32 v4, v2, v3 offset1:1
	s_waitcnt lgkmcnt(0)
	ds_read2_b32 v[8:9], v97 offset1:8
	ds_read2_b32 v[10:11], v97 offset0:65 offset1:73
	ds_read2_b32 v[12:13], v97 offset0:130 offset1:138
	ds_read2_b32 v[14:15], v97 offset0:195 offset1:203
	v_add_u32_e32 v26, 0x400, v97
	s_waitcnt lgkmcnt(3)
	s_waitcnt lgkmcnt(2)
	ds_read2_b32 v[16:17], v26 offset0:4 offset1:12
	ds_read2_b32 v[18:19], v26 offset0:69 offset1:77
	v_cvt_pk_bf16_f32 v4, v8, v10
	s_waitcnt lgkmcnt(3)
	s_waitcnt lgkmcnt(2)
	ds_read2_b32 v[20:21], v26 offset0:134 offset1:142
	ds_read2_b32 v[22:23], v26 offset0:199 offset1:207
	v_cvt_pk_bf16_f32 v5, v12, v14
	s_waitcnt lgkmcnt(3)
	s_waitcnt lgkmcnt(2)
	v_cvt_pk_bf16_f32 v6, v16, v18
	s_waitcnt lgkmcnt(1)
	v_or_b32_e32 v24, s6, v96
	s_lshl_b32 s12, s10, 1
	s_waitcnt lgkmcnt(0)
	v_ashrrev_i32_e32 v25, 31, v24
	v_lshl_add_u64 v[2:3], v[76:77], 0, s[12:13]
	v_lshlrev_b64 v[24:25], 10, v[24:25]
	v_cvt_pk_bf16_f32 v7, v20, v22
	v_lshl_add_u64 v[24:25], v[2:3], 0, v[24:25]
	global_store_dwordx4 v[24:25], v[4:7], off nt
	s_nop 1
	v_cvt_pk_bf16_f32 v4, v9, v11
	v_cvt_pk_bf16_f32 v5, v13, v15
	v_cvt_pk_bf16_f32 v6, v17, v19
	v_cvt_pk_bf16_f32 v7, v21, v23
	v_or_b32_e32 v8, s6, v98
	v_ashrrev_i32_e32 v9, 31, v8
	v_lshlrev_b64 v[8:9], 10, v[8:9]
	ds_read2_b32 v[10:11], v97 offset0:16 offset1:24
	v_lshl_add_u64 v[8:9], v[2:3], 0, v[8:9]
	global_store_dwordx4 v[8:9], v[4:7], off nt
	ds_read2_b32 v[8:9], v97 offset0:81 offset1:89
	ds_read2_b32 v[12:13], v97 offset0:146 offset1:154
	ds_read2_b32 v[14:15], v97 offset0:211 offset1:219
	s_waitcnt lgkmcnt(3)
	s_waitcnt lgkmcnt(2)
	ds_read2_b32 v[16:17], v26 offset0:20 offset1:28
	ds_read2_b32 v[18:19], v26 offset0:85 offset1:93
	v_cvt_pk_bf16_f32 v4, v10, v8
	s_waitcnt lgkmcnt(3)
	s_waitcnt lgkmcnt(2)
	ds_read2_b32 v[20:21], v26 offset0:150 offset1:158
	ds_read2_b32 v[22:23], v26 offset0:215 offset1:223
	v_cvt_pk_bf16_f32 v5, v12, v14
	s_waitcnt lgkmcnt(3)
	s_waitcnt lgkmcnt(2)
	v_cvt_pk_bf16_f32 v6, v16, v18
	s_waitcnt lgkmcnt(1)
	v_or_b32_e32 v24, s6, v99
	s_waitcnt lgkmcnt(0)
	v_ashrrev_i32_e32 v25, 31, v24
	v_lshlrev_b64 v[24:25], 10, v[24:25]
	v_cvt_pk_bf16_f32 v7, v20, v22
	v_lshl_add_u64 v[24:25], v[2:3], 0, v[24:25]
	global_store_dwordx4 v[24:25], v[4:7], off nt
	s_nop 1
	v_cvt_pk_bf16_f32 v4, v11, v9
	v_cvt_pk_bf16_f32 v5, v13, v15
	v_cvt_pk_bf16_f32 v6, v17, v19
	v_cvt_pk_bf16_f32 v7, v21, v23
	v_or_b32_e32 v8, s6, v100
	v_ashrrev_i32_e32 v9, 31, v8
	v_lshlrev_b64 v[8:9], 10, v[8:9]
	ds_read2_b32 v[10:11], v97 offset0:32 offset1:40
	v_lshl_add_u64 v[8:9], v[2:3], 0, v[8:9]
	global_store_dwordx4 v[8:9], v[4:7], off nt
	ds_read2_b32 v[8:9], v97 offset0:97 offset1:105
	ds_read2_b32 v[12:13], v97 offset0:162 offset1:170
	ds_read2_b32 v[14:15], v97 offset0:227 offset1:235
	s_waitcnt lgkmcnt(3)
	s_waitcnt lgkmcnt(2)
	ds_read2_b32 v[16:17], v26 offset0:36 offset1:44
	ds_read2_b32 v[18:19], v26 offset0:101 offset1:109
	v_cvt_pk_bf16_f32 v4, v10, v8
	s_waitcnt lgkmcnt(3)
	s_waitcnt lgkmcnt(2)
	ds_read2_b32 v[20:21], v26 offset0:166 offset1:174
	ds_read2_b32 v[22:23], v26 offset0:231 offset1:239
	v_cvt_pk_bf16_f32 v5, v12, v14
	s_waitcnt lgkmcnt(3)
	s_waitcnt lgkmcnt(2)
	v_cvt_pk_bf16_f32 v6, v16, v18
	s_waitcnt lgkmcnt(1)
	v_or_b32_e32 v24, s6, v101
	s_waitcnt lgkmcnt(0)
	v_ashrrev_i32_e32 v25, 31, v24
	v_lshlrev_b64 v[24:25], 10, v[24:25]
	v_cvt_pk_bf16_f32 v7, v20, v22
	v_lshl_add_u64 v[24:25], v[2:3], 0, v[24:25]
	global_store_dwordx4 v[24:25], v[4:7], off nt
	s_nop 1
	v_cvt_pk_bf16_f32 v4, v11, v9
	v_cvt_pk_bf16_f32 v5, v13, v15
	v_cvt_pk_bf16_f32 v6, v17, v19
	v_cvt_pk_bf16_f32 v7, v21, v23
	v_or_b32_e32 v8, s6, v102
	v_ashrrev_i32_e32 v9, 31, v8
	v_lshlrev_b64 v[8:9], 10, v[8:9]
	ds_read2_b32 v[10:11], v97 offset0:48 offset1:56
	v_lshl_add_u64 v[8:9], v[2:3], 0, v[8:9]
	global_store_dwordx4 v[8:9], v[4:7], off nt
	ds_read2_b32 v[8:9], v97 offset0:113 offset1:121
	ds_read2_b32 v[12:13], v97 offset0:178 offset1:186
	ds_read2_b32 v[14:15], v97 offset0:243 offset1:251
	s_waitcnt lgkmcnt(3)
	s_waitcnt lgkmcnt(2)
	ds_read2_b32 v[16:17], v26 offset0:52 offset1:60
	ds_read2_b32 v[18:19], v26 offset0:117 offset1:125
	v_cvt_pk_bf16_f32 v4, v10, v8
	s_waitcnt lgkmcnt(3)
	s_waitcnt lgkmcnt(2)
	ds_read2_b32 v[20:21], v26 offset0:182 offset1:190
	ds_read2_b32 v[22:23], v26 offset0:247 offset1:255
	v_cvt_pk_bf16_f32 v5, v12, v14
	s_waitcnt lgkmcnt(3)
	s_waitcnt lgkmcnt(2)
	v_cvt_pk_bf16_f32 v6, v16, v18
	s_waitcnt lgkmcnt(1)
	v_or_b32_e32 v24, s6, v103
	s_waitcnt lgkmcnt(0)
	v_ashrrev_i32_e32 v25, 31, v24
	v_lshlrev_b64 v[24:25], 10, v[24:25]
	v_cvt_pk_bf16_f32 v7, v20, v22
	v_lshl_add_u64 v[24:25], v[2:3], 0, v[24:25]
	global_store_dwordx4 v[24:25], v[4:7], off nt
	s_nop 1
	v_cvt_pk_bf16_f32 v4, v11, v9
	v_cvt_pk_bf16_f32 v5, v13, v15
	v_cvt_pk_bf16_f32 v6, v17, v19
	v_cvt_pk_bf16_f32 v7, v21, v23
	v_or_b32_e32 v8, s6, v104
	v_ashrrev_i32_e32 v9, 31, v8
	v_lshlrev_b64 v[8:9], 10, v[8:9]
	v_lshl_add_u64 v[2:3], v[2:3], 0, v[8:9]
	global_store_dwordx4 v[2:3], v[4:7], off nt
	s_waitcnt lgkmcnt(0)

; #define LAS __attribute__((address_space(3)))
; #define WSW(T, off, l) WSP(T, WS_WSET + (size_t)(l) * WSET_STRIDE + (off))
; __device__ __forceinline__ void tr_item(const float* W, int ldw, int k0, int n0, bf16* WT, int ldt, int drow0, LAS float* scr, int lane, const float* kscale = nullptr) {
;     const float* src = W + (size_t)(k0 + (lane >> 4)) * ldw + n0 + (lane & 15) * 4;
;     f32x4 v[16];
; #pragma unroll
;     for (int i = 0; i < 16; ++i) v[i] = __builtin_nontemporal_load((const f32x4*)(src + (size_t)(4 * i) * ldw));
;     LAS float* wp = scr + (lane >> 4) * 65 + (lane & 15) * 4;
; #pragma unroll
;     for (int i = 0; i < 16; ++i) { LAS float* q = wp + (4 * i) * 65; const float ks = kscale ? kscale[k0 + 4 * i + (lane >> 4)] : 1.f; q[0] = v[i].x * ks; q[1] = v[i].y * ks; q[2] = v[i].z * ks; q[3] = v[i].w * ks; }
;     asm volatile("s_waitcnt lgkmcnt(0)" ::: "memory");
; __device__ __forceinline__ void convert_tile(const Args& a, GAS unsigned char* wsb, int l, int t, LAS float* scr, int lane) {
;     ...
;     if (r < I_IN) { const int kb = r / 45, nb = r - kb * 45; tr_item(INP(7) + (size_t)l * DM * INW, INW, kb * 64, nb * 64, WSW(bf16, W_IN, l), DM, nb * 64, scr, lane); return; }
.LBB0_1332:
	s_andn2_b64 vcc, exec, s[6:7]
	s_cbranch_vccnz .LBB0_1334
	s_mul_i32 s6, s17, 0x2d83
	s_lshr_b32 s8, s6, 19
	s_mul_i32 s6, s8, 0xffffffd3
	s_add_i32 s6, s6, s17
	v_lshl_or_b32 v2, s8, 6, v67
	v_readlane_b32 s10, v253, 6
	s_lshl_b32 s6, s6, 6
	v_mul_u32_u24_e32 v146, 0x2d00, v2
	v_readlane_b32 s11, v253, 7
	s_ashr_i32 s7, s6, 31
	s_lshl_b32 s12, s8, 7
	v_lshl_add_u64 v[2:3], s[10:11], 0, v[146:147]
	v_lshl_add_u64 v[2:3], s[6:7], 2, v[2:3]
	v_lshlrev_b32_e32 v146, 2, v66
	v_lshl_add_u64 v[62:63], v[2:3], 0, v[146:147]
	s_mov_b32 s7, 0xb000
	v_add_co_u32_e32 v6, vcc, s7, v62
	s_mov_b32 s7, 0x16000
	s_nop 0
	v_addc_co_u32_e32 v7, vcc, 0, v63, vcc
	v_add_co_u32_e32 v10, vcc, s7, v62
	global_load_dwordx4 v[2:5], v[62:63], off nt
	s_nop 0
	global_load_dwordx4 v[6:9], v[6:7], off offset:1024 nt
	v_addc_co_u32_e32 v11, vcc, 0, v63, vcc
	s_mov_b32 s7, 0x21000
	v_add_co_u32_e32 v14, vcc, s7, v62
	s_mov_b32 s7, 0x2d000
	s_nop 0
	v_addc_co_u32_e32 v15, vcc, 0, v63, vcc
	global_load_dwordx4 v[10:13], v[10:11], off offset:2048 nt
	s_nop 0
	global_load_dwordx4 v[14:17], v[14:15], off offset:3072 nt
	v_add_co_u32_e32 v18, vcc, s7, v62
	s_mov_b32 s7, 0x38000
	s_nop 0
	v_addc_co_u32_e32 v19, vcc, 0, v63, vcc
	v_add_co_u32_e32 v22, vcc, s7, v62
	s_mov_b32 s7, 0x43000
	s_nop 0
	v_addc_co_u32_e32 v23, vcc, 0, v63, vcc
	global_load_dwordx4 v[18:21], v[18:19], off nt
	s_nop 0
	global_load_dwordx4 v[22:25], v[22:23], off offset:1024 nt
	v_add_co_u32_e32 v26, vcc, s7, v62
	s_mov_b32 s7, 0x4e000
	s_nop 0
	v_addc_co_u32_e32 v27, vcc, 0, v63, vcc
	v_add_co_u32_e32 v30, vcc, s7, v62
	s_mov_b32 s7, 0x5a000
	s_nop 0
	v_addc_co_u32_e32 v31, vcc, 0, v63, vcc
	global_load_dwordx4 v[26:29], v[26:27], off offset:2048 nt
	s_nop 0
	global_load_dwordx4 v[30:33], v[30:31], off offset:3072 nt
	v_add_co_u32_e32 v34, vcc, s7, v62
	s_mov_b32 s7, 0x65000
	s_nop 0
	v_addc_co_u32_e32 v35, vcc, 0, v63, vcc
	v_add_co_u32_e32 v38, vcc, s7, v62
	s_mov_b32 s7, 0x70000
	s_nop 0
	v_addc_co_u32_e32 v39, vcc, 0, v63, vcc
	global_load_dwordx4 v[34:37], v[34:35], off nt
	s_nop 0
	global_load_dwordx4 v[38:41], v[38:39], off offset:1024 nt
	v_add_co_u32_e32 v42, vcc, s7, v62
	s_mov_b32 s7, 0x7b000
	s_nop 0
	v_addc_co_u32_e32 v43, vcc, 0, v63, vcc
	v_add_co_u32_e32 v46, vcc, s7, v62
	s_mov_b32 s7, 0x87000
	s_nop 0
	v_addc_co_u32_e32 v47, vcc, 0, v63, vcc
	global_load_dwordx4 v[42:45], v[42:43], off offset:2048 nt
	s_nop 0
	global_load_dwordx4 v[46:49], v[46:47], off offset:3072 nt
	v_add_co_u32_e32 v50, vcc, s7, v62
	s_mov_b32 s7, 0x92000
	s_nop 0
	v_addc_co_u32_e32 v51, vcc, 0, v63, vcc
	v_add_co_u32_e32 v54, vcc, s7, v62
	s_mov_b32 s7, 0x9d000
	s_nop 0
	v_addc_co_u32_e32 v55, vcc, 0, v63, vcc
	global_load_dwordx4 v[50:53], v[50:51], off nt
	s_nop 0
	global_load_dwordx4 v[54:57], v[54:55], off offset:1024 nt
	v_add_co_u32_e32 v58, vcc, s7, v62
	s_mov_b32 s7, 0xa8000
	s_nop 0
	v_addc_co_u32_e32 v59, vcc, 0, v63, vcc
	global_load_dwordx4 v[58:61], v[58:59], off offset:2048 nt
	v_add_co_u32_e32 v62, vcc, s7, v62
	s_nop 1
	v_addc_co_u32_e32 v63, vcc, 0, v63, vcc
	global_load_dwordx4 v[62:65], v[62:63], off offset:3072 nt
	s_waitcnt vmcnt(15)
	ds_write2_b32 v95, v2, v3 offset1:1
	ds_write2_b32 v95, v4, v5 offset0:2 offset1:3
	v_add_u32_e32 v2, 0x410, v95
	s_waitcnt vmcnt(14)
	ds_write2_b32 v2, v6, v7 offset1:1
	v_add_u32_e32 v2, 0x418, v95
	ds_write2_b32 v2, v8, v9 offset1:1
	v_add_u32_e32 v2, 0x820, v95
	s_waitcnt vmcnt(13)
	ds_write2_b32 v2, v10, v11 offset1:1
	v_add_u32_e32 v2, 0x828, v95
	ds_write2_b32 v2, v12, v13 offset1:1
	v_add_u32_e32 v2, 0xc30, v95
	s_waitcnt vmcnt(12)
	ds_write2_b32 v2, v14, v15 offset1:1
	v_add_u32_e32 v2, 0xc38, v95
	ds_write2_b32 v2, v16, v17 offset1:1
	v_add_u32_e32 v2, 0x1040, v95
	s_waitcnt vmcnt(11)
	ds_write2_b32 v2, v18, v19 offset1:1
	v_add_u32_e32 v2, 0x1048, v95
	ds_write2_b32 v2, v20, v21 offset1:1
	v_add_u32_e32 v2, 0x1450, v95
	s_waitcnt vmcnt(10)
	ds_write2_b32 v2, v22, v23 offset1:1
	v_add_u32_e32 v2, 0x1458, v95
	ds_write2_b32 v2, v24, v25 offset1:1
	v_add_u32_e32 v2, 0x1860, v95
	v_or_b32_e32 v24, s6, v96
	v_ashrrev_i32_e32 v25, 31, v24
	v_lshlrev_b64 v[24:25], 12, v[24:25]
	s_waitcnt vmcnt(9)
	ds_write2_b32 v2, v26, v27 offset1:1
	v_add_u32_e32 v2, 0x1868, v95
	ds_write2_b32 v2, v28, v29 offset1:1
	v_add_u32_e32 v2, 0x1c70, v95
	s_waitcnt vmcnt(8)
	ds_write2_b32 v2, v30, v31 offset1:1
	v_add_u32_e32 v2, 0x1c78, v95
	ds_write2_b32 v2, v32, v33 offset1:1
	v_add_u32_e32 v2, 0x2080, v95
	v_add_u32_e32 v26, 0x400, v97
	s_waitcnt vmcnt(7)
	ds_write2_b32 v2, v34, v35 offset1:1
	v_add_u32_e32 v2, 0x2088, v95
	ds_write2_b32 v2, v36, v37 offset1:1
	v_add_u32_e32 v2, 0x2490, v95
	s_waitcnt vmcnt(6)
	ds_write2_b32 v2, v38, v39 offset1:1
	v_add_u32_e32 v2, 0x2498, v95
	ds_write2_b32 v2, v40, v41 offset1:1
	v_add_u32_e32 v2, 0x28a0, v95
	s_waitcnt vmcnt(5)
	ds_write2_b32 v2, v42, v43 offset1:1
	v_add_u32_e32 v2, 0x28a8, v95
	ds_write2_b32 v2, v44, v45 offset1:1
	v_add_u32_e32 v2, 0x2cb0, v95
	s_waitcnt vmcnt(4)
	ds_write2_b32 v2, v46, v47 offset1:1
	v_add_u32_e32 v2, 0x2cb8, v95
	ds_write2_b32 v2, v48, v49 offset1:1
	v_add_u32_e32 v2, 0x30c0, v95
	s_waitcnt vmcnt(3)
	ds_write2_b32 v2, v50, v51 offset1:1
	v_add_u32_e32 v2, 0x30c8, v95
	ds_write2_b32 v2, v52, v53 offset1:1
	v_add_u32_e32 v2, 0x34d0, v95
	s_waitcnt vmcnt(2)
; #define LAS __attribute__((address_space(3)))
; __device__ __forceinline__ unsigned pk2(float lo, float hi) { return f2bf(lo) | (f2bf(hi) << 16); }
; __device__ __forceinline__ void tr_item(const float* W, int ldw, int k0, int n0, bf16* WT, int ldt, int drow0, LAS float* scr, int lane, const float* kscale = nullptr) {
;     ...
;     LAS float* wp = scr + (lane >> 4) * 65 + (lane & 15) * 4;
; #pragma unroll
;     for (int i = 0; i < 16; ++i) { LAS float* q = wp + (4 * i) * 65; const float ks = kscale ? kscale[k0 + 4 * i + (lane >> 4)] : 1.f; q[0] = v[i].x * ks; q[1] = v[i].y * ks; q[2] = v[i].z * ks; q[3] = v[i].w * ks; }
;     asm volatile("s_waitcnt lgkmcnt(0)" ::: "memory");
;     const int kc = lane & 7;
; #pragma unroll
;     for (int j = 0; j < 8; ++j) { const int n = (lane >> 3) + 8 * j; const LAS float* sp = scr + (8 * kc) * 65 + n;
;         u32x4 o; o.x = pk2(sp[0 * 65], sp[1 * 65]); o.y = pk2(sp[2 * 65], sp[3 * 65]); o.z = pk2(sp[4 * 65], sp[5 * 65]); o.w = pk2(sp[6 * 65], sp[7 * 65]);
;         __builtin_nontemporal_store(o, (u32x4*)(WT + (size_t)(drow0 + n) * ldt + k0 + 8 * kc)); }
;     asm volatile("s_waitcnt lgkmcnt(0)" ::: "memory");
; }
	ds_write2_b32 v2, v54, v55 offset1:1
	v_add_u32_e32 v2, 0x34d8, v95
	ds_write2_b32 v2, v56, v57 offset1:1
	v_add_u32_e32 v2, 0x38e0, v95
	s_waitcnt vmcnt(1)
	ds_write2_b32 v2, v58, v59 offset1:1
	v_add_u32_e32 v2, 0x38e8, v95
	ds_write2_b32 v2, v60, v61 offset1:1
	v_add_u32_e32 v2, 0x3cf0, v95
	s_waitcnt vmcnt(0)
	ds_write2_b32 v2, v62, v63 offset1:1
	v_add_u32_e32 v2, 0x3cf8, v95
	ds_write2_b32 v2, v64, v65 offset1:1
	s_waitcnt lgkmcnt(0)
	ds_read2_b32 v[8:9], v97 offset1:8
	ds_read2_b32 v[10:11], v97 offset0:65 offset1:73
	ds_read2_b32 v[12:13], v97 offset0:130 offset1:138
	ds_read2_b32 v[14:15], v97 offset0:195 offset1:203
	ds_read2_b32 v[16:17], v26 offset0:4 offset1:12
	s_waitcnt lgkmcnt(4)
	s_waitcnt lgkmcnt(3)
	ds_read2_b32 v[18:19], v26 offset0:69 offset1:77
	v_cvt_pk_bf16_f32 v4, v8, v10
	s_waitcnt lgkmcnt(3)
	s_waitcnt lgkmcnt(2)
	ds_read2_b32 v[20:21], v26 offset0:134 offset1:142
	ds_read2_b32 v[22:23], v26 offset0:199 offset1:207
	v_cvt_pk_bf16_f32 v5, v12, v14
	s_waitcnt lgkmcnt(3)
	s_waitcnt lgkmcnt(2)
	v_cvt_pk_bf16_f32 v6, v16, v18
	s_waitcnt lgkmcnt(1)
	s_waitcnt lgkmcnt(0)
	v_lshl_add_u64 v[2:3], v[78:79], 0, s[12:13]
	v_cvt_pk_bf16_f32 v7, v20, v22
	v_lshl_add_u64 v[24:25], v[2:3], 0, v[24:25]
	global_store_dwordx4 v[24:25], v[4:7], off nt
	s_nop 1
	v_cvt_pk_bf16_f32 v4, v9, v11
	v_cvt_pk_bf16_f32 v5, v13, v15
	v_cvt_pk_bf16_f32 v6, v17, v19
	v_cvt_pk_bf16_f32 v7, v21, v23
	v_or_b32_e32 v8, s6, v98
	v_ashrrev_i32_e32 v9, 31, v8
	v_lshlrev_b64 v[8:9], 12, v[8:9]
	ds_read2_b32 v[10:11], v97 offset0:16 offset1:24
	v_lshl_add_u64 v[8:9], v[2:3], 0, v[8:9]
	global_store_dwordx4 v[8:9], v[4:7], off nt
	ds_read2_b32 v[8:9], v97 offset0:81 offset1:89
	ds_read2_b32 v[12:13], v97 offset0:146 offset1:154
	ds_read2_b32 v[14:15], v97 offset0:211 offset1:219
	s_waitcnt lgkmcnt(3)
	s_waitcnt lgkmcnt(2)
	ds_read2_b32 v[16:17], v26 offset0:20 offset1:28
	ds_read2_b32 v[18:19], v26 offset0:85 offset1:93
	v_cvt_pk_bf16_f32 v4, v10, v8
	s_waitcnt lgkmcnt(3)
	s_waitcnt lgkmcnt(2)
	ds_read2_b32 v[20:21], v26 offset0:150 offset1:158
	ds_read2_b32 v[22:23], v26 offset0:215 offset1:223
	v_cvt_pk_bf16_f32 v5, v12, v14
	s_waitcnt lgkmcnt(3)
	s_waitcnt lgkmcnt(2)
	v_cvt_pk_bf16_f32 v6, v16, v18
	s_waitcnt lgkmcnt(1)
	v_or_b32_e32 v24, s6, v99
	s_waitcnt lgkmcnt(0)
	v_ashrrev_i32_e32 v25, 31, v24
	v_lshlrev_b64 v[24:25], 12, v[24:25]
	v_cvt_pk_bf16_f32 v7, v20, v22
	v_lshl_add_u64 v[24:25], v[2:3], 0, v[24:25]
	global_store_dwordx4 v[24:25], v[4:7], off nt
	s_nop 1
	v_cvt_pk_bf16_f32 v4, v11, v9
	v_cvt_pk_bf16_f32 v5, v13, v15
	v_cvt_pk_bf16_f32 v6, v17, v19
	v_cvt_pk_bf16_f32 v7, v21, v23
	v_or_b32_e32 v8, s6, v100
	v_ashrrev_i32_e32 v9, 31, v8
	v_lshlrev_b64 v[8:9], 12, v[8:9]
	ds_read2_b32 v[10:11], v97 offset0:32 offset1:40
	v_lshl_add_u64 v[8:9], v[2:3], 0, v[8:9]
	global_store_dwordx4 v[8:9], v[4:7], off nt
	ds_read2_b32 v[8:9], v97 offset0:97 offset1:105
	ds_read2_b32 v[12:13], v97 offset0:162 offset1:170
	ds_read2_b32 v[14:15], v97 offset0:227 offset1:235
	s_waitcnt lgkmcnt(3)
	s_waitcnt lgkmcnt(2)
	ds_read2_b32 v[16:17], v26 offset0:36 offset1:44
	ds_read2_b32 v[18:19], v26 offset0:101 offset1:109
	v_cvt_pk_bf16_f32 v4, v10, v8
	s_waitcnt lgkmcnt(3)
	s_waitcnt lgkmcnt(2)
	ds_read2_b32 v[20:21], v26 offset0:166 offset1:174
	ds_read2_b32 v[22:23], v26 offset0:231 offset1:239
	v_cvt_pk_bf16_f32 v5, v12, v14
	s_waitcnt lgkmcnt(3)
	s_waitcnt lgkmcnt(2)
	v_cvt_pk_bf16_f32 v6, v16, v18
	s_waitcnt lgkmcnt(1)
	v_or_b32_e32 v24, s6, v101
	s_waitcnt lgkmcnt(0)
	v_ashrrev_i32_e32 v25, 31, v24
	v_lshlrev_b64 v[24:25], 12, v[24:25]
	v_cvt_pk_bf16_f32 v7, v20, v22
	v_lshl_add_u64 v[24:25], v[2:3], 0, v[24:25]
	global_store_dwordx4 v[24:25], v[4:7], off nt
	s_nop 1
	v_cvt_pk_bf16_f32 v4, v11, v9
	v_cvt_pk_bf16_f32 v5, v13, v15
	v_cvt_pk_bf16_f32 v6, v17, v19
	v_cvt_pk_bf16_f32 v7, v21, v23
	v_or_b32_e32 v8, s6, v102
	v_ashrrev_i32_e32 v9, 31, v8
	v_lshlrev_b64 v[8:9], 12, v[8:9]
	ds_read2_b32 v[10:11], v97 offset0:48 offset1:56
	v_lshl_add_u64 v[8:9], v[2:3], 0, v[8:9]
	global_store_dwordx4 v[8:9], v[4:7], off nt
	ds_read2_b32 v[8:9], v97 offset0:113 offset1:121
	ds_read2_b32 v[12:13], v97 offset0:178 offset1:186
	ds_read2_b32 v[14:15], v97 offset0:243 offset1:251
	s_waitcnt lgkmcnt(3)
	s_waitcnt lgkmcnt(2)
	ds_read2_b32 v[16:17], v26 offset0:52 offset1:60
	ds_read2_b32 v[18:19], v26 offset0:117 offset1:125
	v_cvt_pk_bf16_f32 v4, v10, v8
	s_waitcnt lgkmcnt(3)
	s_waitcnt lgkmcnt(2)
	ds_read2_b32 v[20:21], v26 offset0:182 offset1:190
	ds_read2_b32 v[22:23], v26 offset0:247 offset1:255
	v_cvt_pk_bf16_f32 v5, v12, v14
	s_waitcnt lgkmcnt(3)
	s_waitcnt lgkmcnt(2)
	v_cvt_pk_bf16_f32 v6, v16, v18
	s_waitcnt lgkmcnt(1)
	v_or_b32_e32 v24, s6, v103
	s_waitcnt lgkmcnt(0)
	v_ashrrev_i32_e32 v25, 31, v24
	v_lshlrev_b64 v[24:25], 12, v[24:25]
	v_cvt_pk_bf16_f32 v7, v20, v22
	v_lshl_add_u64 v[24:25], v[2:3], 0, v[24:25]
	global_store_dwordx4 v[24:25], v[4:7], off nt
	s_nop 1
	v_cvt_pk_bf16_f32 v4, v11, v9
	v_cvt_pk_bf16_f32 v5, v13, v15
	v_cvt_pk_bf16_f32 v6, v17, v19
	v_cvt_pk_bf16_f32 v7, v21, v23
	v_or_b32_e32 v8, s6, v104
	v_ashrrev_i32_e32 v9, 31, v8
	v_lshlrev_b64 v[8:9], 12, v[8:9]
	v_lshl_add_u64 v[2:3], v[2:3], 0, v[8:9]
	global_store_dwordx4 v[2:3], v[4:7], off nt
	s_waitcnt lgkmcnt(0)

; #define LAS __attribute__((address_space(3)))
; #define WSW(T, off, l) WSP(T, WS_WSET + (size_t)(l) * WSET_STRIDE + (off))
; __device__ __forceinline__ void tr_item(const float* W, int ldw, int k0, int n0, bf16* WT, int ldt, int drow0, LAS float* scr, int lane, const float* kscale = nullptr) {
;     const float* src = W + (size_t)(k0 + (lane >> 4)) * ldw + n0 + (lane & 15) * 4;
;     f32x4 v[16];
; #pragma unroll
;     for (int i = 0; i < 16; ++i) v[i] = __builtin_nontemporal_load((const f32x4*)(src + (size_t)(4 * i) * ldw));
;     LAS float* wp = scr + (lane >> 4) * 65 + (lane & 15) * 4;
; #pragma unroll
;     for (int i = 0; i < 16; ++i) { LAS float* q = wp + (4 * i) * 65; const float ks = kscale ? kscale[k0 + 4 * i + (lane >> 4)] : 1.f; q[0] = v[i].x * ks; q[1] = v[i].y * ks; q[2] = v[i].z * ks; q[3] = v[i].w * ks; }
; __device__ __forceinline__ void convert_tile(const Args& a, GAS unsigned char* wsb, int l, int t, LAS float* scr, int lane) {
;     ...
;     if (r < I_OUT) { const int kb = r / 32, nb = r - kb * 32; tr_item(INP(21) + (size_t)l * DM * DM, DM, kb * 64, nb * 64, WSW(bf16, W_OUT, l), DM, nb * 64, scr, lane); return; }
.LBB0_1349:
	s_andn2_b64 vcc, exec, s[6:7]
	s_cbranch_vccnz .LBB0_1351
	s_lshl_b32 s6, s17, 1
	s_and_b32 s6, s6, 0x1fc0
	s_addk_i32 s6, 0xf240
	s_lshl_b32 s7, s17, 6
	v_or_b32_e32 v146, s6, v67
	s_and_b32 s8, s7, 0x7c0
	v_lshlrev_b64 v[2:3], 13, v[146:147]
	v_lshl_add_u64 v[2:3], s[60:61], 0, v[2:3]
	s_lshl_b32 s12, s8, 2
	v_lshl_add_u64 v[2:3], v[2:3], 0, s[12:13]
	v_lshlrev_b32_e32 v146, 2, v66
	v_lshl_add_u64 v[62:63], v[2:3], 0, v[146:147]
	v_add_co_u32_e32 v6, vcc, s83, v62
	s_mov_b32 s7, 0x20000
	s_nop 0
	v_addc_co_u32_e32 v7, vcc, 0, v63, vcc
	v_add_co_u32_e32 v10, vcc, s81, v62
	global_load_dwordx4 v[2:5], v[62:63], off nt
	s_nop 0
	global_load_dwordx4 v[6:9], v[6:7], off nt
	v_addc_co_u32_e32 v11, vcc, 0, v63, vcc
	v_add_co_u32_e32 v14, vcc, s82, v62
	s_nop 1
	v_addc_co_u32_e32 v15, vcc, 0, v63, vcc
	global_load_dwordx4 v[10:13], v[10:11], off nt
	s_nop 0
	global_load_dwordx4 v[14:17], v[14:15], off nt
	v_add_co_u32_e32 v18, vcc, s7, v62
	s_mov_b32 s7, 0x28000
	s_nop 0
	v_addc_co_u32_e32 v19, vcc, 0, v63, vcc
	v_add_co_u32_e32 v22, vcc, s7, v62
	s_mov_b32 s7, 0x30000
	s_nop 0
	v_addc_co_u32_e32 v23, vcc, 0, v63, vcc
	global_load_dwordx4 v[18:21], v[18:19], off nt
	s_nop 0
	global_load_dwordx4 v[22:25], v[22:23], off nt
	v_add_co_u32_e32 v26, vcc, s7, v62
	s_mov_b32 s7, 0x38000
	s_nop 0
	v_addc_co_u32_e32 v27, vcc, 0, v63, vcc
	v_add_co_u32_e32 v30, vcc, s7, v62
	s_mov_b32 s7, 0x40000
	s_nop 0
	v_addc_co_u32_e32 v31, vcc, 0, v63, vcc
	global_load_dwordx4 v[26:29], v[26:27], off nt
	s_nop 0
	global_load_dwordx4 v[30:33], v[30:31], off nt
	v_add_co_u32_e32 v34, vcc, s7, v62
	s_mov_b32 s7, 0x48000
	s_nop 0
	v_addc_co_u32_e32 v35, vcc, 0, v63, vcc
	v_add_co_u32_e32 v38, vcc, s7, v62
	s_mov_b32 s7, 0x50000
	s_nop 0
	v_addc_co_u32_e32 v39, vcc, 0, v63, vcc
	global_load_dwordx4 v[34:37], v[34:35], off nt
	s_nop 0
	global_load_dwordx4 v[38:41], v[38:39], off nt
	v_add_co_u32_e32 v42, vcc, s7, v62
	s_mov_b32 s7, 0x58000
	s_nop 0
	v_addc_co_u32_e32 v43, vcc, 0, v63, vcc
	v_add_co_u32_e32 v46, vcc, s7, v62
	s_mov_b32 s7, 0x60000
	s_nop 0
	v_addc_co_u32_e32 v47, vcc, 0, v63, vcc
	global_load_dwordx4 v[42:45], v[42:43], off nt
	s_nop 0
	global_load_dwordx4 v[46:49], v[46:47], off nt
	v_add_co_u32_e32 v50, vcc, s7, v62
	s_mov_b32 s7, 0x68000
	s_nop 0
	v_addc_co_u32_e32 v51, vcc, 0, v63, vcc
	v_add_co_u32_e32 v54, vcc, s7, v62
	s_mov_b32 s7, 0x70000
	s_nop 0
	v_addc_co_u32_e32 v55, vcc, 0, v63, vcc
	global_load_dwordx4 v[50:53], v[50:51], off nt
	s_nop 0
	global_load_dwordx4 v[54:57], v[54:55], off nt
	v_add_co_u32_e32 v58, vcc, s7, v62
	s_mov_b32 s7, 0x78000
	s_nop 0
	v_addc_co_u32_e32 v59, vcc, 0, v63, vcc
	global_load_dwordx4 v[58:61], v[58:59], off nt
	v_add_co_u32_e32 v62, vcc, s7, v62
	s_mov_b32 s7, s13
	s_nop 0
	v_addc_co_u32_e32 v63, vcc, 0, v63, vcc
	global_load_dwordx4 v[62:65], v[62:63], off nt
	s_waitcnt vmcnt(15)
	ds_write2_b32 v95, v2, v3 offset1:1
	ds_write2_b32 v95, v4, v5 offset0:2 offset1:3
	v_add_u32_e32 v2, 0x410, v95
	s_waitcnt vmcnt(14)
	ds_write2_b32 v2, v6, v7 offset1:1
	v_add_u32_e32 v2, 0x418, v95
	ds_write2_b32 v2, v8, v9 offset1:1
	v_add_u32_e32 v2, 0x820, v95
	s_waitcnt vmcnt(13)
	ds_write2_b32 v2, v10, v11 offset1:1
	v_add_u32_e32 v2, 0x828, v95
	ds_write2_b32 v2, v12, v13 offset1:1
	v_add_u32_e32 v2, 0xc30, v95
	s_waitcnt vmcnt(12)
	ds_write2_b32 v2, v14, v15 offset1:1
	v_add_u32_e32 v2, 0xc38, v95
	ds_write2_b32 v2, v16, v17 offset1:1
	v_add_u32_e32 v2, 0x1040, v95
	s_waitcnt vmcnt(11)
	ds_write2_b32 v2, v18, v19 offset1:1
	v_add_u32_e32 v2, 0x1048, v95
	ds_write2_b32 v2, v20, v21 offset1:1
	v_add_u32_e32 v2, 0x1450, v95
	s_waitcnt vmcnt(10)
	ds_write2_b32 v2, v22, v23 offset1:1
	v_add_u32_e32 v2, 0x1458, v95
	ds_write2_b32 v2, v24, v25 offset1:1
	v_add_u32_e32 v2, 0x1860, v95
	s_waitcnt vmcnt(9)
	ds_write2_b32 v2, v26, v27 offset1:1
	v_add_u32_e32 v2, 0x1868, v95
	ds_write2_b32 v2, v28, v29 offset1:1
	v_add_u32_e32 v2, 0x1c70, v95
	s_waitcnt vmcnt(8)
	ds_write2_b32 v2, v30, v31 offset1:1
	v_add_u32_e32 v2, 0x1c78, v95
	ds_write2_b32 v2, v32, v33 offset1:1
	v_add_u32_e32 v2, 0x2080, v95
	v_add_u32_e32 v26, 0x400, v97
	s_waitcnt vmcnt(7)
	ds_write2_b32 v2, v34, v35 offset1:1
	v_add_u32_e32 v2, 0x2088, v95
	ds_write2_b32 v2, v36, v37 offset1:1
	v_add_u32_e32 v2, 0x2490, v95
	s_waitcnt vmcnt(6)
	ds_write2_b32 v2, v38, v39 offset1:1
	v_add_u32_e32 v2, 0x2498, v95
	ds_write2_b32 v2, v40, v41 offset1:1
	v_add_u32_e32 v2, 0x28a0, v95
	s_waitcnt vmcnt(5)
	ds_write2_b32 v2, v42, v43 offset1:1
	v_add_u32_e32 v2, 0x28a8, v95
	ds_write2_b32 v2, v44, v45 offset1:1
	v_add_u32_e32 v2, 0x2cb0, v95
	s_waitcnt vmcnt(4)
	ds_write2_b32 v2, v46, v47 offset1:1
	v_add_u32_e32 v2, 0x2cb8, v95
	ds_write2_b32 v2, v48, v49 offset1:1
	v_add_u32_e32 v2, 0x30c0, v95
	s_waitcnt vmcnt(3)
	ds_write2_b32 v2, v50, v51 offset1:1
	v_add_u32_e32 v2, 0x30c8, v95
	ds_write2_b32 v2, v52, v53 offset1:1
	v_add_u32_e32 v2, 0x34d0, v95
	s_waitcnt vmcnt(2)
	ds_write2_b32 v2, v54, v55 offset1:1
	v_add_u32_e32 v2, 0x34d8, v95
	ds_write2_b32 v2, v56, v57 offset1:1
	v_add_u32_e32 v2, 0x38e0, v95
	s_waitcnt vmcnt(1)
; #define LAS __attribute__((address_space(3)))
; __device__ __forceinline__ unsigned pk2(float lo, float hi) { return f2bf(lo) | (f2bf(hi) << 16); }
; __device__ __forceinline__ void tr_item(const float* W, int ldw, int k0, int n0, bf16* WT, int ldt, int drow0, LAS float* scr, int lane, const float* kscale = nullptr) {
;     ...
;     const int kc = lane & 7;
; #pragma unroll
;     for (int j = 0; j < 8; ++j) { const int n = (lane >> 3) + 8 * j; const LAS float* sp = scr + (8 * kc) * 65 + n;
;         u32x4 o; o.x = pk2(sp[0 * 65], sp[1 * 65]); o.y = pk2(sp[2 * 65], sp[3 * 65]); o.z = pk2(sp[4 * 65], sp[5 * 65]); o.w = pk2(sp[6 * 65], sp[7 * 65]);
;         __builtin_nontemporal_store(o, (u32x4*)(WT + (size_t)(drow0 + n) * ldt + k0 + 8 * kc)); }
;     asm volatile("s_waitcnt lgkmcnt(0)" ::: "memory");
; }
	ds_write2_b32 v2, v58, v59 offset1:1
	v_add_u32_e32 v2, 0x38e8, v95
	ds_write2_b32 v2, v60, v61 offset1:1
	v_add_u32_e32 v2, 0x3cf0, v95
	s_waitcnt vmcnt(0)
	ds_write2_b32 v2, v62, v63 offset1:1
	v_add_u32_e32 v2, 0x3cf8, v95
	ds_write2_b32 v2, v64, v65 offset1:1
	s_waitcnt lgkmcnt(0)
	ds_read2_b32 v[8:9], v97 offset1:8
	ds_read2_b32 v[10:11], v97 offset0:65 offset1:73
	ds_read2_b32 v[12:13], v97 offset0:130 offset1:138
	ds_read2_b32 v[14:15], v97 offset0:195 offset1:203
	ds_read2_b32 v[16:17], v26 offset0:4 offset1:12
	s_waitcnt lgkmcnt(4)
	s_waitcnt lgkmcnt(3)
	ds_read2_b32 v[18:19], v26 offset0:69 offset1:77
	v_cvt_pk_bf16_f32 v4, v8, v10
	s_waitcnt lgkmcnt(3)
	s_waitcnt lgkmcnt(2)
	ds_read2_b32 v[20:21], v26 offset0:134 offset1:142
	ds_read2_b32 v[22:23], v26 offset0:199 offset1:207
	v_cvt_pk_bf16_f32 v5, v12, v14
	s_waitcnt lgkmcnt(3)
	s_waitcnt lgkmcnt(2)
	v_cvt_pk_bf16_f32 v6, v16, v18
	s_waitcnt lgkmcnt(1)
	s_waitcnt lgkmcnt(0)
	v_cvt_pk_bf16_f32 v7, v20, v22
	v_or_b32_e32 v8, s8, v96
	v_lshl_add_u64 v[2:3], s[6:7], 1, v[84:85]
	v_lshlrev_b32_e32 v146, 12, v8
	v_lshl_add_u64 v[24:25], v[2:3], 0, v[146:147]
	global_store_dwordx4 v[24:25], v[4:7], off nt
	v_or_b32_e32 v10, s8, v98
	s_nop 0
	v_cvt_pk_bf16_f32 v4, v9, v11
	v_cvt_pk_bf16_f32 v5, v13, v15
	v_cvt_pk_bf16_f32 v6, v17, v19
	v_lshlrev_b32_e32 v146, 12, v10
	v_cvt_pk_bf16_f32 v7, v21, v23
	ds_read2_b32 v[8:9], v97 offset0:16 offset1:24
	v_lshl_add_u64 v[10:11], v[2:3], 0, v[146:147]
	global_store_dwordx4 v[10:11], v[4:7], off nt
	ds_read2_b32 v[10:11], v97 offset0:81 offset1:89
	ds_read2_b32 v[12:13], v97 offset0:146 offset1:154
	ds_read2_b32 v[14:15], v97 offset0:211 offset1:219
	s_waitcnt lgkmcnt(3)
	s_waitcnt lgkmcnt(2)
	ds_read2_b32 v[16:17], v26 offset0:20 offset1:28
	ds_read2_b32 v[18:19], v26 offset0:85 offset1:93
	v_cvt_pk_bf16_f32 v4, v8, v10
	s_waitcnt lgkmcnt(3)
	s_waitcnt lgkmcnt(2)
	ds_read2_b32 v[20:21], v26 offset0:150 offset1:158
	ds_read2_b32 v[22:23], v26 offset0:215 offset1:223
	v_cvt_pk_bf16_f32 v5, v12, v14
	s_waitcnt lgkmcnt(3)
	s_waitcnt lgkmcnt(2)
	v_cvt_pk_bf16_f32 v6, v16, v18
	s_waitcnt lgkmcnt(1)
	s_waitcnt lgkmcnt(0)
	v_cvt_pk_bf16_f32 v7, v20, v22
	v_or_b32_e32 v8, s8, v99
	v_lshlrev_b32_e32 v146, 12, v8
	v_lshl_add_u64 v[24:25], v[2:3], 0, v[146:147]
	global_store_dwordx4 v[24:25], v[4:7], off nt
	v_or_b32_e32 v10, s8, v100
	s_nop 0
	v_cvt_pk_bf16_f32 v4, v9, v11
	v_cvt_pk_bf16_f32 v5, v13, v15
	v_cvt_pk_bf16_f32 v6, v17, v19
	v_lshlrev_b32_e32 v146, 12, v10
	v_cvt_pk_bf16_f32 v7, v21, v23
	ds_read2_b32 v[8:9], v97 offset0:32 offset1:40
	v_lshl_add_u64 v[10:11], v[2:3], 0, v[146:147]
	global_store_dwordx4 v[10:11], v[4:7], off nt
	ds_read2_b32 v[10:11], v97 offset0:97 offset1:105
	ds_read2_b32 v[12:13], v97 offset0:162 offset1:170
	ds_read2_b32 v[14:15], v97 offset0:227 offset1:235
	s_waitcnt lgkmcnt(3)
	s_waitcnt lgkmcnt(2)
	ds_read2_b32 v[16:17], v26 offset0:36 offset1:44
	ds_read2_b32 v[18:19], v26 offset0:101 offset1:109
	v_cvt_pk_bf16_f32 v4, v8, v10
	s_waitcnt lgkmcnt(3)
	s_waitcnt lgkmcnt(2)
	ds_read2_b32 v[20:21], v26 offset0:166 offset1:174
	ds_read2_b32 v[22:23], v26 offset0:231 offset1:239
	v_cvt_pk_bf16_f32 v5, v12, v14
	s_waitcnt lgkmcnt(3)
	s_waitcnt lgkmcnt(2)
	v_cvt_pk_bf16_f32 v6, v16, v18
	s_waitcnt lgkmcnt(1)
	s_waitcnt lgkmcnt(0)
	v_cvt_pk_bf16_f32 v7, v20, v22
	v_or_b32_e32 v8, s8, v101
	v_lshlrev_b32_e32 v146, 12, v8
	v_lshl_add_u64 v[24:25], v[2:3], 0, v[146:147]
	global_store_dwordx4 v[24:25], v[4:7], off nt
	v_or_b32_e32 v10, s8, v102
	s_nop 0
	v_cvt_pk_bf16_f32 v4, v9, v11
	v_cvt_pk_bf16_f32 v5, v13, v15
	v_cvt_pk_bf16_f32 v6, v17, v19
	v_lshlrev_b32_e32 v146, 12, v10
	v_cvt_pk_bf16_f32 v7, v21, v23
	ds_read2_b32 v[8:9], v97 offset0:48 offset1:56
	v_lshl_add_u64 v[10:11], v[2:3], 0, v[146:147]
	global_store_dwordx4 v[10:11], v[4:7], off nt
	ds_read2_b32 v[10:11], v97 offset0:113 offset1:121
	ds_read2_b32 v[12:13], v97 offset0:178 offset1:186
	ds_read2_b32 v[14:15], v97 offset0:243 offset1:251
	s_waitcnt lgkmcnt(3)
	s_waitcnt lgkmcnt(2)
	ds_read2_b32 v[16:17], v26 offset0:52 offset1:60
	ds_read2_b32 v[18:19], v26 offset0:117 offset1:125
	v_cvt_pk_bf16_f32 v4, v8, v10
	s_waitcnt lgkmcnt(3)
	s_waitcnt lgkmcnt(2)
	ds_read2_b32 v[20:21], v26 offset0:182 offset1:190
	ds_read2_b32 v[22:23], v26 offset0:247 offset1:255
	v_cvt_pk_bf16_f32 v5, v12, v14
	s_waitcnt lgkmcnt(3)
	s_waitcnt lgkmcnt(2)
	v_cvt_pk_bf16_f32 v6, v16, v18
	s_waitcnt lgkmcnt(1)
	s_waitcnt lgkmcnt(0)
	v_cvt_pk_bf16_f32 v7, v20, v22
	v_or_b32_e32 v8, s8, v103
	v_lshlrev_b32_e32 v146, 12, v8
	v_lshl_add_u64 v[24:25], v[2:3], 0, v[146:147]
	global_store_dwordx4 v[24:25], v[4:7], off nt
	s_nop 1
	v_cvt_pk_bf16_f32 v4, v9, v11
	v_cvt_pk_bf16_f32 v5, v13, v15
	v_cvt_pk_bf16_f32 v6, v17, v19
	v_cvt_pk_bf16_f32 v7, v21, v23
	v_or_b32_e32 v8, s8, v104
	v_lshlrev_b32_e32 v146, 12, v8
	v_lshl_add_u64 v[2:3], v[2:3], 0, v[146:147]
	global_store_dwordx4 v[2:3], v[4:7], off nt
	s_waitcnt lgkmcnt(0)

; #define LAS __attribute__((address_space(3)))
; __device__ __forceinline__ unsigned pk2(float lo, float hi) { return f2bf(lo) | (f2bf(hi) << 16); }
; #define WSW(T, off, l) WSP(T, WS_WSET + (size_t)(l) * WSET_STRIDE + (off))
; __device__ __forceinline__ void tr_item(const float* W, int ldw, int k0, int n0, bf16* WT, int ldt, int drow0, LAS float* scr, int lane, const float* kscale = nullptr) {
;     ...
;     for (int i = 0; i < 16; ++i) { LAS float* q = wp + (4 * i) * 65; const float ks = kscale ? kscale[k0 + 4 * i + (lane >> 4)] : 1.f; q[0] = v[i].x * ks; q[1] = v[i].y * ks; q[2] = v[i].z * ks; q[3] = v[i].w * ks; }
;     asm volatile("s_waitcnt lgkmcnt(0)" ::: "memory");
;     const int kc = lane & 7;
; #pragma unroll
;     for (int j = 0; j < 8; ++j) { const int n = (lane >> 3) + 8 * j; const LAS float* sp = scr + (8 * kc) * 65 + n;
;         u32x4 o; o.x = pk2(sp[0 * 65], sp[1 * 65]); o.y = pk2(sp[2 * 65], sp[3 * 65]); o.z = pk2(sp[4 * 65], sp[5 * 65]); o.w = pk2(sp[6 * 65], sp[7 * 65]);
;         __builtin_nontemporal_store(o, (u32x4*)(WT + (size_t)(drow0 + n) * ldt + k0 + 8 * kc)); }
;     asm volatile("s_waitcnt lgkmcnt(0)" ::: "memory");
; }
; __device__ __forceinline__ void convert_tile(const Args& a, GAS unsigned char* wsb, int l, int t, LAS float* scr, int lane) {
;     ...
;     if (r < I_UKV) { const int kb = r / 32, nb = r - kb * 32; tr_item(INP(18) + (size_t)l * KVRANK * 2048, 2048, kb * 64, nb * 64, WSW(bf16, W_UKV, l), KVRANK, nb * 64, scr, lane, INP(17) + (size_t)l * KVRANK); return; }
.LBB0_1377:
	s_waitcnt vmcnt(0)
	v_pk_mul_f32 v[2:3], v[2:3], v[10:11] op_sel_hi:[1,0]
	v_add_u32_e32 v6, 0x3cf0, v95
	ds_write2_b32 v6, v2, v3 offset1:1
	v_pk_mul_f32 v[2:3], v[4:5], v[10:11] op_sel_hi:[1,0]
	v_add_u32_e32 v4, 0x3cf8, v95
	ds_write2_b32 v4, v2, v3 offset1:1
	s_waitcnt lgkmcnt(0)
	ds_read2_b32 v[8:9], v97 offset1:8
	ds_read2_b32 v[10:11], v97 offset0:65 offset1:73
	ds_read2_b32 v[12:13], v97 offset0:130 offset1:138
	ds_read2_b32 v[14:15], v97 offset0:195 offset1:203
	v_add_u32_e32 v26, 0x400, v97
	s_waitcnt lgkmcnt(3)
	s_waitcnt lgkmcnt(2)
	ds_read2_b32 v[16:17], v26 offset0:4 offset1:12
	ds_read2_b32 v[18:19], v26 offset0:69 offset1:77
	v_cvt_pk_bf16_f32 v4, v8, v10
	s_waitcnt lgkmcnt(3)
	s_waitcnt lgkmcnt(2)
	ds_read2_b32 v[20:21], v26 offset0:134 offset1:142
	ds_read2_b32 v[22:23], v26 offset0:199 offset1:207
	v_cvt_pk_bf16_f32 v5, v12, v14
	s_waitcnt lgkmcnt(3)
	s_waitcnt lgkmcnt(2)
	v_cvt_pk_bf16_f32 v6, v16, v18
	s_waitcnt lgkmcnt(1)
	s_waitcnt lgkmcnt(0)
	s_mov_b32 s7, s13
	v_cvt_pk_bf16_f32 v7, v20, v22
	v_or_b32_e32 v8, s10, v96
	v_lshl_add_u64 v[2:3], s[6:7], 1, v[86:87]
	v_lshlrev_b32_e32 v146, 9, v8
	v_lshl_add_u64 v[24:25], v[2:3], 0, v[146:147]
	global_store_dwordx4 v[24:25], v[4:7], off nt
	v_or_b32_e32 v10, s10, v98
	s_nop 0
	v_cvt_pk_bf16_f32 v4, v9, v11
	v_cvt_pk_bf16_f32 v5, v13, v15
	v_cvt_pk_bf16_f32 v6, v17, v19
	v_lshlrev_b32_e32 v146, 9, v10
	v_cvt_pk_bf16_f32 v7, v21, v23
	ds_read2_b32 v[8:9], v97 offset0:16 offset1:24
	v_lshl_add_u64 v[10:11], v[2:3], 0, v[146:147]
	global_store_dwordx4 v[10:11], v[4:7], off nt
	ds_read2_b32 v[10:11], v97 offset0:81 offset1:89
	ds_read2_b32 v[12:13], v97 offset0:146 offset1:154
	ds_read2_b32 v[14:15], v97 offset0:211 offset1:219
	s_waitcnt lgkmcnt(3)
	s_waitcnt lgkmcnt(2)
	ds_read2_b32 v[16:17], v26 offset0:20 offset1:28
	ds_read2_b32 v[18:19], v26 offset0:85 offset1:93
	v_cvt_pk_bf16_f32 v4, v8, v10
	s_waitcnt lgkmcnt(3)
	s_waitcnt lgkmcnt(2)
	ds_read2_b32 v[20:21], v26 offset0:150 offset1:158
	ds_read2_b32 v[22:23], v26 offset0:215 offset1:223
	v_cvt_pk_bf16_f32 v5, v12, v14
	s_waitcnt lgkmcnt(3)
	s_waitcnt lgkmcnt(2)
	v_cvt_pk_bf16_f32 v6, v16, v18
	s_waitcnt lgkmcnt(1)
	s_waitcnt lgkmcnt(0)
	v_cvt_pk_bf16_f32 v7, v20, v22
	v_or_b32_e32 v8, s10, v99
	v_lshlrev_b32_e32 v146, 9, v8
	v_lshl_add_u64 v[24:25], v[2:3], 0, v[146:147]
	global_store_dwordx4 v[24:25], v[4:7], off nt
	v_or_b32_e32 v10, s10, v100
	s_nop 0
	v_cvt_pk_bf16_f32 v4, v9, v11
	v_cvt_pk_bf16_f32 v5, v13, v15
	v_cvt_pk_bf16_f32 v6, v17, v19
	v_lshlrev_b32_e32 v146, 9, v10
	v_cvt_pk_bf16_f32 v7, v21, v23
	ds_read2_b32 v[8:9], v97 offset0:32 offset1:40
	v_lshl_add_u64 v[10:11], v[2:3], 0, v[146:147]
	global_store_dwordx4 v[10:11], v[4:7], off nt
	ds_read2_b32 v[10:11], v97 offset0:97 offset1:105
	ds_read2_b32 v[12:13], v97 offset0:162 offset1:170
	ds_read2_b32 v[14:15], v97 offset0:227 offset1:235
	s_waitcnt lgkmcnt(3)
	s_waitcnt lgkmcnt(2)
	ds_read2_b32 v[16:17], v26 offset0:36 offset1:44
	ds_read2_b32 v[18:19], v26 offset0:101 offset1:109
	v_cvt_pk_bf16_f32 v4, v8, v10
	s_waitcnt lgkmcnt(3)
	s_waitcnt lgkmcnt(2)
	ds_read2_b32 v[20:21], v26 offset0:166 offset1:174
	ds_read2_b32 v[22:23], v26 offset0:231 offset1:239
	v_cvt_pk_bf16_f32 v5, v12, v14
	s_waitcnt lgkmcnt(3)
	s_waitcnt lgkmcnt(2)
	v_cvt_pk_bf16_f32 v6, v16, v18
	s_waitcnt lgkmcnt(1)
	s_waitcnt lgkmcnt(0)
	v_cvt_pk_bf16_f32 v7, v20, v22
	v_or_b32_e32 v8, s10, v101
	v_lshlrev_b32_e32 v146, 9, v8
	v_lshl_add_u64 v[24:25], v[2:3], 0, v[146:147]
	global_store_dwordx4 v[24:25], v[4:7], off nt
	v_or_b32_e32 v10, s10, v102
	s_nop 0
	v_cvt_pk_bf16_f32 v4, v9, v11
	v_cvt_pk_bf16_f32 v5, v13, v15
	v_cvt_pk_bf16_f32 v6, v17, v19
	v_lshlrev_b32_e32 v146, 9, v10
	v_cvt_pk_bf16_f32 v7, v21, v23
	ds_read2_b32 v[8:9], v97 offset0:48 offset1:56
	v_lshl_add_u64 v[10:11], v[2:3], 0, v[146:147]
	global_store_dwordx4 v[10:11], v[4:7], off nt
	ds_read2_b32 v[10:11], v97 offset0:113 offset1:121
	ds_read2_b32 v[12:13], v97 offset0:178 offset1:186
	ds_read2_b32 v[14:15], v97 offset0:243 offset1:251
	s_waitcnt lgkmcnt(3)
	s_waitcnt lgkmcnt(2)
	ds_read2_b32 v[16:17], v26 offset0:52 offset1:60
	ds_read2_b32 v[18:19], v26 offset0:117 offset1:125
	v_cvt_pk_bf16_f32 v4, v8, v10
	s_waitcnt lgkmcnt(3)
	s_waitcnt lgkmcnt(2)
	ds_read2_b32 v[20:21], v26 offset0:182 offset1:190
	ds_read2_b32 v[22:23], v26 offset0:247 offset1:255
	v_cvt_pk_bf16_f32 v5, v12, v14
	s_waitcnt lgkmcnt(3)
	s_waitcnt lgkmcnt(2)
	v_cvt_pk_bf16_f32 v6, v16, v18
	s_waitcnt lgkmcnt(1)
	s_waitcnt lgkmcnt(0)
	v_cvt_pk_bf16_f32 v7, v20, v22
	v_or_b32_e32 v8, s10, v103
	v_lshlrev_b32_e32 v146, 9, v8
	v_lshl_add_u64 v[24:25], v[2:3], 0, v[146:147]
	global_store_dwordx4 v[24:25], v[4:7], off nt
	s_nop 1
	v_cvt_pk_bf16_f32 v4, v9, v11
	v_cvt_pk_bf16_f32 v5, v13, v15
	v_cvt_pk_bf16_f32 v6, v17, v19
	v_cvt_pk_bf16_f32 v7, v21, v23
	v_or_b32_e32 v8, s10, v104
	v_lshlrev_b32_e32 v146, 9, v8
	v_lshl_add_u64 v[2:3], v[2:3], 0, v[146:147]
	global_store_dwordx4 v[2:3], v[4:7], off nt
	s_waitcnt lgkmcnt(0)

; #define LAS __attribute__((address_space(3)))
; __device__ __forceinline__ unsigned pk2(float lo, float hi) { return f2bf(lo) | (f2bf(hi) << 16); }
; #define WSW(T, off, l) WSP(T, WS_WSET + (size_t)(l) * WSET_STRIDE + (off))
; __device__ __forceinline__ void tr_item(const float* W, int ldw, int k0, int n0, bf16* WT, int ldt, int drow0, LAS float* scr, int lane, const float* kscale = nullptr) {
;     ...
;     for (int i = 0; i < 16; ++i) { LAS float* q = wp + (4 * i) * 65; const float ks = kscale ? kscale[k0 + 4 * i + (lane >> 4)] : 1.f; q[0] = v[i].x * ks; q[1] = v[i].y * ks; q[2] = v[i].z * ks; q[3] = v[i].w * ks; }
;     asm volatile("s_waitcnt lgkmcnt(0)" ::: "memory");
;     const int kc = lane & 7;
; #pragma unroll
;     for (int j = 0; j < 8; ++j) { const int n = (lane >> 3) + 8 * j; const LAS float* sp = scr + (8 * kc) * 65 + n;
;         u32x4 o; o.x = pk2(sp[0 * 65], sp[1 * 65]); o.y = pk2(sp[2 * 65], sp[3 * 65]); o.z = pk2(sp[4 * 65], sp[5 * 65]); o.w = pk2(sp[6 * 65], sp[7 * 65]);
;         __builtin_nontemporal_store(o, (u32x4*)(WT + (size_t)(drow0 + n) * ldt + k0 + 8 * kc)); }
;     asm volatile("s_waitcnt lgkmcnt(0)" ::: "memory");
; }
; __device__ __forceinline__ void convert_tile(const Args& a, GAS unsigned char* wsb, int l, int t, LAS float* scr, int lane) {
;     ...
;     if (r < I_UQ) { const int kb = r / 24, nb = r - kb * 24; tr_item(INP(16) + (size_t)l * QRANK * 1536, 1536, kb * 64, nb * 64, WSW(bf16, W_UQ, l), QRANK, nb * 64, scr, lane, INP(15) + (size_t)l * QRANK); return; }
.LBB0_1404:
	s_waitcnt vmcnt(0)
	v_pk_mul_f32 v[2:3], v[2:3], v[10:11] op_sel_hi:[1,0]
	v_add_u32_e32 v6, 0x3cf0, v95
	ds_write2_b32 v6, v2, v3 offset1:1
	v_pk_mul_f32 v[2:3], v[4:5], v[10:11] op_sel_hi:[1,0]
	v_add_u32_e32 v4, 0x3cf8, v95
	ds_write2_b32 v4, v2, v3 offset1:1
	s_waitcnt lgkmcnt(0)
	ds_read2_b32 v[8:9], v97 offset1:8
	ds_read2_b32 v[10:11], v97 offset0:65 offset1:73
	ds_read2_b32 v[12:13], v97 offset0:130 offset1:138
	ds_read2_b32 v[14:15], v97 offset0:195 offset1:203
	v_add_u32_e32 v26, 0x400, v97
	s_waitcnt lgkmcnt(3)
	s_waitcnt lgkmcnt(2)
	ds_read2_b32 v[16:17], v26 offset0:4 offset1:12
	ds_read2_b32 v[18:19], v26 offset0:69 offset1:77
	v_cvt_pk_bf16_f32 v4, v8, v10
	s_waitcnt lgkmcnt(3)
	s_waitcnt lgkmcnt(2)
	ds_read2_b32 v[20:21], v26 offset0:134 offset1:142
	ds_read2_b32 v[22:23], v26 offset0:199 offset1:207
	v_cvt_pk_bf16_f32 v5, v12, v14
	s_waitcnt lgkmcnt(3)
	s_waitcnt lgkmcnt(2)
	v_cvt_pk_bf16_f32 v6, v16, v18
	s_waitcnt lgkmcnt(1)
	v_or_b32_e32 v24, s6, v96
	s_lshl_b32 s12, s10, 1
	s_waitcnt lgkmcnt(0)
	v_ashrrev_i32_e32 v25, 31, v24
	v_lshl_add_u64 v[2:3], v[88:89], 0, s[12:13]
	v_lshlrev_b64 v[24:25], 10, v[24:25]
	v_cvt_pk_bf16_f32 v7, v20, v22
	v_lshl_add_u64 v[24:25], v[2:3], 0, v[24:25]
	global_store_dwordx4 v[24:25], v[4:7], off nt
	s_nop 1
	v_cvt_pk_bf16_f32 v4, v9, v11
	v_cvt_pk_bf16_f32 v5, v13, v15
	v_cvt_pk_bf16_f32 v6, v17, v19
	v_cvt_pk_bf16_f32 v7, v21, v23
	v_or_b32_e32 v8, s6, v98
	v_ashrrev_i32_e32 v9, 31, v8
	v_lshlrev_b64 v[8:9], 10, v[8:9]
	ds_read2_b32 v[10:11], v97 offset0:16 offset1:24
	v_lshl_add_u64 v[8:9], v[2:3], 0, v[8:9]
	global_store_dwordx4 v[8:9], v[4:7], off nt
	ds_read2_b32 v[8:9], v97 offset0:81 offset1:89
	ds_read2_b32 v[12:13], v97 offset0:146 offset1:154
	ds_read2_b32 v[14:15], v97 offset0:211 offset1:219
	s_waitcnt lgkmcnt(3)
	s_waitcnt lgkmcnt(2)
	ds_read2_b32 v[16:17], v26 offset0:20 offset1:28
	ds_read2_b32 v[18:19], v26 offset0:85 offset1:93
	v_cvt_pk_bf16_f32 v4, v10, v8
	s_waitcnt lgkmcnt(3)
	s_waitcnt lgkmcnt(2)
	ds_read2_b32 v[20:21], v26 offset0:150 offset1:158
	ds_read2_b32 v[22:23], v26 offset0:215 offset1:223
	v_cvt_pk_bf16_f32 v5, v12, v14
	s_waitcnt lgkmcnt(3)
	s_waitcnt lgkmcnt(2)
	v_cvt_pk_bf16_f32 v6, v16, v18
	s_waitcnt lgkmcnt(1)
	v_or_b32_e32 v24, s6, v99
	s_waitcnt lgkmcnt(0)
	v_ashrrev_i32_e32 v25, 31, v24
	v_lshlrev_b64 v[24:25], 10, v[24:25]
	v_cvt_pk_bf16_f32 v7, v20, v22
	v_lshl_add_u64 v[24:25], v[2:3], 0, v[24:25]
	global_store_dwordx4 v[24:25], v[4:7], off nt
	s_nop 1
	v_cvt_pk_bf16_f32 v4, v11, v9
	v_cvt_pk_bf16_f32 v5, v13, v15
	v_cvt_pk_bf16_f32 v6, v17, v19
	v_cvt_pk_bf16_f32 v7, v21, v23
	v_or_b32_e32 v8, s6, v100
	v_ashrrev_i32_e32 v9, 31, v8
	v_lshlrev_b64 v[8:9], 10, v[8:9]
	ds_read2_b32 v[10:11], v97 offset0:32 offset1:40
	v_lshl_add_u64 v[8:9], v[2:3], 0, v[8:9]
	global_store_dwordx4 v[8:9], v[4:7], off nt
	ds_read2_b32 v[8:9], v97 offset0:97 offset1:105
	ds_read2_b32 v[12:13], v97 offset0:162 offset1:170
	ds_read2_b32 v[14:15], v97 offset0:227 offset1:235
	s_waitcnt lgkmcnt(3)
	s_waitcnt lgkmcnt(2)
	ds_read2_b32 v[16:17], v26 offset0:36 offset1:44
	ds_read2_b32 v[18:19], v26 offset0:101 offset1:109
	v_cvt_pk_bf16_f32 v4, v10, v8
	s_waitcnt lgkmcnt(3)
	s_waitcnt lgkmcnt(2)
	ds_read2_b32 v[20:21], v26 offset0:166 offset1:174
	ds_read2_b32 v[22:23], v26 offset0:231 offset1:239
	v_cvt_pk_bf16_f32 v5, v12, v14
	s_waitcnt lgkmcnt(3)
	s_waitcnt lgkmcnt(2)
	v_cvt_pk_bf16_f32 v6, v16, v18
	s_waitcnt lgkmcnt(1)
	v_or_b32_e32 v24, s6, v101
	s_waitcnt lgkmcnt(0)
	v_ashrrev_i32_e32 v25, 31, v24
	v_lshlrev_b64 v[24:25], 10, v[24:25]
	v_cvt_pk_bf16_f32 v7, v20, v22
	v_lshl_add_u64 v[24:25], v[2:3], 0, v[24:25]
	global_store_dwordx4 v[24:25], v[4:7], off nt
	s_nop 1
	v_cvt_pk_bf16_f32 v4, v11, v9
	v_cvt_pk_bf16_f32 v5, v13, v15
	v_cvt_pk_bf16_f32 v6, v17, v19
	v_cvt_pk_bf16_f32 v7, v21, v23
	v_or_b32_e32 v8, s6, v102
	v_ashrrev_i32_e32 v9, 31, v8
	v_lshlrev_b64 v[8:9], 10, v[8:9]
	ds_read2_b32 v[10:11], v97 offset0:48 offset1:56
	v_lshl_add_u64 v[8:9], v[2:3], 0, v[8:9]
	global_store_dwordx4 v[8:9], v[4:7], off nt
	ds_read2_b32 v[8:9], v97 offset0:113 offset1:121
	ds_read2_b32 v[12:13], v97 offset0:178 offset1:186
	ds_read2_b32 v[14:15], v97 offset0:243 offset1:251
	s_waitcnt lgkmcnt(3)
	s_waitcnt lgkmcnt(2)
	ds_read2_b32 v[16:17], v26 offset0:52 offset1:60
	ds_read2_b32 v[18:19], v26 offset0:117 offset1:125
	v_cvt_pk_bf16_f32 v4, v10, v8
	s_waitcnt lgkmcnt(3)
	s_waitcnt lgkmcnt(2)
	ds_read2_b32 v[20:21], v26 offset0:182 offset1:190
	ds_read2_b32 v[22:23], v26 offset0:247 offset1:255
	v_cvt_pk_bf16_f32 v5, v12, v14
	s_waitcnt lgkmcnt(3)
	s_waitcnt lgkmcnt(2)
	v_cvt_pk_bf16_f32 v6, v16, v18
	s_waitcnt lgkmcnt(1)
	v_or_b32_e32 v24, s6, v103
	s_waitcnt lgkmcnt(0)
	v_ashrrev_i32_e32 v25, 31, v24
	v_lshlrev_b64 v[24:25], 10, v[24:25]
	v_cvt_pk_bf16_f32 v7, v20, v22
	v_lshl_add_u64 v[24:25], v[2:3], 0, v[24:25]
	global_store_dwordx4 v[24:25], v[4:7], off nt
	s_nop 1
	v_cvt_pk_bf16_f32 v4, v11, v9
	v_cvt_pk_bf16_f32 v5, v13, v15
	v_cvt_pk_bf16_f32 v6, v17, v19
	v_cvt_pk_bf16_f32 v7, v21, v23
	v_or_b32_e32 v8, s6, v104
	v_ashrrev_i32_e32 v9, 31, v8
	v_lshlrev_b64 v[8:9], 10, v[8:9]
	v_lshl_add_u64 v[2:3], v[2:3], 0, v[8:9]
	global_store_dwordx4 v[2:3], v[4:7], off nt
	s_waitcnt lgkmcnt(0)

; #define LAS __attribute__((address_space(3)))
; #define WSW(T, off, l) WSP(T, WS_WSET + (size_t)(l) * WSET_STRIDE + (off))
; __device__ __forceinline__ void tr_item(const float* W, int ldw, int k0, int n0, bf16* WT, int ldt, int drow0, LAS float* scr, int lane, const float* kscale = nullptr) {
;     const float* src = W + (size_t)(k0 + (lane >> 4)) * ldw + n0 + (lane & 15) * 4;
;     f32x4 v[16];
; #pragma unroll
;     for (int i = 0; i < 16; ++i) v[i] = __builtin_nontemporal_load((const f32x4*)(src + (size_t)(4 * i) * ldw));
;     LAS float* wp = scr + (lane >> 4) * 65 + (lane & 15) * 4;
; #pragma unroll
;     for (int i = 0; i < 16; ++i) { LAS float* q = wp + (4 * i) * 65; const float ks = kscale ? kscale[k0 + 4 * i + (lane >> 4)] : 1.f; q[0] = v[i].x * ks; q[1] = v[i].y * ks; q[2] = v[i].z * ks; q[3] = v[i].w * ks; }
; __device__ __forceinline__ void convert_tile(const Args& a, GAS unsigned char* wsb, int l, int t, LAS float* scr, int lane) {
;     ...
;     if (r < I_IN) { const int kb = r / 45, nb = r - kb * 45; tr_item(INP(7) + (size_t)l * DM * INW, INW, kb * 64, nb * 64, WSW(bf16, W_IN, l), DM, nb * 64, scr, lane); return; }
.LBB0_1406:
	s_andn2_b64 vcc, exec, s[6:7]
	s_cbranch_vccnz .LBB0_1255
	s_mul_hi_i32 s6, s17, 0xb60b60b7
	s_add_i32 s6, s6, s17
	s_lshr_b32 s7, s6, 31
	s_ashr_i32 s6, s6, 5
	s_add_i32 s6, s6, s7
	s_mul_i32 s7, s6, 0xffffffd3
	v_readlane_b32 s44, v253, 52
	s_add_i32 s7, s7, s17
	s_lshl_b32 s8, s6, 6
	v_readlane_b32 s58, v254, 2
	v_readlane_b32 s59, v254, 3
	s_lshl_b32 s6, s7, 6
	v_or_b32_e32 v4, s8, v67
	v_mov_b64_e32 v[2:3], s[58:59]
	s_movk_i32 s7, 0x2d00
	v_mad_i64_i32 v[2:3], s[10:11], v4, s7, v[2:3]
	s_ashr_i32 s7, s6, 31
	v_lshl_add_u64 v[2:3], s[6:7], 2, v[2:3]
	v_lshlrev_b32_e32 v146, 2, v66
	v_lshl_add_u64 v[62:63], v[2:3], 0, v[146:147]
	s_mov_b32 s7, 0xb000
	v_add_co_u32_e32 v6, vcc, s7, v62
	s_mov_b32 s7, 0x16000
	s_nop 0
	v_addc_co_u32_e32 v7, vcc, 0, v63, vcc
	v_add_co_u32_e32 v10, vcc, s7, v62
	global_load_dwordx4 v[2:5], v[62:63], off nt
	s_nop 0
	global_load_dwordx4 v[6:9], v[6:7], off offset:1024 nt
	v_addc_co_u32_e32 v11, vcc, 0, v63, vcc
	s_mov_b32 s7, 0x21000
	v_add_co_u32_e32 v14, vcc, s7, v62
	s_mov_b32 s7, 0x2d000
	s_nop 0
	v_addc_co_u32_e32 v15, vcc, 0, v63, vcc
	global_load_dwordx4 v[10:13], v[10:11], off offset:2048 nt
	s_nop 0
	global_load_dwordx4 v[14:17], v[14:15], off offset:3072 nt
	v_add_co_u32_e32 v18, vcc, s7, v62
	s_mov_b32 s7, 0x38000
	s_nop 0
	v_addc_co_u32_e32 v19, vcc, 0, v63, vcc
	v_add_co_u32_e32 v22, vcc, s7, v62
	s_mov_b32 s7, 0x43000
	s_nop 0
	v_addc_co_u32_e32 v23, vcc, 0, v63, vcc
	global_load_dwordx4 v[18:21], v[18:19], off nt
	s_nop 0
	global_load_dwordx4 v[22:25], v[22:23], off offset:1024 nt
	v_add_co_u32_e32 v26, vcc, s7, v62
	s_mov_b32 s7, 0x4e000
	s_nop 0
	v_addc_co_u32_e32 v27, vcc, 0, v63, vcc
	v_add_co_u32_e32 v30, vcc, s7, v62
	s_mov_b32 s7, 0x5a000
	s_nop 0
	v_addc_co_u32_e32 v31, vcc, 0, v63, vcc
	global_load_dwordx4 v[26:29], v[26:27], off offset:2048 nt
	s_nop 0
	global_load_dwordx4 v[30:33], v[30:31], off offset:3072 nt
	v_add_co_u32_e32 v34, vcc, s7, v62
	s_mov_b32 s7, 0x65000
	s_nop 0
	v_addc_co_u32_e32 v35, vcc, 0, v63, vcc
	v_add_co_u32_e32 v38, vcc, s7, v62
	s_mov_b32 s7, 0x70000
	s_nop 0
	v_addc_co_u32_e32 v39, vcc, 0, v63, vcc
	global_load_dwordx4 v[34:37], v[34:35], off nt
	s_nop 0
	global_load_dwordx4 v[38:41], v[38:39], off offset:1024 nt
	v_add_co_u32_e32 v42, vcc, s7, v62
	s_mov_b32 s7, 0x7b000
	s_nop 0
	v_addc_co_u32_e32 v43, vcc, 0, v63, vcc
	v_add_co_u32_e32 v46, vcc, s7, v62
	s_mov_b32 s7, 0x87000
	s_nop 0
	v_addc_co_u32_e32 v47, vcc, 0, v63, vcc
	global_load_dwordx4 v[42:45], v[42:43], off offset:2048 nt
	s_nop 0
	global_load_dwordx4 v[46:49], v[46:47], off offset:3072 nt
	v_add_co_u32_e32 v50, vcc, s7, v62
	s_mov_b32 s7, 0x92000
	s_nop 0
	v_addc_co_u32_e32 v51, vcc, 0, v63, vcc
	global_load_dwordx4 v[50:53], v[50:51], off nt
	v_add_co_u32_e32 v54, vcc, s7, v62
	s_mov_b32 s7, 0x9d000
	s_nop 0
	v_addc_co_u32_e32 v55, vcc, 0, v63, vcc
	global_load_dwordx4 v[54:57], v[54:55], off offset:1024 nt
	v_add_co_u32_e32 v58, vcc, s7, v62
	s_mov_b32 s7, 0xa8000
	s_nop 0
	v_addc_co_u32_e32 v59, vcc, 0, v63, vcc
	global_load_dwordx4 v[58:61], v[58:59], off offset:2048 nt
	v_add_co_u32_e32 v62, vcc, s7, v62
	s_ashr_i32 s9, s8, 31
	s_nop 0
	v_addc_co_u32_e32 v63, vcc, 0, v63, vcc
	global_load_dwordx4 v[62:65], v[62:63], off offset:3072 nt
	s_waitcnt vmcnt(15)
	ds_write2_b32 v95, v2, v3 offset1:1
	ds_write2_b32 v95, v4, v5 offset0:2 offset1:3
	v_add_u32_e32 v2, 0x410, v95
	s_waitcnt vmcnt(14)
	ds_write2_b32 v2, v6, v7 offset1:1
	v_add_u32_e32 v2, 0x418, v95
	ds_write2_b32 v2, v8, v9 offset1:1
	v_add_u32_e32 v2, 0x820, v95
	v_readlane_b32 s48, v253, 56
	v_readlane_b32 s49, v253, 57
	v_readlane_b32 s50, v253, 58
	s_waitcnt vmcnt(13)
	ds_write2_b32 v2, v10, v11 offset1:1
	v_add_u32_e32 v2, 0x828, v95
	ds_write2_b32 v2, v12, v13 offset1:1
	v_add_u32_e32 v2, 0xc30, v95
	s_waitcnt vmcnt(12)
	ds_write2_b32 v2, v14, v15 offset1:1
	v_add_u32_e32 v2, 0xc38, v95
	ds_write2_b32 v2, v16, v17 offset1:1
	v_add_u32_e32 v2, 0x1040, v95
	v_readlane_b32 s51, v253, 59
	v_readlane_b32 s52, v253, 60
	v_readlane_b32 s53, v253, 61
	s_waitcnt vmcnt(11)
	ds_write2_b32 v2, v18, v19 offset1:1
	v_add_u32_e32 v2, 0x1048, v95
	ds_write2_b32 v2, v20, v21 offset1:1
	v_add_u32_e32 v2, 0x1450, v95
	s_waitcnt vmcnt(10)
	ds_write2_b32 v2, v22, v23 offset1:1
	v_add_u32_e32 v2, 0x1458, v95
	ds_write2_b32 v2, v24, v25 offset1:1
	v_add_u32_e32 v2, 0x1860, v95
	v_or_b32_e32 v24, s6, v96
	v_ashrrev_i32_e32 v25, 31, v24
	v_lshlrev_b64 v[24:25], 12, v[24:25]
	s_waitcnt vmcnt(9)
	ds_write2_b32 v2, v26, v27 offset1:1
	v_add_u32_e32 v2, 0x1868, v95
	ds_write2_b32 v2, v28, v29 offset1:1
	v_add_u32_e32 v2, 0x1c70, v95
	s_waitcnt vmcnt(8)
	ds_write2_b32 v2, v30, v31 offset1:1
	v_add_u32_e32 v2, 0x1c78, v95
	ds_write2_b32 v2, v32, v33 offset1:1
	v_add_u32_e32 v2, 0x2080, v95
	v_add_u32_e32 v26, 0x400, v97
	v_readlane_b32 s54, v253, 62
	v_readlane_b32 s55, v253, 63
	s_waitcnt vmcnt(7)
	ds_write2_b32 v2, v34, v35 offset1:1
	v_add_u32_e32 v2, 0x2088, v95
	ds_write2_b32 v2, v36, v37 offset1:1
	v_add_u32_e32 v2, 0x2490, v95
	s_waitcnt vmcnt(6)
	ds_write2_b32 v2, v38, v39 offset1:1
	v_add_u32_e32 v2, 0x2498, v95
	ds_write2_b32 v2, v40, v41 offset1:1
	v_add_u32_e32 v2, 0x28a0, v95
	v_readlane_b32 s56, v254, 0
	v_readlane_b32 s57, v254, 1
	v_readlane_b32 s48, v254, 35
	s_waitcnt vmcnt(5)
	ds_write2_b32 v2, v42, v43 offset1:1
	v_add_u32_e32 v2, 0x28a8, v95
	ds_write2_b32 v2, v44, v45 offset1:1
	v_add_u32_e32 v2, 0x2cb0, v95
	s_waitcnt vmcnt(4)
	ds_write2_b32 v2, v46, v47 offset1:1
	v_add_u32_e32 v2, 0x2cb8, v95
	ds_write2_b32 v2, v48, v49 offset1:1
	v_add_u32_e32 v2, 0x30c0, v95
	s_waitcnt vmcnt(3)
; #define LAS __attribute__((address_space(3)))
; __device__ __forceinline__ unsigned pk2(float lo, float hi) { return f2bf(lo) | (f2bf(hi) << 16); }
; __device__ __forceinline__ void tr_item(const float* W, int ldw, int k0, int n0, bf16* WT, int ldt, int drow0, LAS float* scr, int lane, const float* kscale = nullptr) {
;     ...
;     const int kc = lane & 7;
; #pragma unroll
;     for (int j = 0; j < 8; ++j) { const int n = (lane >> 3) + 8 * j; const LAS float* sp = scr + (8 * kc) * 65 + n;
;         u32x4 o; o.x = pk2(sp[0 * 65], sp[1 * 65]); o.y = pk2(sp[2 * 65], sp[3 * 65]); o.z = pk2(sp[4 * 65], sp[5 * 65]); o.w = pk2(sp[6 * 65], sp[7 * 65]);
;         __builtin_nontemporal_store(o, (u32x4*)(WT + (size_t)(drow0 + n) * ldt + k0 + 8 * kc)); }
;     asm volatile("s_waitcnt lgkmcnt(0)" ::: "memory");
; }
	ds_write2_b32 v2, v50, v51 offset1:1
	v_add_u32_e32 v2, 0x30c8, v95
	ds_write2_b32 v2, v52, v53 offset1:1
	v_add_u32_e32 v2, 0x34d0, v95
	v_readlane_b32 s49, v254, 36
	s_waitcnt vmcnt(2)
	ds_write2_b32 v2, v54, v55 offset1:1
	v_add_u32_e32 v2, 0x34d8, v95
	ds_write2_b32 v2, v56, v57 offset1:1
	v_add_u32_e32 v2, 0x38e0, v95
	v_readlane_b32 s50, v254, 37
	v_readlane_b32 s51, v254, 38
	s_waitcnt vmcnt(1)
	ds_write2_b32 v2, v58, v59 offset1:1
	v_add_u32_e32 v2, 0x38e8, v95
	ds_write2_b32 v2, v60, v61 offset1:1
	v_add_u32_e32 v2, 0x3cf0, v95
	v_readlane_b32 s52, v254, 39
	v_readlane_b32 s53, v254, 40
	s_waitcnt vmcnt(0)
	ds_write2_b32 v2, v62, v63 offset1:1
	v_add_u32_e32 v2, 0x3cf8, v95
	ds_write2_b32 v2, v64, v65 offset1:1
	s_waitcnt lgkmcnt(0)
	ds_read2_b32 v[8:9], v97 offset1:8
	ds_read2_b32 v[10:11], v97 offset0:65 offset1:73
	ds_read2_b32 v[12:13], v97 offset0:130 offset1:138
	ds_read2_b32 v[14:15], v97 offset0:195 offset1:203
	ds_read2_b32 v[16:17], v26 offset0:4 offset1:12
	s_waitcnt lgkmcnt(4)
	s_waitcnt lgkmcnt(3)
	ds_read2_b32 v[18:19], v26 offset0:69 offset1:77
	v_cvt_pk_bf16_f32 v4, v8, v10
	s_waitcnt lgkmcnt(3)
	s_waitcnt lgkmcnt(2)
	ds_read2_b32 v[20:21], v26 offset0:134 offset1:142
	ds_read2_b32 v[22:23], v26 offset0:199 offset1:207
	v_cvt_pk_bf16_f32 v5, v12, v14
	s_waitcnt lgkmcnt(3)
	s_waitcnt lgkmcnt(2)
	v_cvt_pk_bf16_f32 v6, v16, v18
	s_waitcnt lgkmcnt(1)
	s_waitcnt lgkmcnt(0)
	v_lshl_add_u64 v[2:3], s[8:9], 1, v[90:91]
	v_cvt_pk_bf16_f32 v7, v20, v22
	v_lshl_add_u64 v[24:25], v[2:3], 0, v[24:25]
	global_store_dwordx4 v[24:25], v[4:7], off nt
	s_nop 1
	v_cvt_pk_bf16_f32 v4, v9, v11
	v_cvt_pk_bf16_f32 v5, v13, v15
	v_cvt_pk_bf16_f32 v6, v17, v19
	v_cvt_pk_bf16_f32 v7, v21, v23
	v_or_b32_e32 v8, s6, v98
	v_ashrrev_i32_e32 v9, 31, v8
	v_lshlrev_b64 v[8:9], 12, v[8:9]
	ds_read2_b32 v[10:11], v97 offset0:16 offset1:24
	v_lshl_add_u64 v[8:9], v[2:3], 0, v[8:9]
	global_store_dwordx4 v[8:9], v[4:7], off nt
	ds_read2_b32 v[8:9], v97 offset0:81 offset1:89
	ds_read2_b32 v[12:13], v97 offset0:146 offset1:154
	ds_read2_b32 v[14:15], v97 offset0:211 offset1:219
	s_waitcnt lgkmcnt(3)
	s_waitcnt lgkmcnt(2)
	ds_read2_b32 v[16:17], v26 offset0:20 offset1:28
	ds_read2_b32 v[18:19], v26 offset0:85 offset1:93
	v_cvt_pk_bf16_f32 v4, v10, v8
	s_waitcnt lgkmcnt(3)
	s_waitcnt lgkmcnt(2)
	ds_read2_b32 v[20:21], v26 offset0:150 offset1:158
	ds_read2_b32 v[22:23], v26 offset0:215 offset1:223
	v_cvt_pk_bf16_f32 v5, v12, v14
	s_waitcnt lgkmcnt(3)
	s_waitcnt lgkmcnt(2)
	v_cvt_pk_bf16_f32 v6, v16, v18
	s_waitcnt lgkmcnt(1)
	v_or_b32_e32 v24, s6, v99
	s_waitcnt lgkmcnt(0)
	v_ashrrev_i32_e32 v25, 31, v24
	v_lshlrev_b64 v[24:25], 12, v[24:25]
	v_cvt_pk_bf16_f32 v7, v20, v22
	v_lshl_add_u64 v[24:25], v[2:3], 0, v[24:25]
	global_store_dwordx4 v[24:25], v[4:7], off nt
	s_nop 1
	v_cvt_pk_bf16_f32 v4, v11, v9
	v_cvt_pk_bf16_f32 v5, v13, v15
	v_cvt_pk_bf16_f32 v6, v17, v19
	v_cvt_pk_bf16_f32 v7, v21, v23
	v_or_b32_e32 v8, s6, v100
	v_ashrrev_i32_e32 v9, 31, v8
	v_lshlrev_b64 v[8:9], 12, v[8:9]
	ds_read2_b32 v[10:11], v97 offset0:32 offset1:40
	v_lshl_add_u64 v[8:9], v[2:3], 0, v[8:9]
	global_store_dwordx4 v[8:9], v[4:7], off nt
	ds_read2_b32 v[8:9], v97 offset0:97 offset1:105
	ds_read2_b32 v[12:13], v97 offset0:162 offset1:170
	ds_read2_b32 v[14:15], v97 offset0:227 offset1:235
	s_waitcnt lgkmcnt(3)
	s_waitcnt lgkmcnt(2)
	ds_read2_b32 v[16:17], v26 offset0:36 offset1:44
	ds_read2_b32 v[18:19], v26 offset0:101 offset1:109
	v_cvt_pk_bf16_f32 v4, v10, v8
	s_waitcnt lgkmcnt(3)
	s_waitcnt lgkmcnt(2)
	ds_read2_b32 v[20:21], v26 offset0:166 offset1:174
	ds_read2_b32 v[22:23], v26 offset0:231 offset1:239
	v_cvt_pk_bf16_f32 v5, v12, v14
	s_waitcnt lgkmcnt(3)
	s_waitcnt lgkmcnt(2)
	v_cvt_pk_bf16_f32 v6, v16, v18
	s_waitcnt lgkmcnt(1)
	v_or_b32_e32 v24, s6, v101
	s_waitcnt lgkmcnt(0)
	v_ashrrev_i32_e32 v25, 31, v24
	v_lshlrev_b64 v[24:25], 12, v[24:25]
	v_cvt_pk_bf16_f32 v7, v20, v22
	v_lshl_add_u64 v[24:25], v[2:3], 0, v[24:25]
	global_store_dwordx4 v[24:25], v[4:7], off nt
	s_nop 1
	v_cvt_pk_bf16_f32 v4, v11, v9
	v_cvt_pk_bf16_f32 v5, v13, v15
	v_cvt_pk_bf16_f32 v6, v17, v19
	v_cvt_pk_bf16_f32 v7, v21, v23
	v_or_b32_e32 v8, s6, v102
	v_ashrrev_i32_e32 v9, 31, v8
	v_lshlrev_b64 v[8:9], 12, v[8:9]
	ds_read2_b32 v[10:11], v97 offset0:48 offset1:56
	v_lshl_add_u64 v[8:9], v[2:3], 0, v[8:9]
	global_store_dwordx4 v[8:9], v[4:7], off nt
	ds_read2_b32 v[8:9], v97 offset0:113 offset1:121
	ds_read2_b32 v[12:13], v97 offset0:178 offset1:186
	ds_read2_b32 v[14:15], v97 offset0:243 offset1:251
	s_waitcnt lgkmcnt(3)
	s_waitcnt lgkmcnt(2)
	ds_read2_b32 v[16:17], v26 offset0:52 offset1:60
	ds_read2_b32 v[18:19], v26 offset0:117 offset1:125
	v_cvt_pk_bf16_f32 v4, v10, v8
	s_waitcnt lgkmcnt(3)
	s_waitcnt lgkmcnt(2)
	ds_read2_b32 v[20:21], v26 offset0:182 offset1:190
	ds_read2_b32 v[22:23], v26 offset0:247 offset1:255
	v_cvt_pk_bf16_f32 v5, v12, v14
	s_waitcnt lgkmcnt(3)
	s_waitcnt lgkmcnt(2)
	v_cvt_pk_bf16_f32 v6, v16, v18
	s_waitcnt lgkmcnt(1)
	v_or_b32_e32 v24, s6, v103
	s_waitcnt lgkmcnt(0)
	v_ashrrev_i32_e32 v25, 31, v24
	v_lshlrev_b64 v[24:25], 12, v[24:25]
	v_cvt_pk_bf16_f32 v7, v20, v22
	v_lshl_add_u64 v[24:25], v[2:3], 0, v[24:25]
	global_store_dwordx4 v[24:25], v[4:7], off nt
	s_nop 1
	v_cvt_pk_bf16_f32 v4, v11, v9
	v_cvt_pk_bf16_f32 v5, v13, v15
	v_cvt_pk_bf16_f32 v6, v17, v19
	v_cvt_pk_bf16_f32 v7, v21, v23
	v_or_b32_e32 v8, s6, v104
	v_ashrrev_i32_e32 v9, 31, v8
	v_lshlrev_b64 v[8:9], 12, v[8:9]
	v_lshl_add_u64 v[2:3], v[2:3], 0, v[8:9]
	global_store_dwordx4 v[2:3], v[4:7], off nt
	s_waitcnt lgkmcnt(0)
	v_readlane_b32 s54, v254, 41
	v_readlane_b32 s55, v254, 42
	v_readlane_b32 s58, v254, 45
	v_readlane_b32 s59, v254, 46
	v_readlane_b32 s60, v254, 47
	v_readlane_b32 s61, v254, 48
	v_readlane_b32 s62, v254, 49
	v_readlane_b32 s63, v254, 50
	v_readlane_b32 s45, v253, 53
	v_readlane_b32 s46, v253, 54
	v_readlane_b32 s47, v253, 55
	v_readlane_b32 s56, v254, 43
	v_readlane_b32 s57, v254, 44
	s_branch .LBB0_1255

; #define LAS __attribute__((address_space(3)))
; __device__ __forceinline__ void attn_unit(const bf16* __restrict__ Qraw, const float* __restrict__ ssq, const float* __restrict__ qn, int t0, const bf16* __restrict__ Kh, const bf16* __restrict__ Vh, bf16* __restrict__ Ob, int seq, LAS char* lds, int tid) {
;     ...
;             for (int e = 0; e < 8; ++e) { const float y = bf2f((unsigned short)raw[d0][e]) * sq; ss = fmaf(y, y, ss); }
;         ss += __shfl_xor(ss, 32);
;         const float f = sq * rsqrtf(ss * (1.f / DQK) + EPS) * QSC;
; #pragma unroll
;         for (int d0 = 0; d0 < 8; ++d0) { const f32x4 g0 = *(const f32x4*)(qnb + d0 * 64 + gq), g1 = *(const f32x4*)(qnb + d0 * 64 + 16 + gq);
;             u32x4 w; w.x = pk2(bf2f((unsigned short)raw[d0][0]) * f * g0.x, bf2f((unsigned short)raw[d0][1]) * f * g0.y); w.y = pk2(bf2f((unsigned short)raw[d0][2]) * f * g0.z, bf2f((unsigned short)raw[d0][3]) * f * g0.w);
;             w.z = pk2(bf2f((unsigned short)raw[d0][4]) * f * g1.x, bf2f((unsigned short)raw[d0][5]) * f * g1.y); w.w = pk2(bf2f((unsigned short)raw[d0][6]) * f * g1.z, bf2f((unsigned short)raw[d0][7]) * f * g1.w);
;             if (d0 < NQR) qr[d0 < NQR ? d0 : 0] = __builtin_bit_cast(bf16x8, w); else *reinterpret_cast<LAS bf16x8*>(Ql + (d0 - NQR) * 32) = __builtin_bit_cast(bf16x8, w); }
;         const int t = t0 + wid * QBLK + r32; const float pr = (float)(t >> 6), pc = (float)(t & 63);
; #pragma unroll
;         for (int ax = 0; ax < 2; ++ax) {
;             float x1[8], x2[8];
;             const f32x4 ga0 = *(const f32x4*)(qnb + (128 + 32 * ax) * 4 + gq), ga1 = *(const f32x4*)(qnb + (128 + 32 * ax) * 4 + 16 + gq), gb0 = *(const f32x4*)(qnb + (144 + 32 * ax) * 4 + gq), gb1 = *(const f32x4*)(qnb + (144 + 32 * ax) * 4 + 16 + gq);
;             const float ga[8] = {ga0.x, ga0.y, ga0.z, ga0.w, ga1.x, ga1.y, ga1.z, ga1.w}, gb[8] = {gb0.x, gb0.y, gb0.z, gb0.w, gb1.x, gb1.y, gb1.z, gb1.w};
; #pragma unroll
;             for (int e = 0; e < 8; ++e) { x1[e] = bf2f((unsigned short)raw[8 + 2 * ax][e]) * f * ga[e]; x2[e] = bf2f((unsigned short)raw[9 + 2 * ax][e]) * f * gb[e]; }
;             if (t0 >= 0) { const float p = ax ? pc : pr;
; #pragma unroll
;                 for (int e = 0; e < 8; ++e) { const float inv = __builtin_amdgcn_exp2f(-(float)((gq >> 2) + e) * (13.287712379549449f / 16.f)); float sn, cs; __sincosf(p * inv, &sn, &cs);
.LBB0_1461:
	v_ashrrev_i32_e32 v1, 4, v190
	v_and_b32_e32 v68, 0xfffff0, v1
	v_lshlrev_b32_e32 v69, 1, v1
	v_lshlrev_b32_e32 v66, 3, v190
	v_and_or_b32 v68, v69, 8, v68
	v_and_b32_e32 v67, 0x78, v66
	v_lshrrev_b32_e32 v69, 1, v1
	v_lshrrev_b32_e32 v68, 1, v68
	v_bfe_u32 v66, v66, 5, 2
	v_and_b32_e32 v70, 3, v1
	v_or_b32_e32 v68, v68, v66
	v_and_or_b32 v69, v69, 4, v70
	v_lshlrev_b32_e32 v67, 1, v67
	v_lshlrev_b32_e32 v68, 9, v68
	v_lshlrev_b32_e32 v69, 6, v69
	v_and_b32_e32 v70, 48, v67
	v_or3_b32 v71, v68, v69, v70
	v_add_u32_e32 v68, 32, v1
	v_and_b32_e32 v72, 0xfffff0, v68
	v_lshlrev_b32_e32 v68, 1, v68
	v_and_or_b32 v68, v68, 8, v72
	v_lshrrev_b32_e32 v68, 1, v68
	v_or_b32_e32 v66, v68, v66
	v_lshlrev_b32_e32 v66, 9, v66
	v_or3_b32 v70, v66, v69, v70
	v_lshl_or_b32 v146, v1, 8, v67
	v_mov_b32_e32 v66, v54
	v_mov_b32_e32 v67, v56
	v_mov_b32_e32 v56, v55
	v_mov_b32_e32 v54, v62
	v_mov_b32_e32 v55, v64
	v_mov_b32_e32 v64, v63
	v_mov_b32_e32 v62, v6
	v_mov_b32_e32 v63, v8
	v_mov_b32_e32 v8, v7
	v_mov_b32_e32 v6, v14
	v_mov_b32_e32 v7, v16
	v_mov_b32_e32 v16, v15
	v_mov_b32_e32 v14, v22
	v_mov_b32_e32 v15, v24
	v_mov_b32_e32 v24, v23
	v_mov_b32_e32 v22, v30
	v_mov_b32_e32 v23, v32
	v_mov_b32_e32 v32, v31
	v_mov_b32_e32 v30, v38
	v_mov_b32_e32 v31, v40
	v_mov_b32_e32 v40, v39
	v_mov_b32_e32 v38, v46
	v_mov_b32_e32 v39, v48
	v_mov_b32_e32 v48, v47
	v_pk_mul_f32 v[46:47], v[114:115], v[140:141]
	v_mov_b32_e32 v68, v42
	v_pk_mul_f32 v[38:39], v[38:39], v[46:47]
	v_pk_mul_f32 v[46:47], v[114:115], v[142:143]
	v_mov_b32_e32 v69, v44
	v_pk_mul_f32 v[46:47], v[48:49], v[46:47]
	v_pk_mul_f32 v[48:49], v[114:115], v[148:149]
	v_mov_b32_e32 v44, v43
	v_pk_mul_f32 v[48:49], v[68:69], v[48:49]
	v_pk_mul_f32 v[68:69], v[114:115], v[144:145]
	v_mul_u32_u24_e32 v1, 0x190, v186
	v_pk_mul_f32 v[42:43], v[44:45], v[68:69]
	v_add3_u32 v195, 0, v1, v188
	v_bfe_u32 v1, v43, 16, 1
	v_bfe_u32 v44, v42, 16, 1
	v_add3_u32 v42, v42, v44, s37
	v_add3_u32 v1, v43, v1, s37
	v_bfe_u32 v43, v38, 16, 1
	v_bfe_u32 v44, v39, 16, 1
	v_bfe_u32 v45, v47, 16, 1
	v_bfe_u32 v68, v46, 16, 1
	v_add3_u32 v39, v39, v44, s37
	v_add3_u32 v38, v38, v43, s37
	v_add3_u32 v46, v46, v68, s37
	v_add3_u32 v45, v47, v45, s37
	v_bfe_u32 v47, v48, 16, 1
	v_lshrrev_b32_e32 v38, 16, v38
	v_lshrrev_b32_e32 v39, 16, v39
	v_add3_u32 v47, v48, v47, s37
	v_and_or_b32 v149, v45, s33, v39
	v_and_or_b32 v148, v46, s33, v38
	v_pk_mul_f32 v[38:39], v[114:115], v[138:139]
	v_lshrrev_b32_e32 v43, 16, v47
	v_pk_mul_f32 v[30:31], v[30:31], v[38:39]
	v_pk_mul_f32 v[38:39], v[114:115], v[136:137]
	v_bfe_u32 v68, v49, 16, 1
	v_and_or_b32 v150, v42, s33, v43
	v_pk_mul_f32 v[38:39], v[40:41], v[38:39]
	v_pk_mul_f32 v[40:41], v[114:115], v[134:135]
	v_mov_b32_e32 v42, v34
	v_mov_b32_e32 v43, v36
	v_add3_u32 v49, v49, v68, s37
	v_pk_mul_f32 v[40:41], v[42:43], v[40:41]
	v_pk_mul_f32 v[42:43], v[114:115], v[132:133]
	v_mov_b32_e32 v36, v35
	v_lshrrev_b32_e32 v44, 16, v49
	v_pk_mul_f32 v[34:35], v[36:37], v[42:43]
	v_and_or_b32 v151, v1, s33, v44
	v_bfe_u32 v1, v35, 16, 1
	v_bfe_u32 v36, v34, 16, 1
	v_add3_u32 v34, v34, v36, s37
	v_add3_u32 v1, v35, v1, s37
	v_bfe_u32 v35, v30, 16, 1
	v_bfe_u32 v36, v31, 16, 1
	v_bfe_u32 v37, v39, 16, 1
	v_bfe_u32 v42, v38, 16, 1
	v_add3_u32 v31, v31, v36, s37
	v_add3_u32 v30, v30, v35, s37
	v_add3_u32 v38, v38, v42, s37
	v_add3_u32 v37, v39, v37, s37
	v_bfe_u32 v39, v40, 16, 1
	v_lshrrev_b32_e32 v30, 16, v30
	v_lshrrev_b32_e32 v31, 16, v31
	v_add3_u32 v39, v40, v39, s37
	v_and_or_b32 v153, v37, s33, v31
	v_and_or_b32 v152, v38, s33, v30
	v_pk_mul_f32 v[30:31], v[114:115], v[130:131]
	v_lshrrev_b32_e32 v35, 16, v39
	v_pk_mul_f32 v[22:23], v[22:23], v[30:31]
	v_pk_mul_f32 v[30:31], v[114:115], v[128:129]
	v_bfe_u32 v42, v41, 16, 1
	v_and_or_b32 v154, v34, s33, v35
	v_pk_mul_f32 v[30:31], v[32:33], v[30:31]
	v_pk_mul_f32 v[32:33], v[114:115], v[126:127]
	v_mov_b32_e32 v34, v26
	v_mov_b32_e32 v35, v28
	v_add3_u32 v41, v41, v42, s37
	v_pk_mul_f32 v[32:33], v[34:35], v[32:33]
	v_pk_mul_f32 v[34:35], v[114:115], v[124:125]
	v_mov_b32_e32 v28, v27
	v_lshrrev_b32_e32 v36, 16, v41
	v_pk_mul_f32 v[26:27], v[28:29], v[34:35]
	v_and_or_b32 v155, v1, s33, v36
	v_bfe_u32 v1, v27, 16, 1
	v_bfe_u32 v28, v26, 16, 1
	s_mul_i32 s10, s31, 0x110000
	v_bfe_u32 v29, v31, 16, 1
	v_add3_u32 v26, v26, v28, s37
	v_add3_u32 v1, v27, v1, s37
	v_bfe_u32 v27, v22, 16, 1
	v_bfe_u32 v28, v23, 16, 1
	s_mul_hi_i32 s11, s31, 0x110000
	s_add_u32 s10, s51, s10
	v_bfe_u32 v34, v30, 16, 1
	v_add3_u32 v29, v31, v29, s37
	v_bfe_u32 v31, v32, 16, 1
	v_add3_u32 v23, v23, v28, s37
	v_add3_u32 v22, v22, v27, s37
	s_addc_u32 s11, s52, s11
	v_add3_u32 v30, v30, v34, s37
	v_add3_u32 v31, v32, v31, s37
	v_lshrrev_b32_e32 v22, 16, v22
	v_lshrrev_b32_e32 v23, 16, v23
	v_bfe_u32 v34, v33, 16, 1
	v_lshrrev_b32_e32 v27, 16, v31
	v_and_or_b32 v157, v29, s33, v23
	v_and_or_b32 v156, v30, s33, v22
	v_pk_mul_f32 v[22:23], v[114:115], v[122:123]
	v_lshl_add_u64 v[68:69], s[10:11], 0, v[146:147]
	v_add3_u32 v33, v33, v34, s37
	v_and_or_b32 v158, v26, s33, v27
	v_pk_mul_f32 v[14:15], v[14:15], v[22:23]
	v_pk_mul_f32 v[22:23], v[114:115], v[120:121]
	v_add_co_u32_e32 v26, vcc, s80, v68
	v_lshrrev_b32_e32 v28, 16, v33
	v_pk_mul_f32 v[30:31], v[24:25], v[22:23]
	v_pk_mul_f32 v[22:23], v[114:115], v[118:119]
	v_mov_b32_e32 v24, v18
	v_mov_b32_e32 v25, v20
	v_addc_co_u32_e32 v27, vcc, 0, v69, vcc
	v_and_or_b32 v159, v1, s33, v28
	v_pk_mul_f32 v[32:33], v[24:25], v[22:23]
	global_load_dwordx4 v[22:25], v146, s[10:11]
	v_pk_mul_f32 v[34:35], v[114:115], v[116:117]
	global_load_dwordx4 v[26:29], v[26:27], off
	v_mov_b32_e32 v20, v19
; #define LAS __attribute__((address_space(3)))
; __device__ __forceinline__ unsigned pk2(float lo, float hi) { return f2bf(lo) | (f2bf(hi) << 16); }
; #define VLOAD(k0) do { const char* vp_ = (const char*)Vh + (size_t)(k0) * (DVH * 2); vs0 = *reinterpret_cast<const bf16x8*>(vp_ + vgo); vs1 = *reinterpret_cast<const bf16x8*>(vp_ + 32 * DVH * 2 + vgo); } while (0)
; #define VWRITE(b) do { *(LAS bf16x8*)(V_lds + (b) * SHM_V + vst0) = vs0; *(LAS bf16x8*)(V_lds + (b) * SHM_V + vst1) = vs1; } while (0)
; #define SWAIT() asm volatile("s_waitcnt vmcnt(0)" ::: "memory")
; __device__ __forceinline__ void qkt(f32x16& p0, f32x16& p1, const LAS char* Kl, const bf16x8* qr, const LAS char* Ql, const f32x16& init) {
; #pragma unroll
;     for (int d0 = 0; d0 < 12; ++d0) {
;         const bf16x8 b0 = *reinterpret_cast<const LAS bf16x8*>(Kl + d0 * 32);
;         const bf16x8 b1 = *reinterpret_cast<const LAS bf16x8*>(Kl + 32 * KROWB + d0 * 32);
;         const bf16x8 q = d0 < NQR ? qr[d0 < NQR ? d0 : 0] : *reinterpret_cast<const LAS bf16x8*>(Ql + (d0 - NQR) * 32);
;         p0 = __builtin_amdgcn_mfma_f32_32x32x16_bf16(b0, q, d0 == 0 ? init : p0, 0, 0, 0);
;         p1 = __builtin_amdgcn_mfma_f32_32x32x16_bf16(b1, q, d0 == 0 ? init : p1, 0, 0, 0); }
; __device__ __forceinline__ void attn_unit(const bf16* __restrict__ Qraw, const float* __restrict__ ssq, const float* __restrict__ qn, int t0, const bf16* __restrict__ Kh, const bf16* __restrict__ Vh, bf16* __restrict__ Ob, int seq, LAS char* lds, int tid) {
;     ...
; #pragma unroll
;         for (int d0 = 0; d0 < 8; ++d0) { const f32x4 g0 = *(const f32x4*)(qnb + d0 * 64 + gq), g1 = *(const f32x4*)(qnb + d0 * 64 + 16 + gq);
;             u32x4 w; w.x = pk2(bf2f((unsigned short)raw[d0][0]) * f * g0.x, bf2f((unsigned short)raw[d0][1]) * f * g0.y); w.y = pk2(bf2f((unsigned short)raw[d0][2]) * f * g0.z, bf2f((unsigned short)raw[d0][3]) * f * g0.w);
;             w.z = pk2(bf2f((unsigned short)raw[d0][4]) * f * g1.x, bf2f((unsigned short)raw[d0][5]) * f * g1.y); w.w = pk2(bf2f((unsigned short)raw[d0][6]) * f * g1.z, bf2f((unsigned short)raw[d0][7]) * f * g1.w);
;             if (d0 < NQR) qr[d0 < NQR ? d0 : 0] = __builtin_bit_cast(bf16x8, w); else *reinterpret_cast<LAS bf16x8*>(Ql + (d0 - NQR) * 32) = __builtin_bit_cast(bf16x8, w); }
;     ...
;     DMA_K(0, 0); DMA_K(KVBLK, 1); VLOAD(0); SWAIT(); VWRITE(0); __syncthreads();
	v_pk_mul_f32 v[18:19], v[20:21], v[34:35]
	v_bfe_u32 v21, v31, 16, 1
	v_bfe_u32 v1, v19, 16, 1
	v_bfe_u32 v20, v18, 16, 1
	v_add3_u32 v18, v18, v20, s37
	v_add3_u32 v1, v19, v1, s37
	v_bfe_u32 v19, v14, 16, 1
	v_bfe_u32 v20, v15, 16, 1
	v_bfe_u32 v34, v30, 16, 1
	v_add3_u32 v15, v15, v20, s37
	v_add3_u32 v14, v14, v19, s37
	v_add3_u32 v30, v30, v34, s37
	v_add3_u32 v21, v31, v21, s37
	v_bfe_u32 v31, v32, 16, 1
	v_lshrrev_b32_e32 v14, 16, v14
	v_lshrrev_b32_e32 v15, 16, v15
	v_add3_u32 v31, v32, v31, s37
	v_and_or_b32 v161, v21, s33, v15
	v_and_or_b32 v160, v30, s33, v14
	v_pk_mul_f32 v[14:15], v[114:115], v[112:113]
	v_lshrrev_b32_e32 v19, 16, v31
	v_pk_mul_f32 v[6:7], v[6:7], v[14:15]
	v_pk_mul_f32 v[14:15], v[114:115], v[110:111]
	v_bfe_u32 v34, v33, 16, 1
	v_and_or_b32 v162, v18, s33, v19
	v_pk_mul_f32 v[14:15], v[16:17], v[14:15]
	v_pk_mul_f32 v[16:17], v[114:115], v[108:109]
	v_mov_b32_e32 v18, v10
	v_mov_b32_e32 v19, v12
	v_add3_u32 v33, v33, v34, s37
	v_pk_mul_f32 v[16:17], v[18:19], v[16:17]
	v_pk_mul_f32 v[18:19], v[114:115], v[106:107]
	v_mov_b32_e32 v12, v11
	v_lshrrev_b32_e32 v20, 16, v33
	v_pk_mul_f32 v[10:11], v[12:13], v[18:19]
	v_and_or_b32 v163, v1, s33, v20
	v_bfe_u32 v1, v11, 16, 1
	v_bfe_u32 v12, v10, 16, 1
	v_add3_u32 v10, v10, v12, s37
	v_add3_u32 v1, v11, v1, s37
	v_bfe_u32 v11, v6, 16, 1
	v_bfe_u32 v12, v7, 16, 1
	v_bfe_u32 v13, v15, 16, 1
	v_bfe_u32 v18, v14, 16, 1
	v_add3_u32 v7, v7, v12, s37
	v_add3_u32 v6, v6, v11, s37
	v_add3_u32 v14, v14, v18, s37
	v_add3_u32 v13, v15, v13, s37
	v_bfe_u32 v15, v16, 16, 1
	v_lshrrev_b32_e32 v6, 16, v6
	v_lshrrev_b32_e32 v7, 16, v7
	v_add3_u32 v15, v16, v15, s37
	v_and_or_b32 v165, v13, s33, v7
	v_and_or_b32 v164, v14, s33, v6
	v_pk_mul_f32 v[6:7], v[114:115], v[102:103]
	v_bfe_u32 v18, v17, 16, 1
	v_lshrrev_b32_e32 v11, 16, v15
	v_pk_mul_f32 v[14:15], v[62:63], v[6:7]
	v_pk_mul_f32 v[6:7], v[114:115], v[90:91]
	v_add3_u32 v17, v17, v18, s37
	v_and_or_b32 v166, v10, s33, v11
	v_pk_mul_f32 v[6:7], v[8:9], v[6:7]
	v_pk_mul_f32 v[8:9], v[114:115], v[104:105]
	v_mov_b32_e32 v10, v2
	v_mov_b32_e32 v11, v4
	v_lshrrev_b32_e32 v12, 16, v17
	v_pk_mul_f32 v[16:17], v[10:11], v[8:9]
	v_pk_mul_f32 v[8:9], v[114:115], v[92:93]
	v_mov_b32_e32 v4, v3
	v_add_u32_e32 v198, 0, v71
	v_add_u32_e32 v199, 0, v70
	v_pk_mul_f32 v[8:9], v[4:5], v[8:9]
	s_waitcnt vmcnt(0)
	v_and_or_b32 v167, v1, s33, v12
	v_bfe_u32 v1, v9, 16, 1
	v_bfe_u32 v10, v8, 16, 1
	s_waitcnt vmcnt(0)
	ds_write_b128 v198, v[22:25]
	v_bfe_u32 v11, v7, 16, 1
	ds_write_b128 v199, v[26:29]
	s_waitcnt lgkmcnt(0)
	s_barrier
	ds_read_b128 v[2:5], v195 offset:32768
	v_bfe_u32 v12, v6, 16, 1
	v_add3_u32 v62, v6, v12, s37
	v_add3_u32 v63, v7, v11, s37
	v_add3_u32 v70, v8, v10, s37
	v_add3_u32 v1, v9, v1, s37
	ds_read_b128 v[6:9], v195 offset:45568
	ds_read_b128 v[10:13], v195 offset:32800
	s_waitcnt lgkmcnt(2)
	v_mfma_f32_32x32x16_bf16 v[18:33], v[2:5], v[148:151], 0
	v_bfe_u32 v71, v14, 16, 1
	v_bfe_u32 v2, v15, 16, 1
	v_bfe_u32 v3, v16, 16, 1
	v_bfe_u32 v4, v17, 16, 1
	v_add3_u32 v15, v15, v2, s37
	v_add3_u32 v17, v17, v4, s37
	v_add3_u32 v16, v16, v3, s37
	s_waitcnt lgkmcnt(1)
	v_mfma_f32_32x32x16_bf16 v[34:49], v[6:9], v[148:151], 0
	v_add3_u32 v6, v14, v71, s37
	ds_read_b128 v[2:5], v195 offset:45600
	v_lshrrev_b32_e32 v6, 16, v6
	v_lshrrev_b32_e32 v7, 16, v15
	v_and_or_b32 v169, v63, s33, v7
	v_and_or_b32 v168, v62, s33, v6
	v_pk_mul_f32 v[6:7], v[114:115], v[98:99]
	v_lshrrev_b32_e32 v8, 16, v16
	v_lshrrev_b32_e32 v9, 16, v17
	v_pk_mul_f32 v[14:15], v[54:55], v[6:7]
	v_pk_mul_f32 v[6:7], v[114:115], v[100:101]
	v_and_or_b32 v171, v1, s33, v9
	v_and_or_b32 v170, v70, s33, v8
	v_pk_mul_f32 v[16:17], v[64:65], v[6:7]
	ds_read_b128 v[6:9], v195 offset:32832
	s_waitcnt lgkmcnt(2)
	v_mfma_f32_32x32x16_bf16 v[18:33], v[10:13], v[152:155], v[18:33]
	v_mul_f32_e64 v62, v114, v94
	v_mul_f32_e64 v63, v115, v95
	s_lshl_b32 s10, s16, 2
	s_add_i32 s58, s10, 0
	s_movk_i32 s10, 0x4000
	s_mov_b32 s12, s13
	s_mov_b32 s14, s13
	s_mov_b32 s15, s13
	s_waitcnt lgkmcnt(1)
	v_mfma_f32_32x32x16_bf16 v[34:49], v[2:5], v[152:155], v[34:49]
	v_mul_f32_e64 v2, v114, v96
	v_mul_f32_e64 v3, v115, v97
	v_mov_b32_e32 v4, v58
	v_mov_b32_e32 v5, v60
	v_mul_f32_e64 v54, v4, v2
	v_mul_f32_e64 v55, v5, v3
	ds_read_b128 v[2:5], v195 offset:45632
	ds_read_b128 v[10:13], v195 offset:32864
	v_mov_b32_e32 v60, v59
	v_pk_mul_f32 v[58:59], v[60:61], v[62:63]
	s_waitcnt lgkmcnt(2)
	v_mfma_f32_32x32x16_bf16 v[18:33], v[6:9], v[156:159], v[18:33]
	ds_read_b128 v[6:9], v195 offset:45664
	v_bfe_u32 v60, v58, 16, 1
	v_add3_u32 v58, v58, v60, s37
	v_bfe_u32 v61, v17, 16, 1
	v_bfe_u32 v62, v16, 16, 1
	s_waitcnt lgkmcnt(2)
	v_mfma_f32_32x32x16_bf16 v[34:49], v[2:5], v[156:159], v[34:49]
	v_bfe_u32 v2, v14, 16, 1
	v_bfe_u32 v3, v15, 16, 1
	v_bfe_u32 v4, v54, 16, 1
	v_add3_u32 v2, v14, v2, s37
	v_lshrrev_b32_e32 v14, 16, v2
	v_add3_u32 v16, v16, v62, s37
	s_waitcnt lgkmcnt(1)
	v_mfma_f32_32x32x16_bf16 v[18:33], v[10:13], v[160:163], v[18:33]
	v_add3_u32 v11, v54, v4, s37
	v_add3_u32 v12, v15, v3, s37
	ds_read_b128 v[2:5], v195 offset:32896
	v_lshrrev_b32_e32 v15, 16, v12
	v_add3_u32 v17, v17, v61, s37
	v_and_or_b32 v173, v17, s33, v15
	s_waitcnt lgkmcnt(1)
	v_mfma_f32_32x32x16_bf16 v[34:49], v[6:9], v[160:163], v[34:49]
	v_lshrrev_b32_e32 v6, 16, v11
	v_cvt_pk_bf16_f32 v175, v55, v59
	v_and_or_b32 v174, v58, s33, v6
	ds_read_b128 v[6:9], v195 offset:45696
	ds_read_b128 v[10:13], v195 offset:32928
	v_and_or_b32 v172, v16, s33, v14
	s_mov_b32 s16, s13
	s_waitcnt lgkmcnt(2)
; #define LAS __attribute__((address_space(3)))
; __device__ __forceinline__ void qkt(f32x16& p0, f32x16& p1, const LAS char* Kl, const bf16x8* qr, const LAS char* Ql, const f32x16& init) {
; #pragma unroll
;     for (int d0 = 0; d0 < 12; ++d0) {
;         const bf16x8 b0 = *reinterpret_cast<const LAS bf16x8*>(Kl + d0 * 32);
;         const bf16x8 b1 = *reinterpret_cast<const LAS bf16x8*>(Kl + 32 * KROWB + d0 * 32);
;         const bf16x8 q = d0 < NQR ? qr[d0 < NQR ? d0 : 0] : *reinterpret_cast<const LAS bf16x8*>(Ql + (d0 - NQR) * 32);
;         p0 = __builtin_amdgcn_mfma_f32_32x32x16_bf16(b0, q, d0 == 0 ? init : p0, 0, 0, 0);
;         p1 = __builtin_amdgcn_mfma_f32_32x32x16_bf16(b1, q, d0 == 0 ? init : p1, 0, 0, 0); }
	v_mfma_f32_32x32x16_bf16 v[18:33], v[2:5], v[164:167], v[18:33]
	v_mul_f32_e64 v2, v114, v86
	v_mul_f32_e64 v3, v115, v87
	s_mov_b32 s17, s13
	v_mul_f32_e64 v14, v66, v2
	v_mul_f32_e64 v15, v67, v3
	v_pk_mul_f32 v[2:3], v[114:115], v[88:89]
	s_mov_b32 s18, s13
	v_pk_mul_f32 v[16:17], v[56:57], v[2:3]
	ds_read_b128 v[2:5], v195 offset:45728
	s_waitcnt lgkmcnt(2)
	v_mfma_f32_32x32x16_bf16 v[34:49], v[6:9], v[164:167], v[34:49]
	v_mul_f32_e64 v6, v114, v84
	v_mul_f32_e64 v7, v115, v85
	v_mov_b32_e32 v8, v50
	v_mov_b32_e32 v9, v52
	v_mul_f32_e64 v54, v8, v6
	v_mul_f32_e64 v55, v9, v7
	v_pk_mul_f32 v[6:7], v[114:115], v[82:83]
	v_mov_b32_e32 v52, v51
	v_pk_mul_f32 v[50:51], v[52:53], v[6:7]
	v_bfe_u32 v6, v17, 16, 1
	v_bfe_u32 v7, v16, 16, 1
	v_add3_u32 v16, v16, v7, s37
	v_add3_u32 v17, v17, v6, s37
	ds_read_b128 v[6:9], v195 offset:32960
	s_waitcnt lgkmcnt(2)
	v_mfma_f32_32x32x16_bf16 v[18:33], v[10:13], v[168:171], v[18:33]
	v_bfe_u32 v10, v50, 16, 1
	v_bfe_u32 v1, v51, 16, 1
	v_add3_u32 v50, v50, v10, s37
	v_add3_u32 v1, v51, v1, s37
	v_bfe_u32 v51, v14, 16, 1
	v_bfe_u32 v52, v15, 16, 1
	v_bfe_u32 v53, v54, 16, 1
	s_waitcnt lgkmcnt(1)
	v_mfma_f32_32x32x16_bf16 v[34:49], v[2:5], v[168:171], v[34:49]
	ds_read_b128 v[2:5], v195 offset:45760
	ds_read_b128 v[10:13], v195 offset:32992
	v_add3_u32 v53, v54, v53, s37
	v_add3_u32 v15, v15, v52, s37
	s_mov_b32 s19, s13
	s_mov_b32 s20, s13
	s_mov_b32 s21, s13
	s_mov_b32 s22, s13
	s_waitcnt lgkmcnt(2)
	v_mfma_f32_32x32x16_bf16 v[18:33], v[6:9], v[172:175], v[18:33]
	v_bfe_u32 v6, v55, 16, 1
	v_add3_u32 v55, v55, v6, s37
	v_add3_u32 v6, v14, v51, s37
	v_lshrrev_b32_e32 v14, 16, v6
	ds_read_b128 v[6:9], v195 offset:45792
	v_and_or_b32 v176, v16, s33, v14
	s_mov_b32 s23, s13
	s_waitcnt lgkmcnt(2)
	v_mfma_f32_32x32x16_bf16 v[34:49], v[2:5], v[172:175], v[34:49]
	v_lshrrev_b32_e32 v2, 16, v15
	v_lshrrev_b32_e32 v3, 16, v53
	v_lshrrev_b32_e32 v4, 16, v55
	v_and_or_b32 v179, v1, s33, v4
	v_and_or_b32 v178, v50, s33, v3
	v_and_or_b32 v177, v17, s33, v2
	v_lshlrev_b32_e32 v1, 3, v182
	s_mov_b32 s24, s13
	s_waitcnt lgkmcnt(1)
	v_mfma_f32_32x32x16_bf16 v[18:33], v[10:13], v[176:179], v[18:33]
	s_mov_b32 s25, s13
	s_mov_b32 s26, s13
	s_mov_b32 s27, s13
	s_add_i32 s58, s58, 0x14800
	v_add_u32_e32 v200, 0x8000, v195
	s_mov_b32 s65, 2
	v_cmp_gt_u32_e64 s[40:41], 32, v182
	s_waitcnt lgkmcnt(0)
	v_mfma_f32_32x32x16_bf16 v[34:49], v[6:9], v[176:179], v[34:49]
	ds_read_b128 v[2:5], v195 offset:33024
	ds_read_b128 v[6:9], v189
	ds_read_b128 v[10:13], v189 offset:32
	ds_read_b128 v[14:17], v195 offset:33056
	v_lshl_add_u32 v190, v186, 2, s58
	v_mov_b32_e32 v201, 0
	s_waitcnt lgkmcnt(2)
	v_mfma_f32_32x32x16_bf16 v[18:33], v[2:5], v[6:9], v[18:33]
	ds_read_b128 v[2:5], v195 offset:45824
	ds_read_b128 v[50:53], v195 offset:45856
	s_waitcnt lgkmcnt(1)
	v_mfma_f32_32x32x16_bf16 v[34:49], v[2:5], v[6:9], v[34:49]
	v_lshlrev_b32_e32 v2, 4, v182
	v_and_b32_e32 v2, 0xc0, v2
	v_and_or_b32 v6, v1, 24, v2
	v_lshlrev_b32_e32 v2, 1, v182
	v_and_b32_e32 v7, 32, v2
	ds_read_b128 v[2:5], v195 offset:33088
	v_and_b32_e32 v1, 0x100, v1
	v_mfma_f32_32x32x16_bf16 v[18:33], v[14:17], v[10:13], v[18:33]
	v_or3_b32 v1, v6, v7, v1
	ds_read_b128 v[6:9], v189 offset:64
	v_add_u32_e32 v197, 0, v1
	s_waitcnt lgkmcnt(2)
	v_mfma_f32_32x32x16_bf16 v[34:49], v[50:53], v[10:13], v[34:49]
	ds_read_b128 v[10:13], v195 offset:45888
	ds_read_b128 v[14:17], v195 offset:33120
	ds_read_b128 v[50:53], v189 offset:96
	ds_read_b128 v[54:57], v195 offset:45920
	s_waitcnt lgkmcnt(4)
	v_mfma_f32_32x32x16_bf16 v[18:33], v[2:5], v[6:9], v[18:33]
	s_waitcnt lgkmcnt(3)
	v_mfma_f32_32x32x16_bf16 v[34:49], v[10:13], v[6:9], v[34:49]
	s_waitcnt lgkmcnt(1)
	v_mfma_f32_32x32x16_bf16 v[18:33], v[14:17], v[50:53], v[18:33]
	v_mov_b64_e32 v[2:3], s[12:13]
	v_mov_b64_e32 v[16:17], s[26:27]
	v_mov_b64_e32 v[4:5], s[14:15]
	v_mov_b64_e32 v[6:7], s[16:17]
	v_mov_b64_e32 v[8:9], s[18:19]
	v_mov_b64_e32 v[10:11], s[20:21]
	v_mov_b64_e32 v[12:13], s[22:23]
	s_waitcnt lgkmcnt(0)
; #define VLOAD(k0) do { const char* vp_ = (const char*)Vh + (size_t)(k0) * (DVH * 2); vs0 = *reinterpret_cast<const bf16x8*>(vp_ + vgo); vs1 = *reinterpret_cast<const bf16x8*>(vp_ + 32 * DVH * 2 + vgo); } while (0)
; __device__ __forceinline__ void partialSM_first(f32x16& p0, f32x16& p1, f32x16& negm) {
;     float pmax = p0[0];
; #pragma unroll
;     for (int r = 1; r < 16; ++r) pmax = fmaxf(pmax, p0[r]);
; #pragma unroll
;     for (int r = 0; r < 16; ++r) pmax = fmaxf(pmax, p1[r]);
;     { auto rr = __builtin_amdgcn_permlane32_swap(__float_as_uint(pmax), __float_as_uint(pmax), false, false);
;       pmax = fmaxf(__uint_as_float(rr[0]), __uint_as_float(rr[1])); }
; #pragma unroll
;     for (int r = 0; r < 16; ++r) { p0[r] -= pmax; p1[r] -= pmax; negm[r] = -pmax; }
; #pragma unroll
;     for (int r = 0; r < 16; ++r) p0[r] = __builtin_amdgcn_exp2f(p0[r]);
; }
; __device__ __forceinline__ void attn_unit(const bf16* __restrict__ Qraw, const float* __restrict__ ssq, const float* __restrict__ qn, int t0, const bf16* __restrict__ Kh, const bf16* __restrict__ Vh, bf16* __restrict__ Ob, int seq, LAS char* lds, int tid) {
;     ...
;     VLOAD(KVBLK);
	v_mfma_f32_32x32x16_bf16 v[34:49], v[54:57], v[50:53], v[34:49]
	s_nop 2
	v_max_f32_e32 v50, v19, v19
	v_max_f32_e32 v51, v18, v18
	v_max_f32_e32 v50, v51, v50
	v_max3_f32 v50, v50, v20, v21
	v_max3_f32 v50, v50, v22, v23
	v_max3_f32 v50, v50, v24, v25
	v_max3_f32 v50, v50, v26, v27
	v_max3_f32 v50, v50, v28, v29
	v_max3_f32 v50, v50, v30, v31
	v_max3_f32 v50, v50, v32, v33
	v_max3_f32 v50, v50, v34, v35
	v_max3_f32 v50, v50, v36, v37
	v_max3_f32 v50, v50, v38, v39
	v_max3_f32 v50, v50, v40, v41
	v_max3_f32 v50, v50, v42, v43
	v_max3_f32 v50, v50, v44, v45
	v_max3_f32 v50, v50, v46, v47
	v_max3_f32 v54, v50, v48, v49
	v_add_co_u32_e32 v50, vcc, s10, v68
	s_movk_i32 s10, 0x6000
	s_nop 0
	v_addc_co_u32_e32 v51, vcc, 0, v69, vcc
	v_add_co_u32_e32 v52, vcc, s10, v68
	v_mov_b32_e32 v55, v54
	s_nop 0
	v_addc_co_u32_e32 v53, vcc, 0, v69, vcc
	global_load_dwordx4 v[114:117], v[50:51], off
	global_load_dwordx4 v[118:121], v[52:53], off
	v_permlane32_swap_b32_e32 v54, v55
	v_max_f32_e32 v50, v55, v55
	v_max_f32_e32 v51, v54, v54
	v_max_f32_e32 v50, v51, v50
	v_sub_f32_e32 v18, v18, v50
	v_exp_f32_e32 v228, v18
	v_sub_f32_e32 v18, v19, v50
	v_exp_f32_e32 v231, v18
	v_sub_f32_e32 v18, v20, v50
	v_exp_f32_e32 v229, v18
	v_sub_f32_e32 v18, v21, v50
	v_exp_f32_e32 v232, v18
	v_sub_f32_e32 v18, v22, v50
	v_exp_f32_e32 v230, v18
	v_sub_f32_e32 v18, v23, v50
	v_exp_f32_e32 v233, v18
	v_sub_f32_e32 v18, v24, v50
	v_exp_f32_e32 v226, v18
	v_sub_f32_e32 v18, v25, v50
	v_exp_f32_e32 v227, v18
	v_sub_f32_e32 v18, v26, v50
	v_exp_f32_e32 v204, v18
	v_sub_f32_e32 v18, v27, v50
	v_exp_f32_e32 v206, v18
	v_sub_f32_e32 v18, v28, v50
	v_exp_f32_e32 v205, v18
	v_sub_f32_e32 v18, v29, v50
	v_exp_f32_e32 v207, v18
	v_sub_f32_e32 v18, v30, v50
	v_exp_f32_e32 v184, v18
	v_sub_f32_e32 v18, v31, v50
	v_exp_f32_e32 v202, v18
	v_sub_f32_e32 v18, v32, v50
	v_exp_f32_e32 v185, v18
	v_sub_f32_e32 v18, v33, v50
	v_exp_f32_e32 v203, v18
	s_add_i32 s10, 0, 0x4000
	v_mov_b64_e32 v[14:15], s[24:25]
	v_xor_b32_e32 v82, 0x80000000, v50
	v_sub_f32_e32 v113, v49, v50
	v_sub_f32_e32 v112, v48, v50
	v_sub_f32_e32 v111, v47, v50
	v_sub_f32_e32 v110, v46, v50
	v_sub_f32_e32 v109, v45, v50
	v_sub_f32_e32 v108, v44, v50
	v_sub_f32_e32 v107, v43, v50
	v_sub_f32_e32 v106, v42, v50
	v_sub_f32_e32 v105, v41, v50
	v_sub_f32_e32 v104, v40, v50
	v_sub_f32_e32 v103, v39, v50
	v_sub_f32_e32 v102, v38, v50
	v_sub_f32_e32 v101, v37, v50
	v_sub_f32_e32 v100, v36, v50
	v_sub_f32_e32 v99, v35, v50
	v_sub_f32_e32 v98, v34, v50
	v_add_u32_e32 v191, s10, v1
	v_mov_b32_e32 v1, 0x110000
	v_mov_b64_e32 v[64:65], v[16:17]
	v_mov_b64_e32 v[48:49], v[16:17]
	v_mov_b64_e32 v[32:33], v[16:17]
	v_mad_i64_i32 v[182:183], s[10:11], s31, v1, v[146:147]
	v_mov_b64_e32 v[62:63], v[14:15]
	v_mov_b64_e32 v[60:61], v[12:13]
	v_mov_b64_e32 v[58:59], v[10:11]
	v_mov_b64_e32 v[56:57], v[8:9]
	v_mov_b64_e32 v[54:55], v[6:7]
	v_mov_b64_e32 v[52:53], v[4:5]
	v_mov_b64_e32 v[50:51], v[2:3]
	v_mov_b64_e32 v[46:47], v[14:15]
	v_mov_b64_e32 v[44:45], v[12:13]
	v_mov_b64_e32 v[42:43], v[10:11]
	v_mov_b64_e32 v[40:41], v[8:9]
	v_mov_b64_e32 v[38:39], v[6:7]
	v_mov_b64_e32 v[36:37], v[4:5]
	v_mov_b64_e32 v[34:35], v[2:3]
	v_mov_b64_e32 v[30:31], v[14:15]
	v_mov_b64_e32 v[28:29], v[12:13]
	v_mov_b64_e32 v[26:27], v[10:11]
	v_mov_b64_e32 v[24:25], v[8:9]
	v_mov_b64_e32 v[22:23], v[6:7]
	v_mov_b64_e32 v[20:21], v[4:5]
	v_mov_b64_e32 v[18:19], v[2:3]
	v_mov_b32_e32 v83, v82
	v_mov_b32_e32 v84, v82
	v_mov_b32_e32 v85, v82
	v_mov_b32_e32 v86, v82
	v_mov_b32_e32 v87, v82
	v_mov_b32_e32 v88, v82
	v_mov_b32_e32 v89, v82
	v_mov_b32_e32 v90, v82
	v_mov_b32_e32 v91, v82
	v_mov_b32_e32 v92, v82
	v_mov_b32_e32 v93, v82
	v_mov_b32_e32 v94, v82
	v_mov_b32_e32 v95, v82
	v_mov_b32_e32 v96, v82
	v_mov_b32_e32 v97, v82
	s_mov_b32 s12, 0x4138aa3b
	s_mov_b64 s[20:21], 0x2000
	s_barrier

; #define LAS __attribute__((address_space(3)))
; #define WSW(T, off, l) WSP(T, WS_WSET + (size_t)(l) * WSET_STRIDE + (off))
; __device__ __forceinline__ void tr_item(const float* W, int ldw, int k0, int n0, bf16* WT, int ldt, int drow0, LAS float* scr, int lane, const float* kscale = nullptr) {
;     const float* src = W + (size_t)(k0 + (lane >> 4)) * ldw + n0 + (lane & 15) * 4;
;     f32x4 v[16];
; #pragma unroll
;     for (int i = 0; i < 16; ++i) v[i] = __builtin_nontemporal_load((const f32x4*)(src + (size_t)(4 * i) * ldw));
;     LAS float* wp = scr + (lane >> 4) * 65 + (lane & 15) * 4;
; #pragma unroll
;     for (int i = 0; i < 16; ++i) { LAS float* q = wp + (4 * i) * 65; const float ks = kscale ? kscale[k0 + 4 * i + (lane >> 4)] : 1.f; q[0] = v[i].x * ks; q[1] = v[i].y * ks; q[2] = v[i].z * ks; q[3] = v[i].w * ks; }
; __device__ __forceinline__ void convert_tile(const Args& a, GAS unsigned char* wsb, int l, int t, LAS float* scr, int lane) {
;     ...
;     if (r < I_OUT) { const int kb = r / 32, nb = r - kb * 32; tr_item(INP(21) + (size_t)l * DM * DM, DM, kb * 64, nb * 64, WSW(bf16, W_OUT, l), DM, nb * 64, scr, lane); return; }
.LBB0_1515:
	s_andn2_b64 vcc, exec, s[4:5]
	s_cbranch_vccnz .LBB0_1517
	s_lshl_b32 s4, s15, 1
	s_and_b32 s4, s4, 0x1fc0
	s_addk_i32 s4, 0xf240
	s_lshl_b32 s5, s15, 6
	v_or_b32_e32 v2, s4, v67
	v_mov_b32_e32 v3, v147
	v_readlane_b32 s8, v252, 60
	s_and_b32 s6, s5, 0x7c0
	v_lshlrev_b64 v[2:3], 13, v[2:3]
	v_readlane_b32 s9, v252, 61
	s_lshl_b32 s12, s6, 2
	v_lshlrev_b32_e32 v4, 2, v66
	v_lshl_add_u64 v[2:3], s[8:9], 0, v[2:3]
	v_lshl_add_u64 v[2:3], v[2:3], 0, s[12:13]
	v_mov_b32_e32 v5, v147
	v_lshl_add_u64 v[62:63], v[2:3], 0, v[4:5]
	v_add_co_u32_e32 v6, vcc, s83, v62
	s_mov_b32 s5, 0x20000
	s_nop 0
	v_addc_co_u32_e32 v7, vcc, 0, v63, vcc
	v_add_co_u32_e32 v10, vcc, s81, v62
	global_load_dwordx4 v[2:5], v[62:63], off nt
	s_nop 0
	global_load_dwordx4 v[6:9], v[6:7], off nt
	v_addc_co_u32_e32 v11, vcc, 0, v63, vcc
	v_add_co_u32_e32 v14, vcc, s82, v62
	v_add_u32_e32 v1, 0x410, v95
	s_nop 0
	v_addc_co_u32_e32 v15, vcc, 0, v63, vcc
	global_load_dwordx4 v[10:13], v[10:11], off nt
	s_nop 0
	global_load_dwordx4 v[14:17], v[14:15], off nt
	v_add_co_u32_e32 v18, vcc, s5, v62
	s_mov_b32 s5, 0x28000
	s_nop 0
	v_addc_co_u32_e32 v19, vcc, 0, v63, vcc
	v_add_co_u32_e32 v22, vcc, s5, v62
	s_mov_b32 s5, 0x30000
	s_nop 0
	v_addc_co_u32_e32 v23, vcc, 0, v63, vcc
	global_load_dwordx4 v[18:21], v[18:19], off nt
	s_nop 0
	global_load_dwordx4 v[22:25], v[22:23], off nt
	v_add_co_u32_e32 v26, vcc, s5, v62
	s_mov_b32 s5, 0x38000
	s_nop 0
	v_addc_co_u32_e32 v27, vcc, 0, v63, vcc
	v_add_co_u32_e32 v30, vcc, s5, v62
	s_mov_b32 s5, 0x40000
	s_nop 0
	v_addc_co_u32_e32 v31, vcc, 0, v63, vcc
	global_load_dwordx4 v[26:29], v[26:27], off nt
	s_nop 0
	global_load_dwordx4 v[30:33], v[30:31], off nt
	v_add_co_u32_e32 v34, vcc, s5, v62
	s_mov_b32 s5, 0x48000
	s_nop 0
	v_addc_co_u32_e32 v35, vcc, 0, v63, vcc
	v_add_co_u32_e32 v38, vcc, s5, v62
	s_mov_b32 s5, 0x50000
	s_nop 0
	v_addc_co_u32_e32 v39, vcc, 0, v63, vcc
	global_load_dwordx4 v[34:37], v[34:35], off nt
	s_nop 0
	global_load_dwordx4 v[38:41], v[38:39], off nt
	v_add_co_u32_e32 v42, vcc, s5, v62
	s_mov_b32 s5, 0x58000
	s_nop 0
	v_addc_co_u32_e32 v43, vcc, 0, v63, vcc
	v_add_co_u32_e32 v46, vcc, s5, v62
	s_mov_b32 s5, 0x60000
	s_nop 0
	v_addc_co_u32_e32 v47, vcc, 0, v63, vcc
	global_load_dwordx4 v[42:45], v[42:43], off nt
	s_nop 0
	global_load_dwordx4 v[46:49], v[46:47], off nt
	v_add_co_u32_e32 v50, vcc, s5, v62
	s_mov_b32 s5, 0x68000
	s_nop 0
	v_addc_co_u32_e32 v51, vcc, 0, v63, vcc
	v_add_co_u32_e32 v54, vcc, s5, v62
	s_mov_b32 s5, 0x70000
	s_nop 0
	v_addc_co_u32_e32 v55, vcc, 0, v63, vcc
	global_load_dwordx4 v[50:53], v[50:51], off nt
	s_nop 0
	global_load_dwordx4 v[54:57], v[54:55], off nt
	v_add_co_u32_e32 v58, vcc, s5, v62
	s_mov_b32 s5, 0x78000
	s_nop 0
	v_addc_co_u32_e32 v59, vcc, 0, v63, vcc
	global_load_dwordx4 v[58:61], v[58:59], off nt
	v_add_co_u32_e32 v62, vcc, s5, v62
	s_mov_b32 s5, s13
	s_nop 0
	v_addc_co_u32_e32 v63, vcc, 0, v63, vcc
	global_load_dwordx4 v[62:65], v[62:63], off nt
	s_waitcnt vmcnt(15)
	ds_write2_b32 v95, v2, v3 offset1:1
	ds_write2_b32 v95, v4, v5 offset0:2 offset1:3
	s_waitcnt vmcnt(14)
	ds_write2_b32 v1, v6, v7 offset1:1
	v_add_u32_e32 v1, 0x418, v95
	ds_write2_b32 v1, v8, v9 offset1:1
	v_add_u32_e32 v1, 0x820, v95
	v_lshl_add_u64 v[2:3], s[4:5], 1, v[72:73]
	s_waitcnt vmcnt(13)
	ds_write2_b32 v1, v10, v11 offset1:1
	v_add_u32_e32 v1, 0x828, v95
	ds_write2_b32 v1, v12, v13 offset1:1
	v_add_u32_e32 v1, 0xc30, v95
	s_waitcnt vmcnt(12)
	ds_write2_b32 v1, v14, v15 offset1:1
	v_add_u32_e32 v1, 0xc38, v95
	ds_write2_b32 v1, v16, v17 offset1:1
	v_add_u32_e32 v1, 0x1040, v95
	s_waitcnt vmcnt(11)
	ds_write2_b32 v1, v18, v19 offset1:1
	v_add_u32_e32 v1, 0x1048, v95
	ds_write2_b32 v1, v20, v21 offset1:1
	v_add_u32_e32 v1, 0x1450, v95
	s_waitcnt vmcnt(10)
	ds_write2_b32 v1, v22, v23 offset1:1
	v_add_u32_e32 v1, 0x1458, v95
	ds_write2_b32 v1, v24, v25 offset1:1
	v_add_u32_e32 v1, 0x1860, v95
	v_mov_b32_e32 v25, v147
	s_waitcnt vmcnt(9)
	ds_write2_b32 v1, v26, v27 offset1:1
	v_add_u32_e32 v1, 0x1868, v95
	ds_write2_b32 v1, v28, v29 offset1:1
	v_add_u32_e32 v1, 0x1c70, v95
	s_waitcnt vmcnt(8)
	ds_write2_b32 v1, v30, v31 offset1:1
	v_add_u32_e32 v1, 0x1c78, v95
	ds_write2_b32 v1, v32, v33 offset1:1
	v_add_u32_e32 v1, 0x2080, v95
	v_add_u32_e32 v26, 0x400, v97
	s_waitcnt vmcnt(7)
	ds_write2_b32 v1, v34, v35 offset1:1
	v_add_u32_e32 v1, 0x2088, v95
	ds_write2_b32 v1, v36, v37 offset1:1
	v_add_u32_e32 v1, 0x2490, v95
	s_waitcnt vmcnt(6)
	ds_write2_b32 v1, v38, v39 offset1:1
	v_add_u32_e32 v1, 0x2498, v95
	ds_write2_b32 v1, v40, v41 offset1:1
	v_add_u32_e32 v1, 0x28a0, v95
	s_waitcnt vmcnt(5)
	ds_write2_b32 v1, v42, v43 offset1:1
	v_add_u32_e32 v1, 0x28a8, v95
	ds_write2_b32 v1, v44, v45 offset1:1
	v_add_u32_e32 v1, 0x2cb0, v95
	s_waitcnt vmcnt(4)
	ds_write2_b32 v1, v46, v47 offset1:1
	v_add_u32_e32 v1, 0x2cb8, v95
	ds_write2_b32 v1, v48, v49 offset1:1
	v_add_u32_e32 v1, 0x30c0, v95
	s_waitcnt vmcnt(3)
	ds_write2_b32 v1, v50, v51 offset1:1
	v_add_u32_e32 v1, 0x30c8, v95
	ds_write2_b32 v1, v52, v53 offset1:1
	v_add_u32_e32 v1, 0x34d0, v95
	s_waitcnt vmcnt(2)
; #define LAS __attribute__((address_space(3)))
; __device__ __forceinline__ unsigned pk2(float lo, float hi) { return f2bf(lo) | (f2bf(hi) << 16); }
; __device__ __forceinline__ void tr_item(const float* W, int ldw, int k0, int n0, bf16* WT, int ldt, int drow0, LAS float* scr, int lane, const float* kscale = nullptr) {
;     ...
;     const int kc = lane & 7;
; #pragma unroll
;     for (int j = 0; j < 8; ++j) { const int n = (lane >> 3) + 8 * j; const LAS float* sp = scr + (8 * kc) * 65 + n;
;         u32x4 o; o.x = pk2(sp[0 * 65], sp[1 * 65]); o.y = pk2(sp[2 * 65], sp[3 * 65]); o.z = pk2(sp[4 * 65], sp[5 * 65]); o.w = pk2(sp[6 * 65], sp[7 * 65]);
;         __builtin_nontemporal_store(o, (u32x4*)(WT + (size_t)(drow0 + n) * ldt + k0 + 8 * kc)); }
;     asm volatile("s_waitcnt lgkmcnt(0)" ::: "memory");
; }
	ds_write2_b32 v1, v54, v55 offset1:1
	v_add_u32_e32 v1, 0x34d8, v95
	ds_write2_b32 v1, v56, v57 offset1:1
	v_add_u32_e32 v1, 0x38e0, v95
	s_waitcnt vmcnt(1)
	ds_write2_b32 v1, v58, v59 offset1:1
	v_add_u32_e32 v1, 0x38e8, v95
	ds_write2_b32 v1, v60, v61 offset1:1
	v_add_u32_e32 v1, 0x3cf0, v95
	s_waitcnt vmcnt(0)
	ds_write2_b32 v1, v62, v63 offset1:1
	v_add_u32_e32 v1, 0x3cf8, v95
	ds_write2_b32 v1, v64, v65 offset1:1
	s_waitcnt lgkmcnt(0)
	ds_read2_b32 v[8:9], v97 offset1:8
	ds_read2_b32 v[10:11], v97 offset0:65 offset1:73
	ds_read2_b32 v[12:13], v97 offset0:130 offset1:138
	ds_read2_b32 v[14:15], v97 offset0:195 offset1:203
	ds_read2_b32 v[16:17], v26 offset0:4 offset1:12
	s_waitcnt lgkmcnt(4)
	s_waitcnt lgkmcnt(3)
	ds_read2_b32 v[18:19], v26 offset0:69 offset1:77
	v_cvt_pk_bf16_f32 v4, v8, v10
	s_waitcnt lgkmcnt(3)
	s_waitcnt lgkmcnt(2)
	ds_read2_b32 v[20:21], v26 offset0:134 offset1:142
	ds_read2_b32 v[22:23], v26 offset0:199 offset1:207
	v_cvt_pk_bf16_f32 v5, v12, v14
	s_waitcnt lgkmcnt(3)
	s_waitcnt lgkmcnt(2)
	v_cvt_pk_bf16_f32 v6, v16, v18
	s_waitcnt lgkmcnt(1)
	s_waitcnt lgkmcnt(0)
	v_cvt_pk_bf16_f32 v7, v20, v22
	v_or_b32_e32 v1, s6, v96
	v_lshlrev_b32_e32 v24, 12, v1
	v_lshl_add_u64 v[24:25], v[2:3], 0, v[24:25]
	global_store_dwordx4 v[24:25], v[4:7], off nt
	s_nop 1
	v_cvt_pk_bf16_f32 v4, v9, v11
	v_cvt_pk_bf16_f32 v5, v13, v15
	v_cvt_pk_bf16_f32 v6, v17, v19
	v_cvt_pk_bf16_f32 v7, v21, v23
	v_or_b32_e32 v1, s6, v98
	v_lshlrev_b32_e32 v8, 12, v1
	v_mov_b32_e32 v9, v147
	ds_read2_b32 v[10:11], v97 offset0:16 offset1:24
	v_lshl_add_u64 v[8:9], v[2:3], 0, v[8:9]
	global_store_dwordx4 v[8:9], v[4:7], off nt
	ds_read2_b32 v[8:9], v97 offset0:81 offset1:89
	ds_read2_b32 v[12:13], v97 offset0:146 offset1:154
	ds_read2_b32 v[14:15], v97 offset0:211 offset1:219
	s_waitcnt lgkmcnt(3)
	s_waitcnt lgkmcnt(2)
	ds_read2_b32 v[16:17], v26 offset0:20 offset1:28
	ds_read2_b32 v[18:19], v26 offset0:85 offset1:93
	v_cvt_pk_bf16_f32 v4, v10, v8
	s_waitcnt lgkmcnt(3)
	s_waitcnt lgkmcnt(2)
	ds_read2_b32 v[20:21], v26 offset0:150 offset1:158
	ds_read2_b32 v[22:23], v26 offset0:215 offset1:223
	v_cvt_pk_bf16_f32 v5, v12, v14
	s_waitcnt lgkmcnt(3)
	s_waitcnt lgkmcnt(2)
	v_cvt_pk_bf16_f32 v6, v16, v18
	s_waitcnt lgkmcnt(1)
	s_waitcnt lgkmcnt(0)
	v_cvt_pk_bf16_f32 v7, v20, v22
	v_or_b32_e32 v1, s6, v99
	v_lshlrev_b32_e32 v24, 12, v1
	v_mov_b32_e32 v25, v147
	v_lshl_add_u64 v[24:25], v[2:3], 0, v[24:25]
	global_store_dwordx4 v[24:25], v[4:7], off nt
	s_nop 1
	v_cvt_pk_bf16_f32 v4, v11, v9
	v_cvt_pk_bf16_f32 v5, v13, v15
	v_cvt_pk_bf16_f32 v6, v17, v19
	v_cvt_pk_bf16_f32 v7, v21, v23
	v_or_b32_e32 v1, s6, v100
	v_lshlrev_b32_e32 v8, 12, v1
	v_mov_b32_e32 v9, v147
	ds_read2_b32 v[10:11], v97 offset0:32 offset1:40
	v_lshl_add_u64 v[8:9], v[2:3], 0, v[8:9]
	global_store_dwordx4 v[8:9], v[4:7], off nt
	ds_read2_b32 v[8:9], v97 offset0:97 offset1:105
	ds_read2_b32 v[12:13], v97 offset0:162 offset1:170
	ds_read2_b32 v[14:15], v97 offset0:227 offset1:235
	s_waitcnt lgkmcnt(3)
	s_waitcnt lgkmcnt(2)
	ds_read2_b32 v[16:17], v26 offset0:36 offset1:44
	ds_read2_b32 v[18:19], v26 offset0:101 offset1:109
	v_cvt_pk_bf16_f32 v4, v10, v8
	s_waitcnt lgkmcnt(3)
	s_waitcnt lgkmcnt(2)
	ds_read2_b32 v[20:21], v26 offset0:166 offset1:174
	ds_read2_b32 v[22:23], v26 offset0:231 offset1:239
	v_cvt_pk_bf16_f32 v5, v12, v14
	s_waitcnt lgkmcnt(3)
	s_waitcnt lgkmcnt(2)
	v_cvt_pk_bf16_f32 v6, v16, v18
	s_waitcnt lgkmcnt(1)
	s_waitcnt lgkmcnt(0)
	v_cvt_pk_bf16_f32 v7, v20, v22
	v_or_b32_e32 v1, s6, v101
	v_lshlrev_b32_e32 v24, 12, v1
	v_mov_b32_e32 v25, v147
	v_lshl_add_u64 v[24:25], v[2:3], 0, v[24:25]
	global_store_dwordx4 v[24:25], v[4:7], off nt
	s_nop 1
	v_cvt_pk_bf16_f32 v4, v11, v9
	v_cvt_pk_bf16_f32 v5, v13, v15
	v_cvt_pk_bf16_f32 v6, v17, v19
	v_cvt_pk_bf16_f32 v7, v21, v23
	v_or_b32_e32 v1, s6, v102
	v_lshlrev_b32_e32 v8, 12, v1
	v_mov_b32_e32 v9, v147
	ds_read2_b32 v[10:11], v97 offset0:48 offset1:56
	v_lshl_add_u64 v[8:9], v[2:3], 0, v[8:9]
	global_store_dwordx4 v[8:9], v[4:7], off nt
	ds_read2_b32 v[8:9], v97 offset0:113 offset1:121
	ds_read2_b32 v[12:13], v97 offset0:178 offset1:186
	ds_read2_b32 v[14:15], v97 offset0:243 offset1:251
	s_waitcnt lgkmcnt(3)
	s_waitcnt lgkmcnt(2)
	ds_read2_b32 v[16:17], v26 offset0:52 offset1:60
	ds_read2_b32 v[18:19], v26 offset0:117 offset1:125
	v_cvt_pk_bf16_f32 v4, v10, v8
	s_waitcnt lgkmcnt(3)
	s_waitcnt lgkmcnt(2)
	ds_read2_b32 v[20:21], v26 offset0:182 offset1:190
	ds_read2_b32 v[22:23], v26 offset0:247 offset1:255
	v_cvt_pk_bf16_f32 v5, v12, v14
	s_waitcnt lgkmcnt(3)
	s_waitcnt lgkmcnt(2)
	v_cvt_pk_bf16_f32 v6, v16, v18
	s_waitcnt lgkmcnt(1)
	s_waitcnt lgkmcnt(0)
	v_cvt_pk_bf16_f32 v7, v20, v22
	v_or_b32_e32 v1, s6, v103
	v_lshlrev_b32_e32 v24, 12, v1
	v_mov_b32_e32 v25, v147
	v_lshl_add_u64 v[24:25], v[2:3], 0, v[24:25]
	global_store_dwordx4 v[24:25], v[4:7], off nt
	s_nop 1
	v_cvt_pk_bf16_f32 v4, v11, v9
	v_cvt_pk_bf16_f32 v5, v13, v15
	v_cvt_pk_bf16_f32 v6, v17, v19
	v_cvt_pk_bf16_f32 v7, v21, v23
	v_or_b32_e32 v1, s6, v104
	v_lshlrev_b32_e32 v8, 12, v1
	v_mov_b32_e32 v9, v147
	v_lshl_add_u64 v[2:3], v[2:3], 0, v[8:9]
	global_store_dwordx4 v[2:3], v[4:7], off nt
	s_waitcnt lgkmcnt(0)

; #define LAS __attribute__((address_space(3)))
; __device__ __forceinline__ unsigned pk2(float lo, float hi) { return f2bf(lo) | (f2bf(hi) << 16); }
; #define WSW(T, off, l) WSP(T, WS_WSET + (size_t)(l) * WSET_STRIDE + (off))
; __device__ __forceinline__ void tr_item(const float* W, int ldw, int k0, int n0, bf16* WT, int ldt, int drow0, LAS float* scr, int lane, const float* kscale = nullptr) {
;     ...
;     for (int i = 0; i < 16; ++i) { LAS float* q = wp + (4 * i) * 65; const float ks = kscale ? kscale[k0 + 4 * i + (lane >> 4)] : 1.f; q[0] = v[i].x * ks; q[1] = v[i].y * ks; q[2] = v[i].z * ks; q[3] = v[i].w * ks; }
;     asm volatile("s_waitcnt lgkmcnt(0)" ::: "memory");
;     const int kc = lane & 7;
; #pragma unroll
;     for (int j = 0; j < 8; ++j) { const int n = (lane >> 3) + 8 * j; const LAS float* sp = scr + (8 * kc) * 65 + n;
;         u32x4 o; o.x = pk2(sp[0 * 65], sp[1 * 65]); o.y = pk2(sp[2 * 65], sp[3 * 65]); o.z = pk2(sp[4 * 65], sp[5 * 65]); o.w = pk2(sp[6 * 65], sp[7 * 65]);
;         __builtin_nontemporal_store(o, (u32x4*)(WT + (size_t)(drow0 + n) * ldt + k0 + 8 * kc)); }
;     asm volatile("s_waitcnt lgkmcnt(0)" ::: "memory");
; }
; __device__ __forceinline__ void convert_tile(const Args& a, GAS unsigned char* wsb, int l, int t, LAS float* scr, int lane) {
;     ...
;     if (r < I_UKV) { const int kb = r / 32, nb = r - kb * 32; tr_item(INP(18) + (size_t)l * KVRANK * 2048, 2048, kb * 64, nb * 64, WSW(bf16, W_UKV, l), KVRANK, nb * 64, scr, lane, INP(17) + (size_t)l * KVRANK); return; }
.LBB0_1543:
	s_waitcnt vmcnt(0)
	v_pk_mul_f32 v[2:3], v[2:3], v[10:11] op_sel_hi:[1,0]
	v_add_u32_e32 v1, 0x3cf0, v95
	ds_write2_b32 v1, v2, v3 offset1:1
	v_pk_mul_f32 v[2:3], v[4:5], v[10:11] op_sel_hi:[1,0]
	v_add_u32_e32 v1, 0x3cf8, v95
	ds_write2_b32 v1, v2, v3 offset1:1
	s_waitcnt lgkmcnt(0)
	ds_read2_b32 v[8:9], v97 offset1:8
	ds_read2_b32 v[10:11], v97 offset0:65 offset1:73
	ds_read2_b32 v[12:13], v97 offset0:130 offset1:138
	ds_read2_b32 v[14:15], v97 offset0:195 offset1:203
	v_add_u32_e32 v26, 0x400, v97
	s_waitcnt lgkmcnt(3)
	s_waitcnt lgkmcnt(2)
	ds_read2_b32 v[16:17], v26 offset0:4 offset1:12
	ds_read2_b32 v[18:19], v26 offset0:69 offset1:77
	v_cvt_pk_bf16_f32 v4, v8, v10
	s_waitcnt lgkmcnt(3)
	s_waitcnt lgkmcnt(2)
	ds_read2_b32 v[20:21], v26 offset0:134 offset1:142
	ds_read2_b32 v[22:23], v26 offset0:199 offset1:207
	v_cvt_pk_bf16_f32 v5, v12, v14
	s_waitcnt lgkmcnt(3)
	s_waitcnt lgkmcnt(2)
	v_cvt_pk_bf16_f32 v6, v16, v18
	s_waitcnt lgkmcnt(1)
	s_waitcnt lgkmcnt(0)
	s_mov_b32 s5, s13
	v_cvt_pk_bf16_f32 v7, v20, v22
	v_or_b32_e32 v1, s8, v96
	v_lshl_add_u64 v[2:3], s[4:5], 1, v[74:75]
	v_lshlrev_b32_e32 v146, 9, v1
	v_lshl_add_u64 v[24:25], v[2:3], 0, v[146:147]
	global_store_dwordx4 v[24:25], v[4:7], off nt
	s_nop 1
	v_cvt_pk_bf16_f32 v4, v9, v11
	v_cvt_pk_bf16_f32 v5, v13, v15
	v_cvt_pk_bf16_f32 v6, v17, v19
	v_cvt_pk_bf16_f32 v7, v21, v23
	v_or_b32_e32 v1, s8, v98
	v_lshlrev_b32_e32 v146, 9, v1
	ds_read2_b32 v[8:9], v97 offset0:16 offset1:24
	v_lshl_add_u64 v[10:11], v[2:3], 0, v[146:147]
	global_store_dwordx4 v[10:11], v[4:7], off nt
	ds_read2_b32 v[10:11], v97 offset0:81 offset1:89
	ds_read2_b32 v[12:13], v97 offset0:146 offset1:154
	ds_read2_b32 v[14:15], v97 offset0:211 offset1:219
	s_waitcnt lgkmcnt(3)
	s_waitcnt lgkmcnt(2)
	ds_read2_b32 v[16:17], v26 offset0:20 offset1:28
	ds_read2_b32 v[18:19], v26 offset0:85 offset1:93
	v_cvt_pk_bf16_f32 v4, v8, v10
	s_waitcnt lgkmcnt(3)
	s_waitcnt lgkmcnt(2)
	ds_read2_b32 v[20:21], v26 offset0:150 offset1:158
	ds_read2_b32 v[22:23], v26 offset0:215 offset1:223
	v_cvt_pk_bf16_f32 v5, v12, v14
	s_waitcnt lgkmcnt(3)
	s_waitcnt lgkmcnt(2)
	v_cvt_pk_bf16_f32 v6, v16, v18
	s_waitcnt lgkmcnt(1)
	s_waitcnt lgkmcnt(0)
	v_cvt_pk_bf16_f32 v7, v20, v22
	v_or_b32_e32 v1, s8, v99
	v_lshlrev_b32_e32 v146, 9, v1
	v_lshl_add_u64 v[24:25], v[2:3], 0, v[146:147]
	global_store_dwordx4 v[24:25], v[4:7], off nt
	s_nop 1
	v_cvt_pk_bf16_f32 v4, v9, v11
	v_cvt_pk_bf16_f32 v5, v13, v15
	v_cvt_pk_bf16_f32 v6, v17, v19
	v_cvt_pk_bf16_f32 v7, v21, v23
	v_or_b32_e32 v1, s8, v100
	v_lshlrev_b32_e32 v146, 9, v1
	ds_read2_b32 v[8:9], v97 offset0:32 offset1:40
	v_lshl_add_u64 v[10:11], v[2:3], 0, v[146:147]
	global_store_dwordx4 v[10:11], v[4:7], off nt
	ds_read2_b32 v[10:11], v97 offset0:97 offset1:105
	ds_read2_b32 v[12:13], v97 offset0:162 offset1:170
	ds_read2_b32 v[14:15], v97 offset0:227 offset1:235
	s_waitcnt lgkmcnt(3)
	s_waitcnt lgkmcnt(2)
	ds_read2_b32 v[16:17], v26 offset0:36 offset1:44
	ds_read2_b32 v[18:19], v26 offset0:101 offset1:109
	v_cvt_pk_bf16_f32 v4, v8, v10
	s_waitcnt lgkmcnt(3)
	s_waitcnt lgkmcnt(2)
	ds_read2_b32 v[20:21], v26 offset0:166 offset1:174
	ds_read2_b32 v[22:23], v26 offset0:231 offset1:239
	v_cvt_pk_bf16_f32 v5, v12, v14
	s_waitcnt lgkmcnt(3)
	s_waitcnt lgkmcnt(2)
	v_cvt_pk_bf16_f32 v6, v16, v18
	s_waitcnt lgkmcnt(1)
	s_waitcnt lgkmcnt(0)
	v_cvt_pk_bf16_f32 v7, v20, v22
	v_or_b32_e32 v1, s8, v101
	v_lshlrev_b32_e32 v146, 9, v1
	v_lshl_add_u64 v[24:25], v[2:3], 0, v[146:147]
	global_store_dwordx4 v[24:25], v[4:7], off nt
	s_nop 1
	v_cvt_pk_bf16_f32 v4, v9, v11
	v_cvt_pk_bf16_f32 v5, v13, v15
	v_cvt_pk_bf16_f32 v6, v17, v19
	v_cvt_pk_bf16_f32 v7, v21, v23
	v_or_b32_e32 v1, s8, v102
	v_lshlrev_b32_e32 v146, 9, v1
	ds_read2_b32 v[8:9], v97 offset0:48 offset1:56
	v_lshl_add_u64 v[10:11], v[2:3], 0, v[146:147]
	global_store_dwordx4 v[10:11], v[4:7], off nt
	ds_read2_b32 v[10:11], v97 offset0:113 offset1:121
	ds_read2_b32 v[12:13], v97 offset0:178 offset1:186
	ds_read2_b32 v[14:15], v97 offset0:243 offset1:251
	s_waitcnt lgkmcnt(3)
	s_waitcnt lgkmcnt(2)
	ds_read2_b32 v[16:17], v26 offset0:52 offset1:60
	ds_read2_b32 v[18:19], v26 offset0:117 offset1:125
	v_cvt_pk_bf16_f32 v4, v8, v10
	s_waitcnt lgkmcnt(3)
	s_waitcnt lgkmcnt(2)
	ds_read2_b32 v[20:21], v26 offset0:182 offset1:190
	ds_read2_b32 v[22:23], v26 offset0:247 offset1:255
	v_cvt_pk_bf16_f32 v5, v12, v14
	s_waitcnt lgkmcnt(3)
	s_waitcnt lgkmcnt(2)
	v_cvt_pk_bf16_f32 v6, v16, v18
	s_waitcnt lgkmcnt(1)
	s_waitcnt lgkmcnt(0)
	v_cvt_pk_bf16_f32 v7, v20, v22
	v_or_b32_e32 v1, s8, v103
	v_lshlrev_b32_e32 v146, 9, v1
	v_lshl_add_u64 v[24:25], v[2:3], 0, v[146:147]
	global_store_dwordx4 v[24:25], v[4:7], off nt
	s_nop 1
	v_cvt_pk_bf16_f32 v4, v9, v11
	v_cvt_pk_bf16_f32 v5, v13, v15
	v_cvt_pk_bf16_f32 v6, v17, v19
	v_cvt_pk_bf16_f32 v7, v21, v23
	v_or_b32_e32 v1, s8, v104
	v_lshlrev_b32_e32 v146, 9, v1
	v_lshl_add_u64 v[2:3], v[2:3], 0, v[146:147]
	global_store_dwordx4 v[2:3], v[4:7], off nt
	s_waitcnt lgkmcnt(0)

; #define LAS __attribute__((address_space(3)))
; __device__ __forceinline__ unsigned pk2(float lo, float hi) { return f2bf(lo) | (f2bf(hi) << 16); }
; #define WSW(T, off, l) WSP(T, WS_WSET + (size_t)(l) * WSET_STRIDE + (off))
; __device__ __forceinline__ void tr_item(const float* W, int ldw, int k0, int n0, bf16* WT, int ldt, int drow0, LAS float* scr, int lane, const float* kscale = nullptr) {
;     ...
;     for (int i = 0; i < 16; ++i) { LAS float* q = wp + (4 * i) * 65; const float ks = kscale ? kscale[k0 + 4 * i + (lane >> 4)] : 1.f; q[0] = v[i].x * ks; q[1] = v[i].y * ks; q[2] = v[i].z * ks; q[3] = v[i].w * ks; }
;     asm volatile("s_waitcnt lgkmcnt(0)" ::: "memory");
;     const int kc = lane & 7;
; #pragma unroll
;     for (int j = 0; j < 8; ++j) { const int n = (lane >> 3) + 8 * j; const LAS float* sp = scr + (8 * kc) * 65 + n;
;         u32x4 o; o.x = pk2(sp[0 * 65], sp[1 * 65]); o.y = pk2(sp[2 * 65], sp[3 * 65]); o.z = pk2(sp[4 * 65], sp[5 * 65]); o.w = pk2(sp[6 * 65], sp[7 * 65]);
;         __builtin_nontemporal_store(o, (u32x4*)(WT + (size_t)(drow0 + n) * ldt + k0 + 8 * kc)); }
;     asm volatile("s_waitcnt lgkmcnt(0)" ::: "memory");
; }
; __device__ __forceinline__ void convert_tile(const Args& a, GAS unsigned char* wsb, int l, int t, LAS float* scr, int lane) {
;     ...
;     if (r < I_UQ) { const int kb = r / 24, nb = r - kb * 24; tr_item(INP(16) + (size_t)l * QRANK * 1536, 1536, kb * 64, nb * 64, WSW(bf16, W_UQ, l), QRANK, nb * 64, scr, lane, INP(15) + (size_t)l * QRANK); return; }
.LBB0_1570:
	s_waitcnt vmcnt(0)
	v_pk_mul_f32 v[2:3], v[2:3], v[10:11] op_sel_hi:[1,0]
	v_add_u32_e32 v1, 0x3cf0, v95
	ds_write2_b32 v1, v2, v3 offset1:1
	v_pk_mul_f32 v[2:3], v[4:5], v[10:11] op_sel_hi:[1,0]
	v_add_u32_e32 v1, 0x3cf8, v95
	ds_write2_b32 v1, v2, v3 offset1:1
	s_waitcnt lgkmcnt(0)
	ds_read2_b32 v[8:9], v97 offset1:8
	ds_read2_b32 v[10:11], v97 offset0:65 offset1:73
	ds_read2_b32 v[12:13], v97 offset0:130 offset1:138
	ds_read2_b32 v[14:15], v97 offset0:195 offset1:203
	v_add_u32_e32 v26, 0x400, v97
	s_waitcnt lgkmcnt(3)
	s_waitcnt lgkmcnt(2)
	ds_read2_b32 v[16:17], v26 offset0:4 offset1:12
	ds_read2_b32 v[18:19], v26 offset0:69 offset1:77
	v_cvt_pk_bf16_f32 v4, v8, v10
	s_waitcnt lgkmcnt(3)
	s_waitcnt lgkmcnt(2)
	ds_read2_b32 v[20:21], v26 offset0:134 offset1:142
	ds_read2_b32 v[22:23], v26 offset0:199 offset1:207
	v_cvt_pk_bf16_f32 v5, v12, v14
	s_waitcnt lgkmcnt(3)
	s_waitcnt lgkmcnt(2)
	v_cvt_pk_bf16_f32 v6, v16, v18
	s_waitcnt lgkmcnt(1)
	v_or_b32_e32 v24, s4, v96
	s_lshl_b32 s12, s8, 1
	s_waitcnt lgkmcnt(0)
	v_ashrrev_i32_e32 v25, 31, v24
	v_lshl_add_u64 v[2:3], v[76:77], 0, s[12:13]
	v_lshlrev_b64 v[24:25], 10, v[24:25]
	v_cvt_pk_bf16_f32 v7, v20, v22
	v_lshl_add_u64 v[24:25], v[2:3], 0, v[24:25]
	global_store_dwordx4 v[24:25], v[4:7], off nt
	s_nop 1
	v_cvt_pk_bf16_f32 v4, v9, v11
	v_cvt_pk_bf16_f32 v5, v13, v15
	v_cvt_pk_bf16_f32 v6, v17, v19
	v_or_b32_e32 v8, s4, v98
	v_ashrrev_i32_e32 v9, 31, v8
	v_lshlrev_b64 v[8:9], 10, v[8:9]
	v_cvt_pk_bf16_f32 v7, v21, v23
	ds_read2_b32 v[10:11], v97 offset0:16 offset1:24
	v_lshl_add_u64 v[8:9], v[2:3], 0, v[8:9]
	global_store_dwordx4 v[8:9], v[4:7], off nt
	ds_read2_b32 v[8:9], v97 offset0:81 offset1:89
	ds_read2_b32 v[12:13], v97 offset0:146 offset1:154
	ds_read2_b32 v[14:15], v97 offset0:211 offset1:219
	s_waitcnt lgkmcnt(3)
	s_waitcnt lgkmcnt(2)
	ds_read2_b32 v[16:17], v26 offset0:20 offset1:28
	ds_read2_b32 v[18:19], v26 offset0:85 offset1:93
	v_cvt_pk_bf16_f32 v4, v10, v8
	s_waitcnt lgkmcnt(3)
	s_waitcnt lgkmcnt(2)
	ds_read2_b32 v[20:21], v26 offset0:150 offset1:158
	ds_read2_b32 v[22:23], v26 offset0:215 offset1:223
	v_cvt_pk_bf16_f32 v5, v12, v14
	s_waitcnt lgkmcnt(3)
	s_waitcnt lgkmcnt(2)
	v_cvt_pk_bf16_f32 v6, v16, v18
	s_waitcnt lgkmcnt(1)
	v_or_b32_e32 v24, s4, v99
	s_waitcnt lgkmcnt(0)
	v_ashrrev_i32_e32 v25, 31, v24
	v_lshlrev_b64 v[24:25], 10, v[24:25]
	v_cvt_pk_bf16_f32 v7, v20, v22
	v_lshl_add_u64 v[24:25], v[2:3], 0, v[24:25]
	global_store_dwordx4 v[24:25], v[4:7], off nt
	s_nop 1
	v_cvt_pk_bf16_f32 v4, v11, v9
	v_cvt_pk_bf16_f32 v5, v13, v15
	v_cvt_pk_bf16_f32 v6, v17, v19
	v_or_b32_e32 v8, s4, v100
	v_ashrrev_i32_e32 v9, 31, v8
	v_lshlrev_b64 v[8:9], 10, v[8:9]
	v_cvt_pk_bf16_f32 v7, v21, v23
	ds_read2_b32 v[10:11], v97 offset0:32 offset1:40
	v_lshl_add_u64 v[8:9], v[2:3], 0, v[8:9]
	global_store_dwordx4 v[8:9], v[4:7], off nt
	ds_read2_b32 v[8:9], v97 offset0:97 offset1:105
	ds_read2_b32 v[12:13], v97 offset0:162 offset1:170
	ds_read2_b32 v[14:15], v97 offset0:227 offset1:235
	s_waitcnt lgkmcnt(3)
	s_waitcnt lgkmcnt(2)
	ds_read2_b32 v[16:17], v26 offset0:36 offset1:44
	ds_read2_b32 v[18:19], v26 offset0:101 offset1:109
	v_cvt_pk_bf16_f32 v4, v10, v8
	s_waitcnt lgkmcnt(3)
	s_waitcnt lgkmcnt(2)
	ds_read2_b32 v[20:21], v26 offset0:166 offset1:174
	ds_read2_b32 v[22:23], v26 offset0:231 offset1:239
	v_cvt_pk_bf16_f32 v5, v12, v14
	s_waitcnt lgkmcnt(3)
	s_waitcnt lgkmcnt(2)
	v_cvt_pk_bf16_f32 v6, v16, v18
	s_waitcnt lgkmcnt(1)
	v_or_b32_e32 v24, s4, v101
	s_waitcnt lgkmcnt(0)
	v_ashrrev_i32_e32 v25, 31, v24
	v_lshlrev_b64 v[24:25], 10, v[24:25]
	v_cvt_pk_bf16_f32 v7, v20, v22
	v_lshl_add_u64 v[24:25], v[2:3], 0, v[24:25]
	global_store_dwordx4 v[24:25], v[4:7], off nt
	s_nop 1
	v_cvt_pk_bf16_f32 v4, v11, v9
	v_cvt_pk_bf16_f32 v5, v13, v15
	v_cvt_pk_bf16_f32 v6, v17, v19
	v_or_b32_e32 v8, s4, v102
	v_ashrrev_i32_e32 v9, 31, v8
	v_lshlrev_b64 v[8:9], 10, v[8:9]
	v_cvt_pk_bf16_f32 v7, v21, v23
	ds_read2_b32 v[10:11], v97 offset0:48 offset1:56
	v_lshl_add_u64 v[8:9], v[2:3], 0, v[8:9]
	global_store_dwordx4 v[8:9], v[4:7], off nt
	ds_read2_b32 v[8:9], v97 offset0:113 offset1:121
	ds_read2_b32 v[12:13], v97 offset0:178 offset1:186
	ds_read2_b32 v[14:15], v97 offset0:243 offset1:251
	s_waitcnt lgkmcnt(3)
	s_waitcnt lgkmcnt(2)
	ds_read2_b32 v[16:17], v26 offset0:52 offset1:60
	ds_read2_b32 v[18:19], v26 offset0:117 offset1:125
	v_cvt_pk_bf16_f32 v4, v10, v8
	s_waitcnt lgkmcnt(3)
	s_waitcnt lgkmcnt(2)
	ds_read2_b32 v[20:21], v26 offset0:182 offset1:190
	ds_read2_b32 v[22:23], v26 offset0:247 offset1:255
	v_cvt_pk_bf16_f32 v5, v12, v14
	s_waitcnt lgkmcnt(3)
	s_waitcnt lgkmcnt(2)
	v_cvt_pk_bf16_f32 v6, v16, v18
	s_waitcnt lgkmcnt(1)
	v_or_b32_e32 v24, s4, v103
	s_waitcnt lgkmcnt(0)
	v_ashrrev_i32_e32 v25, 31, v24
	v_lshlrev_b64 v[24:25], 10, v[24:25]
	v_cvt_pk_bf16_f32 v7, v20, v22
	v_lshl_add_u64 v[24:25], v[2:3], 0, v[24:25]
	global_store_dwordx4 v[24:25], v[4:7], off nt
	s_nop 1
	v_cvt_pk_bf16_f32 v4, v11, v9
	v_cvt_pk_bf16_f32 v5, v13, v15
	v_cvt_pk_bf16_f32 v6, v17, v19
	v_or_b32_e32 v8, s4, v104
	v_ashrrev_i32_e32 v9, 31, v8
	v_lshlrev_b64 v[8:9], 10, v[8:9]
	v_cvt_pk_bf16_f32 v7, v21, v23
	v_lshl_add_u64 v[2:3], v[2:3], 0, v[8:9]
	global_store_dwordx4 v[2:3], v[4:7], off nt
	s_waitcnt lgkmcnt(0)

; #define LAS __attribute__((address_space(3)))
; #define WSW(T, off, l) WSP(T, WS_WSET + (size_t)(l) * WSET_STRIDE + (off))
; __device__ __forceinline__ void tr_item(const float* W, int ldw, int k0, int n0, bf16* WT, int ldt, int drow0, LAS float* scr, int lane, const float* kscale = nullptr) {
;     const float* src = W + (size_t)(k0 + (lane >> 4)) * ldw + n0 + (lane & 15) * 4;
;     f32x4 v[16];
; #pragma unroll
;     for (int i = 0; i < 16; ++i) v[i] = __builtin_nontemporal_load((const f32x4*)(src + (size_t)(4 * i) * ldw));
;     LAS float* wp = scr + (lane >> 4) * 65 + (lane & 15) * 4;
; #pragma unroll
;     for (int i = 0; i < 16; ++i) { LAS float* q = wp + (4 * i) * 65; const float ks = kscale ? kscale[k0 + 4 * i + (lane >> 4)] : 1.f; q[0] = v[i].x * ks; q[1] = v[i].y * ks; q[2] = v[i].z * ks; q[3] = v[i].w * ks; }
;     asm volatile("s_waitcnt lgkmcnt(0)" ::: "memory");
; __device__ __forceinline__ void convert_tile(const Args& a, GAS unsigned char* wsb, int l, int t, LAS float* scr, int lane) {
;     ...
;     if (r < I_IN) { const int kb = r / 45, nb = r - kb * 45; tr_item(INP(7) + (size_t)l * DM * INW, INW, kb * 64, nb * 64, WSW(bf16, W_IN, l), DM, nb * 64, scr, lane); return; }
.LBB0_1572:
	s_andn2_b64 vcc, exec, s[4:5]
	s_cbranch_vccnz .LBB0_1574
	s_mul_i32 s4, s15, 0x2d83
	s_lshr_b32 s6, s4, 19
	s_mul_i32 s4, s6, 0xffffffd3
	s_add_i32 s4, s4, s15
	v_lshl_or_b32 v1, s6, 6, v67
	v_readlane_b32 s8, v253, 6
	s_lshl_b32 s4, s4, 6
	v_mul_u32_u24_e32 v2, 0x2d00, v1
	v_mov_b32_e32 v3, v147
	v_readlane_b32 s9, v253, 7
	s_ashr_i32 s5, s4, 31
	v_lshlrev_b32_e32 v4, 2, v66
	v_lshl_add_u64 v[2:3], s[8:9], 0, v[2:3]
	v_lshl_add_u64 v[2:3], s[4:5], 2, v[2:3]
	v_mov_b32_e32 v5, v147
	v_lshl_add_u64 v[62:63], v[2:3], 0, v[4:5]
	s_mov_b32 s5, 0xb000
	v_add_co_u32_e32 v6, vcc, s5, v62
	s_mov_b32 s5, 0x16000
	s_nop 0
	v_addc_co_u32_e32 v7, vcc, 0, v63, vcc
	v_add_co_u32_e32 v10, vcc, s5, v62
	global_load_dwordx4 v[2:5], v[62:63], off nt
	s_nop 0
	global_load_dwordx4 v[6:9], v[6:7], off offset:1024 nt
	v_addc_co_u32_e32 v11, vcc, 0, v63, vcc
	s_mov_b32 s5, 0x21000
	v_add_co_u32_e32 v14, vcc, s5, v62
	s_mov_b32 s5, 0x2d000
	s_nop 0
	v_addc_co_u32_e32 v15, vcc, 0, v63, vcc
	global_load_dwordx4 v[10:13], v[10:11], off offset:2048 nt
	s_nop 0
	global_load_dwordx4 v[14:17], v[14:15], off offset:3072 nt
	v_add_co_u32_e32 v18, vcc, s5, v62
	s_mov_b32 s5, 0x38000
	s_nop 0
	v_addc_co_u32_e32 v19, vcc, 0, v63, vcc
	v_add_co_u32_e32 v22, vcc, s5, v62
	s_mov_b32 s5, 0x43000
	s_nop 0
	v_addc_co_u32_e32 v23, vcc, 0, v63, vcc
	global_load_dwordx4 v[18:21], v[18:19], off nt
	s_nop 0
	global_load_dwordx4 v[22:25], v[22:23], off offset:1024 nt
	v_add_co_u32_e32 v26, vcc, s5, v62
	s_mov_b32 s5, 0x4e000
	s_nop 0
	v_addc_co_u32_e32 v27, vcc, 0, v63, vcc
	v_add_co_u32_e32 v30, vcc, s5, v62
	s_mov_b32 s5, 0x5a000
	s_nop 0
	v_addc_co_u32_e32 v31, vcc, 0, v63, vcc
	global_load_dwordx4 v[26:29], v[26:27], off offset:2048 nt
	s_nop 0
	global_load_dwordx4 v[30:33], v[30:31], off offset:3072 nt
	v_add_co_u32_e32 v34, vcc, s5, v62
	s_mov_b32 s5, 0x65000
	s_nop 0
	v_addc_co_u32_e32 v35, vcc, 0, v63, vcc
	v_add_co_u32_e32 v38, vcc, s5, v62
	s_mov_b32 s5, 0x70000
	s_nop 0
	v_addc_co_u32_e32 v39, vcc, 0, v63, vcc
	global_load_dwordx4 v[34:37], v[34:35], off nt
	s_nop 0
	global_load_dwordx4 v[38:41], v[38:39], off offset:1024 nt
	v_add_co_u32_e32 v42, vcc, s5, v62
	s_mov_b32 s5, 0x7b000
	s_nop 0
	v_addc_co_u32_e32 v43, vcc, 0, v63, vcc
	v_add_co_u32_e32 v46, vcc, s5, v62
	s_mov_b32 s5, 0x87000
	s_nop 0
	v_addc_co_u32_e32 v47, vcc, 0, v63, vcc
	global_load_dwordx4 v[42:45], v[42:43], off offset:2048 nt
	s_nop 0
	global_load_dwordx4 v[46:49], v[46:47], off offset:3072 nt
	v_add_co_u32_e32 v50, vcc, s5, v62
	s_mov_b32 s5, 0x92000
	s_nop 0
	v_addc_co_u32_e32 v51, vcc, 0, v63, vcc
	v_add_co_u32_e32 v54, vcc, s5, v62
	s_mov_b32 s5, 0x9d000
	s_nop 0
	v_addc_co_u32_e32 v55, vcc, 0, v63, vcc
	global_load_dwordx4 v[50:53], v[50:51], off nt
	s_nop 0
	global_load_dwordx4 v[54:57], v[54:55], off offset:1024 nt
	v_add_co_u32_e32 v58, vcc, s5, v62
	s_mov_b32 s5, 0xa8000
	s_nop 0
	v_addc_co_u32_e32 v59, vcc, 0, v63, vcc
	global_load_dwordx4 v[58:61], v[58:59], off offset:2048 nt
	v_add_co_u32_e32 v62, vcc, s5, v62
	v_add_u32_e32 v1, 0x410, v95
	s_nop 0
	v_addc_co_u32_e32 v63, vcc, 0, v63, vcc
	global_load_dwordx4 v[62:65], v[62:63], off offset:3072 nt
	s_waitcnt vmcnt(15)
	ds_write2_b32 v95, v2, v3 offset1:1
	ds_write2_b32 v95, v4, v5 offset0:2 offset1:3
	s_waitcnt vmcnt(14)
	ds_write2_b32 v1, v6, v7 offset1:1
	v_add_u32_e32 v1, 0x418, v95
	ds_write2_b32 v1, v8, v9 offset1:1
	v_add_u32_e32 v1, 0x820, v95
	s_lshl_b32 s12, s6, 7
	v_lshl_add_u64 v[2:3], v[78:79], 0, s[12:13]
	s_waitcnt vmcnt(13)
	ds_write2_b32 v1, v10, v11 offset1:1
	v_add_u32_e32 v1, 0x828, v95
	ds_write2_b32 v1, v12, v13 offset1:1
	v_add_u32_e32 v1, 0xc30, v95
	s_waitcnt vmcnt(12)
	ds_write2_b32 v1, v14, v15 offset1:1
	v_add_u32_e32 v1, 0xc38, v95
	ds_write2_b32 v1, v16, v17 offset1:1
	v_add_u32_e32 v1, 0x1040, v95
	s_waitcnt vmcnt(11)
	ds_write2_b32 v1, v18, v19 offset1:1
	v_add_u32_e32 v1, 0x1048, v95
	ds_write2_b32 v1, v20, v21 offset1:1
	v_add_u32_e32 v1, 0x1450, v95
	s_waitcnt vmcnt(10)
	ds_write2_b32 v1, v22, v23 offset1:1
	v_add_u32_e32 v1, 0x1458, v95
	ds_write2_b32 v1, v24, v25 offset1:1
	v_add_u32_e32 v1, 0x1860, v95
	v_or_b32_e32 v24, s4, v96
	v_ashrrev_i32_e32 v25, 31, v24
	v_lshlrev_b64 v[24:25], 12, v[24:25]
	s_waitcnt vmcnt(9)
	ds_write2_b32 v1, v26, v27 offset1:1
	v_add_u32_e32 v1, 0x1868, v95
	ds_write2_b32 v1, v28, v29 offset1:1
	v_add_u32_e32 v1, 0x1c70, v95
	s_waitcnt vmcnt(8)
	ds_write2_b32 v1, v30, v31 offset1:1
	v_add_u32_e32 v1, 0x1c78, v95
	ds_write2_b32 v1, v32, v33 offset1:1
	v_add_u32_e32 v1, 0x2080, v95
	v_add_u32_e32 v26, 0x400, v97
	v_lshl_add_u64 v[24:25], v[2:3], 0, v[24:25]
	s_waitcnt vmcnt(7)
	ds_write2_b32 v1, v34, v35 offset1:1
	v_add_u32_e32 v1, 0x2088, v95
	ds_write2_b32 v1, v36, v37 offset1:1
	v_add_u32_e32 v1, 0x2490, v95
	s_waitcnt vmcnt(6)
	ds_write2_b32 v1, v38, v39 offset1:1
	v_add_u32_e32 v1, 0x2498, v95
	ds_write2_b32 v1, v40, v41 offset1:1
	v_add_u32_e32 v1, 0x28a0, v95
	s_waitcnt vmcnt(5)
	ds_write2_b32 v1, v42, v43 offset1:1
	v_add_u32_e32 v1, 0x28a8, v95
	ds_write2_b32 v1, v44, v45 offset1:1
	v_add_u32_e32 v1, 0x2cb0, v95
	s_waitcnt vmcnt(4)
	ds_write2_b32 v1, v46, v47 offset1:1
	v_add_u32_e32 v1, 0x2cb8, v95
	ds_write2_b32 v1, v48, v49 offset1:1
	v_add_u32_e32 v1, 0x30c0, v95
	s_waitcnt vmcnt(3)
; #define LAS __attribute__((address_space(3)))
; __device__ __forceinline__ unsigned f2bf(float f) { unsigned u = __builtin_bit_cast(unsigned, f); return (u + 0x7fffu + ((u >> 16) & 1u)) >> 16; }
; __device__ __forceinline__ unsigned pk2(float lo, float hi) { return f2bf(lo) | (f2bf(hi) << 16); }
; __device__ __forceinline__ void tr_item(const float* W, int ldw, int k0, int n0, bf16* WT, int ldt, int drow0, LAS float* scr, int lane, const float* kscale = nullptr) {
;     ...
;     const int kc = lane & 7;
; #pragma unroll
;     for (int j = 0; j < 8; ++j) { const int n = (lane >> 3) + 8 * j; const LAS float* sp = scr + (8 * kc) * 65 + n;
;         u32x4 o; o.x = pk2(sp[0 * 65], sp[1 * 65]); o.y = pk2(sp[2 * 65], sp[3 * 65]); o.z = pk2(sp[4 * 65], sp[5 * 65]); o.w = pk2(sp[6 * 65], sp[7 * 65]);
;         __builtin_nontemporal_store(o, (u32x4*)(WT + (size_t)(drow0 + n) * ldt + k0 + 8 * kc)); }
;     asm volatile("s_waitcnt lgkmcnt(0)" ::: "memory");
	ds_write2_b32 v1, v50, v51 offset1:1
	v_add_u32_e32 v1, 0x30c8, v95
	ds_write2_b32 v1, v52, v53 offset1:1
	v_add_u32_e32 v1, 0x34d0, v95
	s_waitcnt vmcnt(2)
	ds_write2_b32 v1, v54, v55 offset1:1
	v_add_u32_e32 v1, 0x34d8, v95
	ds_write2_b32 v1, v56, v57 offset1:1
	v_add_u32_e32 v1, 0x38e0, v95
	s_waitcnt vmcnt(1)
	ds_write2_b32 v1, v58, v59 offset1:1
	v_add_u32_e32 v1, 0x38e8, v95
	ds_write2_b32 v1, v60, v61 offset1:1
	v_add_u32_e32 v1, 0x3cf0, v95
	s_waitcnt vmcnt(0)
	ds_write2_b32 v1, v62, v63 offset1:1
	v_add_u32_e32 v1, 0x3cf8, v95
	ds_write2_b32 v1, v64, v65 offset1:1
	s_waitcnt lgkmcnt(0)
	ds_read2_b32 v[8:9], v97 offset1:8
	ds_read2_b32 v[10:11], v97 offset0:65 offset1:73
	ds_read2_b32 v[12:13], v97 offset0:130 offset1:138
	ds_read2_b32 v[14:15], v97 offset0:195 offset1:203
	ds_read2_b32 v[16:17], v26 offset0:4 offset1:12
	s_waitcnt lgkmcnt(4)
	s_waitcnt lgkmcnt(3)
	ds_read2_b32 v[18:19], v26 offset0:69 offset1:77
	v_cvt_pk_bf16_f32 v4, v8, v10
	s_waitcnt lgkmcnt(3)
	s_waitcnt lgkmcnt(2)
	ds_read2_b32 v[20:21], v26 offset0:134 offset1:142
	ds_read2_b32 v[22:23], v26 offset0:199 offset1:207
	v_cvt_pk_bf16_f32 v5, v12, v14
	s_waitcnt lgkmcnt(3)
	s_waitcnt lgkmcnt(2)
	v_cvt_pk_bf16_f32 v6, v16, v18
	s_waitcnt lgkmcnt(1)
	s_waitcnt lgkmcnt(0)
	v_cvt_pk_bf16_f32 v7, v20, v22
	global_store_dwordx4 v[24:25], v[4:7], off nt
	s_nop 1
	v_cvt_pk_bf16_f32 v4, v9, v11
	v_cvt_pk_bf16_f32 v5, v13, v15
	v_cvt_pk_bf16_f32 v6, v17, v19
	v_or_b32_e32 v8, s4, v98
	v_ashrrev_i32_e32 v9, 31, v8
	v_lshlrev_b64 v[8:9], 12, v[8:9]
	v_cvt_pk_bf16_f32 v7, v21, v23
	ds_read2_b32 v[10:11], v97 offset0:16 offset1:24
	v_lshl_add_u64 v[8:9], v[2:3], 0, v[8:9]
	global_store_dwordx4 v[8:9], v[4:7], off nt
	ds_read2_b32 v[8:9], v97 offset0:81 offset1:89
	ds_read2_b32 v[12:13], v97 offset0:146 offset1:154
	ds_read2_b32 v[14:15], v97 offset0:211 offset1:219
	s_waitcnt lgkmcnt(3)
	s_waitcnt lgkmcnt(2)
	ds_read2_b32 v[16:17], v26 offset0:20 offset1:28
	ds_read2_b32 v[18:19], v26 offset0:85 offset1:93
	v_cvt_pk_bf16_f32 v4, v10, v8
	s_waitcnt lgkmcnt(3)
	s_waitcnt lgkmcnt(2)
	ds_read2_b32 v[20:21], v26 offset0:150 offset1:158
	ds_read2_b32 v[22:23], v26 offset0:215 offset1:223
	v_cvt_pk_bf16_f32 v5, v12, v14
	s_waitcnt lgkmcnt(3)
	s_waitcnt lgkmcnt(2)
	v_cvt_pk_bf16_f32 v6, v16, v18
	s_waitcnt lgkmcnt(1)
	v_or_b32_e32 v24, s4, v99
	s_waitcnt lgkmcnt(0)
	v_ashrrev_i32_e32 v25, 31, v24
	v_lshlrev_b64 v[24:25], 12, v[24:25]
	v_cvt_pk_bf16_f32 v7, v20, v22
	v_lshl_add_u64 v[24:25], v[2:3], 0, v[24:25]
	global_store_dwordx4 v[24:25], v[4:7], off nt
	s_nop 1
	v_cvt_pk_bf16_f32 v4, v11, v9
	v_cvt_pk_bf16_f32 v5, v13, v15
	v_cvt_pk_bf16_f32 v6, v17, v19
	v_or_b32_e32 v8, s4, v100
	v_ashrrev_i32_e32 v9, 31, v8
	v_lshlrev_b64 v[8:9], 12, v[8:9]
	v_cvt_pk_bf16_f32 v7, v21, v23
	ds_read2_b32 v[10:11], v97 offset0:32 offset1:40
	v_lshl_add_u64 v[8:9], v[2:3], 0, v[8:9]
	global_store_dwordx4 v[8:9], v[4:7], off nt
	ds_read2_b32 v[8:9], v97 offset0:97 offset1:105
	ds_read2_b32 v[12:13], v97 offset0:162 offset1:170
	ds_read2_b32 v[14:15], v97 offset0:227 offset1:235
	s_waitcnt lgkmcnt(3)
	s_waitcnt lgkmcnt(2)
	ds_read2_b32 v[16:17], v26 offset0:36 offset1:44
	ds_read2_b32 v[18:19], v26 offset0:101 offset1:109
	v_cvt_pk_bf16_f32 v4, v10, v8
	s_waitcnt lgkmcnt(3)
	s_waitcnt lgkmcnt(2)
	ds_read2_b32 v[20:21], v26 offset0:166 offset1:174
	ds_read2_b32 v[22:23], v26 offset0:231 offset1:239
	v_cvt_pk_bf16_f32 v5, v12, v14
	s_waitcnt lgkmcnt(3)
	s_waitcnt lgkmcnt(2)
	v_cvt_pk_bf16_f32 v6, v16, v18
	s_waitcnt lgkmcnt(1)
	v_or_b32_e32 v24, s4, v101
	s_waitcnt lgkmcnt(0)
	v_ashrrev_i32_e32 v25, 31, v24
	v_lshlrev_b64 v[24:25], 12, v[24:25]
	v_cvt_pk_bf16_f32 v7, v20, v22
	v_lshl_add_u64 v[24:25], v[2:3], 0, v[24:25]
	global_store_dwordx4 v[24:25], v[4:7], off nt
	s_nop 1
	v_cvt_pk_bf16_f32 v4, v11, v9
	v_cvt_pk_bf16_f32 v5, v13, v15
	v_cvt_pk_bf16_f32 v6, v17, v19
	v_or_b32_e32 v8, s4, v102
	v_ashrrev_i32_e32 v9, 31, v8
	v_lshlrev_b64 v[8:9], 12, v[8:9]
	v_cvt_pk_bf16_f32 v7, v21, v23
	ds_read2_b32 v[10:11], v97 offset0:48 offset1:56
	v_lshl_add_u64 v[8:9], v[2:3], 0, v[8:9]
	global_store_dwordx4 v[8:9], v[4:7], off nt
	ds_read2_b32 v[8:9], v97 offset0:113 offset1:121
	ds_read2_b32 v[12:13], v97 offset0:178 offset1:186
	ds_read2_b32 v[14:15], v97 offset0:243 offset1:251
	s_waitcnt lgkmcnt(3)
	s_waitcnt lgkmcnt(2)
	ds_read2_b32 v[16:17], v26 offset0:52 offset1:60
	ds_read2_b32 v[18:19], v26 offset0:117 offset1:125
	v_cvt_pk_bf16_f32 v4, v10, v8
	s_waitcnt lgkmcnt(3)
	s_waitcnt lgkmcnt(2)
	ds_read2_b32 v[20:21], v26 offset0:182 offset1:190
	ds_read2_b32 v[22:23], v26 offset0:247 offset1:255
	v_cvt_pk_bf16_f32 v5, v12, v14
	s_waitcnt lgkmcnt(3)
	s_waitcnt lgkmcnt(2)
	v_cvt_pk_bf16_f32 v6, v16, v18
	s_waitcnt lgkmcnt(1)
	v_or_b32_e32 v24, s4, v103
	s_waitcnt lgkmcnt(0)
	v_ashrrev_i32_e32 v25, 31, v24
	v_lshlrev_b64 v[24:25], 12, v[24:25]
	v_cvt_pk_bf16_f32 v7, v20, v22
	v_lshl_add_u64 v[24:25], v[2:3], 0, v[24:25]
	global_store_dwordx4 v[24:25], v[4:7], off nt
	s_nop 1
	v_cvt_pk_bf16_f32 v4, v11, v9
	v_cvt_pk_bf16_f32 v5, v13, v15
	v_cvt_pk_bf16_f32 v6, v17, v19
	v_or_b32_e32 v8, s4, v104
	v_ashrrev_i32_e32 v9, 31, v8
	v_lshlrev_b64 v[8:9], 12, v[8:9]
	v_cvt_pk_bf16_f32 v7, v21, v23
	v_lshl_add_u64 v[2:3], v[2:3], 0, v[8:9]
	global_store_dwordx4 v[2:3], v[4:7], off nt
	s_waitcnt lgkmcnt(0)

; #define LAS __attribute__((address_space(3)))
; #define WSW(T, off, l) WSP(T, WS_WSET + (size_t)(l) * WSET_STRIDE + (off))
; __device__ __forceinline__ void tr_item(const float* W, int ldw, int k0, int n0, bf16* WT, int ldt, int drow0, LAS float* scr, int lane, const float* kscale = nullptr) {
;     const float* src = W + (size_t)(k0 + (lane >> 4)) * ldw + n0 + (lane & 15) * 4;
;     f32x4 v[16];
; #pragma unroll
;     for (int i = 0; i < 16; ++i) v[i] = __builtin_nontemporal_load((const f32x4*)(src + (size_t)(4 * i) * ldw));
;     LAS float* wp = scr + (lane >> 4) * 65 + (lane & 15) * 4;
; #pragma unroll
;     for (int i = 0; i < 16; ++i) { LAS float* q = wp + (4 * i) * 65; const float ks = kscale ? kscale[k0 + 4 * i + (lane >> 4)] : 1.f; q[0] = v[i].x * ks; q[1] = v[i].y * ks; q[2] = v[i].z * ks; q[3] = v[i].w * ks; }
;     asm volatile("s_waitcnt lgkmcnt(0)" ::: "memory");
; __device__ __forceinline__ void convert_tile(const Args& a, GAS unsigned char* wsb, int l, int t, LAS float* scr, int lane) {
;     ...
;     if (r < I_OUT) { const int kb = r / 32, nb = r - kb * 32; tr_item(INP(21) + (size_t)l * DM * DM, DM, kb * 64, nb * 64, WSW(bf16, W_OUT, l), DM, nb * 64, scr, lane); return; }
.LBB0_1589:
	s_andn2_b64 vcc, exec, s[4:5]
	s_cbranch_vccnz .LBB0_1591
	s_lshl_b32 s4, s15, 1
	s_and_b32 s4, s4, 0x1fc0
	s_addk_i32 s4, 0xf240
	s_lshl_b32 s5, s15, 6
	v_or_b32_e32 v146, s4, v67
	s_and_b32 s6, s5, 0x7c0
	v_lshlrev_b64 v[2:3], 13, v[146:147]
	v_lshl_add_u64 v[2:3], s[60:61], 0, v[2:3]
	s_lshl_b32 s12, s6, 2
	v_lshl_add_u64 v[2:3], v[2:3], 0, s[12:13]
	v_lshlrev_b32_e32 v146, 2, v66
	v_lshl_add_u64 v[62:63], v[2:3], 0, v[146:147]
	v_add_co_u32_e32 v6, vcc, s83, v62
	s_mov_b32 s5, 0x20000
	s_nop 0
	v_addc_co_u32_e32 v7, vcc, 0, v63, vcc
	v_add_co_u32_e32 v10, vcc, s81, v62
	global_load_dwordx4 v[2:5], v[62:63], off nt
	s_nop 0
	global_load_dwordx4 v[6:9], v[6:7], off nt
	v_addc_co_u32_e32 v11, vcc, 0, v63, vcc
	v_add_co_u32_e32 v14, vcc, s82, v62
	v_add_u32_e32 v1, 0x410, v95
	s_nop 0
	v_addc_co_u32_e32 v15, vcc, 0, v63, vcc
	global_load_dwordx4 v[10:13], v[10:11], off nt
	s_nop 0
	global_load_dwordx4 v[14:17], v[14:15], off nt
	v_add_co_u32_e32 v18, vcc, s5, v62
	s_mov_b32 s5, 0x28000
	s_nop 0
	v_addc_co_u32_e32 v19, vcc, 0, v63, vcc
	v_add_co_u32_e32 v22, vcc, s5, v62
	s_mov_b32 s5, 0x30000
	s_nop 0
	v_addc_co_u32_e32 v23, vcc, 0, v63, vcc
	global_load_dwordx4 v[18:21], v[18:19], off nt
	s_nop 0
	global_load_dwordx4 v[22:25], v[22:23], off nt
	v_add_co_u32_e32 v26, vcc, s5, v62
	s_mov_b32 s5, 0x38000
	s_nop 0
	v_addc_co_u32_e32 v27, vcc, 0, v63, vcc
	v_add_co_u32_e32 v30, vcc, s5, v62
	s_mov_b32 s5, 0x40000
	s_nop 0
	v_addc_co_u32_e32 v31, vcc, 0, v63, vcc
	global_load_dwordx4 v[26:29], v[26:27], off nt
	s_nop 0
	global_load_dwordx4 v[30:33], v[30:31], off nt
	v_add_co_u32_e32 v34, vcc, s5, v62
	s_mov_b32 s5, 0x48000
	s_nop 0
	v_addc_co_u32_e32 v35, vcc, 0, v63, vcc
	v_add_co_u32_e32 v38, vcc, s5, v62
	s_mov_b32 s5, 0x50000
	s_nop 0
	v_addc_co_u32_e32 v39, vcc, 0, v63, vcc
	global_load_dwordx4 v[34:37], v[34:35], off nt
	s_nop 0
	global_load_dwordx4 v[38:41], v[38:39], off nt
	v_add_co_u32_e32 v42, vcc, s5, v62
	s_mov_b32 s5, 0x58000
	s_nop 0
	v_addc_co_u32_e32 v43, vcc, 0, v63, vcc
	v_add_co_u32_e32 v46, vcc, s5, v62
	s_mov_b32 s5, 0x60000
	s_nop 0
	v_addc_co_u32_e32 v47, vcc, 0, v63, vcc
	global_load_dwordx4 v[42:45], v[42:43], off nt
	s_nop 0
	global_load_dwordx4 v[46:49], v[46:47], off nt
	v_add_co_u32_e32 v50, vcc, s5, v62
	s_mov_b32 s5, 0x68000
	s_nop 0
	v_addc_co_u32_e32 v51, vcc, 0, v63, vcc
	v_add_co_u32_e32 v54, vcc, s5, v62
	s_mov_b32 s5, 0x70000
	s_nop 0
	v_addc_co_u32_e32 v55, vcc, 0, v63, vcc
	global_load_dwordx4 v[50:53], v[50:51], off nt
	s_nop 0
	global_load_dwordx4 v[54:57], v[54:55], off nt
	v_add_co_u32_e32 v58, vcc, s5, v62
	s_mov_b32 s5, 0x78000
	s_nop 0
	v_addc_co_u32_e32 v59, vcc, 0, v63, vcc
	global_load_dwordx4 v[58:61], v[58:59], off nt
	v_add_co_u32_e32 v62, vcc, s5, v62
	s_mov_b32 s5, s13
	s_nop 0
	v_addc_co_u32_e32 v63, vcc, 0, v63, vcc
	global_load_dwordx4 v[62:65], v[62:63], off nt
	s_waitcnt vmcnt(15)
	ds_write2_b32 v95, v2, v3 offset1:1
	ds_write2_b32 v95, v4, v5 offset0:2 offset1:3
	s_waitcnt vmcnt(14)
	ds_write2_b32 v1, v6, v7 offset1:1
	v_add_u32_e32 v1, 0x418, v95
	ds_write2_b32 v1, v8, v9 offset1:1
	v_add_u32_e32 v1, 0x820, v95
	v_lshl_add_u64 v[2:3], s[4:5], 1, v[84:85]
	s_waitcnt vmcnt(13)
	ds_write2_b32 v1, v10, v11 offset1:1
	v_add_u32_e32 v1, 0x828, v95
	ds_write2_b32 v1, v12, v13 offset1:1
	v_add_u32_e32 v1, 0xc30, v95
	s_waitcnt vmcnt(12)
	ds_write2_b32 v1, v14, v15 offset1:1
	v_add_u32_e32 v1, 0xc38, v95
	ds_write2_b32 v1, v16, v17 offset1:1
	v_add_u32_e32 v1, 0x1040, v95
	s_waitcnt vmcnt(11)
	ds_write2_b32 v1, v18, v19 offset1:1
	v_add_u32_e32 v1, 0x1048, v95
	ds_write2_b32 v1, v20, v21 offset1:1
	v_add_u32_e32 v1, 0x1450, v95
	s_waitcnt vmcnt(10)
	ds_write2_b32 v1, v22, v23 offset1:1
	v_add_u32_e32 v1, 0x1458, v95
	ds_write2_b32 v1, v24, v25 offset1:1
	v_add_u32_e32 v1, 0x1860, v95
	s_waitcnt vmcnt(9)
	ds_write2_b32 v1, v26, v27 offset1:1
	v_add_u32_e32 v1, 0x1868, v95
	ds_write2_b32 v1, v28, v29 offset1:1
	v_add_u32_e32 v1, 0x1c70, v95
	s_waitcnt vmcnt(8)
	ds_write2_b32 v1, v30, v31 offset1:1
	v_add_u32_e32 v1, 0x1c78, v95
	ds_write2_b32 v1, v32, v33 offset1:1
	v_add_u32_e32 v1, 0x2080, v95
	v_add_u32_e32 v26, 0x400, v97
	s_waitcnt vmcnt(7)
	ds_write2_b32 v1, v34, v35 offset1:1
	v_add_u32_e32 v1, 0x2088, v95
	ds_write2_b32 v1, v36, v37 offset1:1
	v_add_u32_e32 v1, 0x2490, v95
	s_waitcnt vmcnt(6)
	ds_write2_b32 v1, v38, v39 offset1:1
	v_add_u32_e32 v1, 0x2498, v95
	ds_write2_b32 v1, v40, v41 offset1:1
	v_add_u32_e32 v1, 0x28a0, v95
	s_waitcnt vmcnt(5)
	ds_write2_b32 v1, v42, v43 offset1:1
	v_add_u32_e32 v1, 0x28a8, v95
	ds_write2_b32 v1, v44, v45 offset1:1
	v_add_u32_e32 v1, 0x2cb0, v95
	s_waitcnt vmcnt(4)
	ds_write2_b32 v1, v46, v47 offset1:1
	v_add_u32_e32 v1, 0x2cb8, v95
	ds_write2_b32 v1, v48, v49 offset1:1
	v_add_u32_e32 v1, 0x30c0, v95
	s_waitcnt vmcnt(3)
	ds_write2_b32 v1, v50, v51 offset1:1
	v_add_u32_e32 v1, 0x30c8, v95
	ds_write2_b32 v1, v52, v53 offset1:1
	v_add_u32_e32 v1, 0x34d0, v95
	s_waitcnt vmcnt(2)
; #define LAS __attribute__((address_space(3)))
; __device__ __forceinline__ unsigned f2bf(float f) { unsigned u = __builtin_bit_cast(unsigned, f); return (u + 0x7fffu + ((u >> 16) & 1u)) >> 16; }
; __device__ __forceinline__ unsigned pk2(float lo, float hi) { return f2bf(lo) | (f2bf(hi) << 16); }
; __device__ __forceinline__ void tr_item(const float* W, int ldw, int k0, int n0, bf16* WT, int ldt, int drow0, LAS float* scr, int lane, const float* kscale = nullptr) {
;     ...
;     const int kc = lane & 7;
; #pragma unroll
;     for (int j = 0; j < 8; ++j) { const int n = (lane >> 3) + 8 * j; const LAS float* sp = scr + (8 * kc) * 65 + n;
;         u32x4 o; o.x = pk2(sp[0 * 65], sp[1 * 65]); o.y = pk2(sp[2 * 65], sp[3 * 65]); o.z = pk2(sp[4 * 65], sp[5 * 65]); o.w = pk2(sp[6 * 65], sp[7 * 65]);
;         __builtin_nontemporal_store(o, (u32x4*)(WT + (size_t)(drow0 + n) * ldt + k0 + 8 * kc)); }
;     asm volatile("s_waitcnt lgkmcnt(0)" ::: "memory");
	ds_write2_b32 v1, v54, v55 offset1:1
	v_add_u32_e32 v1, 0x34d8, v95
	ds_write2_b32 v1, v56, v57 offset1:1
	v_add_u32_e32 v1, 0x38e0, v95
	s_waitcnt vmcnt(1)
	ds_write2_b32 v1, v58, v59 offset1:1
	v_add_u32_e32 v1, 0x38e8, v95
	ds_write2_b32 v1, v60, v61 offset1:1
	v_add_u32_e32 v1, 0x3cf0, v95
	s_waitcnt vmcnt(0)
	ds_write2_b32 v1, v62, v63 offset1:1
	v_add_u32_e32 v1, 0x3cf8, v95
	ds_write2_b32 v1, v64, v65 offset1:1
	s_waitcnt lgkmcnt(0)
	ds_read2_b32 v[8:9], v97 offset1:8
	ds_read2_b32 v[10:11], v97 offset0:65 offset1:73
	ds_read2_b32 v[12:13], v97 offset0:130 offset1:138
	ds_read2_b32 v[14:15], v97 offset0:195 offset1:203
	ds_read2_b32 v[16:17], v26 offset0:4 offset1:12
	s_waitcnt lgkmcnt(4)
	s_waitcnt lgkmcnt(3)
	ds_read2_b32 v[18:19], v26 offset0:69 offset1:77
	v_cvt_pk_bf16_f32 v4, v8, v10
	s_waitcnt lgkmcnt(3)
	s_waitcnt lgkmcnt(2)
	ds_read2_b32 v[20:21], v26 offset0:134 offset1:142
	ds_read2_b32 v[22:23], v26 offset0:199 offset1:207
	v_cvt_pk_bf16_f32 v5, v12, v14
	s_waitcnt lgkmcnt(3)
	s_waitcnt lgkmcnt(2)
	v_cvt_pk_bf16_f32 v6, v16, v18
	s_waitcnt lgkmcnt(1)
	s_waitcnt lgkmcnt(0)
	v_cvt_pk_bf16_f32 v7, v20, v22
	v_or_b32_e32 v1, s6, v96
	v_lshlrev_b32_e32 v146, 12, v1
	v_lshl_add_u64 v[24:25], v[2:3], 0, v[146:147]
	global_store_dwordx4 v[24:25], v[4:7], off nt
	s_nop 1
	v_cvt_pk_bf16_f32 v4, v9, v11
	v_cvt_pk_bf16_f32 v5, v13, v15
	v_cvt_pk_bf16_f32 v6, v17, v19
	v_cvt_pk_bf16_f32 v7, v21, v23
	v_or_b32_e32 v1, s6, v98
	v_lshlrev_b32_e32 v146, 12, v1
	ds_read2_b32 v[8:9], v97 offset0:16 offset1:24
	v_lshl_add_u64 v[10:11], v[2:3], 0, v[146:147]
	global_store_dwordx4 v[10:11], v[4:7], off nt
	ds_read2_b32 v[10:11], v97 offset0:81 offset1:89
	ds_read2_b32 v[12:13], v97 offset0:146 offset1:154
	ds_read2_b32 v[14:15], v97 offset0:211 offset1:219
	s_waitcnt lgkmcnt(3)
	s_waitcnt lgkmcnt(2)
	ds_read2_b32 v[16:17], v26 offset0:20 offset1:28
	ds_read2_b32 v[18:19], v26 offset0:85 offset1:93
	v_cvt_pk_bf16_f32 v4, v8, v10
	s_waitcnt lgkmcnt(3)
	s_waitcnt lgkmcnt(2)
	ds_read2_b32 v[20:21], v26 offset0:150 offset1:158
	ds_read2_b32 v[22:23], v26 offset0:215 offset1:223
	v_cvt_pk_bf16_f32 v5, v12, v14
	s_waitcnt lgkmcnt(3)
	s_waitcnt lgkmcnt(2)
	v_cvt_pk_bf16_f32 v6, v16, v18
	s_waitcnt lgkmcnt(1)
	s_waitcnt lgkmcnt(0)
	v_cvt_pk_bf16_f32 v7, v20, v22
	v_or_b32_e32 v1, s6, v99
	v_lshlrev_b32_e32 v146, 12, v1
	v_lshl_add_u64 v[24:25], v[2:3], 0, v[146:147]
	global_store_dwordx4 v[24:25], v[4:7], off nt
	s_nop 1
	v_cvt_pk_bf16_f32 v4, v9, v11
	v_cvt_pk_bf16_f32 v5, v13, v15
	v_cvt_pk_bf16_f32 v6, v17, v19
	v_cvt_pk_bf16_f32 v7, v21, v23
	v_or_b32_e32 v1, s6, v100
	v_lshlrev_b32_e32 v146, 12, v1
	ds_read2_b32 v[8:9], v97 offset0:32 offset1:40
	v_lshl_add_u64 v[10:11], v[2:3], 0, v[146:147]
	global_store_dwordx4 v[10:11], v[4:7], off nt
	ds_read2_b32 v[10:11], v97 offset0:97 offset1:105
	ds_read2_b32 v[12:13], v97 offset0:162 offset1:170
	ds_read2_b32 v[14:15], v97 offset0:227 offset1:235
	s_waitcnt lgkmcnt(3)
	s_waitcnt lgkmcnt(2)
	ds_read2_b32 v[16:17], v26 offset0:36 offset1:44
	ds_read2_b32 v[18:19], v26 offset0:101 offset1:109
	v_cvt_pk_bf16_f32 v4, v8, v10
	s_waitcnt lgkmcnt(3)
	s_waitcnt lgkmcnt(2)
	ds_read2_b32 v[20:21], v26 offset0:166 offset1:174
	ds_read2_b32 v[22:23], v26 offset0:231 offset1:239
	v_cvt_pk_bf16_f32 v5, v12, v14
	s_waitcnt lgkmcnt(3)
	s_waitcnt lgkmcnt(2)
	v_cvt_pk_bf16_f32 v6, v16, v18
	s_waitcnt lgkmcnt(1)
	s_waitcnt lgkmcnt(0)
	v_cvt_pk_bf16_f32 v7, v20, v22
	v_or_b32_e32 v1, s6, v101
	v_lshlrev_b32_e32 v146, 12, v1
	v_lshl_add_u64 v[24:25], v[2:3], 0, v[146:147]
	global_store_dwordx4 v[24:25], v[4:7], off nt
	s_nop 1
	v_cvt_pk_bf16_f32 v4, v9, v11
	v_cvt_pk_bf16_f32 v5, v13, v15
	v_cvt_pk_bf16_f32 v6, v17, v19
	v_cvt_pk_bf16_f32 v7, v21, v23
	v_or_b32_e32 v1, s6, v102
	v_lshlrev_b32_e32 v146, 12, v1
	ds_read2_b32 v[8:9], v97 offset0:48 offset1:56
	v_lshl_add_u64 v[10:11], v[2:3], 0, v[146:147]
	global_store_dwordx4 v[10:11], v[4:7], off nt
	ds_read2_b32 v[10:11], v97 offset0:113 offset1:121
	ds_read2_b32 v[12:13], v97 offset0:178 offset1:186
	ds_read2_b32 v[14:15], v97 offset0:243 offset1:251
	s_waitcnt lgkmcnt(3)
	s_waitcnt lgkmcnt(2)
	ds_read2_b32 v[16:17], v26 offset0:52 offset1:60
	ds_read2_b32 v[18:19], v26 offset0:117 offset1:125
	v_cvt_pk_bf16_f32 v4, v8, v10
	s_waitcnt lgkmcnt(3)
	s_waitcnt lgkmcnt(2)
	ds_read2_b32 v[20:21], v26 offset0:182 offset1:190
	ds_read2_b32 v[22:23], v26 offset0:247 offset1:255
	v_cvt_pk_bf16_f32 v5, v12, v14
	s_waitcnt lgkmcnt(3)
	s_waitcnt lgkmcnt(2)
	v_cvt_pk_bf16_f32 v6, v16, v18
	s_waitcnt lgkmcnt(1)
	s_waitcnt lgkmcnt(0)
	v_cvt_pk_bf16_f32 v7, v20, v22
	v_or_b32_e32 v1, s6, v103
	v_lshlrev_b32_e32 v146, 12, v1
	v_lshl_add_u64 v[24:25], v[2:3], 0, v[146:147]
	global_store_dwordx4 v[24:25], v[4:7], off nt
	s_nop 1
	v_cvt_pk_bf16_f32 v4, v9, v11
	v_cvt_pk_bf16_f32 v5, v13, v15
	v_cvt_pk_bf16_f32 v6, v17, v19
	v_cvt_pk_bf16_f32 v7, v21, v23
	v_or_b32_e32 v1, s6, v104
	v_lshlrev_b32_e32 v146, 12, v1
	v_lshl_add_u64 v[2:3], v[2:3], 0, v[146:147]
	global_store_dwordx4 v[2:3], v[4:7], off nt
	s_waitcnt lgkmcnt(0)

; #define LAS __attribute__((address_space(3)))
; __device__ __forceinline__ unsigned f2bf(float f) { unsigned u = __builtin_bit_cast(unsigned, f); return (u + 0x7fffu + ((u >> 16) & 1u)) >> 16; }
; __device__ __forceinline__ unsigned pk2(float lo, float hi) { return f2bf(lo) | (f2bf(hi) << 16); }
; __device__ __forceinline__ void tr_item(const float* W, int ldw, int k0, int n0, bf16* WT, int ldt, int drow0, LAS float* scr, int lane, const float* kscale = nullptr) {
;     ...
;     for (int i = 0; i < 16; ++i) { LAS float* q = wp + (4 * i) * 65; const float ks = kscale ? kscale[k0 + 4 * i + (lane >> 4)] : 1.f; q[0] = v[i].x * ks; q[1] = v[i].y * ks; q[2] = v[i].z * ks; q[3] = v[i].w * ks; }
;     asm volatile("s_waitcnt lgkmcnt(0)" ::: "memory");
;     const int kc = lane & 7;
; #pragma unroll
;     for (int j = 0; j < 8; ++j) { const int n = (lane >> 3) + 8 * j; const LAS float* sp = scr + (8 * kc) * 65 + n;
;         u32x4 o; o.x = pk2(sp[0 * 65], sp[1 * 65]); o.y = pk2(sp[2 * 65], sp[3 * 65]); o.z = pk2(sp[4 * 65], sp[5 * 65]); o.w = pk2(sp[6 * 65], sp[7 * 65]);
;         __builtin_nontemporal_store(o, (u32x4*)(WT + (size_t)(drow0 + n) * ldt + k0 + 8 * kc)); }
;     asm volatile("s_waitcnt lgkmcnt(0)" ::: "memory");
.LBB0_1617:
	s_waitcnt vmcnt(0)
	v_pk_mul_f32 v[2:3], v[2:3], v[10:11] op_sel_hi:[1,0]
	v_add_u32_e32 v1, 0x3cf0, v95
	ds_write2_b32 v1, v2, v3 offset1:1
	v_pk_mul_f32 v[2:3], v[4:5], v[10:11] op_sel_hi:[1,0]
	v_add_u32_e32 v1, 0x3cf8, v95
	ds_write2_b32 v1, v2, v3 offset1:1
	s_waitcnt lgkmcnt(0)
	ds_read2_b32 v[8:9], v97 offset1:8
	ds_read2_b32 v[10:11], v97 offset0:65 offset1:73
	ds_read2_b32 v[12:13], v97 offset0:130 offset1:138
	ds_read2_b32 v[14:15], v97 offset0:195 offset1:203
	v_add_u32_e32 v26, 0x400, v97
	s_waitcnt lgkmcnt(3)
	s_waitcnt lgkmcnt(2)
	ds_read2_b32 v[16:17], v26 offset0:4 offset1:12
	ds_read2_b32 v[18:19], v26 offset0:69 offset1:77
	v_cvt_pk_bf16_f32 v4, v8, v10
	s_waitcnt lgkmcnt(3)
	s_waitcnt lgkmcnt(2)
	ds_read2_b32 v[20:21], v26 offset0:134 offset1:142
	ds_read2_b32 v[22:23], v26 offset0:199 offset1:207
	v_cvt_pk_bf16_f32 v5, v12, v14
	s_waitcnt lgkmcnt(3)
	s_waitcnt lgkmcnt(2)
	v_cvt_pk_bf16_f32 v6, v16, v18
	s_waitcnt lgkmcnt(1)
	s_waitcnt lgkmcnt(0)
	s_mov_b32 s5, s13
	v_cvt_pk_bf16_f32 v7, v20, v22
	v_or_b32_e32 v1, s8, v96
	v_lshl_add_u64 v[2:3], s[4:5], 1, v[86:87]
	v_lshlrev_b32_e32 v146, 9, v1
	v_lshl_add_u64 v[24:25], v[2:3], 0, v[146:147]
	global_store_dwordx4 v[24:25], v[4:7], off nt
	s_nop 1
	v_cvt_pk_bf16_f32 v4, v9, v11
	v_cvt_pk_bf16_f32 v5, v13, v15
	v_cvt_pk_bf16_f32 v6, v17, v19
	v_cvt_pk_bf16_f32 v7, v21, v23
	v_or_b32_e32 v1, s8, v98
	v_lshlrev_b32_e32 v146, 9, v1
	ds_read2_b32 v[8:9], v97 offset0:16 offset1:24
	v_lshl_add_u64 v[10:11], v[2:3], 0, v[146:147]
	global_store_dwordx4 v[10:11], v[4:7], off nt
	ds_read2_b32 v[10:11], v97 offset0:81 offset1:89
	ds_read2_b32 v[12:13], v97 offset0:146 offset1:154
	ds_read2_b32 v[14:15], v97 offset0:211 offset1:219
	s_waitcnt lgkmcnt(3)
	s_waitcnt lgkmcnt(2)
	ds_read2_b32 v[16:17], v26 offset0:20 offset1:28
	ds_read2_b32 v[18:19], v26 offset0:85 offset1:93
	v_cvt_pk_bf16_f32 v4, v8, v10
	s_waitcnt lgkmcnt(3)
	s_waitcnt lgkmcnt(2)
	ds_read2_b32 v[20:21], v26 offset0:150 offset1:158
	ds_read2_b32 v[22:23], v26 offset0:215 offset1:223
	v_cvt_pk_bf16_f32 v5, v12, v14
	s_waitcnt lgkmcnt(3)
	s_waitcnt lgkmcnt(2)
	v_cvt_pk_bf16_f32 v6, v16, v18
	s_waitcnt lgkmcnt(1)
	s_waitcnt lgkmcnt(0)
	v_cvt_pk_bf16_f32 v7, v20, v22
	v_or_b32_e32 v1, s8, v99
	v_lshlrev_b32_e32 v146, 9, v1
	v_lshl_add_u64 v[24:25], v[2:3], 0, v[146:147]
	global_store_dwordx4 v[24:25], v[4:7], off nt
	s_nop 1
	v_cvt_pk_bf16_f32 v4, v9, v11
	v_cvt_pk_bf16_f32 v5, v13, v15
	v_cvt_pk_bf16_f32 v6, v17, v19
	v_cvt_pk_bf16_f32 v7, v21, v23
	v_or_b32_e32 v1, s8, v100
	v_lshlrev_b32_e32 v146, 9, v1
	ds_read2_b32 v[8:9], v97 offset0:32 offset1:40
	v_lshl_add_u64 v[10:11], v[2:3], 0, v[146:147]
	global_store_dwordx4 v[10:11], v[4:7], off nt
	ds_read2_b32 v[10:11], v97 offset0:97 offset1:105
	ds_read2_b32 v[12:13], v97 offset0:162 offset1:170
	ds_read2_b32 v[14:15], v97 offset0:227 offset1:235
	s_waitcnt lgkmcnt(3)
	s_waitcnt lgkmcnt(2)
	ds_read2_b32 v[16:17], v26 offset0:36 offset1:44
	ds_read2_b32 v[18:19], v26 offset0:101 offset1:109
	v_cvt_pk_bf16_f32 v4, v8, v10
	s_waitcnt lgkmcnt(3)
	s_waitcnt lgkmcnt(2)
	ds_read2_b32 v[20:21], v26 offset0:166 offset1:174
	ds_read2_b32 v[22:23], v26 offset0:231 offset1:239
	v_cvt_pk_bf16_f32 v5, v12, v14
	s_waitcnt lgkmcnt(3)
	s_waitcnt lgkmcnt(2)
	v_cvt_pk_bf16_f32 v6, v16, v18
	s_waitcnt lgkmcnt(1)
	s_waitcnt lgkmcnt(0)
	v_cvt_pk_bf16_f32 v7, v20, v22
	v_or_b32_e32 v1, s8, v101
	v_lshlrev_b32_e32 v146, 9, v1
	v_lshl_add_u64 v[24:25], v[2:3], 0, v[146:147]
	global_store_dwordx4 v[24:25], v[4:7], off nt
	s_nop 1
	v_cvt_pk_bf16_f32 v4, v9, v11
	v_cvt_pk_bf16_f32 v5, v13, v15
	v_cvt_pk_bf16_f32 v6, v17, v19
	v_cvt_pk_bf16_f32 v7, v21, v23
	v_or_b32_e32 v1, s8, v102
	v_lshlrev_b32_e32 v146, 9, v1
	ds_read2_b32 v[8:9], v97 offset0:48 offset1:56
	v_lshl_add_u64 v[10:11], v[2:3], 0, v[146:147]
	global_store_dwordx4 v[10:11], v[4:7], off nt
	ds_read2_b32 v[10:11], v97 offset0:113 offset1:121
	ds_read2_b32 v[12:13], v97 offset0:178 offset1:186
	ds_read2_b32 v[14:15], v97 offset0:243 offset1:251
	s_waitcnt lgkmcnt(3)
	s_waitcnt lgkmcnt(2)
	ds_read2_b32 v[16:17], v26 offset0:52 offset1:60
	ds_read2_b32 v[18:19], v26 offset0:117 offset1:125
	v_cvt_pk_bf16_f32 v4, v8, v10
	s_waitcnt lgkmcnt(3)
	s_waitcnt lgkmcnt(2)
	ds_read2_b32 v[20:21], v26 offset0:182 offset1:190
	ds_read2_b32 v[22:23], v26 offset0:247 offset1:255
	v_cvt_pk_bf16_f32 v5, v12, v14
	s_waitcnt lgkmcnt(3)
	s_waitcnt lgkmcnt(2)
	v_cvt_pk_bf16_f32 v6, v16, v18
	s_waitcnt lgkmcnt(1)
	s_waitcnt lgkmcnt(0)
	v_cvt_pk_bf16_f32 v7, v20, v22
	v_or_b32_e32 v1, s8, v103
	v_lshlrev_b32_e32 v146, 9, v1
	v_lshl_add_u64 v[24:25], v[2:3], 0, v[146:147]
	global_store_dwordx4 v[24:25], v[4:7], off nt
	s_nop 1
	v_cvt_pk_bf16_f32 v4, v9, v11
	v_cvt_pk_bf16_f32 v5, v13, v15
	v_cvt_pk_bf16_f32 v6, v17, v19
	v_cvt_pk_bf16_f32 v7, v21, v23
	v_or_b32_e32 v1, s8, v104
	v_lshlrev_b32_e32 v146, 9, v1
	v_lshl_add_u64 v[2:3], v[2:3], 0, v[146:147]
	global_store_dwordx4 v[2:3], v[4:7], off nt
	s_waitcnt lgkmcnt(0)

; #define LAS __attribute__((address_space(3)))
; __device__ __forceinline__ unsigned f2bf(float f) { unsigned u = __builtin_bit_cast(unsigned, f); return (u + 0x7fffu + ((u >> 16) & 1u)) >> 16; }
; __device__ __forceinline__ unsigned pk2(float lo, float hi) { return f2bf(lo) | (f2bf(hi) << 16); }
; __device__ __forceinline__ void tr_item(const float* W, int ldw, int k0, int n0, bf16* WT, int ldt, int drow0, LAS float* scr, int lane, const float* kscale = nullptr) {
;     ...
;     for (int i = 0; i < 16; ++i) { LAS float* q = wp + (4 * i) * 65; const float ks = kscale ? kscale[k0 + 4 * i + (lane >> 4)] : 1.f; q[0] = v[i].x * ks; q[1] = v[i].y * ks; q[2] = v[i].z * ks; q[3] = v[i].w * ks; }
;     asm volatile("s_waitcnt lgkmcnt(0)" ::: "memory");
;     const int kc = lane & 7;
; #pragma unroll
;     for (int j = 0; j < 8; ++j) { const int n = (lane >> 3) + 8 * j; const LAS float* sp = scr + (8 * kc) * 65 + n;
;         u32x4 o; o.x = pk2(sp[0 * 65], sp[1 * 65]); o.y = pk2(sp[2 * 65], sp[3 * 65]); o.z = pk2(sp[4 * 65], sp[5 * 65]); o.w = pk2(sp[6 * 65], sp[7 * 65]);
;         __builtin_nontemporal_store(o, (u32x4*)(WT + (size_t)(drow0 + n) * ldt + k0 + 8 * kc)); }
;     asm volatile("s_waitcnt lgkmcnt(0)" ::: "memory");
.LBB0_1644:
	s_waitcnt vmcnt(0)
	v_pk_mul_f32 v[2:3], v[2:3], v[10:11] op_sel_hi:[1,0]
	v_add_u32_e32 v1, 0x3cf0, v95
	ds_write2_b32 v1, v2, v3 offset1:1
	v_pk_mul_f32 v[2:3], v[4:5], v[10:11] op_sel_hi:[1,0]
	v_add_u32_e32 v1, 0x3cf8, v95
	ds_write2_b32 v1, v2, v3 offset1:1
	s_waitcnt lgkmcnt(0)
	ds_read2_b32 v[8:9], v97 offset1:8
	ds_read2_b32 v[10:11], v97 offset0:65 offset1:73
	ds_read2_b32 v[12:13], v97 offset0:130 offset1:138
	ds_read2_b32 v[14:15], v97 offset0:195 offset1:203
	v_add_u32_e32 v26, 0x400, v97
	s_waitcnt lgkmcnt(3)
	s_waitcnt lgkmcnt(2)
	ds_read2_b32 v[16:17], v26 offset0:4 offset1:12
	ds_read2_b32 v[18:19], v26 offset0:69 offset1:77
	v_cvt_pk_bf16_f32 v4, v8, v10
	s_waitcnt lgkmcnt(3)
	s_waitcnt lgkmcnt(2)
	ds_read2_b32 v[20:21], v26 offset0:134 offset1:142
	ds_read2_b32 v[22:23], v26 offset0:199 offset1:207
	v_cvt_pk_bf16_f32 v5, v12, v14
	s_waitcnt lgkmcnt(3)
	s_waitcnt lgkmcnt(2)
	v_cvt_pk_bf16_f32 v6, v16, v18
	s_waitcnt lgkmcnt(1)
	v_or_b32_e32 v24, s4, v96
	s_lshl_b32 s12, s8, 1
	s_waitcnt lgkmcnt(0)
	v_ashrrev_i32_e32 v25, 31, v24
	v_lshl_add_u64 v[2:3], v[88:89], 0, s[12:13]
	v_lshlrev_b64 v[24:25], 10, v[24:25]
	v_cvt_pk_bf16_f32 v7, v20, v22
	v_lshl_add_u64 v[24:25], v[2:3], 0, v[24:25]
	global_store_dwordx4 v[24:25], v[4:7], off nt
	s_nop 1
	v_cvt_pk_bf16_f32 v4, v9, v11
	v_cvt_pk_bf16_f32 v5, v13, v15
	v_cvt_pk_bf16_f32 v6, v17, v19
	v_or_b32_e32 v8, s4, v98
	v_ashrrev_i32_e32 v9, 31, v8
	v_lshlrev_b64 v[8:9], 10, v[8:9]
	v_cvt_pk_bf16_f32 v7, v21, v23
	ds_read2_b32 v[10:11], v97 offset0:16 offset1:24
	v_lshl_add_u64 v[8:9], v[2:3], 0, v[8:9]
	global_store_dwordx4 v[8:9], v[4:7], off nt
	ds_read2_b32 v[8:9], v97 offset0:81 offset1:89
	ds_read2_b32 v[12:13], v97 offset0:146 offset1:154
	ds_read2_b32 v[14:15], v97 offset0:211 offset1:219
	s_waitcnt lgkmcnt(3)
	s_waitcnt lgkmcnt(2)
	ds_read2_b32 v[16:17], v26 offset0:20 offset1:28
	ds_read2_b32 v[18:19], v26 offset0:85 offset1:93
	v_cvt_pk_bf16_f32 v4, v10, v8
	s_waitcnt lgkmcnt(3)
	s_waitcnt lgkmcnt(2)
	ds_read2_b32 v[20:21], v26 offset0:150 offset1:158
	ds_read2_b32 v[22:23], v26 offset0:215 offset1:223
	v_cvt_pk_bf16_f32 v5, v12, v14
	s_waitcnt lgkmcnt(3)
	s_waitcnt lgkmcnt(2)
	v_cvt_pk_bf16_f32 v6, v16, v18
	s_waitcnt lgkmcnt(1)
	v_or_b32_e32 v24, s4, v99
	s_waitcnt lgkmcnt(0)
	v_ashrrev_i32_e32 v25, 31, v24
	v_lshlrev_b64 v[24:25], 10, v[24:25]
	v_cvt_pk_bf16_f32 v7, v20, v22
	v_lshl_add_u64 v[24:25], v[2:3], 0, v[24:25]
	global_store_dwordx4 v[24:25], v[4:7], off nt
	s_nop 1
	v_cvt_pk_bf16_f32 v4, v11, v9
	v_cvt_pk_bf16_f32 v5, v13, v15
	v_cvt_pk_bf16_f32 v6, v17, v19
	v_or_b32_e32 v8, s4, v100
	v_ashrrev_i32_e32 v9, 31, v8
	v_lshlrev_b64 v[8:9], 10, v[8:9]
	v_cvt_pk_bf16_f32 v7, v21, v23
	ds_read2_b32 v[10:11], v97 offset0:32 offset1:40
	v_lshl_add_u64 v[8:9], v[2:3], 0, v[8:9]
	global_store_dwordx4 v[8:9], v[4:7], off nt
	ds_read2_b32 v[8:9], v97 offset0:97 offset1:105
	ds_read2_b32 v[12:13], v97 offset0:162 offset1:170
	ds_read2_b32 v[14:15], v97 offset0:227 offset1:235
	s_waitcnt lgkmcnt(3)
	s_waitcnt lgkmcnt(2)
	ds_read2_b32 v[16:17], v26 offset0:36 offset1:44
	ds_read2_b32 v[18:19], v26 offset0:101 offset1:109
	v_cvt_pk_bf16_f32 v4, v10, v8
	s_waitcnt lgkmcnt(3)
	s_waitcnt lgkmcnt(2)
	ds_read2_b32 v[20:21], v26 offset0:166 offset1:174
	ds_read2_b32 v[22:23], v26 offset0:231 offset1:239
	v_cvt_pk_bf16_f32 v5, v12, v14
	s_waitcnt lgkmcnt(3)
	s_waitcnt lgkmcnt(2)
	v_cvt_pk_bf16_f32 v6, v16, v18
	s_waitcnt lgkmcnt(1)
	v_or_b32_e32 v24, s4, v101
	s_waitcnt lgkmcnt(0)
	v_ashrrev_i32_e32 v25, 31, v24
	v_lshlrev_b64 v[24:25], 10, v[24:25]
	v_cvt_pk_bf16_f32 v7, v20, v22
	v_lshl_add_u64 v[24:25], v[2:3], 0, v[24:25]
	global_store_dwordx4 v[24:25], v[4:7], off nt
	s_nop 1
	v_cvt_pk_bf16_f32 v4, v11, v9
	v_cvt_pk_bf16_f32 v5, v13, v15
	v_cvt_pk_bf16_f32 v6, v17, v19
	v_or_b32_e32 v8, s4, v102
	v_ashrrev_i32_e32 v9, 31, v8
	v_lshlrev_b64 v[8:9], 10, v[8:9]
	v_cvt_pk_bf16_f32 v7, v21, v23
	ds_read2_b32 v[10:11], v97 offset0:48 offset1:56
	v_lshl_add_u64 v[8:9], v[2:3], 0, v[8:9]
	global_store_dwordx4 v[8:9], v[4:7], off nt
	ds_read2_b32 v[8:9], v97 offset0:113 offset1:121
	ds_read2_b32 v[12:13], v97 offset0:178 offset1:186
	ds_read2_b32 v[14:15], v97 offset0:243 offset1:251
	s_waitcnt lgkmcnt(3)
	s_waitcnt lgkmcnt(2)
	ds_read2_b32 v[16:17], v26 offset0:52 offset1:60
	ds_read2_b32 v[18:19], v26 offset0:117 offset1:125
	v_cvt_pk_bf16_f32 v4, v10, v8
	s_waitcnt lgkmcnt(3)
	s_waitcnt lgkmcnt(2)
	ds_read2_b32 v[20:21], v26 offset0:182 offset1:190
	ds_read2_b32 v[22:23], v26 offset0:247 offset1:255
	v_cvt_pk_bf16_f32 v5, v12, v14
	s_waitcnt lgkmcnt(3)
	s_waitcnt lgkmcnt(2)
	v_cvt_pk_bf16_f32 v6, v16, v18
	s_waitcnt lgkmcnt(1)
	v_or_b32_e32 v24, s4, v103
	s_waitcnt lgkmcnt(0)
	v_ashrrev_i32_e32 v25, 31, v24
	v_lshlrev_b64 v[24:25], 10, v[24:25]
	v_cvt_pk_bf16_f32 v7, v20, v22
	v_lshl_add_u64 v[24:25], v[2:3], 0, v[24:25]
	global_store_dwordx4 v[24:25], v[4:7], off nt
	s_nop 1
	v_cvt_pk_bf16_f32 v4, v11, v9
	v_cvt_pk_bf16_f32 v5, v13, v15
	v_cvt_pk_bf16_f32 v6, v17, v19
	v_or_b32_e32 v8, s4, v104
	v_ashrrev_i32_e32 v9, 31, v8
	v_lshlrev_b64 v[8:9], 10, v[8:9]
	v_cvt_pk_bf16_f32 v7, v21, v23
	v_lshl_add_u64 v[2:3], v[2:3], 0, v[8:9]
	global_store_dwordx4 v[2:3], v[4:7], off nt
	s_waitcnt lgkmcnt(0)

; #define LAS __attribute__((address_space(3)))
; #define WSW(T, off, l) WSP(T, WS_WSET + (size_t)(l) * WSET_STRIDE + (off))
; __device__ __forceinline__ void tr_item(const float* W, int ldw, int k0, int n0, bf16* WT, int ldt, int drow0, LAS float* scr, int lane, const float* kscale = nullptr) {
;     const float* src = W + (size_t)(k0 + (lane >> 4)) * ldw + n0 + (lane & 15) * 4;
;     f32x4 v[16];
; #pragma unroll
;     for (int i = 0; i < 16; ++i) v[i] = __builtin_nontemporal_load((const f32x4*)(src + (size_t)(4 * i) * ldw));
;     LAS float* wp = scr + (lane >> 4) * 65 + (lane & 15) * 4;
; #pragma unroll
;     for (int i = 0; i < 16; ++i) { LAS float* q = wp + (4 * i) * 65; const float ks = kscale ? kscale[k0 + 4 * i + (lane >> 4)] : 1.f; q[0] = v[i].x * ks; q[1] = v[i].y * ks; q[2] = v[i].z * ks; q[3] = v[i].w * ks; }
;     asm volatile("s_waitcnt lgkmcnt(0)" ::: "memory");
; __device__ __forceinline__ void convert_tile(const Args& a, GAS unsigned char* wsb, int l, int t, LAS float* scr, int lane) {
;     ...
;     if (r < I_IN) { const int kb = r / 45, nb = r - kb * 45; tr_item(INP(7) + (size_t)l * DM * INW, INW, kb * 64, nb * 64, WSW(bf16, W_IN, l), DM, nb * 64, scr, lane); return; }
.LBB0_1646:
	s_andn2_b64 vcc, exec, s[4:5]
	s_cbranch_vccnz .LBB0_1495
	s_mul_hi_i32 s4, s15, 0xb60b60b7
	s_add_i32 s4, s4, s15
	s_lshr_b32 s5, s4, 31
	s_ashr_i32 s4, s4, 5
	s_add_i32 s4, s4, s5
	s_mul_i32 s5, s4, 0xffffffd3
	v_readlane_b32 s40, v253, 52
	s_add_i32 s5, s5, s15
	s_lshl_b32 s6, s4, 6
	v_readlane_b32 s54, v254, 2
	v_readlane_b32 s55, v254, 3
	s_lshl_b32 s4, s5, 6
	v_or_b32_e32 v1, s6, v67
	v_mov_b64_e32 v[2:3], s[54:55]
	s_movk_i32 s5, 0x2d00
	v_mad_i64_i32 v[2:3], s[8:9], v1, s5, v[2:3]
	s_ashr_i32 s5, s4, 31
	v_lshl_add_u64 v[2:3], s[4:5], 2, v[2:3]
	v_lshlrev_b32_e32 v146, 2, v66
	v_lshl_add_u64 v[62:63], v[2:3], 0, v[146:147]
	s_mov_b32 s5, 0xb000
	v_add_co_u32_e32 v6, vcc, s5, v62
	s_mov_b32 s5, 0x16000
	s_nop 0
	v_addc_co_u32_e32 v7, vcc, 0, v63, vcc
	v_add_co_u32_e32 v10, vcc, s5, v62
	global_load_dwordx4 v[2:5], v[62:63], off nt
	s_nop 0
	global_load_dwordx4 v[6:9], v[6:7], off offset:1024 nt
	v_addc_co_u32_e32 v11, vcc, 0, v63, vcc
	s_mov_b32 s5, 0x21000
	v_add_co_u32_e32 v14, vcc, s5, v62
	s_mov_b32 s5, 0x2d000
	s_nop 0
	v_addc_co_u32_e32 v15, vcc, 0, v63, vcc
	global_load_dwordx4 v[10:13], v[10:11], off offset:2048 nt
	s_nop 0
	global_load_dwordx4 v[14:17], v[14:15], off offset:3072 nt
	v_add_co_u32_e32 v18, vcc, s5, v62
	s_mov_b32 s5, 0x38000
	s_nop 0
	v_addc_co_u32_e32 v19, vcc, 0, v63, vcc
	v_add_co_u32_e32 v22, vcc, s5, v62
	s_mov_b32 s5, 0x43000
	s_nop 0
	v_addc_co_u32_e32 v23, vcc, 0, v63, vcc
	global_load_dwordx4 v[18:21], v[18:19], off nt
	s_nop 0
	global_load_dwordx4 v[22:25], v[22:23], off offset:1024 nt
	v_add_co_u32_e32 v26, vcc, s5, v62
	s_mov_b32 s5, 0x4e000
	s_nop 0
	v_addc_co_u32_e32 v27, vcc, 0, v63, vcc
	v_add_co_u32_e32 v30, vcc, s5, v62
	s_mov_b32 s5, 0x5a000
	s_nop 0
	v_addc_co_u32_e32 v31, vcc, 0, v63, vcc
	global_load_dwordx4 v[26:29], v[26:27], off offset:2048 nt
	s_nop 0
	global_load_dwordx4 v[30:33], v[30:31], off offset:3072 nt
	v_add_co_u32_e32 v34, vcc, s5, v62
	s_mov_b32 s5, 0x65000
	s_nop 0
	v_addc_co_u32_e32 v35, vcc, 0, v63, vcc
	v_add_co_u32_e32 v38, vcc, s5, v62
	s_mov_b32 s5, 0x70000
	s_nop 0
	v_addc_co_u32_e32 v39, vcc, 0, v63, vcc
	global_load_dwordx4 v[34:37], v[34:35], off nt
	s_nop 0
	global_load_dwordx4 v[38:41], v[38:39], off offset:1024 nt
	v_add_co_u32_e32 v42, vcc, s5, v62
	s_mov_b32 s5, 0x7b000
	s_nop 0
	v_addc_co_u32_e32 v43, vcc, 0, v63, vcc
	v_add_co_u32_e32 v46, vcc, s5, v62
	s_mov_b32 s5, 0x87000
	s_nop 0
	v_addc_co_u32_e32 v47, vcc, 0, v63, vcc
	global_load_dwordx4 v[42:45], v[42:43], off offset:2048 nt
	s_nop 0
	global_load_dwordx4 v[46:49], v[46:47], off offset:3072 nt
	v_add_co_u32_e32 v50, vcc, s5, v62
	s_mov_b32 s5, 0x92000
	s_nop 0
	v_addc_co_u32_e32 v51, vcc, 0, v63, vcc
	global_load_dwordx4 v[50:53], v[50:51], off nt
	v_add_co_u32_e32 v54, vcc, s5, v62
	s_mov_b32 s5, 0x9d000
	s_nop 0
	v_addc_co_u32_e32 v55, vcc, 0, v63, vcc
	global_load_dwordx4 v[54:57], v[54:55], off offset:1024 nt
	v_add_co_u32_e32 v58, vcc, s5, v62
	s_mov_b32 s5, 0xa8000
	s_nop 0
	v_addc_co_u32_e32 v59, vcc, 0, v63, vcc
	global_load_dwordx4 v[58:61], v[58:59], off offset:2048 nt
	v_add_co_u32_e32 v62, vcc, s5, v62
	v_add_u32_e32 v1, 0x410, v95
	s_nop 0
	v_addc_co_u32_e32 v63, vcc, 0, v63, vcc
	global_load_dwordx4 v[62:65], v[62:63], off offset:3072 nt
	s_waitcnt vmcnt(15)
	ds_write2_b32 v95, v2, v3 offset1:1
	ds_write2_b32 v95, v4, v5 offset0:2 offset1:3
	s_waitcnt vmcnt(14)
	ds_write2_b32 v1, v6, v7 offset1:1
	v_add_u32_e32 v1, 0x418, v95
	ds_write2_b32 v1, v8, v9 offset1:1
	v_add_u32_e32 v1, 0x820, v95
	s_ashr_i32 s7, s6, 31
	v_lshl_add_u64 v[2:3], s[6:7], 1, v[90:91]
	v_readlane_b32 s48, v253, 60
	v_readlane_b32 s49, v253, 61
	s_waitcnt vmcnt(13)
	ds_write2_b32 v1, v10, v11 offset1:1
	v_add_u32_e32 v1, 0x828, v95
	ds_write2_b32 v1, v12, v13 offset1:1
	v_add_u32_e32 v1, 0xc30, v95
	s_waitcnt vmcnt(12)
	ds_write2_b32 v1, v14, v15 offset1:1
	v_add_u32_e32 v1, 0xc38, v95
	ds_write2_b32 v1, v16, v17 offset1:1
	v_add_u32_e32 v1, 0x1040, v95
	v_readlane_b32 s50, v253, 62
	v_readlane_b32 s51, v253, 63
	v_readlane_b32 s52, v254, 0
	s_waitcnt vmcnt(11)
	ds_write2_b32 v1, v18, v19 offset1:1
	v_add_u32_e32 v1, 0x1048, v95
	ds_write2_b32 v1, v20, v21 offset1:1
	v_add_u32_e32 v1, 0x1450, v95
	s_waitcnt vmcnt(10)
	ds_write2_b32 v1, v22, v23 offset1:1
	v_add_u32_e32 v1, 0x1458, v95
	ds_write2_b32 v1, v24, v25 offset1:1
	v_add_u32_e32 v1, 0x1860, v95
	v_or_b32_e32 v24, s4, v96
	v_ashrrev_i32_e32 v25, 31, v24
	v_lshlrev_b64 v[24:25], 12, v[24:25]
	s_waitcnt vmcnt(9)
	ds_write2_b32 v1, v26, v27 offset1:1
	v_add_u32_e32 v1, 0x1868, v95
	ds_write2_b32 v1, v28, v29 offset1:1
	v_add_u32_e32 v1, 0x1c70, v95
	s_waitcnt vmcnt(8)
	ds_write2_b32 v1, v30, v31 offset1:1
	v_add_u32_e32 v1, 0x1c78, v95
	ds_write2_b32 v1, v32, v33 offset1:1
	v_add_u32_e32 v1, 0x2080, v95
	v_add_u32_e32 v26, 0x400, v97
	v_lshl_add_u64 v[24:25], v[2:3], 0, v[24:25]
	v_readlane_b32 s53, v254, 1
	s_waitcnt vmcnt(7)
	ds_write2_b32 v1, v34, v35 offset1:1
	v_add_u32_e32 v1, 0x2088, v95
	ds_write2_b32 v1, v36, v37 offset1:1
	v_add_u32_e32 v1, 0x2490, v95
	s_waitcnt vmcnt(6)
	ds_write2_b32 v1, v38, v39 offset1:1
	v_add_u32_e32 v1, 0x2498, v95
	ds_write2_b32 v1, v40, v41 offset1:1
	v_add_u32_e32 v1, 0x28a0, v95
	v_readlane_b32 s48, v254, 35
	v_readlane_b32 s49, v254, 36
	v_readlane_b32 s50, v254, 37
	s_waitcnt vmcnt(5)
	ds_write2_b32 v1, v42, v43 offset1:1
	v_add_u32_e32 v1, 0x28a8, v95
	ds_write2_b32 v1, v44, v45 offset1:1
	v_add_u32_e32 v1, 0x2cb0, v95
	s_waitcnt vmcnt(4)
	ds_write2_b32 v1, v46, v47 offset1:1
	v_add_u32_e32 v1, 0x2cb8, v95
	ds_write2_b32 v1, v48, v49 offset1:1
	v_add_u32_e32 v1, 0x30c0, v95
	s_waitcnt vmcnt(3)
; #define LAS __attribute__((address_space(3)))
; __device__ __forceinline__ unsigned f2bf(float f) { unsigned u = __builtin_bit_cast(unsigned, f); return (u + 0x7fffu + ((u >> 16) & 1u)) >> 16; }
; __device__ __forceinline__ unsigned pk2(float lo, float hi) { return f2bf(lo) | (f2bf(hi) << 16); }
; __device__ __forceinline__ void tr_item(const float* W, int ldw, int k0, int n0, bf16* WT, int ldt, int drow0, LAS float* scr, int lane, const float* kscale = nullptr) {
;     ...
;     const int kc = lane & 7;
; #pragma unroll
;     for (int j = 0; j < 8; ++j) { const int n = (lane >> 3) + 8 * j; const LAS float* sp = scr + (8 * kc) * 65 + n;
;         u32x4 o; o.x = pk2(sp[0 * 65], sp[1 * 65]); o.y = pk2(sp[2 * 65], sp[3 * 65]); o.z = pk2(sp[4 * 65], sp[5 * 65]); o.w = pk2(sp[6 * 65], sp[7 * 65]);
;         __builtin_nontemporal_store(o, (u32x4*)(WT + (size_t)(drow0 + n) * ldt + k0 + 8 * kc)); }
;     asm volatile("s_waitcnt lgkmcnt(0)" ::: "memory");
	ds_write2_b32 v1, v50, v51 offset1:1
	v_add_u32_e32 v1, 0x30c8, v95
	ds_write2_b32 v1, v52, v53 offset1:1
	v_add_u32_e32 v1, 0x34d0, v95
	v_readlane_b32 s51, v254, 38
	s_waitcnt vmcnt(2)
	ds_write2_b32 v1, v54, v55 offset1:1
	v_add_u32_e32 v1, 0x34d8, v95
	ds_write2_b32 v1, v56, v57 offset1:1
	v_add_u32_e32 v1, 0x38e0, v95
	v_readlane_b32 s52, v254, 39
	v_readlane_b32 s53, v254, 40
	s_waitcnt vmcnt(1)
	ds_write2_b32 v1, v58, v59 offset1:1
	v_add_u32_e32 v1, 0x38e8, v95
	ds_write2_b32 v1, v60, v61 offset1:1
	v_add_u32_e32 v1, 0x3cf0, v95
	v_readlane_b32 s54, v254, 41
	v_readlane_b32 s55, v254, 42
	s_waitcnt vmcnt(0)
	ds_write2_b32 v1, v62, v63 offset1:1
	v_add_u32_e32 v1, 0x3cf8, v95
	ds_write2_b32 v1, v64, v65 offset1:1
	s_waitcnt lgkmcnt(0)
	ds_read2_b32 v[8:9], v97 offset1:8
	ds_read2_b32 v[10:11], v97 offset0:65 offset1:73
	ds_read2_b32 v[12:13], v97 offset0:130 offset1:138
	ds_read2_b32 v[14:15], v97 offset0:195 offset1:203
	ds_read2_b32 v[16:17], v26 offset0:4 offset1:12
	s_waitcnt lgkmcnt(4)
	s_waitcnt lgkmcnt(3)
	ds_read2_b32 v[18:19], v26 offset0:69 offset1:77
	v_cvt_pk_bf16_f32 v4, v8, v10
	s_waitcnt lgkmcnt(3)
	s_waitcnt lgkmcnt(2)
	ds_read2_b32 v[20:21], v26 offset0:134 offset1:142
	ds_read2_b32 v[22:23], v26 offset0:199 offset1:207
	v_cvt_pk_bf16_f32 v5, v12, v14
	s_waitcnt lgkmcnt(3)
	s_waitcnt lgkmcnt(2)
	v_cvt_pk_bf16_f32 v6, v16, v18
	s_waitcnt lgkmcnt(1)
	s_waitcnt lgkmcnt(0)
	v_cvt_pk_bf16_f32 v7, v20, v22
	global_store_dwordx4 v[24:25], v[4:7], off nt
	s_nop 1
	v_cvt_pk_bf16_f32 v4, v9, v11
	v_cvt_pk_bf16_f32 v5, v13, v15
	v_cvt_pk_bf16_f32 v6, v17, v19
	v_or_b32_e32 v8, s4, v98
	v_ashrrev_i32_e32 v9, 31, v8
	v_lshlrev_b64 v[8:9], 12, v[8:9]
	v_cvt_pk_bf16_f32 v7, v21, v23
	ds_read2_b32 v[10:11], v97 offset0:16 offset1:24
	v_lshl_add_u64 v[8:9], v[2:3], 0, v[8:9]
	global_store_dwordx4 v[8:9], v[4:7], off nt
	ds_read2_b32 v[8:9], v97 offset0:81 offset1:89
	ds_read2_b32 v[12:13], v97 offset0:146 offset1:154
	ds_read2_b32 v[14:15], v97 offset0:211 offset1:219
	s_waitcnt lgkmcnt(3)
	s_waitcnt lgkmcnt(2)
	ds_read2_b32 v[16:17], v26 offset0:20 offset1:28
	ds_read2_b32 v[18:19], v26 offset0:85 offset1:93
	v_cvt_pk_bf16_f32 v4, v10, v8
	s_waitcnt lgkmcnt(3)
	s_waitcnt lgkmcnt(2)
	ds_read2_b32 v[20:21], v26 offset0:150 offset1:158
	ds_read2_b32 v[22:23], v26 offset0:215 offset1:223
	v_cvt_pk_bf16_f32 v5, v12, v14
	s_waitcnt lgkmcnt(3)
	s_waitcnt lgkmcnt(2)
	v_cvt_pk_bf16_f32 v6, v16, v18
	s_waitcnt lgkmcnt(1)
	v_or_b32_e32 v24, s4, v99
	s_waitcnt lgkmcnt(0)
	v_ashrrev_i32_e32 v25, 31, v24
	v_lshlrev_b64 v[24:25], 12, v[24:25]
	v_cvt_pk_bf16_f32 v7, v20, v22
	v_lshl_add_u64 v[24:25], v[2:3], 0, v[24:25]
	global_store_dwordx4 v[24:25], v[4:7], off nt
	s_nop 1
	v_cvt_pk_bf16_f32 v4, v11, v9
	v_cvt_pk_bf16_f32 v5, v13, v15
	v_cvt_pk_bf16_f32 v6, v17, v19
	v_or_b32_e32 v8, s4, v100
	v_ashrrev_i32_e32 v9, 31, v8
	v_lshlrev_b64 v[8:9], 12, v[8:9]
	v_cvt_pk_bf16_f32 v7, v21, v23
	ds_read2_b32 v[10:11], v97 offset0:32 offset1:40
	v_lshl_add_u64 v[8:9], v[2:3], 0, v[8:9]
	global_store_dwordx4 v[8:9], v[4:7], off nt
	ds_read2_b32 v[8:9], v97 offset0:97 offset1:105
	ds_read2_b32 v[12:13], v97 offset0:162 offset1:170
	ds_read2_b32 v[14:15], v97 offset0:227 offset1:235
	s_waitcnt lgkmcnt(3)
	s_waitcnt lgkmcnt(2)
	ds_read2_b32 v[16:17], v26 offset0:36 offset1:44
	ds_read2_b32 v[18:19], v26 offset0:101 offset1:109
	v_cvt_pk_bf16_f32 v4, v10, v8
	s_waitcnt lgkmcnt(3)
	s_waitcnt lgkmcnt(2)
	ds_read2_b32 v[20:21], v26 offset0:166 offset1:174
	ds_read2_b32 v[22:23], v26 offset0:231 offset1:239
	v_cvt_pk_bf16_f32 v5, v12, v14
	s_waitcnt lgkmcnt(3)
	s_waitcnt lgkmcnt(2)
	v_cvt_pk_bf16_f32 v6, v16, v18
	s_waitcnt lgkmcnt(1)
	v_or_b32_e32 v24, s4, v101
	s_waitcnt lgkmcnt(0)
	v_ashrrev_i32_e32 v25, 31, v24
	v_lshlrev_b64 v[24:25], 12, v[24:25]
	v_cvt_pk_bf16_f32 v7, v20, v22
	v_lshl_add_u64 v[24:25], v[2:3], 0, v[24:25]
	global_store_dwordx4 v[24:25], v[4:7], off nt
	s_nop 1
	v_cvt_pk_bf16_f32 v4, v11, v9
	v_cvt_pk_bf16_f32 v5, v13, v15
	v_cvt_pk_bf16_f32 v6, v17, v19
	v_or_b32_e32 v8, s4, v102
	v_ashrrev_i32_e32 v9, 31, v8
	v_lshlrev_b64 v[8:9], 12, v[8:9]
	v_cvt_pk_bf16_f32 v7, v21, v23
	ds_read2_b32 v[10:11], v97 offset0:48 offset1:56
	v_lshl_add_u64 v[8:9], v[2:3], 0, v[8:9]
	global_store_dwordx4 v[8:9], v[4:7], off nt
	ds_read2_b32 v[8:9], v97 offset0:113 offset1:121
	ds_read2_b32 v[12:13], v97 offset0:178 offset1:186
	ds_read2_b32 v[14:15], v97 offset0:243 offset1:251
	s_waitcnt lgkmcnt(3)
	s_waitcnt lgkmcnt(2)
	ds_read2_b32 v[16:17], v26 offset0:52 offset1:60
	ds_read2_b32 v[18:19], v26 offset0:117 offset1:125
	v_cvt_pk_bf16_f32 v4, v10, v8
	s_waitcnt lgkmcnt(3)
	s_waitcnt lgkmcnt(2)
	ds_read2_b32 v[20:21], v26 offset0:182 offset1:190
	ds_read2_b32 v[22:23], v26 offset0:247 offset1:255
	v_cvt_pk_bf16_f32 v5, v12, v14
	s_waitcnt lgkmcnt(3)
	s_waitcnt lgkmcnt(2)
	v_cvt_pk_bf16_f32 v6, v16, v18
	s_waitcnt lgkmcnt(1)
	v_or_b32_e32 v24, s4, v103
	s_waitcnt lgkmcnt(0)
	v_ashrrev_i32_e32 v25, 31, v24
	v_lshlrev_b64 v[24:25], 12, v[24:25]
	v_cvt_pk_bf16_f32 v7, v20, v22
	v_lshl_add_u64 v[24:25], v[2:3], 0, v[24:25]
	global_store_dwordx4 v[24:25], v[4:7], off nt
	s_nop 1
	v_cvt_pk_bf16_f32 v4, v11, v9
	v_cvt_pk_bf16_f32 v5, v13, v15
	v_cvt_pk_bf16_f32 v6, v17, v19
	v_or_b32_e32 v8, s4, v104
	v_ashrrev_i32_e32 v9, 31, v8
	v_lshlrev_b64 v[8:9], 12, v[8:9]
	v_cvt_pk_bf16_f32 v7, v21, v23
	v_lshl_add_u64 v[2:3], v[2:3], 0, v[8:9]
	global_store_dwordx4 v[2:3], v[4:7], off nt
	s_waitcnt lgkmcnt(0)
	v_readlane_b32 s58, v254, 45
	v_readlane_b32 s59, v254, 46
	v_readlane_b32 s60, v254, 47
	v_readlane_b32 s61, v254, 48
	v_readlane_b32 s62, v254, 49
	v_readlane_b32 s63, v254, 50
	v_readlane_b32 s41, v253, 53
	v_readlane_b32 s42, v253, 54
	v_readlane_b32 s43, v253, 55
	v_readlane_b32 s44, v253, 56
	v_readlane_b32 s45, v253, 57
	v_readlane_b32 s46, v253, 58
	v_readlane_b32 s47, v253, 59
	v_readlane_b32 s56, v254, 43
	v_readlane_b32 s57, v254, 44
	s_branch .LBB0_1495

; __device__ __forceinline__ unsigned f2bf(float f) { unsigned u = __builtin_bit_cast(unsigned, f); return (u + 0x7fffu + ((u >> 16) & 1u)) >> 16; }
; __device__ __forceinline__ unsigned pk2(float lo, float hi) { return f2bf(lo) | (f2bf(hi) << 16); }
;     __device__ __forceinline__ void epi(const f32x4 (&acc)[2][2][4][2], const Unit& u, int wr, int wc, int fr, int fq) const {
;     ...
;                     const f32x4 g0 = *(const f32x4*)(g1 + cofs * 4 + lcol * 4), g1v = *(const f32x4*)(g1 + cofs * 4 + lcol * 4 + 16);
;                     f32x4 x0, x1v;
;                     if (f32in) { x0 = *(const f32x4*)(xin + (ro + cofs) * 4 + loff4); x1v = *(const f32x4*)(xin + (ro + cofs) * 4 + loff4 + 16); }
;                     else { const u32x4 w = *(const u32x4*)(xin + (ro + cofs) * 2 + loff2); x0 = (f32x4){bflo(w.x), bfhi(w.x), bflo(w.y), bfhi(w.y)}; x1v = (f32x4){bflo(w.z), bfhi(w.z), bflo(w.w), bfhi(w.w)}; }
;                     const f32x4 o0 = x0 + g0 * acc[ai][bj][m][0], o1 = x1v + g1v * acc[ai][bj][m][1];
;                     u32x4 ow; ow.x = pk2(o0[0], o0[1]); ow.y = pk2(o0[2], o0[3]); ow.z = pk2(o1[0], o1[1]); ow.w = pk2(o1[2], o1[3]);
;                     *(u32x4*)(xo + (ro + cofs) * 2 + loff2) = ow; }
.LBB0_1779:
	s_waitcnt vmcnt(0)
	v_pk_fma_f32 v[126:127], v[126:127], v[134:135], v[142:143]
	v_pk_fma_f32 v[132:133], v[124:125], v[132:133], v[140:141]
	v_pk_fma_f32 v[124:125], v[122:123], v[130:131], v[138:139]
	v_pk_fma_f32 v[128:129], v[128:129], v[136:137], v[144:145]
	v_cvt_pk_bf16_f32 v122, v126, v127
	v_cvt_pk_bf16_f32 v123, v128, v129
	v_bfe_u32 v1, v124, 16, 1
	v_add3_u32 v1, v124, v1, s37
	v_bfe_u32 v124, v125, 16, 1
	s_add_u32 s12, s69, s42
	v_lshrrev_b32_e32 v1, 16, v1
	v_add3_u32 v124, v125, v124, s37
	s_addc_u32 s17, s70, s43
	v_and_or_b32 v124, v124, s33, v1
	s_add_u32 s24, s12, s44
	s_addc_u32 s25, s17, s45
	v_lshl_add_u64 v[160:161], s[24:25], 0, v[146:147]
	v_cvt_pk_bf16_f32 v125, v132, v133
	global_store_dwordx4 v[160:161], v[122:125], off
	global_load_dwordx4 v[122:125], v[164:165], off offset:528
	s_nop 0
	global_load_dwordx4 v[126:129], v[164:165], off offset:512
	s_and_b64 vcc, exec, s[40:41]
	s_cbranch_vccnz .LBB0_1830
	global_load_dwordx4 v[130:133], v[162:163], off offset:528
	global_load_dwordx4 v[134:137], v[162:163], off offset:512
	s_cbranch_execnz .LBB0_1782

; __device__ __forceinline__ unsigned f2bf(float f) { unsigned u = __builtin_bit_cast(unsigned, f); return (u + 0x7fffu + ((u >> 16) & 1u)) >> 16; }
; __device__ __forceinline__ unsigned pk2(float lo, float hi) { return f2bf(lo) | (f2bf(hi) << 16); }
;     __device__ __forceinline__ void epi(const f32x4 (&acc)[2][2][4][2], const Unit& u, int wr, int wc, int fr, int fq) const {
;     ...
;                     const f32x4 g0 = *(const f32x4*)(g1 + cofs * 4 + lcol * 4), g1v = *(const f32x4*)(g1 + cofs * 4 + lcol * 4 + 16);
;                     f32x4 x0, x1v;
;                     if (f32in) { x0 = *(const f32x4*)(xin + (ro + cofs) * 4 + loff4); x1v = *(const f32x4*)(xin + (ro + cofs) * 4 + loff4 + 16); }
;                     else { const u32x4 w = *(const u32x4*)(xin + (ro + cofs) * 2 + loff2); x0 = (f32x4){bflo(w.x), bfhi(w.x), bflo(w.y), bfhi(w.y)}; x1v = (f32x4){bflo(w.z), bfhi(w.z), bflo(w.w), bfhi(w.w)}; }
;                     const f32x4 o0 = x0 + g0 * acc[ai][bj][m][0], o1 = x1v + g1v * acc[ai][bj][m][1];
;                     u32x4 ow; ow.x = pk2(o0[0], o0[1]); ow.y = pk2(o0[2], o0[3]); ow.z = pk2(o1[0], o1[1]); ow.w = pk2(o1[2], o1[3]);
;                     *(u32x4*)(xo + (ro + cofs) * 2 + loff2) = ow; }
.LBB0_1782:
	s_waitcnt vmcnt(0)
	v_pk_fma_f32 v[118:119], v[118:119], v[126:127], v[134:135]
	v_pk_fma_f32 v[124:125], v[116:117], v[124:125], v[132:133]
	v_pk_fma_f32 v[116:117], v[114:115], v[122:123], v[130:131]
	v_pk_fma_f32 v[120:121], v[120:121], v[128:129], v[136:137]
	v_cvt_pk_bf16_f32 v114, v118, v119
	v_cvt_pk_bf16_f32 v115, v120, v121
	v_bfe_u32 v1, v116, 16, 1
	v_add3_u32 v1, v116, v1, s37
	v_bfe_u32 v116, v117, 16, 1
	v_lshrrev_b32_e32 v1, 16, v1
	v_add3_u32 v116, v117, v116, s37
	v_and_or_b32 v116, v116, s33, v1
	v_cvt_pk_bf16_f32 v117, v124, v125
	global_store_dwordx4 v[160:161], v[114:117], off offset:256
	global_load_dwordx4 v[114:117], v[164:165], off offset:16
	global_load_dwordx4 v[118:121], v[164:165], off
	s_and_b64 vcc, exec, s[40:41]
	s_cbranch_vccnz .LBB0_1831
	s_mov_b64 s[24:25], 0x20000
	v_add_co_u32_e32 v124, vcc, 0x20000, v162
	v_lshl_add_u64 v[122:123], v[162:163], 0, s[24:25]
	s_nop 0
	v_addc_co_u32_e32 v125, vcc, 0, v163, vcc
	global_load_dwordx4 v[126:129], v[124:125], off
	s_nop 0
	global_load_dwordx4 v[122:125], v[122:123], off offset:16
	s_cbranch_execnz .LBB0_1785

; __device__ __forceinline__ unsigned f2bf(float f) { unsigned u = __builtin_bit_cast(unsigned, f); return (u + 0x7fffu + ((u >> 16) & 1u)) >> 16; }
; __device__ __forceinline__ unsigned pk2(float lo, float hi) { return f2bf(lo) | (f2bf(hi) << 16); }
;     __device__ __forceinline__ void epi(const f32x4 (&acc)[2][2][4][2], const Unit& u, int wr, int wc, int fr, int fq) const {
;     ...
;                     const f32x4 g0 = *(const f32x4*)(g1 + cofs * 4 + lcol * 4), g1v = *(const f32x4*)(g1 + cofs * 4 + lcol * 4 + 16);
;                     f32x4 x0, x1v;
;                     if (f32in) { x0 = *(const f32x4*)(xin + (ro + cofs) * 4 + loff4); x1v = *(const f32x4*)(xin + (ro + cofs) * 4 + loff4 + 16); }
;                     else { const u32x4 w = *(const u32x4*)(xin + (ro + cofs) * 2 + loff2); x0 = (f32x4){bflo(w.x), bfhi(w.x), bflo(w.y), bfhi(w.y)}; x1v = (f32x4){bflo(w.z), bfhi(w.z), bflo(w.w), bfhi(w.w)}; }
;                     const f32x4 o0 = x0 + g0 * acc[ai][bj][m][0], o1 = x1v + g1v * acc[ai][bj][m][1];
;                     u32x4 ow; ow.x = pk2(o0[0], o0[1]); ow.y = pk2(o0[2], o0[3]); ow.z = pk2(o1[0], o1[1]); ow.w = pk2(o1[2], o1[3]);
;                     *(u32x4*)(xo + (ro + cofs) * 2 + loff2) = ow; }
.LBB0_1785:
	s_waitcnt vmcnt(0)
	v_pk_fma_f32 v[110:111], v[110:111], v[118:119], v[126:127]
	v_pk_fma_f32 v[116:117], v[108:109], v[116:117], v[124:125]
	v_pk_fma_f32 v[108:109], v[106:107], v[114:115], v[122:123]
	v_pk_fma_f32 v[112:113], v[112:113], v[120:121], v[128:129]
	v_cvt_pk_bf16_f32 v106, v110, v111
	v_cvt_pk_bf16_f32 v107, v112, v113
	v_bfe_u32 v1, v108, 16, 1
	v_add3_u32 v1, v108, v1, s37
	v_bfe_u32 v108, v109, 16, 1
	v_lshrrev_b32_e32 v1, 16, v1
	v_add3_u32 v108, v109, v108, s37
	v_and_or_b32 v108, v108, s33, v1
	v_add_co_u32_e32 v110, vcc, 0x10000, v160
	v_cvt_pk_bf16_f32 v109, v116, v117
	s_nop 0
	v_addc_co_u32_e32 v111, vcc, 0, v161, vcc
	global_store_dwordx4 v[110:111], v[106:109], off
	global_load_dwordx4 v[106:109], v[164:165], off offset:528
	s_nop 0
	global_load_dwordx4 v[110:113], v[164:165], off offset:512
	s_and_b64 vcc, exec, s[40:41]
	s_cbranch_vccnz .LBB0_1832
	s_mov_b64 s[24:25], 0x20200
	v_add_co_u32_e32 v116, vcc, 0x20000, v162
	v_lshl_add_u64 v[114:115], v[162:163], 0, s[24:25]
	s_nop 0
	v_addc_co_u32_e32 v117, vcc, 0, v163, vcc
	global_load_dwordx4 v[118:121], v[116:117], off offset:512
	s_nop 0
	global_load_dwordx4 v[114:117], v[114:115], off offset:16
	s_cbranch_execnz .LBB0_1788

; __device__ __forceinline__ unsigned f2bf(float f) { unsigned u = __builtin_bit_cast(unsigned, f); return (u + 0x7fffu + ((u >> 16) & 1u)) >> 16; }
; __device__ __forceinline__ unsigned pk2(float lo, float hi) { return f2bf(lo) | (f2bf(hi) << 16); }
;     __device__ __forceinline__ void epi(const f32x4 (&acc)[2][2][4][2], const Unit& u, int wr, int wc, int fr, int fq) const {
;     ...
;                     const f32x4 g0 = *(const f32x4*)(g1 + cofs * 4 + lcol * 4), g1v = *(const f32x4*)(g1 + cofs * 4 + lcol * 4 + 16);
;                     f32x4 x0, x1v;
;                     if (f32in) { x0 = *(const f32x4*)(xin + (ro + cofs) * 4 + loff4); x1v = *(const f32x4*)(xin + (ro + cofs) * 4 + loff4 + 16); }
;                     else { const u32x4 w = *(const u32x4*)(xin + (ro + cofs) * 2 + loff2); x0 = (f32x4){bflo(w.x), bfhi(w.x), bflo(w.y), bfhi(w.y)}; x1v = (f32x4){bflo(w.z), bfhi(w.z), bflo(w.w), bfhi(w.w)}; }
;                     const f32x4 o0 = x0 + g0 * acc[ai][bj][m][0], o1 = x1v + g1v * acc[ai][bj][m][1];
;                     u32x4 ow; ow.x = pk2(o0[0], o0[1]); ow.y = pk2(o0[2], o0[3]); ow.z = pk2(o1[0], o1[1]); ow.w = pk2(o1[2], o1[3]);
;                     *(u32x4*)(xo + (ro + cofs) * 2 + loff2) = ow; }
.LBB0_1788:
	s_waitcnt vmcnt(0)
	v_pk_fma_f32 v[102:103], v[102:103], v[110:111], v[118:119]
	v_pk_fma_f32 v[108:109], v[100:101], v[108:109], v[116:117]
	v_pk_fma_f32 v[100:101], v[98:99], v[106:107], v[114:115]
	v_pk_fma_f32 v[104:105], v[104:105], v[112:113], v[120:121]
	v_cvt_pk_bf16_f32 v98, v102, v103
	v_cvt_pk_bf16_f32 v99, v104, v105
	v_bfe_u32 v1, v100, 16, 1
	v_add3_u32 v1, v100, v1, s37
	v_bfe_u32 v100, v101, 16, 1
	v_lshrrev_b32_e32 v1, 16, v1
	v_add3_u32 v100, v101, v100, s37
	v_and_or_b32 v100, v100, s33, v1
	v_add_co_u32_e32 v102, vcc, 0x10000, v160
	v_cvt_pk_bf16_f32 v101, v108, v109
	s_nop 0
	v_addc_co_u32_e32 v103, vcc, 0, v161, vcc
	global_store_dwordx4 v[102:103], v[98:101], off offset:256
	global_load_dwordx4 v[98:101], v[164:165], off offset:16
	global_load_dwordx4 v[102:105], v[164:165], off
	s_and_b64 vcc, exec, s[40:41]
	s_cbranch_vccnz .LBB0_1833
	s_mov_b64 s[24:25], 0x40000
	v_add_co_u32_e32 v108, vcc, 0x40000, v162
	v_lshl_add_u64 v[106:107], v[162:163], 0, s[24:25]
	s_nop 0
	v_addc_co_u32_e32 v109, vcc, 0, v163, vcc
	global_load_dwordx4 v[110:113], v[108:109], off
	s_nop 0
	global_load_dwordx4 v[106:109], v[106:107], off offset:16
	s_cbranch_execnz .LBB0_1791

; __device__ __forceinline__ unsigned f2bf(float f) { unsigned u = __builtin_bit_cast(unsigned, f); return (u + 0x7fffu + ((u >> 16) & 1u)) >> 16; }
; __device__ __forceinline__ unsigned pk2(float lo, float hi) { return f2bf(lo) | (f2bf(hi) << 16); }
;     __device__ __forceinline__ void epi(const f32x4 (&acc)[2][2][4][2], const Unit& u, int wr, int wc, int fr, int fq) const {
;     ...
;                     const f32x4 g0 = *(const f32x4*)(g1 + cofs * 4 + lcol * 4), g1v = *(const f32x4*)(g1 + cofs * 4 + lcol * 4 + 16);
;                     f32x4 x0, x1v;
;                     if (f32in) { x0 = *(const f32x4*)(xin + (ro + cofs) * 4 + loff4); x1v = *(const f32x4*)(xin + (ro + cofs) * 4 + loff4 + 16); }
;                     else { const u32x4 w = *(const u32x4*)(xin + (ro + cofs) * 2 + loff2); x0 = (f32x4){bflo(w.x), bfhi(w.x), bflo(w.y), bfhi(w.y)}; x1v = (f32x4){bflo(w.z), bfhi(w.z), bflo(w.w), bfhi(w.w)}; }
;                     const f32x4 o0 = x0 + g0 * acc[ai][bj][m][0], o1 = x1v + g1v * acc[ai][bj][m][1];
;                     u32x4 ow; ow.x = pk2(o0[0], o0[1]); ow.y = pk2(o0[2], o0[3]); ow.z = pk2(o1[0], o1[1]); ow.w = pk2(o1[2], o1[3]);
;                     *(u32x4*)(xo + (ro + cofs) * 2 + loff2) = ow; }
.LBB0_1791:
	s_waitcnt vmcnt(0)
	v_pk_fma_f32 v[94:95], v[94:95], v[102:103], v[110:111]
	v_pk_fma_f32 v[100:101], v[92:93], v[100:101], v[108:109]
	v_pk_fma_f32 v[92:93], v[90:91], v[98:99], v[106:107]
	v_pk_fma_f32 v[96:97], v[96:97], v[104:105], v[112:113]
	v_cvt_pk_bf16_f32 v90, v94, v95
	v_cvt_pk_bf16_f32 v91, v96, v97
	v_bfe_u32 v1, v92, 16, 1
	v_add3_u32 v1, v92, v1, s37
	v_bfe_u32 v92, v93, 16, 1
	v_lshrrev_b32_e32 v1, 16, v1
	v_add3_u32 v92, v93, v92, s37
	v_and_or_b32 v92, v92, s33, v1
	v_add_co_u32_e32 v94, vcc, 0x20000, v160
	v_cvt_pk_bf16_f32 v93, v100, v101
	s_nop 0
	v_addc_co_u32_e32 v95, vcc, 0, v161, vcc
	global_store_dwordx4 v[94:95], v[90:93], off
	global_load_dwordx4 v[90:93], v[164:165], off offset:528
	s_nop 0
	global_load_dwordx4 v[94:97], v[164:165], off offset:512
	s_and_b64 vcc, exec, s[40:41]
	s_cbranch_vccnz .LBB0_1834
	s_mov_b64 s[24:25], 0x40200
	v_add_co_u32_e32 v100, vcc, 0x40000, v162
	v_lshl_add_u64 v[98:99], v[162:163], 0, s[24:25]
	s_nop 0
	v_addc_co_u32_e32 v101, vcc, 0, v163, vcc
	global_load_dwordx4 v[102:105], v[100:101], off offset:512
	s_nop 0
	global_load_dwordx4 v[98:101], v[98:99], off offset:16
	s_cbranch_execnz .LBB0_1794

; __device__ __forceinline__ unsigned f2bf(float f) { unsigned u = __builtin_bit_cast(unsigned, f); return (u + 0x7fffu + ((u >> 16) & 1u)) >> 16; }
; __device__ __forceinline__ unsigned pk2(float lo, float hi) { return f2bf(lo) | (f2bf(hi) << 16); }
;     __device__ __forceinline__ void epi(const f32x4 (&acc)[2][2][4][2], const Unit& u, int wr, int wc, int fr, int fq) const {
;     ...
;                     const f32x4 g0 = *(const f32x4*)(g1 + cofs * 4 + lcol * 4), g1v = *(const f32x4*)(g1 + cofs * 4 + lcol * 4 + 16);
;                     f32x4 x0, x1v;
;                     if (f32in) { x0 = *(const f32x4*)(xin + (ro + cofs) * 4 + loff4); x1v = *(const f32x4*)(xin + (ro + cofs) * 4 + loff4 + 16); }
;                     else { const u32x4 w = *(const u32x4*)(xin + (ro + cofs) * 2 + loff2); x0 = (f32x4){bflo(w.x), bfhi(w.x), bflo(w.y), bfhi(w.y)}; x1v = (f32x4){bflo(w.z), bfhi(w.z), bflo(w.w), bfhi(w.w)}; }
;                     const f32x4 o0 = x0 + g0 * acc[ai][bj][m][0], o1 = x1v + g1v * acc[ai][bj][m][1];
;                     u32x4 ow; ow.x = pk2(o0[0], o0[1]); ow.y = pk2(o0[2], o0[3]); ow.z = pk2(o1[0], o1[1]); ow.w = pk2(o1[2], o1[3]);
;                     *(u32x4*)(xo + (ro + cofs) * 2 + loff2) = ow; }
.LBB0_1794:
	s_waitcnt vmcnt(0)
	v_pk_fma_f32 v[86:87], v[86:87], v[94:95], v[102:103]
	v_pk_fma_f32 v[92:93], v[84:85], v[92:93], v[100:101]
	v_pk_fma_f32 v[84:85], v[82:83], v[90:91], v[98:99]
	v_pk_fma_f32 v[88:89], v[88:89], v[96:97], v[104:105]
	v_cvt_pk_bf16_f32 v82, v86, v87
	v_cvt_pk_bf16_f32 v83, v88, v89
	v_bfe_u32 v1, v84, 16, 1
	v_add3_u32 v1, v84, v1, s37
	v_bfe_u32 v84, v85, 16, 1
	v_lshrrev_b32_e32 v1, 16, v1
	v_add3_u32 v84, v85, v84, s37
	v_and_or_b32 v84, v84, s33, v1
	v_add_co_u32_e32 v86, vcc, 0x20000, v160
	v_cvt_pk_bf16_f32 v85, v92, v93
	s_nop 0
	v_addc_co_u32_e32 v87, vcc, 0, v161, vcc
	global_store_dwordx4 v[86:87], v[82:85], off offset:256
	global_load_dwordx4 v[82:85], v[164:165], off offset:16
	global_load_dwordx4 v[86:89], v[164:165], off
	s_and_b64 vcc, exec, s[40:41]
	s_cbranch_vccnz .LBB0_1835
	s_mov_b64 s[24:25], 0x60000
	v_add_co_u32_e32 v92, vcc, 0x60000, v162
	v_lshl_add_u64 v[90:91], v[162:163], 0, s[24:25]
	s_nop 0
	v_addc_co_u32_e32 v93, vcc, 0, v163, vcc
	global_load_dwordx4 v[94:97], v[92:93], off
	s_nop 0
	global_load_dwordx4 v[90:93], v[90:91], off offset:16
	s_cbranch_execnz .LBB0_1797

; __device__ __forceinline__ unsigned f2bf(float f) { unsigned u = __builtin_bit_cast(unsigned, f); return (u + 0x7fffu + ((u >> 16) & 1u)) >> 16; }
; __device__ __forceinline__ unsigned pk2(float lo, float hi) { return f2bf(lo) | (f2bf(hi) << 16); }
;     __device__ __forceinline__ void epi(const f32x4 (&acc)[2][2][4][2], const Unit& u, int wr, int wc, int fr, int fq) const {
;     ...
;                     const f32x4 g0 = *(const f32x4*)(g1 + cofs * 4 + lcol * 4), g1v = *(const f32x4*)(g1 + cofs * 4 + lcol * 4 + 16);
;                     f32x4 x0, x1v;
;                     if (f32in) { x0 = *(const f32x4*)(xin + (ro + cofs) * 4 + loff4); x1v = *(const f32x4*)(xin + (ro + cofs) * 4 + loff4 + 16); }
;                     else { const u32x4 w = *(const u32x4*)(xin + (ro + cofs) * 2 + loff2); x0 = (f32x4){bflo(w.x), bfhi(w.x), bflo(w.y), bfhi(w.y)}; x1v = (f32x4){bflo(w.z), bfhi(w.z), bflo(w.w), bfhi(w.w)}; }
;                     const f32x4 o0 = x0 + g0 * acc[ai][bj][m][0], o1 = x1v + g1v * acc[ai][bj][m][1];
;                     u32x4 ow; ow.x = pk2(o0[0], o0[1]); ow.y = pk2(o0[2], o0[3]); ow.z = pk2(o1[0], o1[1]); ow.w = pk2(o1[2], o1[3]);
;                     *(u32x4*)(xo + (ro + cofs) * 2 + loff2) = ow; }
.LBB0_1797:
	s_waitcnt vmcnt(0)
	v_pk_fma_f32 v[78:79], v[78:79], v[86:87], v[94:95]
	v_pk_fma_f32 v[84:85], v[76:77], v[84:85], v[92:93]
	v_pk_fma_f32 v[76:77], v[74:75], v[82:83], v[90:91]
	v_pk_fma_f32 v[80:81], v[80:81], v[88:89], v[96:97]
	v_cvt_pk_bf16_f32 v74, v78, v79
	v_cvt_pk_bf16_f32 v75, v80, v81
	v_bfe_u32 v1, v76, 16, 1
	v_add3_u32 v1, v76, v1, s37
	v_bfe_u32 v76, v77, 16, 1
	v_lshrrev_b32_e32 v1, 16, v1
	v_add3_u32 v76, v77, v76, s37
	v_and_or_b32 v76, v76, s33, v1
	v_add_co_u32_e32 v78, vcc, 0x30000, v160
	v_cvt_pk_bf16_f32 v77, v84, v85
	s_nop 0
	v_addc_co_u32_e32 v79, vcc, 0, v161, vcc
	global_store_dwordx4 v[78:79], v[74:77], off
	global_load_dwordx4 v[74:77], v[164:165], off offset:528
	s_nop 0
	global_load_dwordx4 v[78:81], v[164:165], off offset:512
	s_and_b64 vcc, exec, s[40:41]
	s_cbranch_vccnz .LBB0_1836
	s_mov_b64 s[24:25], 0x60200
	v_add_co_u32_e32 v84, vcc, 0x60000, v162
	v_lshl_add_u64 v[82:83], v[162:163], 0, s[24:25]
	s_nop 0
	v_addc_co_u32_e32 v85, vcc, 0, v163, vcc
	global_load_dwordx4 v[86:89], v[84:85], off offset:512
	s_nop 0
	global_load_dwordx4 v[82:85], v[82:83], off offset:16
	s_cbranch_execnz .LBB0_1800

; __device__ __forceinline__ unsigned f2bf(float f) { unsigned u = __builtin_bit_cast(unsigned, f); return (u + 0x7fffu + ((u >> 16) & 1u)) >> 16; }
; __device__ __forceinline__ unsigned pk2(float lo, float hi) { return f2bf(lo) | (f2bf(hi) << 16); }
;     __device__ __forceinline__ void epi(const f32x4 (&acc)[2][2][4][2], const Unit& u, int wr, int wc, int fr, int fq) const {
;     ...
;                     const f32x4 g0 = *(const f32x4*)(g1 + cofs * 4 + lcol * 4), g1v = *(const f32x4*)(g1 + cofs * 4 + lcol * 4 + 16);
;                     f32x4 x0, x1v;
;                     if (f32in) { x0 = *(const f32x4*)(xin + (ro + cofs) * 4 + loff4); x1v = *(const f32x4*)(xin + (ro + cofs) * 4 + loff4 + 16); }
;                     else { const u32x4 w = *(const u32x4*)(xin + (ro + cofs) * 2 + loff2); x0 = (f32x4){bflo(w.x), bfhi(w.x), bflo(w.y), bfhi(w.y)}; x1v = (f32x4){bflo(w.z), bfhi(w.z), bflo(w.w), bfhi(w.w)}; }
;                     const f32x4 o0 = x0 + g0 * acc[ai][bj][m][0], o1 = x1v + g1v * acc[ai][bj][m][1];
;                     u32x4 ow; ow.x = pk2(o0[0], o0[1]); ow.y = pk2(o0[2], o0[3]); ow.z = pk2(o1[0], o1[1]); ow.w = pk2(o1[2], o1[3]);
;                     *(u32x4*)(xo + (ro + cofs) * 2 + loff2) = ow; }
.LBB0_1800:
	s_waitcnt vmcnt(0)
	v_pk_fma_f32 v[70:71], v[70:71], v[78:79], v[86:87]
	v_pk_fma_f32 v[76:77], v[68:69], v[76:77], v[84:85]
	v_pk_fma_f32 v[68:69], v[66:67], v[74:75], v[82:83]
	v_pk_fma_f32 v[72:73], v[72:73], v[80:81], v[88:89]
	v_cvt_pk_bf16_f32 v66, v70, v71
	v_cvt_pk_bf16_f32 v67, v72, v73
	v_bfe_u32 v1, v68, 16, 1
	v_add3_u32 v1, v68, v1, s37
	v_bfe_u32 v68, v69, 16, 1
	v_lshrrev_b32_e32 v1, 16, v1
	v_add3_u32 v68, v69, v68, s37
	v_and_or_b32 v68, v68, s33, v1
	v_add_co_u32_e32 v70, vcc, 0x30000, v160
	v_cvt_pk_bf16_f32 v69, v76, v77
	s_nop 0
	v_addc_co_u32_e32 v71, vcc, 0, v161, vcc
	global_store_dwordx4 v[70:71], v[66:69], off offset:256
	global_load_dwordx4 v[66:69], v[164:165], off offset:16
	global_load_dwordx4 v[70:73], v[164:165], off
	s_and_b64 vcc, exec, s[40:41]
	s_cbranch_vccnz .LBB0_1837
	s_mov_b64 s[24:25], 0x100000
	v_add_co_u32_e32 v76, vcc, 0x100000, v162
	v_lshl_add_u64 v[74:75], v[162:163], 0, s[24:25]
	s_nop 0
	v_addc_co_u32_e32 v77, vcc, 0, v163, vcc
	global_load_dwordx4 v[78:81], v[76:77], off
	s_nop 0
	global_load_dwordx4 v[74:77], v[74:75], off offset:16
	s_cbranch_execnz .LBB0_1803

; __device__ __forceinline__ unsigned f2bf(float f) { unsigned u = __builtin_bit_cast(unsigned, f); return (u + 0x7fffu + ((u >> 16) & 1u)) >> 16; }
; __device__ __forceinline__ unsigned pk2(float lo, float hi) { return f2bf(lo) | (f2bf(hi) << 16); }
;     __device__ __forceinline__ void epi(const f32x4 (&acc)[2][2][4][2], const Unit& u, int wr, int wc, int fr, int fq) const {
;     ...
;                     const f32x4 g0 = *(const f32x4*)(g1 + cofs * 4 + lcol * 4), g1v = *(const f32x4*)(g1 + cofs * 4 + lcol * 4 + 16);
;                     f32x4 x0, x1v;
;                     if (f32in) { x0 = *(const f32x4*)(xin + (ro + cofs) * 4 + loff4); x1v = *(const f32x4*)(xin + (ro + cofs) * 4 + loff4 + 16); }
;                     else { const u32x4 w = *(const u32x4*)(xin + (ro + cofs) * 2 + loff2); x0 = (f32x4){bflo(w.x), bfhi(w.x), bflo(w.y), bfhi(w.y)}; x1v = (f32x4){bflo(w.z), bfhi(w.z), bflo(w.w), bfhi(w.w)}; }
;                     const f32x4 o0 = x0 + g0 * acc[ai][bj][m][0], o1 = x1v + g1v * acc[ai][bj][m][1];
;                     u32x4 ow; ow.x = pk2(o0[0], o0[1]); ow.y = pk2(o0[2], o0[3]); ow.z = pk2(o1[0], o1[1]); ow.w = pk2(o1[2], o1[3]);
;                     *(u32x4*)(xo + (ro + cofs) * 2 + loff2) = ow; }
.LBB0_1803:
	s_waitcnt vmcnt(0)
	v_pk_fma_f32 v[62:63], v[62:63], v[70:71], v[78:79]
	v_pk_fma_f32 v[68:69], v[60:61], v[68:69], v[76:77]
	v_pk_fma_f32 v[60:61], v[58:59], v[66:67], v[74:75]
	v_pk_fma_f32 v[64:65], v[64:65], v[72:73], v[80:81]
	v_cvt_pk_bf16_f32 v58, v62, v63
	v_cvt_pk_bf16_f32 v59, v64, v65
	v_bfe_u32 v1, v60, 16, 1
	v_add3_u32 v1, v60, v1, s37
	v_bfe_u32 v60, v61, 16, 1
	v_lshrrev_b32_e32 v1, 16, v1
	v_add3_u32 v60, v61, v60, s37
	v_and_or_b32 v60, v60, s33, v1
	v_add_co_u32_e32 v62, vcc, 0x80000, v160
	v_cvt_pk_bf16_f32 v61, v68, v69
	s_nop 0
	v_addc_co_u32_e32 v63, vcc, 0, v161, vcc
	global_store_dwordx4 v[62:63], v[58:61], off
	global_load_dwordx4 v[58:61], v[164:165], off offset:528
	s_nop 0
	global_load_dwordx4 v[62:65], v[164:165], off offset:512
	s_and_b64 vcc, exec, s[40:41]
	s_cbranch_vccnz .LBB0_1838
	s_mov_b64 s[24:25], 0x100200
	v_add_co_u32_e32 v68, vcc, 0x100000, v162
	v_lshl_add_u64 v[66:67], v[162:163], 0, s[24:25]
	s_nop 0
	v_addc_co_u32_e32 v69, vcc, 0, v163, vcc
	global_load_dwordx4 v[70:73], v[68:69], off offset:512
	s_nop 0
	global_load_dwordx4 v[66:69], v[66:67], off offset:16
	s_cbranch_execnz .LBB0_1806

; __device__ __forceinline__ unsigned f2bf(float f) { unsigned u = __builtin_bit_cast(unsigned, f); return (u + 0x7fffu + ((u >> 16) & 1u)) >> 16; }
; __device__ __forceinline__ unsigned pk2(float lo, float hi) { return f2bf(lo) | (f2bf(hi) << 16); }
;     __device__ __forceinline__ void epi(const f32x4 (&acc)[2][2][4][2], const Unit& u, int wr, int wc, int fr, int fq) const {
;     ...
;                     const f32x4 g0 = *(const f32x4*)(g1 + cofs * 4 + lcol * 4), g1v = *(const f32x4*)(g1 + cofs * 4 + lcol * 4 + 16);
;                     f32x4 x0, x1v;
;                     if (f32in) { x0 = *(const f32x4*)(xin + (ro + cofs) * 4 + loff4); x1v = *(const f32x4*)(xin + (ro + cofs) * 4 + loff4 + 16); }
;                     else { const u32x4 w = *(const u32x4*)(xin + (ro + cofs) * 2 + loff2); x0 = (f32x4){bflo(w.x), bfhi(w.x), bflo(w.y), bfhi(w.y)}; x1v = (f32x4){bflo(w.z), bfhi(w.z), bflo(w.w), bfhi(w.w)}; }
;                     const f32x4 o0 = x0 + g0 * acc[ai][bj][m][0], o1 = x1v + g1v * acc[ai][bj][m][1];
;                     u32x4 ow; ow.x = pk2(o0[0], o0[1]); ow.y = pk2(o0[2], o0[3]); ow.z = pk2(o1[0], o1[1]); ow.w = pk2(o1[2], o1[3]);
;                     *(u32x4*)(xo + (ro + cofs) * 2 + loff2) = ow; }
.LBB0_1806:
	s_waitcnt vmcnt(0)
	v_pk_fma_f32 v[54:55], v[54:55], v[62:63], v[70:71]
	v_pk_fma_f32 v[60:61], v[52:53], v[60:61], v[68:69]
	v_pk_fma_f32 v[52:53], v[50:51], v[58:59], v[66:67]
	v_pk_fma_f32 v[56:57], v[56:57], v[64:65], v[72:73]
	v_cvt_pk_bf16_f32 v50, v54, v55
	v_cvt_pk_bf16_f32 v51, v56, v57
	v_bfe_u32 v1, v52, 16, 1
	v_add3_u32 v1, v52, v1, s37
	v_bfe_u32 v52, v53, 16, 1
	v_lshrrev_b32_e32 v1, 16, v1
	v_add3_u32 v52, v53, v52, s37
	v_and_or_b32 v52, v52, s33, v1
	v_add_co_u32_e32 v54, vcc, 0x80000, v160
	v_cvt_pk_bf16_f32 v53, v60, v61
	s_nop 0
	v_addc_co_u32_e32 v55, vcc, 0, v161, vcc
	global_store_dwordx4 v[54:55], v[50:53], off offset:256
	global_load_dwordx4 v[50:53], v[164:165], off offset:16
	global_load_dwordx4 v[54:57], v[164:165], off
	s_and_b64 vcc, exec, s[40:41]
	s_cbranch_vccnz .LBB0_1839
	s_mov_b64 s[24:25], 0x120000
	v_add_co_u32_e32 v60, vcc, 0x120000, v162
	v_lshl_add_u64 v[58:59], v[162:163], 0, s[24:25]
	s_nop 0
	v_addc_co_u32_e32 v61, vcc, 0, v163, vcc
	global_load_dwordx4 v[62:65], v[60:61], off
	s_nop 0
	global_load_dwordx4 v[58:61], v[58:59], off offset:16
	s_cbranch_execnz .LBB0_1809

; __device__ __forceinline__ unsigned f2bf(float f) { unsigned u = __builtin_bit_cast(unsigned, f); return (u + 0x7fffu + ((u >> 16) & 1u)) >> 16; }
; __device__ __forceinline__ unsigned pk2(float lo, float hi) { return f2bf(lo) | (f2bf(hi) << 16); }
;     __device__ __forceinline__ void epi(const f32x4 (&acc)[2][2][4][2], const Unit& u, int wr, int wc, int fr, int fq) const {
;     ...
;                     const f32x4 g0 = *(const f32x4*)(g1 + cofs * 4 + lcol * 4), g1v = *(const f32x4*)(g1 + cofs * 4 + lcol * 4 + 16);
;                     f32x4 x0, x1v;
;                     if (f32in) { x0 = *(const f32x4*)(xin + (ro + cofs) * 4 + loff4); x1v = *(const f32x4*)(xin + (ro + cofs) * 4 + loff4 + 16); }
;                     else { const u32x4 w = *(const u32x4*)(xin + (ro + cofs) * 2 + loff2); x0 = (f32x4){bflo(w.x), bfhi(w.x), bflo(w.y), bfhi(w.y)}; x1v = (f32x4){bflo(w.z), bfhi(w.z), bflo(w.w), bfhi(w.w)}; }
;                     const f32x4 o0 = x0 + g0 * acc[ai][bj][m][0], o1 = x1v + g1v * acc[ai][bj][m][1];
;                     u32x4 ow; ow.x = pk2(o0[0], o0[1]); ow.y = pk2(o0[2], o0[3]); ow.z = pk2(o1[0], o1[1]); ow.w = pk2(o1[2], o1[3]);
;                     *(u32x4*)(xo + (ro + cofs) * 2 + loff2) = ow; }
.LBB0_1809:
	s_waitcnt vmcnt(0)
	v_pk_fma_f32 v[46:47], v[46:47], v[54:55], v[62:63]
	v_pk_fma_f32 v[52:53], v[44:45], v[52:53], v[60:61]
	v_pk_fma_f32 v[44:45], v[42:43], v[50:51], v[58:59]
	v_pk_fma_f32 v[48:49], v[48:49], v[56:57], v[64:65]
	v_cvt_pk_bf16_f32 v42, v46, v47
	v_cvt_pk_bf16_f32 v43, v48, v49
	v_bfe_u32 v1, v44, 16, 1
	v_add3_u32 v1, v44, v1, s37
	v_bfe_u32 v44, v45, 16, 1
	v_lshrrev_b32_e32 v1, 16, v1
	v_add3_u32 v44, v45, v44, s37
	v_and_or_b32 v44, v44, s33, v1
	v_add_co_u32_e32 v46, vcc, 0x90000, v160
	v_cvt_pk_bf16_f32 v45, v52, v53
	s_nop 0
	v_addc_co_u32_e32 v47, vcc, 0, v161, vcc
	global_store_dwordx4 v[46:47], v[42:45], off
	global_load_dwordx4 v[42:45], v[164:165], off offset:528
	s_nop 0
	global_load_dwordx4 v[46:49], v[164:165], off offset:512
	s_and_b64 vcc, exec, s[40:41]
	s_cbranch_vccnz .LBB0_1840
	s_mov_b64 s[24:25], 0x120200
	v_add_co_u32_e32 v52, vcc, 0x120000, v162
	v_lshl_add_u64 v[50:51], v[162:163], 0, s[24:25]
	s_nop 0
	v_addc_co_u32_e32 v53, vcc, 0, v163, vcc
	global_load_dwordx4 v[54:57], v[52:53], off offset:512
	s_nop 0
	global_load_dwordx4 v[50:53], v[50:51], off offset:16
	s_cbranch_execnz .LBB0_1812

; __device__ __forceinline__ unsigned f2bf(float f) { unsigned u = __builtin_bit_cast(unsigned, f); return (u + 0x7fffu + ((u >> 16) & 1u)) >> 16; }
; __device__ __forceinline__ unsigned pk2(float lo, float hi) { return f2bf(lo) | (f2bf(hi) << 16); }
;     __device__ __forceinline__ void epi(const f32x4 (&acc)[2][2][4][2], const Unit& u, int wr, int wc, int fr, int fq) const {
;     ...
;                     const f32x4 g0 = *(const f32x4*)(g1 + cofs * 4 + lcol * 4), g1v = *(const f32x4*)(g1 + cofs * 4 + lcol * 4 + 16);
;                     f32x4 x0, x1v;
;                     if (f32in) { x0 = *(const f32x4*)(xin + (ro + cofs) * 4 + loff4); x1v = *(const f32x4*)(xin + (ro + cofs) * 4 + loff4 + 16); }
;                     else { const u32x4 w = *(const u32x4*)(xin + (ro + cofs) * 2 + loff2); x0 = (f32x4){bflo(w.x), bfhi(w.x), bflo(w.y), bfhi(w.y)}; x1v = (f32x4){bflo(w.z), bfhi(w.z), bflo(w.w), bfhi(w.w)}; }
;                     const f32x4 o0 = x0 + g0 * acc[ai][bj][m][0], o1 = x1v + g1v * acc[ai][bj][m][1];
;                     u32x4 ow; ow.x = pk2(o0[0], o0[1]); ow.y = pk2(o0[2], o0[3]); ow.z = pk2(o1[0], o1[1]); ow.w = pk2(o1[2], o1[3]);
;                     *(u32x4*)(xo + (ro + cofs) * 2 + loff2) = ow; }
.LBB0_1812:
	s_waitcnt vmcnt(0)
	v_pk_fma_f32 v[38:39], v[38:39], v[46:47], v[54:55]
	v_pk_fma_f32 v[44:45], v[36:37], v[44:45], v[52:53]
	v_pk_fma_f32 v[36:37], v[34:35], v[42:43], v[50:51]
	v_pk_fma_f32 v[40:41], v[40:41], v[48:49], v[56:57]
	v_cvt_pk_bf16_f32 v34, v38, v39
	v_cvt_pk_bf16_f32 v35, v40, v41
	v_bfe_u32 v1, v36, 16, 1
	v_add3_u32 v1, v36, v1, s37
	v_bfe_u32 v36, v37, 16, 1
	v_lshrrev_b32_e32 v1, 16, v1
	v_add3_u32 v36, v37, v36, s37
	v_and_or_b32 v36, v36, s33, v1
	v_add_co_u32_e32 v38, vcc, 0x90000, v160
	v_cvt_pk_bf16_f32 v37, v44, v45
	s_nop 0
	v_addc_co_u32_e32 v39, vcc, 0, v161, vcc
	global_store_dwordx4 v[38:39], v[34:37], off offset:256
	global_load_dwordx4 v[34:37], v[164:165], off offset:16
	global_load_dwordx4 v[38:41], v[164:165], off
	s_and_b64 vcc, exec, s[40:41]
	s_cbranch_vccnz .LBB0_1841
	s_mov_b64 s[24:25], 0x140000
	v_add_co_u32_e32 v44, vcc, 0x140000, v162
	v_lshl_add_u64 v[42:43], v[162:163], 0, s[24:25]
	s_nop 0
	v_addc_co_u32_e32 v45, vcc, 0, v163, vcc
	global_load_dwordx4 v[46:49], v[44:45], off
	s_nop 0
	global_load_dwordx4 v[42:45], v[42:43], off offset:16
	s_cbranch_execnz .LBB0_1815

; __device__ __forceinline__ unsigned f2bf(float f) { unsigned u = __builtin_bit_cast(unsigned, f); return (u + 0x7fffu + ((u >> 16) & 1u)) >> 16; }
; __device__ __forceinline__ unsigned pk2(float lo, float hi) { return f2bf(lo) | (f2bf(hi) << 16); }
;     __device__ __forceinline__ void epi(const f32x4 (&acc)[2][2][4][2], const Unit& u, int wr, int wc, int fr, int fq) const {
;     ...
;                     const f32x4 g0 = *(const f32x4*)(g1 + cofs * 4 + lcol * 4), g1v = *(const f32x4*)(g1 + cofs * 4 + lcol * 4 + 16);
;                     f32x4 x0, x1v;
;                     if (f32in) { x0 = *(const f32x4*)(xin + (ro + cofs) * 4 + loff4); x1v = *(const f32x4*)(xin + (ro + cofs) * 4 + loff4 + 16); }
;                     else { const u32x4 w = *(const u32x4*)(xin + (ro + cofs) * 2 + loff2); x0 = (f32x4){bflo(w.x), bfhi(w.x), bflo(w.y), bfhi(w.y)}; x1v = (f32x4){bflo(w.z), bfhi(w.z), bflo(w.w), bfhi(w.w)}; }
;                     const f32x4 o0 = x0 + g0 * acc[ai][bj][m][0], o1 = x1v + g1v * acc[ai][bj][m][1];
;                     u32x4 ow; ow.x = pk2(o0[0], o0[1]); ow.y = pk2(o0[2], o0[3]); ow.z = pk2(o1[0], o1[1]); ow.w = pk2(o1[2], o1[3]);
;                     *(u32x4*)(xo + (ro + cofs) * 2 + loff2) = ow; }
.LBB0_1815:
	s_waitcnt vmcnt(0)
	v_pk_fma_f32 v[30:31], v[30:31], v[38:39], v[46:47]
	v_pk_fma_f32 v[36:37], v[28:29], v[36:37], v[44:45]
	v_pk_fma_f32 v[28:29], v[26:27], v[34:35], v[42:43]
	v_pk_fma_f32 v[32:33], v[32:33], v[40:41], v[48:49]
	v_cvt_pk_bf16_f32 v26, v30, v31
	v_cvt_pk_bf16_f32 v27, v32, v33
	v_bfe_u32 v1, v28, 16, 1
	v_add3_u32 v1, v28, v1, s37
	v_bfe_u32 v28, v29, 16, 1
	v_lshrrev_b32_e32 v1, 16, v1
	v_add3_u32 v28, v29, v28, s37
	v_and_or_b32 v28, v28, s33, v1
	v_add_co_u32_e32 v30, vcc, 0xa0000, v160
	v_cvt_pk_bf16_f32 v29, v36, v37
	s_nop 0
	v_addc_co_u32_e32 v31, vcc, 0, v161, vcc
	global_store_dwordx4 v[30:31], v[26:29], off
	global_load_dwordx4 v[26:29], v[164:165], off offset:528
	s_nop 0
	global_load_dwordx4 v[30:33], v[164:165], off offset:512
	s_and_b64 vcc, exec, s[40:41]
	s_cbranch_vccnz .LBB0_1842
	s_mov_b64 s[24:25], 0x140200
	v_add_co_u32_e32 v36, vcc, 0x140000, v162
	v_lshl_add_u64 v[34:35], v[162:163], 0, s[24:25]
	s_nop 0
	v_addc_co_u32_e32 v37, vcc, 0, v163, vcc
	global_load_dwordx4 v[38:41], v[36:37], off offset:512
	s_nop 0
	global_load_dwordx4 v[34:37], v[34:35], off offset:16
	s_cbranch_execnz .LBB0_1818

; __device__ __forceinline__ unsigned f2bf(float f) { unsigned u = __builtin_bit_cast(unsigned, f); return (u + 0x7fffu + ((u >> 16) & 1u)) >> 16; }
; __device__ __forceinline__ unsigned pk2(float lo, float hi) { return f2bf(lo) | (f2bf(hi) << 16); }
;     __device__ __forceinline__ void epi(const f32x4 (&acc)[2][2][4][2], const Unit& u, int wr, int wc, int fr, int fq) const {
;     ...
;                     const f32x4 g0 = *(const f32x4*)(g1 + cofs * 4 + lcol * 4), g1v = *(const f32x4*)(g1 + cofs * 4 + lcol * 4 + 16);
;                     f32x4 x0, x1v;
;                     if (f32in) { x0 = *(const f32x4*)(xin + (ro + cofs) * 4 + loff4); x1v = *(const f32x4*)(xin + (ro + cofs) * 4 + loff4 + 16); }
;                     else { const u32x4 w = *(const u32x4*)(xin + (ro + cofs) * 2 + loff2); x0 = (f32x4){bflo(w.x), bfhi(w.x), bflo(w.y), bfhi(w.y)}; x1v = (f32x4){bflo(w.z), bfhi(w.z), bflo(w.w), bfhi(w.w)}; }
;                     const f32x4 o0 = x0 + g0 * acc[ai][bj][m][0], o1 = x1v + g1v * acc[ai][bj][m][1];
;                     u32x4 ow; ow.x = pk2(o0[0], o0[1]); ow.y = pk2(o0[2], o0[3]); ow.z = pk2(o1[0], o1[1]); ow.w = pk2(o1[2], o1[3]);
;                     *(u32x4*)(xo + (ro + cofs) * 2 + loff2) = ow; }
.LBB0_1818:
	s_waitcnt vmcnt(0)
	v_pk_fma_f32 v[22:23], v[22:23], v[30:31], v[38:39]
	v_pk_fma_f32 v[28:29], v[20:21], v[28:29], v[36:37]
	v_pk_fma_f32 v[20:21], v[18:19], v[26:27], v[34:35]
	v_pk_fma_f32 v[24:25], v[24:25], v[32:33], v[40:41]
	v_cvt_pk_bf16_f32 v18, v22, v23
	v_cvt_pk_bf16_f32 v19, v24, v25
	v_bfe_u32 v1, v20, 16, 1
	v_add3_u32 v1, v20, v1, s37
	v_bfe_u32 v20, v21, 16, 1
	v_lshrrev_b32_e32 v1, 16, v1
	v_add3_u32 v20, v21, v20, s37
	v_and_or_b32 v20, v20, s33, v1
	v_add_co_u32_e32 v22, vcc, 0xa0000, v160
	v_cvt_pk_bf16_f32 v21, v28, v29
	s_nop 0
	v_addc_co_u32_e32 v23, vcc, 0, v161, vcc
	global_store_dwordx4 v[22:23], v[18:21], off offset:256
	global_load_dwordx4 v[18:21], v[164:165], off offset:16
	global_load_dwordx4 v[22:25], v[164:165], off
	s_and_b64 vcc, exec, s[40:41]
	s_cbranch_vccnz .LBB0_1843
	s_mov_b64 s[24:25], 0x160000
	v_add_co_u32_e32 v28, vcc, 0x160000, v162
	v_lshl_add_u64 v[26:27], v[162:163], 0, s[24:25]
	s_nop 0
	v_addc_co_u32_e32 v29, vcc, 0, v163, vcc
	global_load_dwordx4 v[30:33], v[28:29], off
	s_nop 0
	global_load_dwordx4 v[26:29], v[26:27], off offset:16
	s_cbranch_execnz .LBB0_1821

; __device__ __forceinline__ unsigned f2bf(float f) { unsigned u = __builtin_bit_cast(unsigned, f); return (u + 0x7fffu + ((u >> 16) & 1u)) >> 16; }
; __device__ __forceinline__ unsigned pk2(float lo, float hi) { return f2bf(lo) | (f2bf(hi) << 16); }
;     __device__ __forceinline__ void epi(const f32x4 (&acc)[2][2][4][2], const Unit& u, int wr, int wc, int fr, int fq) const {
;     ...
;                     const f32x4 g0 = *(const f32x4*)(g1 + cofs * 4 + lcol * 4), g1v = *(const f32x4*)(g1 + cofs * 4 + lcol * 4 + 16);
;                     f32x4 x0, x1v;
;                     if (f32in) { x0 = *(const f32x4*)(xin + (ro + cofs) * 4 + loff4); x1v = *(const f32x4*)(xin + (ro + cofs) * 4 + loff4 + 16); }
;                     else { const u32x4 w = *(const u32x4*)(xin + (ro + cofs) * 2 + loff2); x0 = (f32x4){bflo(w.x), bfhi(w.x), bflo(w.y), bfhi(w.y)}; x1v = (f32x4){bflo(w.z), bfhi(w.z), bflo(w.w), bfhi(w.w)}; }
;                     const f32x4 o0 = x0 + g0 * acc[ai][bj][m][0], o1 = x1v + g1v * acc[ai][bj][m][1];
;                     u32x4 ow; ow.x = pk2(o0[0], o0[1]); ow.y = pk2(o0[2], o0[3]); ow.z = pk2(o1[0], o1[1]); ow.w = pk2(o1[2], o1[3]);
;                     *(u32x4*)(xo + (ro + cofs) * 2 + loff2) = ow; }
.LBB0_1821:
	s_waitcnt vmcnt(0)
	v_pk_fma_f32 v[14:15], v[14:15], v[22:23], v[30:31]
	v_pk_fma_f32 v[20:21], v[12:13], v[20:21], v[28:29]
	v_pk_fma_f32 v[12:13], v[10:11], v[18:19], v[26:27]
	v_pk_fma_f32 v[16:17], v[16:17], v[24:25], v[32:33]
	v_cvt_pk_bf16_f32 v10, v14, v15
	v_cvt_pk_bf16_f32 v11, v16, v17
	v_bfe_u32 v1, v12, 16, 1
	v_add3_u32 v1, v12, v1, s37
	v_bfe_u32 v12, v13, 16, 1
	v_lshrrev_b32_e32 v1, 16, v1
	v_add3_u32 v12, v13, v12, s37
	v_and_or_b32 v12, v12, s33, v1
	v_add_co_u32_e32 v14, vcc, 0xb0000, v160
	v_cvt_pk_bf16_f32 v13, v20, v21
	s_nop 0
	v_addc_co_u32_e32 v15, vcc, 0, v161, vcc
	global_store_dwordx4 v[14:15], v[10:13], off
	global_load_dwordx4 v[10:13], v[164:165], off offset:528
	s_nop 0
	global_load_dwordx4 v[14:17], v[164:165], off offset:512
	s_and_b64 vcc, exec, s[40:41]
	s_cbranch_vccnz .LBB0_1844
	s_mov_b64 s[24:25], 0x160200
	v_add_co_u32_e32 v20, vcc, 0x160000, v162
	v_lshl_add_u64 v[18:19], v[162:163], 0, s[24:25]
	s_nop 0
	v_addc_co_u32_e32 v21, vcc, 0, v163, vcc
	global_load_dwordx4 v[22:25], v[20:21], off offset:512
	s_nop 0
	global_load_dwordx4 v[18:21], v[18:19], off offset:16
	s_cbranch_execnz .LBB0_1824

; __device__ __forceinline__ unsigned pk2(float lo, float hi) { return f2bf(lo) | (f2bf(hi) << 16); }
; #define PG8_BAR __builtin_amdgcn_s_barrier()
; template <class P>
; __device__ __forceinline__ void gemm_phase(LAS unsigned char* lds, const P& p) {
;     ...
;         if (wr == 0) PG8_BAR;
;         p.epi(acc, cur, wr, wc, fr, fq);
;         if (!has_next) break;
; #pragma unroll
;         for (int a = 0; a < 2; ++a)
; #pragma unroll
;             for (int b = 0; b < 2; ++b)
; #pragma unroll
;                 for (int m = 0; m < 4; ++m)
; #pragma unroll
;                     for (int n = 0; n < 2; ++n) acc[a][b][m][n] = (f32x4){0.f, 0.f, 0.f, 0.f};
;         cur = nxt; cA = nA; cB = nB; ++ui;
;         if (wr == 1) PG8_BAR;
;     __device__ __forceinline__ void epi(const f32x4 (&acc)[2][2][4][2], const Unit& u, int wr, int wc, int fr, int fq) const {
;     ...
;                     const f32x4 g0 = *(const f32x4*)(g1 + cofs * 4 + lcol * 4), g1v = *(const f32x4*)(g1 + cofs * 4 + lcol * 4 + 16);
;                     f32x4 x0, x1v;
;                     if (f32in) { x0 = *(const f32x4*)(xin + (ro + cofs) * 4 + loff4); x1v = *(const f32x4*)(xin + (ro + cofs) * 4 + loff4 + 16); }
;                     else { const u32x4 w = *(const u32x4*)(xin + (ro + cofs) * 2 + loff2); x0 = (f32x4){bflo(w.x), bfhi(w.x), bflo(w.y), bfhi(w.y)}; x1v = (f32x4){bflo(w.z), bfhi(w.z), bflo(w.w), bfhi(w.w)}; }
;                     const f32x4 o0 = x0 + g0 * acc[ai][bj][m][0], o1 = x1v + g1v * acc[ai][bj][m][1];
;                     u32x4 ow; ow.x = pk2(o0[0], o0[1]); ow.y = pk2(o0[2], o0[3]); ow.z = pk2(o1[0], o1[1]); ow.w = pk2(o1[2], o1[3]);
;                     *(u32x4*)(xo + (ro + cofs) * 2 + loff2) = ow; }
;                 asm volatile("" ::: "memory"); }
.LBB0_1824:
	s_waitcnt vmcnt(0)
	v_pk_fma_f32 v[6:7], v[6:7], v[14:15], v[22:23]
	v_pk_fma_f32 v[12:13], v[4:5], v[12:13], v[20:21]
	v_pk_fma_f32 v[4:5], v[2:3], v[10:11], v[18:19]
	v_pk_fma_f32 v[8:9], v[8:9], v[16:17], v[24:25]
	v_cvt_pk_bf16_f32 v2, v6, v7
	v_cvt_pk_bf16_f32 v3, v8, v9
	v_bfe_u32 v1, v4, 16, 1
	v_add3_u32 v1, v4, v1, s37
	v_bfe_u32 v4, v5, 16, 1
	v_lshrrev_b32_e32 v1, 16, v1
	v_add3_u32 v4, v5, v4, s37
	v_and_or_b32 v4, v4, s33, v1
	v_add_co_u32_e32 v6, vcc, 0xb0000, v160
	v_cvt_pk_bf16_f32 v5, v12, v13
	s_nop 0
	v_addc_co_u32_e32 v7, vcc, 0, v161, vcc
	global_store_dwordx4 v[6:7], v[2:5], off offset:256
	s_andn2_b64 vcc, exec, s[38:39]
	s_mov_b64 s[24:25], -1
	s_cbranch_vccnz .LBB0_1761
	s_andn2_b64 vcc, exec, s[4:5]
	s_cbranch_vccnz .LBB0_1760
	s_barrier
	s_branch .LBB0_1760

; __device__ __forceinline__ unsigned f2bf(float f) { unsigned u = __builtin_bit_cast(unsigned, f); return (u + 0x7fffu + ((u >> 16) & 1u)) >> 16; }
; __device__ __forceinline__ unsigned pk2(float lo, float hi) { return f2bf(lo) | (f2bf(hi) << 16); }
;     __device__ __forceinline__ void epi(const f32x4 (&acc)[2][2][4][2], const Unit& u, int wr, int wc, int fr, int fq) const {
;     ...
;                     const f32x4 g0 = *(const f32x4*)(g1 + cofs * 4 + lcol * 4), g1v = *(const f32x4*)(g1 + cofs * 4 + lcol * 4 + 16);
;                     f32x4 x0, x1v;
;                     if (f32in) { x0 = *(const f32x4*)(xin + (ro + cofs) * 4 + loff4); x1v = *(const f32x4*)(xin + (ro + cofs) * 4 + loff4 + 16); }
;                     else { const u32x4 w = *(const u32x4*)(xin + (ro + cofs) * 2 + loff2); x0 = (f32x4){bflo(w.x), bfhi(w.x), bflo(w.y), bfhi(w.y)}; x1v = (f32x4){bflo(w.z), bfhi(w.z), bflo(w.w), bfhi(w.w)}; }
;                     const f32x4 o0 = x0 + g0 * acc[ai][bj][m][0], o1 = x1v + g1v * acc[ai][bj][m][1];
;                     u32x4 ow; ow.x = pk2(o0[0], o0[1]); ow.y = pk2(o0[2], o0[3]); ow.z = pk2(o1[0], o1[1]); ow.w = pk2(o1[2], o1[3]);
;                     *(u32x4*)(xo + (ro + cofs) * 2 + loff2) = ow; }
.LBB0_1960:
	s_waitcnt vmcnt(0)
	v_pk_fma_f32 v[126:127], v[126:127], v[134:135], v[142:143]
	v_pk_fma_f32 v[132:133], v[124:125], v[132:133], v[140:141]
	v_pk_fma_f32 v[124:125], v[122:123], v[130:131], v[138:139]
	v_pk_fma_f32 v[128:129], v[128:129], v[136:137], v[144:145]
	v_cvt_pk_bf16_f32 v122, v126, v127
	v_cvt_pk_bf16_f32 v123, v128, v129
	v_bfe_u32 v1, v124, 16, 1
	v_add3_u32 v1, v124, v1, s37
	v_bfe_u32 v124, v125, 16, 1
	s_add_u32 s19, s64, s40
	v_lshrrev_b32_e32 v1, 16, v1
	v_add3_u32 v124, v125, v124, s37
	s_addc_u32 s21, s65, s41
	v_and_or_b32 v124, v124, s33, v1
	s_add_u32 s26, s19, s42
	s_addc_u32 s27, s21, s43
	v_lshl_add_u64 v[160:161], s[26:27], 0, v[146:147]
	v_cvt_pk_bf16_f32 v125, v132, v133
	global_store_dwordx4 v[160:161], v[122:125], off
	global_load_dwordx4 v[122:125], v[164:165], off offset:528
	s_nop 0
	global_load_dwordx4 v[126:129], v[164:165], off offset:512
	s_and_b64 vcc, exec, s[38:39]
	s_cbranch_vccnz .LBB0_2011
	global_load_dwordx4 v[130:133], v[162:163], off offset:528
	global_load_dwordx4 v[134:137], v[162:163], off offset:512
	s_cbranch_execnz .LBB0_1963

; __device__ __forceinline__ unsigned f2bf(float f) { unsigned u = __builtin_bit_cast(unsigned, f); return (u + 0x7fffu + ((u >> 16) & 1u)) >> 16; }
; __device__ __forceinline__ unsigned pk2(float lo, float hi) { return f2bf(lo) | (f2bf(hi) << 16); }
;     __device__ __forceinline__ void epi(const f32x4 (&acc)[2][2][4][2], const Unit& u, int wr, int wc, int fr, int fq) const {
;     ...
;                     const f32x4 g0 = *(const f32x4*)(g1 + cofs * 4 + lcol * 4), g1v = *(const f32x4*)(g1 + cofs * 4 + lcol * 4 + 16);
;                     f32x4 x0, x1v;
;                     if (f32in) { x0 = *(const f32x4*)(xin + (ro + cofs) * 4 + loff4); x1v = *(const f32x4*)(xin + (ro + cofs) * 4 + loff4 + 16); }
;                     else { const u32x4 w = *(const u32x4*)(xin + (ro + cofs) * 2 + loff2); x0 = (f32x4){bflo(w.x), bfhi(w.x), bflo(w.y), bfhi(w.y)}; x1v = (f32x4){bflo(w.z), bfhi(w.z), bflo(w.w), bfhi(w.w)}; }
;                     const f32x4 o0 = x0 + g0 * acc[ai][bj][m][0], o1 = x1v + g1v * acc[ai][bj][m][1];
;                     u32x4 ow; ow.x = pk2(o0[0], o0[1]); ow.y = pk2(o0[2], o0[3]); ow.z = pk2(o1[0], o1[1]); ow.w = pk2(o1[2], o1[3]);
;                     *(u32x4*)(xo + (ro + cofs) * 2 + loff2) = ow; }
.LBB0_1963:
	s_waitcnt vmcnt(0)
	v_pk_fma_f32 v[118:119], v[118:119], v[126:127], v[134:135]
	v_pk_fma_f32 v[124:125], v[116:117], v[124:125], v[132:133]
	v_pk_fma_f32 v[116:117], v[114:115], v[122:123], v[130:131]
	v_pk_fma_f32 v[120:121], v[120:121], v[128:129], v[136:137]
	v_cvt_pk_bf16_f32 v114, v118, v119
	v_cvt_pk_bf16_f32 v115, v120, v121
	v_bfe_u32 v1, v116, 16, 1
	v_add3_u32 v1, v116, v1, s37
	v_bfe_u32 v116, v117, 16, 1
	v_lshrrev_b32_e32 v1, 16, v1
	v_add3_u32 v116, v117, v116, s37
	v_and_or_b32 v116, v116, s33, v1
	v_cvt_pk_bf16_f32 v117, v124, v125
	global_store_dwordx4 v[160:161], v[114:117], off offset:256
	global_load_dwordx4 v[114:117], v[164:165], off offset:16
	global_load_dwordx4 v[118:121], v[164:165], off
	s_and_b64 vcc, exec, s[38:39]
	s_cbranch_vccnz .LBB0_2012
	s_mov_b64 s[26:27], 0x20000
	v_add_co_u32_e32 v124, vcc, 0x20000, v162
	v_lshl_add_u64 v[122:123], v[162:163], 0, s[26:27]
	s_nop 0
	v_addc_co_u32_e32 v125, vcc, 0, v163, vcc
	global_load_dwordx4 v[126:129], v[124:125], off
	s_nop 0
	global_load_dwordx4 v[122:125], v[122:123], off offset:16
	s_cbranch_execnz .LBB0_1966

; __device__ __forceinline__ unsigned f2bf(float f) { unsigned u = __builtin_bit_cast(unsigned, f); return (u + 0x7fffu + ((u >> 16) & 1u)) >> 16; }
; __device__ __forceinline__ unsigned pk2(float lo, float hi) { return f2bf(lo) | (f2bf(hi) << 16); }
;     __device__ __forceinline__ void epi(const f32x4 (&acc)[2][2][4][2], const Unit& u, int wr, int wc, int fr, int fq) const {
;     ...
;                     const f32x4 g0 = *(const f32x4*)(g1 + cofs * 4 + lcol * 4), g1v = *(const f32x4*)(g1 + cofs * 4 + lcol * 4 + 16);
;                     f32x4 x0, x1v;
;                     if (f32in) { x0 = *(const f32x4*)(xin + (ro + cofs) * 4 + loff4); x1v = *(const f32x4*)(xin + (ro + cofs) * 4 + loff4 + 16); }
;                     else { const u32x4 w = *(const u32x4*)(xin + (ro + cofs) * 2 + loff2); x0 = (f32x4){bflo(w.x), bfhi(w.x), bflo(w.y), bfhi(w.y)}; x1v = (f32x4){bflo(w.z), bfhi(w.z), bflo(w.w), bfhi(w.w)}; }
;                     const f32x4 o0 = x0 + g0 * acc[ai][bj][m][0], o1 = x1v + g1v * acc[ai][bj][m][1];
;                     u32x4 ow; ow.x = pk2(o0[0], o0[1]); ow.y = pk2(o0[2], o0[3]); ow.z = pk2(o1[0], o1[1]); ow.w = pk2(o1[2], o1[3]);
;                     *(u32x4*)(xo + (ro + cofs) * 2 + loff2) = ow; }
.LBB0_1966:
	s_waitcnt vmcnt(0)
	v_pk_fma_f32 v[110:111], v[110:111], v[118:119], v[126:127]
	v_pk_fma_f32 v[116:117], v[108:109], v[116:117], v[124:125]
	v_pk_fma_f32 v[108:109], v[106:107], v[114:115], v[122:123]
	v_pk_fma_f32 v[112:113], v[112:113], v[120:121], v[128:129]
	v_cvt_pk_bf16_f32 v106, v110, v111
	v_cvt_pk_bf16_f32 v107, v112, v113
	v_bfe_u32 v1, v108, 16, 1
	v_add3_u32 v1, v108, v1, s37
	v_bfe_u32 v108, v109, 16, 1
	v_lshrrev_b32_e32 v1, 16, v1
	v_add3_u32 v108, v109, v108, s37
	v_and_or_b32 v108, v108, s33, v1
	v_add_co_u32_e32 v110, vcc, 0x10000, v160
	v_cvt_pk_bf16_f32 v109, v116, v117
	s_nop 0
	v_addc_co_u32_e32 v111, vcc, 0, v161, vcc
	global_store_dwordx4 v[110:111], v[106:109], off
	global_load_dwordx4 v[106:109], v[164:165], off offset:528
	s_nop 0
	global_load_dwordx4 v[110:113], v[164:165], off offset:512
	s_and_b64 vcc, exec, s[38:39]
	s_cbranch_vccnz .LBB0_2013
	s_mov_b64 s[26:27], 0x20200
	v_add_co_u32_e32 v116, vcc, 0x20000, v162
	v_lshl_add_u64 v[114:115], v[162:163], 0, s[26:27]
	s_nop 0
	v_addc_co_u32_e32 v117, vcc, 0, v163, vcc
	global_load_dwordx4 v[118:121], v[116:117], off offset:512
	s_nop 0
	global_load_dwordx4 v[114:117], v[114:115], off offset:16
	s_cbranch_execnz .LBB0_1969

; __device__ __forceinline__ unsigned f2bf(float f) { unsigned u = __builtin_bit_cast(unsigned, f); return (u + 0x7fffu + ((u >> 16) & 1u)) >> 16; }
; __device__ __forceinline__ unsigned pk2(float lo, float hi) { return f2bf(lo) | (f2bf(hi) << 16); }
;     __device__ __forceinline__ void epi(const f32x4 (&acc)[2][2][4][2], const Unit& u, int wr, int wc, int fr, int fq) const {
;     ...
;                     const f32x4 g0 = *(const f32x4*)(g1 + cofs * 4 + lcol * 4), g1v = *(const f32x4*)(g1 + cofs * 4 + lcol * 4 + 16);
;                     f32x4 x0, x1v;
;                     if (f32in) { x0 = *(const f32x4*)(xin + (ro + cofs) * 4 + loff4); x1v = *(const f32x4*)(xin + (ro + cofs) * 4 + loff4 + 16); }
;                     else { const u32x4 w = *(const u32x4*)(xin + (ro + cofs) * 2 + loff2); x0 = (f32x4){bflo(w.x), bfhi(w.x), bflo(w.y), bfhi(w.y)}; x1v = (f32x4){bflo(w.z), bfhi(w.z), bflo(w.w), bfhi(w.w)}; }
;                     const f32x4 o0 = x0 + g0 * acc[ai][bj][m][0], o1 = x1v + g1v * acc[ai][bj][m][1];
;                     u32x4 ow; ow.x = pk2(o0[0], o0[1]); ow.y = pk2(o0[2], o0[3]); ow.z = pk2(o1[0], o1[1]); ow.w = pk2(o1[2], o1[3]);
;                     *(u32x4*)(xo + (ro + cofs) * 2 + loff2) = ow; }
.LBB0_1969:
	s_waitcnt vmcnt(0)
	v_pk_fma_f32 v[102:103], v[102:103], v[110:111], v[118:119]
	v_pk_fma_f32 v[108:109], v[100:101], v[108:109], v[116:117]
	v_pk_fma_f32 v[100:101], v[98:99], v[106:107], v[114:115]
	v_pk_fma_f32 v[104:105], v[104:105], v[112:113], v[120:121]
	v_cvt_pk_bf16_f32 v98, v102, v103
	v_cvt_pk_bf16_f32 v99, v104, v105
	v_bfe_u32 v1, v100, 16, 1
	v_add3_u32 v1, v100, v1, s37
	v_bfe_u32 v100, v101, 16, 1
	v_lshrrev_b32_e32 v1, 16, v1
	v_add3_u32 v100, v101, v100, s37
	v_and_or_b32 v100, v100, s33, v1
	v_add_co_u32_e32 v102, vcc, 0x10000, v160
	v_cvt_pk_bf16_f32 v101, v108, v109
	s_nop 0
	v_addc_co_u32_e32 v103, vcc, 0, v161, vcc
	global_store_dwordx4 v[102:103], v[98:101], off offset:256
	global_load_dwordx4 v[98:101], v[164:165], off offset:16
	global_load_dwordx4 v[102:105], v[164:165], off
	s_and_b64 vcc, exec, s[38:39]
	s_cbranch_vccnz .LBB0_2014
	s_mov_b64 s[26:27], 0x40000
	v_add_co_u32_e32 v108, vcc, 0x40000, v162
	v_lshl_add_u64 v[106:107], v[162:163], 0, s[26:27]
	s_nop 0
	v_addc_co_u32_e32 v109, vcc, 0, v163, vcc
	global_load_dwordx4 v[110:113], v[108:109], off
	s_nop 0
	global_load_dwordx4 v[106:109], v[106:107], off offset:16
	s_cbranch_execnz .LBB0_1972

; __device__ __forceinline__ unsigned f2bf(float f) { unsigned u = __builtin_bit_cast(unsigned, f); return (u + 0x7fffu + ((u >> 16) & 1u)) >> 16; }
; __device__ __forceinline__ unsigned pk2(float lo, float hi) { return f2bf(lo) | (f2bf(hi) << 16); }
;     __device__ __forceinline__ void epi(const f32x4 (&acc)[2][2][4][2], const Unit& u, int wr, int wc, int fr, int fq) const {
;     ...
;                     const f32x4 g0 = *(const f32x4*)(g1 + cofs * 4 + lcol * 4), g1v = *(const f32x4*)(g1 + cofs * 4 + lcol * 4 + 16);
;                     f32x4 x0, x1v;
;                     if (f32in) { x0 = *(const f32x4*)(xin + (ro + cofs) * 4 + loff4); x1v = *(const f32x4*)(xin + (ro + cofs) * 4 + loff4 + 16); }
;                     else { const u32x4 w = *(const u32x4*)(xin + (ro + cofs) * 2 + loff2); x0 = (f32x4){bflo(w.x), bfhi(w.x), bflo(w.y), bfhi(w.y)}; x1v = (f32x4){bflo(w.z), bfhi(w.z), bflo(w.w), bfhi(w.w)}; }
;                     const f32x4 o0 = x0 + g0 * acc[ai][bj][m][0], o1 = x1v + g1v * acc[ai][bj][m][1];
;                     u32x4 ow; ow.x = pk2(o0[0], o0[1]); ow.y = pk2(o0[2], o0[3]); ow.z = pk2(o1[0], o1[1]); ow.w = pk2(o1[2], o1[3]);
;                     *(u32x4*)(xo + (ro + cofs) * 2 + loff2) = ow; }
.LBB0_1972:
	s_waitcnt vmcnt(0)
	v_pk_fma_f32 v[94:95], v[94:95], v[102:103], v[110:111]
	v_pk_fma_f32 v[100:101], v[92:93], v[100:101], v[108:109]
	v_pk_fma_f32 v[92:93], v[90:91], v[98:99], v[106:107]
	v_pk_fma_f32 v[96:97], v[96:97], v[104:105], v[112:113]
	v_cvt_pk_bf16_f32 v90, v94, v95
	v_cvt_pk_bf16_f32 v91, v96, v97
	v_bfe_u32 v1, v92, 16, 1
	v_add3_u32 v1, v92, v1, s37
	v_bfe_u32 v92, v93, 16, 1
	v_lshrrev_b32_e32 v1, 16, v1
	v_add3_u32 v92, v93, v92, s37
	v_and_or_b32 v92, v92, s33, v1
	v_add_co_u32_e32 v94, vcc, 0x20000, v160
	v_cvt_pk_bf16_f32 v93, v100, v101
	s_nop 0
	v_addc_co_u32_e32 v95, vcc, 0, v161, vcc
	global_store_dwordx4 v[94:95], v[90:93], off
	global_load_dwordx4 v[90:93], v[164:165], off offset:528
	s_nop 0
	global_load_dwordx4 v[94:97], v[164:165], off offset:512
	s_and_b64 vcc, exec, s[38:39]
	s_cbranch_vccnz .LBB0_2015
	s_mov_b64 s[26:27], 0x40200
	v_add_co_u32_e32 v100, vcc, 0x40000, v162
	v_lshl_add_u64 v[98:99], v[162:163], 0, s[26:27]
	s_nop 0
	v_addc_co_u32_e32 v101, vcc, 0, v163, vcc
	global_load_dwordx4 v[102:105], v[100:101], off offset:512
	s_nop 0
	global_load_dwordx4 v[98:101], v[98:99], off offset:16
	s_cbranch_execnz .LBB0_1975

; __device__ __forceinline__ unsigned f2bf(float f) { unsigned u = __builtin_bit_cast(unsigned, f); return (u + 0x7fffu + ((u >> 16) & 1u)) >> 16; }
; __device__ __forceinline__ unsigned pk2(float lo, float hi) { return f2bf(lo) | (f2bf(hi) << 16); }
;     __device__ __forceinline__ void epi(const f32x4 (&acc)[2][2][4][2], const Unit& u, int wr, int wc, int fr, int fq) const {
;     ...
;                     const f32x4 g0 = *(const f32x4*)(g1 + cofs * 4 + lcol * 4), g1v = *(const f32x4*)(g1 + cofs * 4 + lcol * 4 + 16);
;                     f32x4 x0, x1v;
;                     if (f32in) { x0 = *(const f32x4*)(xin + (ro + cofs) * 4 + loff4); x1v = *(const f32x4*)(xin + (ro + cofs) * 4 + loff4 + 16); }
;                     else { const u32x4 w = *(const u32x4*)(xin + (ro + cofs) * 2 + loff2); x0 = (f32x4){bflo(w.x), bfhi(w.x), bflo(w.y), bfhi(w.y)}; x1v = (f32x4){bflo(w.z), bfhi(w.z), bflo(w.w), bfhi(w.w)}; }
;                     const f32x4 o0 = x0 + g0 * acc[ai][bj][m][0], o1 = x1v + g1v * acc[ai][bj][m][1];
;                     u32x4 ow; ow.x = pk2(o0[0], o0[1]); ow.y = pk2(o0[2], o0[3]); ow.z = pk2(o1[0], o1[1]); ow.w = pk2(o1[2], o1[3]);
;                     *(u32x4*)(xo + (ro + cofs) * 2 + loff2) = ow; }
.LBB0_1975:
	s_waitcnt vmcnt(0)
	v_pk_fma_f32 v[86:87], v[86:87], v[94:95], v[102:103]
	v_pk_fma_f32 v[92:93], v[84:85], v[92:93], v[100:101]
	v_pk_fma_f32 v[84:85], v[82:83], v[90:91], v[98:99]
	v_pk_fma_f32 v[88:89], v[88:89], v[96:97], v[104:105]
	v_cvt_pk_bf16_f32 v82, v86, v87
	v_cvt_pk_bf16_f32 v83, v88, v89
	v_bfe_u32 v1, v84, 16, 1
	v_add3_u32 v1, v84, v1, s37
	v_bfe_u32 v84, v85, 16, 1
	v_lshrrev_b32_e32 v1, 16, v1
	v_add3_u32 v84, v85, v84, s37
	v_and_or_b32 v84, v84, s33, v1
	v_add_co_u32_e32 v86, vcc, 0x20000, v160
	v_cvt_pk_bf16_f32 v85, v92, v93
	s_nop 0
	v_addc_co_u32_e32 v87, vcc, 0, v161, vcc
	global_store_dwordx4 v[86:87], v[82:85], off offset:256
	global_load_dwordx4 v[82:85], v[164:165], off offset:16
	global_load_dwordx4 v[86:89], v[164:165], off
	s_and_b64 vcc, exec, s[38:39]
	s_cbranch_vccnz .LBB0_2016
	s_mov_b64 s[26:27], 0x60000
	v_add_co_u32_e32 v92, vcc, 0x60000, v162
	v_lshl_add_u64 v[90:91], v[162:163], 0, s[26:27]
	s_nop 0
	v_addc_co_u32_e32 v93, vcc, 0, v163, vcc
	global_load_dwordx4 v[94:97], v[92:93], off
	s_nop 0
	global_load_dwordx4 v[90:93], v[90:91], off offset:16
	s_cbranch_execnz .LBB0_1978

; __device__ __forceinline__ unsigned f2bf(float f) { unsigned u = __builtin_bit_cast(unsigned, f); return (u + 0x7fffu + ((u >> 16) & 1u)) >> 16; }
; __device__ __forceinline__ unsigned pk2(float lo, float hi) { return f2bf(lo) | (f2bf(hi) << 16); }
;     __device__ __forceinline__ void epi(const f32x4 (&acc)[2][2][4][2], const Unit& u, int wr, int wc, int fr, int fq) const {
;     ...
;                     const f32x4 g0 = *(const f32x4*)(g1 + cofs * 4 + lcol * 4), g1v = *(const f32x4*)(g1 + cofs * 4 + lcol * 4 + 16);
;                     f32x4 x0, x1v;
;                     if (f32in) { x0 = *(const f32x4*)(xin + (ro + cofs) * 4 + loff4); x1v = *(const f32x4*)(xin + (ro + cofs) * 4 + loff4 + 16); }
;                     else { const u32x4 w = *(const u32x4*)(xin + (ro + cofs) * 2 + loff2); x0 = (f32x4){bflo(w.x), bfhi(w.x), bflo(w.y), bfhi(w.y)}; x1v = (f32x4){bflo(w.z), bfhi(w.z), bflo(w.w), bfhi(w.w)}; }
;                     const f32x4 o0 = x0 + g0 * acc[ai][bj][m][0], o1 = x1v + g1v * acc[ai][bj][m][1];
;                     u32x4 ow; ow.x = pk2(o0[0], o0[1]); ow.y = pk2(o0[2], o0[3]); ow.z = pk2(o1[0], o1[1]); ow.w = pk2(o1[2], o1[3]);
;                     *(u32x4*)(xo + (ro + cofs) * 2 + loff2) = ow; }
.LBB0_1978:
	s_waitcnt vmcnt(0)
	v_pk_fma_f32 v[78:79], v[78:79], v[86:87], v[94:95]
	v_pk_fma_f32 v[84:85], v[76:77], v[84:85], v[92:93]
	v_pk_fma_f32 v[76:77], v[74:75], v[82:83], v[90:91]
	v_pk_fma_f32 v[80:81], v[80:81], v[88:89], v[96:97]
	v_cvt_pk_bf16_f32 v74, v78, v79
	v_cvt_pk_bf16_f32 v75, v80, v81
	v_bfe_u32 v1, v76, 16, 1
	v_add3_u32 v1, v76, v1, s37
	v_bfe_u32 v76, v77, 16, 1
	v_lshrrev_b32_e32 v1, 16, v1
	v_add3_u32 v76, v77, v76, s37
	v_and_or_b32 v76, v76, s33, v1
	v_add_co_u32_e32 v78, vcc, 0x30000, v160
	v_cvt_pk_bf16_f32 v77, v84, v85
	s_nop 0
	v_addc_co_u32_e32 v79, vcc, 0, v161, vcc
	global_store_dwordx4 v[78:79], v[74:77], off
	global_load_dwordx4 v[74:77], v[164:165], off offset:528
	s_nop 0
	global_load_dwordx4 v[78:81], v[164:165], off offset:512
	s_and_b64 vcc, exec, s[38:39]
	s_cbranch_vccnz .LBB0_2017
	s_mov_b64 s[26:27], 0x60200
	v_add_co_u32_e32 v84, vcc, 0x60000, v162
	v_lshl_add_u64 v[82:83], v[162:163], 0, s[26:27]
	s_nop 0
	v_addc_co_u32_e32 v85, vcc, 0, v163, vcc
	global_load_dwordx4 v[86:89], v[84:85], off offset:512
	s_nop 0
	global_load_dwordx4 v[82:85], v[82:83], off offset:16
	s_cbranch_execnz .LBB0_1981

; __device__ __forceinline__ unsigned f2bf(float f) { unsigned u = __builtin_bit_cast(unsigned, f); return (u + 0x7fffu + ((u >> 16) & 1u)) >> 16; }
; __device__ __forceinline__ unsigned pk2(float lo, float hi) { return f2bf(lo) | (f2bf(hi) << 16); }
;     __device__ __forceinline__ void epi(const f32x4 (&acc)[2][2][4][2], const Unit& u, int wr, int wc, int fr, int fq) const {
;     ...
;                     const f32x4 g0 = *(const f32x4*)(g1 + cofs * 4 + lcol * 4), g1v = *(const f32x4*)(g1 + cofs * 4 + lcol * 4 + 16);
;                     f32x4 x0, x1v;
;                     if (f32in) { x0 = *(const f32x4*)(xin + (ro + cofs) * 4 + loff4); x1v = *(const f32x4*)(xin + (ro + cofs) * 4 + loff4 + 16); }
;                     else { const u32x4 w = *(const u32x4*)(xin + (ro + cofs) * 2 + loff2); x0 = (f32x4){bflo(w.x), bfhi(w.x), bflo(w.y), bfhi(w.y)}; x1v = (f32x4){bflo(w.z), bfhi(w.z), bflo(w.w), bfhi(w.w)}; }
;                     const f32x4 o0 = x0 + g0 * acc[ai][bj][m][0], o1 = x1v + g1v * acc[ai][bj][m][1];
;                     u32x4 ow; ow.x = pk2(o0[0], o0[1]); ow.y = pk2(o0[2], o0[3]); ow.z = pk2(o1[0], o1[1]); ow.w = pk2(o1[2], o1[3]);
;                     *(u32x4*)(xo + (ro + cofs) * 2 + loff2) = ow; }
.LBB0_1981:
	s_waitcnt vmcnt(0)
	v_pk_fma_f32 v[70:71], v[70:71], v[78:79], v[86:87]
	v_pk_fma_f32 v[76:77], v[68:69], v[76:77], v[84:85]
	v_pk_fma_f32 v[68:69], v[66:67], v[74:75], v[82:83]
	v_pk_fma_f32 v[72:73], v[72:73], v[80:81], v[88:89]
	v_cvt_pk_bf16_f32 v66, v70, v71
	v_cvt_pk_bf16_f32 v67, v72, v73
	v_bfe_u32 v1, v68, 16, 1
	v_add3_u32 v1, v68, v1, s37
	v_bfe_u32 v68, v69, 16, 1
	v_lshrrev_b32_e32 v1, 16, v1
	v_add3_u32 v68, v69, v68, s37
	v_and_or_b32 v68, v68, s33, v1
	v_add_co_u32_e32 v70, vcc, 0x30000, v160
	v_cvt_pk_bf16_f32 v69, v76, v77
	s_nop 0
	v_addc_co_u32_e32 v71, vcc, 0, v161, vcc
	global_store_dwordx4 v[70:71], v[66:69], off offset:256
	global_load_dwordx4 v[66:69], v[164:165], off offset:16
	global_load_dwordx4 v[70:73], v[164:165], off
	s_and_b64 vcc, exec, s[38:39]
	s_cbranch_vccnz .LBB0_2018
	s_mov_b64 s[26:27], 0x100000
	v_add_co_u32_e32 v76, vcc, 0x100000, v162
	v_lshl_add_u64 v[74:75], v[162:163], 0, s[26:27]
	s_nop 0
	v_addc_co_u32_e32 v77, vcc, 0, v163, vcc
	global_load_dwordx4 v[78:81], v[76:77], off
	s_nop 0
	global_load_dwordx4 v[74:77], v[74:75], off offset:16
	s_cbranch_execnz .LBB0_1984

; __device__ __forceinline__ unsigned f2bf(float f) { unsigned u = __builtin_bit_cast(unsigned, f); return (u + 0x7fffu + ((u >> 16) & 1u)) >> 16; }
; __device__ __forceinline__ unsigned pk2(float lo, float hi) { return f2bf(lo) | (f2bf(hi) << 16); }
;     __device__ __forceinline__ void epi(const f32x4 (&acc)[2][2][4][2], const Unit& u, int wr, int wc, int fr, int fq) const {
;     ...
;                     const f32x4 g0 = *(const f32x4*)(g1 + cofs * 4 + lcol * 4), g1v = *(const f32x4*)(g1 + cofs * 4 + lcol * 4 + 16);
;                     f32x4 x0, x1v;
;                     if (f32in) { x0 = *(const f32x4*)(xin + (ro + cofs) * 4 + loff4); x1v = *(const f32x4*)(xin + (ro + cofs) * 4 + loff4 + 16); }
;                     else { const u32x4 w = *(const u32x4*)(xin + (ro + cofs) * 2 + loff2); x0 = (f32x4){bflo(w.x), bfhi(w.x), bflo(w.y), bfhi(w.y)}; x1v = (f32x4){bflo(w.z), bfhi(w.z), bflo(w.w), bfhi(w.w)}; }
;                     const f32x4 o0 = x0 + g0 * acc[ai][bj][m][0], o1 = x1v + g1v * acc[ai][bj][m][1];
;                     u32x4 ow; ow.x = pk2(o0[0], o0[1]); ow.y = pk2(o0[2], o0[3]); ow.z = pk2(o1[0], o1[1]); ow.w = pk2(o1[2], o1[3]);
;                     *(u32x4*)(xo + (ro + cofs) * 2 + loff2) = ow; }
.LBB0_1984:
	s_waitcnt vmcnt(0)
	v_pk_fma_f32 v[62:63], v[62:63], v[70:71], v[78:79]
	v_pk_fma_f32 v[68:69], v[60:61], v[68:69], v[76:77]
	v_pk_fma_f32 v[60:61], v[58:59], v[66:67], v[74:75]
	v_pk_fma_f32 v[64:65], v[64:65], v[72:73], v[80:81]
	v_cvt_pk_bf16_f32 v58, v62, v63
	v_cvt_pk_bf16_f32 v59, v64, v65
	v_bfe_u32 v1, v60, 16, 1
	v_add3_u32 v1, v60, v1, s37
	v_bfe_u32 v60, v61, 16, 1
	v_lshrrev_b32_e32 v1, 16, v1
	v_add3_u32 v60, v61, v60, s37
	v_and_or_b32 v60, v60, s33, v1
	v_add_co_u32_e32 v62, vcc, 0x80000, v160
	v_cvt_pk_bf16_f32 v61, v68, v69
	s_nop 0
	v_addc_co_u32_e32 v63, vcc, 0, v161, vcc
	global_store_dwordx4 v[62:63], v[58:61], off
	global_load_dwordx4 v[58:61], v[164:165], off offset:528
	s_nop 0
	global_load_dwordx4 v[62:65], v[164:165], off offset:512
	s_and_b64 vcc, exec, s[38:39]
	s_cbranch_vccnz .LBB0_2019
	s_mov_b64 s[26:27], 0x100200
	v_add_co_u32_e32 v68, vcc, 0x100000, v162
	v_lshl_add_u64 v[66:67], v[162:163], 0, s[26:27]
	s_nop 0
	v_addc_co_u32_e32 v69, vcc, 0, v163, vcc
	global_load_dwordx4 v[70:73], v[68:69], off offset:512
	s_nop 0
	global_load_dwordx4 v[66:69], v[66:67], off offset:16
	s_cbranch_execnz .LBB0_1987

; __device__ __forceinline__ unsigned f2bf(float f) { unsigned u = __builtin_bit_cast(unsigned, f); return (u + 0x7fffu + ((u >> 16) & 1u)) >> 16; }
; __device__ __forceinline__ unsigned pk2(float lo, float hi) { return f2bf(lo) | (f2bf(hi) << 16); }
;     __device__ __forceinline__ void epi(const f32x4 (&acc)[2][2][4][2], const Unit& u, int wr, int wc, int fr, int fq) const {
;     ...
;                     const f32x4 g0 = *(const f32x4*)(g1 + cofs * 4 + lcol * 4), g1v = *(const f32x4*)(g1 + cofs * 4 + lcol * 4 + 16);
;                     f32x4 x0, x1v;
;                     if (f32in) { x0 = *(const f32x4*)(xin + (ro + cofs) * 4 + loff4); x1v = *(const f32x4*)(xin + (ro + cofs) * 4 + loff4 + 16); }
;                     else { const u32x4 w = *(const u32x4*)(xin + (ro + cofs) * 2 + loff2); x0 = (f32x4){bflo(w.x), bfhi(w.x), bflo(w.y), bfhi(w.y)}; x1v = (f32x4){bflo(w.z), bfhi(w.z), bflo(w.w), bfhi(w.w)}; }
;                     const f32x4 o0 = x0 + g0 * acc[ai][bj][m][0], o1 = x1v + g1v * acc[ai][bj][m][1];
;                     u32x4 ow; ow.x = pk2(o0[0], o0[1]); ow.y = pk2(o0[2], o0[3]); ow.z = pk2(o1[0], o1[1]); ow.w = pk2(o1[2], o1[3]);
;                     *(u32x4*)(xo + (ro + cofs) * 2 + loff2) = ow; }
.LBB0_1987:
	s_waitcnt vmcnt(0)
	v_pk_fma_f32 v[54:55], v[54:55], v[62:63], v[70:71]
	v_pk_fma_f32 v[60:61], v[52:53], v[60:61], v[68:69]
	v_pk_fma_f32 v[52:53], v[50:51], v[58:59], v[66:67]
	v_pk_fma_f32 v[56:57], v[56:57], v[64:65], v[72:73]
	v_cvt_pk_bf16_f32 v50, v54, v55
	v_cvt_pk_bf16_f32 v51, v56, v57
	v_bfe_u32 v1, v52, 16, 1
	v_add3_u32 v1, v52, v1, s37
	v_bfe_u32 v52, v53, 16, 1
	v_lshrrev_b32_e32 v1, 16, v1
	v_add3_u32 v52, v53, v52, s37
	v_and_or_b32 v52, v52, s33, v1
	v_add_co_u32_e32 v54, vcc, 0x80000, v160
	v_cvt_pk_bf16_f32 v53, v60, v61
	s_nop 0
	v_addc_co_u32_e32 v55, vcc, 0, v161, vcc
	global_store_dwordx4 v[54:55], v[50:53], off offset:256
	global_load_dwordx4 v[50:53], v[164:165], off offset:16
	global_load_dwordx4 v[54:57], v[164:165], off
	s_and_b64 vcc, exec, s[38:39]
	s_cbranch_vccnz .LBB0_2020
	s_mov_b64 s[26:27], 0x120000
	v_add_co_u32_e32 v60, vcc, 0x120000, v162
	v_lshl_add_u64 v[58:59], v[162:163], 0, s[26:27]
	s_nop 0
	v_addc_co_u32_e32 v61, vcc, 0, v163, vcc
	global_load_dwordx4 v[62:65], v[60:61], off
	s_nop 0
	global_load_dwordx4 v[58:61], v[58:59], off offset:16
	s_cbranch_execnz .LBB0_1990

; __device__ __forceinline__ unsigned f2bf(float f) { unsigned u = __builtin_bit_cast(unsigned, f); return (u + 0x7fffu + ((u >> 16) & 1u)) >> 16; }
; __device__ __forceinline__ unsigned pk2(float lo, float hi) { return f2bf(lo) | (f2bf(hi) << 16); }
;     __device__ __forceinline__ void epi(const f32x4 (&acc)[2][2][4][2], const Unit& u, int wr, int wc, int fr, int fq) const {
;     ...
;                     const f32x4 g0 = *(const f32x4*)(g1 + cofs * 4 + lcol * 4), g1v = *(const f32x4*)(g1 + cofs * 4 + lcol * 4 + 16);
;                     f32x4 x0, x1v;
;                     if (f32in) { x0 = *(const f32x4*)(xin + (ro + cofs) * 4 + loff4); x1v = *(const f32x4*)(xin + (ro + cofs) * 4 + loff4 + 16); }
;                     else { const u32x4 w = *(const u32x4*)(xin + (ro + cofs) * 2 + loff2); x0 = (f32x4){bflo(w.x), bfhi(w.x), bflo(w.y), bfhi(w.y)}; x1v = (f32x4){bflo(w.z), bfhi(w.z), bflo(w.w), bfhi(w.w)}; }
;                     const f32x4 o0 = x0 + g0 * acc[ai][bj][m][0], o1 = x1v + g1v * acc[ai][bj][m][1];
;                     u32x4 ow; ow.x = pk2(o0[0], o0[1]); ow.y = pk2(o0[2], o0[3]); ow.z = pk2(o1[0], o1[1]); ow.w = pk2(o1[2], o1[3]);
;                     *(u32x4*)(xo + (ro + cofs) * 2 + loff2) = ow; }
.LBB0_1990:
	s_waitcnt vmcnt(0)
	v_pk_fma_f32 v[46:47], v[46:47], v[54:55], v[62:63]
	v_pk_fma_f32 v[52:53], v[44:45], v[52:53], v[60:61]
	v_pk_fma_f32 v[44:45], v[42:43], v[50:51], v[58:59]
	v_pk_fma_f32 v[48:49], v[48:49], v[56:57], v[64:65]
	v_cvt_pk_bf16_f32 v42, v46, v47
	v_cvt_pk_bf16_f32 v43, v48, v49
	v_bfe_u32 v1, v44, 16, 1
	v_add3_u32 v1, v44, v1, s37
	v_bfe_u32 v44, v45, 16, 1
	v_lshrrev_b32_e32 v1, 16, v1
	v_add3_u32 v44, v45, v44, s37
	v_and_or_b32 v44, v44, s33, v1
	v_add_co_u32_e32 v46, vcc, 0x90000, v160
	v_cvt_pk_bf16_f32 v45, v52, v53
	s_nop 0
	v_addc_co_u32_e32 v47, vcc, 0, v161, vcc
	global_store_dwordx4 v[46:47], v[42:45], off
	global_load_dwordx4 v[42:45], v[164:165], off offset:528
	s_nop 0
	global_load_dwordx4 v[46:49], v[164:165], off offset:512
	s_and_b64 vcc, exec, s[38:39]
	s_cbranch_vccnz .LBB0_2021
	s_mov_b64 s[26:27], 0x120200
	v_add_co_u32_e32 v52, vcc, 0x120000, v162
	v_lshl_add_u64 v[50:51], v[162:163], 0, s[26:27]
	s_nop 0
	v_addc_co_u32_e32 v53, vcc, 0, v163, vcc
	global_load_dwordx4 v[54:57], v[52:53], off offset:512
	s_nop 0
	global_load_dwordx4 v[50:53], v[50:51], off offset:16
	s_cbranch_execnz .LBB0_1993

; __device__ __forceinline__ unsigned f2bf(float f) { unsigned u = __builtin_bit_cast(unsigned, f); return (u + 0x7fffu + ((u >> 16) & 1u)) >> 16; }
; __device__ __forceinline__ unsigned pk2(float lo, float hi) { return f2bf(lo) | (f2bf(hi) << 16); }
;     __device__ __forceinline__ void epi(const f32x4 (&acc)[2][2][4][2], const Unit& u, int wr, int wc, int fr, int fq) const {
;     ...
;                     const f32x4 g0 = *(const f32x4*)(g1 + cofs * 4 + lcol * 4), g1v = *(const f32x4*)(g1 + cofs * 4 + lcol * 4 + 16);
;                     f32x4 x0, x1v;
;                     if (f32in) { x0 = *(const f32x4*)(xin + (ro + cofs) * 4 + loff4); x1v = *(const f32x4*)(xin + (ro + cofs) * 4 + loff4 + 16); }
;                     else { const u32x4 w = *(const u32x4*)(xin + (ro + cofs) * 2 + loff2); x0 = (f32x4){bflo(w.x), bfhi(w.x), bflo(w.y), bfhi(w.y)}; x1v = (f32x4){bflo(w.z), bfhi(w.z), bflo(w.w), bfhi(w.w)}; }
;                     const f32x4 o0 = x0 + g0 * acc[ai][bj][m][0], o1 = x1v + g1v * acc[ai][bj][m][1];
;                     u32x4 ow; ow.x = pk2(o0[0], o0[1]); ow.y = pk2(o0[2], o0[3]); ow.z = pk2(o1[0], o1[1]); ow.w = pk2(o1[2], o1[3]);
;                     *(u32x4*)(xo + (ro + cofs) * 2 + loff2) = ow; }
.LBB0_1993:
	s_waitcnt vmcnt(0)
	v_pk_fma_f32 v[38:39], v[38:39], v[46:47], v[54:55]
	v_pk_fma_f32 v[44:45], v[36:37], v[44:45], v[52:53]
	v_pk_fma_f32 v[36:37], v[34:35], v[42:43], v[50:51]
	v_pk_fma_f32 v[40:41], v[40:41], v[48:49], v[56:57]
	v_cvt_pk_bf16_f32 v34, v38, v39
	v_cvt_pk_bf16_f32 v35, v40, v41
	v_bfe_u32 v1, v36, 16, 1
	v_add3_u32 v1, v36, v1, s37
	v_bfe_u32 v36, v37, 16, 1
	v_lshrrev_b32_e32 v1, 16, v1
	v_add3_u32 v36, v37, v36, s37
	v_and_or_b32 v36, v36, s33, v1
	v_add_co_u32_e32 v38, vcc, 0x90000, v160
	v_cvt_pk_bf16_f32 v37, v44, v45
	s_nop 0
	v_addc_co_u32_e32 v39, vcc, 0, v161, vcc
	global_store_dwordx4 v[38:39], v[34:37], off offset:256
	global_load_dwordx4 v[34:37], v[164:165], off offset:16
	global_load_dwordx4 v[38:41], v[164:165], off
	s_and_b64 vcc, exec, s[38:39]
	s_cbranch_vccnz .LBB0_2022
	s_mov_b64 s[26:27], 0x140000
	v_add_co_u32_e32 v44, vcc, 0x140000, v162
	v_lshl_add_u64 v[42:43], v[162:163], 0, s[26:27]
	s_nop 0
	v_addc_co_u32_e32 v45, vcc, 0, v163, vcc
	global_load_dwordx4 v[46:49], v[44:45], off
	s_nop 0
	global_load_dwordx4 v[42:45], v[42:43], off offset:16
	s_cbranch_execnz .LBB0_1996

; __device__ __forceinline__ unsigned f2bf(float f) { unsigned u = __builtin_bit_cast(unsigned, f); return (u + 0x7fffu + ((u >> 16) & 1u)) >> 16; }
; __device__ __forceinline__ unsigned pk2(float lo, float hi) { return f2bf(lo) | (f2bf(hi) << 16); }
;     __device__ __forceinline__ void epi(const f32x4 (&acc)[2][2][4][2], const Unit& u, int wr, int wc, int fr, int fq) const {
;     ...
;                     const f32x4 g0 = *(const f32x4*)(g1 + cofs * 4 + lcol * 4), g1v = *(const f32x4*)(g1 + cofs * 4 + lcol * 4 + 16);
;                     f32x4 x0, x1v;
;                     if (f32in) { x0 = *(const f32x4*)(xin + (ro + cofs) * 4 + loff4); x1v = *(const f32x4*)(xin + (ro + cofs) * 4 + loff4 + 16); }
;                     else { const u32x4 w = *(const u32x4*)(xin + (ro + cofs) * 2 + loff2); x0 = (f32x4){bflo(w.x), bfhi(w.x), bflo(w.y), bfhi(w.y)}; x1v = (f32x4){bflo(w.z), bfhi(w.z), bflo(w.w), bfhi(w.w)}; }
;                     const f32x4 o0 = x0 + g0 * acc[ai][bj][m][0], o1 = x1v + g1v * acc[ai][bj][m][1];
;                     u32x4 ow; ow.x = pk2(o0[0], o0[1]); ow.y = pk2(o0[2], o0[3]); ow.z = pk2(o1[0], o1[1]); ow.w = pk2(o1[2], o1[3]);
;                     *(u32x4*)(xo + (ro + cofs) * 2 + loff2) = ow; }
.LBB0_1996:
	s_waitcnt vmcnt(0)
	v_pk_fma_f32 v[30:31], v[30:31], v[38:39], v[46:47]
	v_pk_fma_f32 v[36:37], v[28:29], v[36:37], v[44:45]
	v_pk_fma_f32 v[28:29], v[26:27], v[34:35], v[42:43]
	v_pk_fma_f32 v[32:33], v[32:33], v[40:41], v[48:49]
	v_cvt_pk_bf16_f32 v26, v30, v31
	v_cvt_pk_bf16_f32 v27, v32, v33
	v_bfe_u32 v1, v28, 16, 1
	v_add3_u32 v1, v28, v1, s37
	v_bfe_u32 v28, v29, 16, 1
	v_lshrrev_b32_e32 v1, 16, v1
	v_add3_u32 v28, v29, v28, s37
	v_and_or_b32 v28, v28, s33, v1
	v_add_co_u32_e32 v30, vcc, 0xa0000, v160
	v_cvt_pk_bf16_f32 v29, v36, v37
	s_nop 0
	v_addc_co_u32_e32 v31, vcc, 0, v161, vcc
	global_store_dwordx4 v[30:31], v[26:29], off
	global_load_dwordx4 v[26:29], v[164:165], off offset:528
	s_nop 0
	global_load_dwordx4 v[30:33], v[164:165], off offset:512
	s_and_b64 vcc, exec, s[38:39]
	s_cbranch_vccnz .LBB0_2023
	s_mov_b64 s[26:27], 0x140200
	v_add_co_u32_e32 v36, vcc, 0x140000, v162
	v_lshl_add_u64 v[34:35], v[162:163], 0, s[26:27]
	s_nop 0
	v_addc_co_u32_e32 v37, vcc, 0, v163, vcc
	global_load_dwordx4 v[38:41], v[36:37], off offset:512
	s_nop 0
	global_load_dwordx4 v[34:37], v[34:35], off offset:16
	s_cbranch_execnz .LBB0_1999

; __device__ __forceinline__ unsigned f2bf(float f) { unsigned u = __builtin_bit_cast(unsigned, f); return (u + 0x7fffu + ((u >> 16) & 1u)) >> 16; }
; __device__ __forceinline__ unsigned pk2(float lo, float hi) { return f2bf(lo) | (f2bf(hi) << 16); }
;     __device__ __forceinline__ void epi(const f32x4 (&acc)[2][2][4][2], const Unit& u, int wr, int wc, int fr, int fq) const {
;     ...
;                     const f32x4 g0 = *(const f32x4*)(g1 + cofs * 4 + lcol * 4), g1v = *(const f32x4*)(g1 + cofs * 4 + lcol * 4 + 16);
;                     f32x4 x0, x1v;
;                     if (f32in) { x0 = *(const f32x4*)(xin + (ro + cofs) * 4 + loff4); x1v = *(const f32x4*)(xin + (ro + cofs) * 4 + loff4 + 16); }
;                     else { const u32x4 w = *(const u32x4*)(xin + (ro + cofs) * 2 + loff2); x0 = (f32x4){bflo(w.x), bfhi(w.x), bflo(w.y), bfhi(w.y)}; x1v = (f32x4){bflo(w.z), bfhi(w.z), bflo(w.w), bfhi(w.w)}; }
;                     const f32x4 o0 = x0 + g0 * acc[ai][bj][m][0], o1 = x1v + g1v * acc[ai][bj][m][1];
;                     u32x4 ow; ow.x = pk2(o0[0], o0[1]); ow.y = pk2(o0[2], o0[3]); ow.z = pk2(o1[0], o1[1]); ow.w = pk2(o1[2], o1[3]);
;                     *(u32x4*)(xo + (ro + cofs) * 2 + loff2) = ow; }
.LBB0_1999:
	s_waitcnt vmcnt(0)
	v_pk_fma_f32 v[22:23], v[22:23], v[30:31], v[38:39]
	v_pk_fma_f32 v[28:29], v[20:21], v[28:29], v[36:37]
	v_pk_fma_f32 v[20:21], v[18:19], v[26:27], v[34:35]
	v_pk_fma_f32 v[24:25], v[24:25], v[32:33], v[40:41]
	v_cvt_pk_bf16_f32 v18, v22, v23
	v_cvt_pk_bf16_f32 v19, v24, v25
	v_bfe_u32 v1, v20, 16, 1
	v_add3_u32 v1, v20, v1, s37
	v_bfe_u32 v20, v21, 16, 1
	v_lshrrev_b32_e32 v1, 16, v1
	v_add3_u32 v20, v21, v20, s37
	v_and_or_b32 v20, v20, s33, v1
	v_add_co_u32_e32 v22, vcc, 0xa0000, v160
	v_cvt_pk_bf16_f32 v21, v28, v29
	s_nop 0
	v_addc_co_u32_e32 v23, vcc, 0, v161, vcc
	global_store_dwordx4 v[22:23], v[18:21], off offset:256
	global_load_dwordx4 v[18:21], v[164:165], off offset:16
	global_load_dwordx4 v[22:25], v[164:165], off
	s_and_b64 vcc, exec, s[38:39]
	s_cbranch_vccnz .LBB0_2024
	s_mov_b64 s[26:27], 0x160000
	v_add_co_u32_e32 v28, vcc, 0x160000, v162
	v_lshl_add_u64 v[26:27], v[162:163], 0, s[26:27]
	s_nop 0
	v_addc_co_u32_e32 v29, vcc, 0, v163, vcc
	global_load_dwordx4 v[30:33], v[28:29], off
	s_nop 0
	global_load_dwordx4 v[26:29], v[26:27], off offset:16
	s_cbranch_execnz .LBB0_2002

; __device__ __forceinline__ unsigned f2bf(float f) { unsigned u = __builtin_bit_cast(unsigned, f); return (u + 0x7fffu + ((u >> 16) & 1u)) >> 16; }
; __device__ __forceinline__ unsigned pk2(float lo, float hi) { return f2bf(lo) | (f2bf(hi) << 16); }
;     __device__ __forceinline__ void epi(const f32x4 (&acc)[2][2][4][2], const Unit& u, int wr, int wc, int fr, int fq) const {
;     ...
;                     const f32x4 g0 = *(const f32x4*)(g1 + cofs * 4 + lcol * 4), g1v = *(const f32x4*)(g1 + cofs * 4 + lcol * 4 + 16);
;                     f32x4 x0, x1v;
;                     if (f32in) { x0 = *(const f32x4*)(xin + (ro + cofs) * 4 + loff4); x1v = *(const f32x4*)(xin + (ro + cofs) * 4 + loff4 + 16); }
;                     else { const u32x4 w = *(const u32x4*)(xin + (ro + cofs) * 2 + loff2); x0 = (f32x4){bflo(w.x), bfhi(w.x), bflo(w.y), bfhi(w.y)}; x1v = (f32x4){bflo(w.z), bfhi(w.z), bflo(w.w), bfhi(w.w)}; }
;                     const f32x4 o0 = x0 + g0 * acc[ai][bj][m][0], o1 = x1v + g1v * acc[ai][bj][m][1];
;                     u32x4 ow; ow.x = pk2(o0[0], o0[1]); ow.y = pk2(o0[2], o0[3]); ow.z = pk2(o1[0], o1[1]); ow.w = pk2(o1[2], o1[3]);
;                     *(u32x4*)(xo + (ro + cofs) * 2 + loff2) = ow; }
.LBB0_2002:
	s_waitcnt vmcnt(0)
	v_pk_fma_f32 v[14:15], v[14:15], v[22:23], v[30:31]
	v_pk_fma_f32 v[20:21], v[12:13], v[20:21], v[28:29]
	v_pk_fma_f32 v[12:13], v[10:11], v[18:19], v[26:27]
	v_pk_fma_f32 v[16:17], v[16:17], v[24:25], v[32:33]
	v_cvt_pk_bf16_f32 v10, v14, v15
	v_cvt_pk_bf16_f32 v11, v16, v17
	v_bfe_u32 v1, v12, 16, 1
	v_add3_u32 v1, v12, v1, s37
	v_bfe_u32 v12, v13, 16, 1
	v_lshrrev_b32_e32 v1, 16, v1
	v_add3_u32 v12, v13, v12, s37
	v_and_or_b32 v12, v12, s33, v1
	v_add_co_u32_e32 v14, vcc, 0xb0000, v160
	v_cvt_pk_bf16_f32 v13, v20, v21
	s_nop 0
	v_addc_co_u32_e32 v15, vcc, 0, v161, vcc
	global_store_dwordx4 v[14:15], v[10:13], off
	global_load_dwordx4 v[10:13], v[164:165], off offset:528
	s_nop 0
	global_load_dwordx4 v[14:17], v[164:165], off offset:512
	s_and_b64 vcc, exec, s[38:39]
	s_cbranch_vccnz .LBB0_2025
	s_mov_b64 s[26:27], 0x160200
	v_add_co_u32_e32 v20, vcc, 0x160000, v162
	v_lshl_add_u64 v[18:19], v[162:163], 0, s[26:27]
	s_nop 0
	v_addc_co_u32_e32 v21, vcc, 0, v163, vcc
	global_load_dwordx4 v[22:25], v[20:21], off offset:512
	s_nop 0
	global_load_dwordx4 v[18:21], v[18:19], off offset:16
	s_cbranch_execnz .LBB0_2005

; __device__ __forceinline__ unsigned pk2(float lo, float hi) { return f2bf(lo) | (f2bf(hi) << 16); }
; #define PG8_BAR __builtin_amdgcn_s_barrier()
; template <class P>
; __device__ __forceinline__ void gemm_phase(LAS unsigned char* lds, const P& p) {
;     ...
;         if (wr == 0) PG8_BAR;
;         p.epi(acc, cur, wr, wc, fr, fq);
;         if (!has_next) break;
; #pragma unroll
;         for (int a = 0; a < 2; ++a)
; #pragma unroll
;             for (int b = 0; b < 2; ++b)
; #pragma unroll
;                 for (int m = 0; m < 4; ++m)
; #pragma unroll
;                     for (int n = 0; n < 2; ++n) acc[a][b][m][n] = (f32x4){0.f, 0.f, 0.f, 0.f};
;         cur = nxt; cA = nA; cB = nB; ++ui;
;         if (wr == 1) PG8_BAR;
;     __device__ __forceinline__ void epi(const f32x4 (&acc)[2][2][4][2], const Unit& u, int wr, int wc, int fr, int fq) const {
;     ...
;                     const f32x4 g0 = *(const f32x4*)(g1 + cofs * 4 + lcol * 4), g1v = *(const f32x4*)(g1 + cofs * 4 + lcol * 4 + 16);
;                     f32x4 x0, x1v;
;                     if (f32in) { x0 = *(const f32x4*)(xin + (ro + cofs) * 4 + loff4); x1v = *(const f32x4*)(xin + (ro + cofs) * 4 + loff4 + 16); }
;                     else { const u32x4 w = *(const u32x4*)(xin + (ro + cofs) * 2 + loff2); x0 = (f32x4){bflo(w.x), bfhi(w.x), bflo(w.y), bfhi(w.y)}; x1v = (f32x4){bflo(w.z), bfhi(w.z), bflo(w.w), bfhi(w.w)}; }
;                     const f32x4 o0 = x0 + g0 * acc[ai][bj][m][0], o1 = x1v + g1v * acc[ai][bj][m][1];
;                     u32x4 ow; ow.x = pk2(o0[0], o0[1]); ow.y = pk2(o0[2], o0[3]); ow.z = pk2(o1[0], o1[1]); ow.w = pk2(o1[2], o1[3]);
;                     *(u32x4*)(xo + (ro + cofs) * 2 + loff2) = ow; }
;                 asm volatile("" ::: "memory"); }
.LBB0_2005:
	s_waitcnt vmcnt(0)
	v_pk_fma_f32 v[6:7], v[6:7], v[14:15], v[22:23]
	v_pk_fma_f32 v[12:13], v[4:5], v[12:13], v[20:21]
	v_pk_fma_f32 v[4:5], v[2:3], v[10:11], v[18:19]
	v_pk_fma_f32 v[8:9], v[8:9], v[16:17], v[24:25]
	v_cvt_pk_bf16_f32 v2, v6, v7
	v_cvt_pk_bf16_f32 v3, v8, v9
	v_bfe_u32 v1, v4, 16, 1
	v_add3_u32 v1, v4, v1, s37
	v_bfe_u32 v4, v5, 16, 1
	v_lshrrev_b32_e32 v1, 16, v1
	v_add3_u32 v4, v5, v4, s37
	v_and_or_b32 v4, v4, s33, v1
	v_add_co_u32_e32 v6, vcc, 0xb0000, v160
	v_cvt_pk_bf16_f32 v5, v12, v13
	s_nop 0
	v_addc_co_u32_e32 v7, vcc, 0, v161, vcc
	global_store_dwordx4 v[6:7], v[2:5], off offset:256
	s_andn2_b64 vcc, exec, s[16:17]
	s_mov_b64 s[16:17], -1
	s_cbranch_vccnz .LBB0_1938
	s_andn2_b64 vcc, exec, s[4:5]
	s_cbranch_vccnz .LBB0_1937
	s_barrier
	s_branch .LBB0_1937

; #define LAS __attribute__((address_space(3)))
; #define WSW(T, off, l) WSP(T, WS_WSET + (size_t)(l) * WSET_STRIDE + (off))
; __device__ __forceinline__ void tr_item(const float* W, int ldw, int k0, int n0, bf16* WT, int ldt, int drow0, LAS float* scr, int lane, const float* kscale = nullptr) {
;     const float* src = W + (size_t)(k0 + (lane >> 4)) * ldw + n0 + (lane & 15) * 4;
;     f32x4 v[16];
; #pragma unroll
;     for (int i = 0; i < 16; ++i) v[i] = __builtin_nontemporal_load((const f32x4*)(src + (size_t)(4 * i) * ldw));
;     LAS float* wp = scr + (lane >> 4) * 65 + (lane & 15) * 4;
; #pragma unroll
;     for (int i = 0; i < 16; ++i) { LAS float* q = wp + (4 * i) * 65; const float ks = kscale ? kscale[k0 + 4 * i + (lane >> 4)] : 1.f; q[0] = v[i].x * ks; q[1] = v[i].y * ks; q[2] = v[i].z * ks; q[3] = v[i].w * ks; }
;     asm volatile("s_waitcnt lgkmcnt(0)" ::: "memory");
; __device__ __forceinline__ void convert_tile(const Args& a, GAS unsigned char* wsb, int l, int t, LAS float* scr, int lane) {
;     ...
;     if (r < I_OUT) { const int kb = r / 32, nb = r - kb * 32; tr_item(INP(21) + (size_t)l * DM * DM, DM, kb * 64, nb * 64, WSW(bf16, W_OUT, l), DM, nb * 64, scr, lane); return; }
.LBB0_2355:
	s_andn2_b64 vcc, exec, s[6:7]
	s_cbranch_vccnz .LBB0_2357
	s_lshl_b32 s6, s17, 1
	s_and_b32 s6, s6, 0x1fc0
	s_addk_i32 s6, 0xf240
	s_lshl_b32 s7, s17, 6
	v_or_b32_e32 v2, s6, v67
	v_mov_b32_e32 v3, v147
	v_readlane_b32 s10, v252, 60
	s_and_b32 s8, s7, 0x7c0
	v_lshlrev_b64 v[2:3], 13, v[2:3]
	v_readlane_b32 s11, v252, 61
	s_lshl_b32 s12, s8, 2
	v_lshlrev_b32_e32 v4, 2, v66
	v_lshl_add_u64 v[2:3], s[10:11], 0, v[2:3]
	v_lshl_add_u64 v[2:3], v[2:3], 0, s[12:13]
	v_mov_b32_e32 v5, v147
	v_lshl_add_u64 v[62:63], v[2:3], 0, v[4:5]
	v_add_co_u32_e32 v6, vcc, s83, v62
	s_mov_b32 s7, 0x20000
	s_nop 0
	v_addc_co_u32_e32 v7, vcc, 0, v63, vcc
	v_add_co_u32_e32 v10, vcc, s81, v62
	global_load_dwordx4 v[2:5], v[62:63], off nt
	s_nop 0
	global_load_dwordx4 v[6:9], v[6:7], off nt
	v_addc_co_u32_e32 v11, vcc, 0, v63, vcc
	v_add_co_u32_e32 v14, vcc, s82, v62
	v_add_u32_e32 v1, 0x410, v95
	s_nop 0
	v_addc_co_u32_e32 v15, vcc, 0, v63, vcc
	global_load_dwordx4 v[10:13], v[10:11], off nt
	s_nop 0
	global_load_dwordx4 v[14:17], v[14:15], off nt
	v_add_co_u32_e32 v18, vcc, s7, v62
	s_mov_b32 s7, 0x28000
	s_nop 0
	v_addc_co_u32_e32 v19, vcc, 0, v63, vcc
	v_add_co_u32_e32 v22, vcc, s7, v62
	s_mov_b32 s7, 0x30000
	s_nop 0
	v_addc_co_u32_e32 v23, vcc, 0, v63, vcc
	global_load_dwordx4 v[18:21], v[18:19], off nt
	s_nop 0
	global_load_dwordx4 v[22:25], v[22:23], off nt
	v_add_co_u32_e32 v26, vcc, s7, v62
	s_mov_b32 s7, 0x38000
	s_nop 0
	v_addc_co_u32_e32 v27, vcc, 0, v63, vcc
	v_add_co_u32_e32 v30, vcc, s7, v62
	s_mov_b32 s7, 0x40000
	s_nop 0
	v_addc_co_u32_e32 v31, vcc, 0, v63, vcc
	global_load_dwordx4 v[26:29], v[26:27], off nt
	s_nop 0
	global_load_dwordx4 v[30:33], v[30:31], off nt
	v_add_co_u32_e32 v34, vcc, s7, v62
	s_mov_b32 s7, 0x48000
	s_nop 0
	v_addc_co_u32_e32 v35, vcc, 0, v63, vcc
	v_add_co_u32_e32 v38, vcc, s7, v62
	s_mov_b32 s7, 0x50000
	s_nop 0
	v_addc_co_u32_e32 v39, vcc, 0, v63, vcc
	global_load_dwordx4 v[34:37], v[34:35], off nt
	s_nop 0
	global_load_dwordx4 v[38:41], v[38:39], off nt
	v_add_co_u32_e32 v42, vcc, s7, v62
	s_mov_b32 s7, 0x58000
	s_nop 0
	v_addc_co_u32_e32 v43, vcc, 0, v63, vcc
	v_add_co_u32_e32 v46, vcc, s7, v62
	s_mov_b32 s7, 0x60000
	s_nop 0
	v_addc_co_u32_e32 v47, vcc, 0, v63, vcc
	global_load_dwordx4 v[42:45], v[42:43], off nt
	s_nop 0
	global_load_dwordx4 v[46:49], v[46:47], off nt
	v_add_co_u32_e32 v50, vcc, s7, v62
	s_mov_b32 s7, 0x68000
	s_nop 0
	v_addc_co_u32_e32 v51, vcc, 0, v63, vcc
	v_add_co_u32_e32 v54, vcc, s7, v62
	s_mov_b32 s7, 0x70000
	s_nop 0
	v_addc_co_u32_e32 v55, vcc, 0, v63, vcc
	global_load_dwordx4 v[50:53], v[50:51], off nt
	s_nop 0
	global_load_dwordx4 v[54:57], v[54:55], off nt
	v_add_co_u32_e32 v58, vcc, s7, v62
	s_mov_b32 s7, 0x78000
	s_nop 0
	v_addc_co_u32_e32 v59, vcc, 0, v63, vcc
	global_load_dwordx4 v[58:61], v[58:59], off nt
	v_add_co_u32_e32 v62, vcc, s7, v62
	s_mov_b32 s7, s13
	s_nop 0
	v_addc_co_u32_e32 v63, vcc, 0, v63, vcc
	global_load_dwordx4 v[62:65], v[62:63], off nt
	s_waitcnt vmcnt(15)
	ds_write2_b32 v95, v2, v3 offset1:1
	ds_write2_b32 v95, v4, v5 offset0:2 offset1:3
	s_waitcnt vmcnt(14)
	ds_write2_b32 v1, v6, v7 offset1:1
	v_add_u32_e32 v1, 0x418, v95
	ds_write2_b32 v1, v8, v9 offset1:1
	v_add_u32_e32 v1, 0x820, v95
	v_lshl_add_u64 v[2:3], s[6:7], 1, v[72:73]
	s_waitcnt vmcnt(13)
	ds_write2_b32 v1, v10, v11 offset1:1
	v_add_u32_e32 v1, 0x828, v95
	ds_write2_b32 v1, v12, v13 offset1:1
	v_add_u32_e32 v1, 0xc30, v95
	s_waitcnt vmcnt(12)
	ds_write2_b32 v1, v14, v15 offset1:1
	v_add_u32_e32 v1, 0xc38, v95
	ds_write2_b32 v1, v16, v17 offset1:1
	v_add_u32_e32 v1, 0x1040, v95
	s_waitcnt vmcnt(11)
	ds_write2_b32 v1, v18, v19 offset1:1
	v_add_u32_e32 v1, 0x1048, v95
	ds_write2_b32 v1, v20, v21 offset1:1
	v_add_u32_e32 v1, 0x1450, v95
	s_waitcnt vmcnt(10)
	ds_write2_b32 v1, v22, v23 offset1:1
	v_add_u32_e32 v1, 0x1458, v95
	ds_write2_b32 v1, v24, v25 offset1:1
	v_add_u32_e32 v1, 0x1860, v95
	v_mov_b32_e32 v25, v147
	s_waitcnt vmcnt(9)
	ds_write2_b32 v1, v26, v27 offset1:1
	v_add_u32_e32 v1, 0x1868, v95
	ds_write2_b32 v1, v28, v29 offset1:1
	v_add_u32_e32 v1, 0x1c70, v95
	s_waitcnt vmcnt(8)
	ds_write2_b32 v1, v30, v31 offset1:1
	v_add_u32_e32 v1, 0x1c78, v95
	ds_write2_b32 v1, v32, v33 offset1:1
	v_add_u32_e32 v1, 0x2080, v95
	v_add_u32_e32 v26, 0x400, v97
	s_waitcnt vmcnt(7)
	ds_write2_b32 v1, v34, v35 offset1:1
	v_add_u32_e32 v1, 0x2088, v95
	ds_write2_b32 v1, v36, v37 offset1:1
	v_add_u32_e32 v1, 0x2490, v95
	s_waitcnt vmcnt(6)
	ds_write2_b32 v1, v38, v39 offset1:1
	v_add_u32_e32 v1, 0x2498, v95
	ds_write2_b32 v1, v40, v41 offset1:1
	v_add_u32_e32 v1, 0x28a0, v95
	s_waitcnt vmcnt(5)
	ds_write2_b32 v1, v42, v43 offset1:1
	v_add_u32_e32 v1, 0x28a8, v95
	ds_write2_b32 v1, v44, v45 offset1:1
	v_add_u32_e32 v1, 0x2cb0, v95
	s_waitcnt vmcnt(4)
	ds_write2_b32 v1, v46, v47 offset1:1
	v_add_u32_e32 v1, 0x2cb8, v95
	ds_write2_b32 v1, v48, v49 offset1:1
	v_add_u32_e32 v1, 0x30c0, v95
	s_waitcnt vmcnt(3)
	ds_write2_b32 v1, v50, v51 offset1:1
	v_add_u32_e32 v1, 0x30c8, v95
	ds_write2_b32 v1, v52, v53 offset1:1
	v_add_u32_e32 v1, 0x34d0, v95
	s_waitcnt vmcnt(2)
; #define LAS __attribute__((address_space(3)))
; __device__ __forceinline__ unsigned pk2(float lo, float hi) { return f2bf(lo) | (f2bf(hi) << 16); }
; __device__ __forceinline__ void tr_item(const float* W, int ldw, int k0, int n0, bf16* WT, int ldt, int drow0, LAS float* scr, int lane, const float* kscale = nullptr) {
;     ...
;     const int kc = lane & 7;
; #pragma unroll
;     for (int j = 0; j < 8; ++j) { const int n = (lane >> 3) + 8 * j; const LAS float* sp = scr + (8 * kc) * 65 + n;
;         u32x4 o; o.x = pk2(sp[0 * 65], sp[1 * 65]); o.y = pk2(sp[2 * 65], sp[3 * 65]); o.z = pk2(sp[4 * 65], sp[5 * 65]); o.w = pk2(sp[6 * 65], sp[7 * 65]);
;         __builtin_nontemporal_store(o, (u32x4*)(WT + (size_t)(drow0 + n) * ldt + k0 + 8 * kc)); }
;     asm volatile("s_waitcnt lgkmcnt(0)" ::: "memory");
; }
	ds_write2_b32 v1, v54, v55 offset1:1
	v_add_u32_e32 v1, 0x34d8, v95
	ds_write2_b32 v1, v56, v57 offset1:1
	v_add_u32_e32 v1, 0x38e0, v95
	s_waitcnt vmcnt(1)
	ds_write2_b32 v1, v58, v59 offset1:1
	v_add_u32_e32 v1, 0x38e8, v95
	ds_write2_b32 v1, v60, v61 offset1:1
	v_add_u32_e32 v1, 0x3cf0, v95
	s_waitcnt vmcnt(0)
	ds_write2_b32 v1, v62, v63 offset1:1
	v_add_u32_e32 v1, 0x3cf8, v95
	ds_write2_b32 v1, v64, v65 offset1:1
	s_waitcnt lgkmcnt(0)
	ds_read2_b32 v[8:9], v97 offset1:8
	ds_read2_b32 v[10:11], v97 offset0:65 offset1:73
	ds_read2_b32 v[12:13], v97 offset0:130 offset1:138
	ds_read2_b32 v[14:15], v97 offset0:195 offset1:203
	ds_read2_b32 v[16:17], v26 offset0:4 offset1:12
	s_waitcnt lgkmcnt(4)
	s_waitcnt lgkmcnt(3)
	ds_read2_b32 v[18:19], v26 offset0:69 offset1:77
	v_cvt_pk_bf16_f32 v4, v8, v10
	s_waitcnt lgkmcnt(3)
	s_waitcnt lgkmcnt(2)
	ds_read2_b32 v[20:21], v26 offset0:134 offset1:142
	ds_read2_b32 v[22:23], v26 offset0:199 offset1:207
	v_cvt_pk_bf16_f32 v5, v12, v14
	s_waitcnt lgkmcnt(3)
	s_waitcnt lgkmcnt(2)
	v_cvt_pk_bf16_f32 v6, v16, v18
	s_waitcnt lgkmcnt(1)
	s_waitcnt lgkmcnt(0)
	v_cvt_pk_bf16_f32 v7, v20, v22
	v_or_b32_e32 v1, s8, v96
	v_lshlrev_b32_e32 v24, 12, v1
	v_lshl_add_u64 v[24:25], v[2:3], 0, v[24:25]
	global_store_dwordx4 v[24:25], v[4:7], off nt
	s_nop 1
	v_cvt_pk_bf16_f32 v4, v9, v11
	v_cvt_pk_bf16_f32 v5, v13, v15
	v_cvt_pk_bf16_f32 v6, v17, v19
	v_cvt_pk_bf16_f32 v7, v21, v23
	v_or_b32_e32 v1, s8, v98
	v_lshlrev_b32_e32 v8, 12, v1
	v_mov_b32_e32 v9, v147
	ds_read2_b32 v[10:11], v97 offset0:16 offset1:24
	v_lshl_add_u64 v[8:9], v[2:3], 0, v[8:9]
	global_store_dwordx4 v[8:9], v[4:7], off nt
	ds_read2_b32 v[8:9], v97 offset0:81 offset1:89
	ds_read2_b32 v[12:13], v97 offset0:146 offset1:154
	ds_read2_b32 v[14:15], v97 offset0:211 offset1:219
	s_waitcnt lgkmcnt(3)
	s_waitcnt lgkmcnt(2)
	ds_read2_b32 v[16:17], v26 offset0:20 offset1:28
	ds_read2_b32 v[18:19], v26 offset0:85 offset1:93
	v_cvt_pk_bf16_f32 v4, v10, v8
	s_waitcnt lgkmcnt(3)
	s_waitcnt lgkmcnt(2)
	ds_read2_b32 v[20:21], v26 offset0:150 offset1:158
	ds_read2_b32 v[22:23], v26 offset0:215 offset1:223
	v_cvt_pk_bf16_f32 v5, v12, v14
	s_waitcnt lgkmcnt(3)
	s_waitcnt lgkmcnt(2)
	v_cvt_pk_bf16_f32 v6, v16, v18
	s_waitcnt lgkmcnt(1)
	s_waitcnt lgkmcnt(0)
	v_cvt_pk_bf16_f32 v7, v20, v22
	v_or_b32_e32 v1, s8, v99
	v_lshlrev_b32_e32 v24, 12, v1
	v_mov_b32_e32 v25, v147
	v_lshl_add_u64 v[24:25], v[2:3], 0, v[24:25]
	global_store_dwordx4 v[24:25], v[4:7], off nt
	s_nop 1
	v_cvt_pk_bf16_f32 v4, v11, v9
	v_cvt_pk_bf16_f32 v5, v13, v15
	v_cvt_pk_bf16_f32 v6, v17, v19
	v_cvt_pk_bf16_f32 v7, v21, v23
	v_or_b32_e32 v1, s8, v100
	v_lshlrev_b32_e32 v8, 12, v1
	v_mov_b32_e32 v9, v147
	ds_read2_b32 v[10:11], v97 offset0:32 offset1:40
	v_lshl_add_u64 v[8:9], v[2:3], 0, v[8:9]
	global_store_dwordx4 v[8:9], v[4:7], off nt
	ds_read2_b32 v[8:9], v97 offset0:97 offset1:105
	ds_read2_b32 v[12:13], v97 offset0:162 offset1:170
	ds_read2_b32 v[14:15], v97 offset0:227 offset1:235
	s_waitcnt lgkmcnt(3)
	s_waitcnt lgkmcnt(2)
	ds_read2_b32 v[16:17], v26 offset0:36 offset1:44
	ds_read2_b32 v[18:19], v26 offset0:101 offset1:109
	v_cvt_pk_bf16_f32 v4, v10, v8
	s_waitcnt lgkmcnt(3)
	s_waitcnt lgkmcnt(2)
	ds_read2_b32 v[20:21], v26 offset0:166 offset1:174
	ds_read2_b32 v[22:23], v26 offset0:231 offset1:239
	v_cvt_pk_bf16_f32 v5, v12, v14
	s_waitcnt lgkmcnt(3)
	s_waitcnt lgkmcnt(2)
	v_cvt_pk_bf16_f32 v6, v16, v18
	s_waitcnt lgkmcnt(1)
	s_waitcnt lgkmcnt(0)
	v_cvt_pk_bf16_f32 v7, v20, v22
	v_or_b32_e32 v1, s8, v101
	v_lshlrev_b32_e32 v24, 12, v1
	v_mov_b32_e32 v25, v147
	v_lshl_add_u64 v[24:25], v[2:3], 0, v[24:25]
	global_store_dwordx4 v[24:25], v[4:7], off nt
	s_nop 1
	v_cvt_pk_bf16_f32 v4, v11, v9
	v_cvt_pk_bf16_f32 v5, v13, v15
	v_cvt_pk_bf16_f32 v6, v17, v19
	v_cvt_pk_bf16_f32 v7, v21, v23
	v_or_b32_e32 v1, s8, v102
	v_lshlrev_b32_e32 v8, 12, v1
	v_mov_b32_e32 v9, v147
	ds_read2_b32 v[10:11], v97 offset0:48 offset1:56
	v_lshl_add_u64 v[8:9], v[2:3], 0, v[8:9]
	global_store_dwordx4 v[8:9], v[4:7], off nt
	ds_read2_b32 v[8:9], v97 offset0:113 offset1:121
	ds_read2_b32 v[12:13], v97 offset0:178 offset1:186
	ds_read2_b32 v[14:15], v97 offset0:243 offset1:251
	s_waitcnt lgkmcnt(3)
	s_waitcnt lgkmcnt(2)
	ds_read2_b32 v[16:17], v26 offset0:52 offset1:60
	ds_read2_b32 v[18:19], v26 offset0:117 offset1:125
	v_cvt_pk_bf16_f32 v4, v10, v8
	s_waitcnt lgkmcnt(3)
	s_waitcnt lgkmcnt(2)
	ds_read2_b32 v[20:21], v26 offset0:182 offset1:190
	ds_read2_b32 v[22:23], v26 offset0:247 offset1:255
	v_cvt_pk_bf16_f32 v5, v12, v14
	s_waitcnt lgkmcnt(3)
	s_waitcnt lgkmcnt(2)
	v_cvt_pk_bf16_f32 v6, v16, v18
	s_waitcnt lgkmcnt(1)
	s_waitcnt lgkmcnt(0)
	v_cvt_pk_bf16_f32 v7, v20, v22
	v_or_b32_e32 v1, s8, v103
	v_lshlrev_b32_e32 v24, 12, v1
	v_mov_b32_e32 v25, v147
	v_lshl_add_u64 v[24:25], v[2:3], 0, v[24:25]
	global_store_dwordx4 v[24:25], v[4:7], off nt
	s_nop 1
	v_cvt_pk_bf16_f32 v4, v11, v9
	v_cvt_pk_bf16_f32 v5, v13, v15
	v_cvt_pk_bf16_f32 v6, v17, v19
	v_cvt_pk_bf16_f32 v7, v21, v23
	v_or_b32_e32 v1, s8, v104
	v_lshlrev_b32_e32 v8, 12, v1
	v_mov_b32_e32 v9, v147
	v_lshl_add_u64 v[2:3], v[2:3], 0, v[8:9]
	global_store_dwordx4 v[2:3], v[4:7], off nt
	s_waitcnt lgkmcnt(0)

; #define LAS __attribute__((address_space(3)))
; __device__ __forceinline__ unsigned pk2(float lo, float hi) { return f2bf(lo) | (f2bf(hi) << 16); }
; __device__ __forceinline__ void tr_item(const float* W, int ldw, int k0, int n0, bf16* WT, int ldt, int drow0, LAS float* scr, int lane, const float* kscale = nullptr) {
;     ...
;     for (int i = 0; i < 16; ++i) { LAS float* q = wp + (4 * i) * 65; const float ks = kscale ? kscale[k0 + 4 * i + (lane >> 4)] : 1.f; q[0] = v[i].x * ks; q[1] = v[i].y * ks; q[2] = v[i].z * ks; q[3] = v[i].w * ks; }
;     asm volatile("s_waitcnt lgkmcnt(0)" ::: "memory");
;     const int kc = lane & 7;
; #pragma unroll
;     for (int j = 0; j < 8; ++j) { const int n = (lane >> 3) + 8 * j; const LAS float* sp = scr + (8 * kc) * 65 + n;
;         u32x4 o; o.x = pk2(sp[0 * 65], sp[1 * 65]); o.y = pk2(sp[2 * 65], sp[3 * 65]); o.z = pk2(sp[4 * 65], sp[5 * 65]); o.w = pk2(sp[6 * 65], sp[7 * 65]);
;         __builtin_nontemporal_store(o, (u32x4*)(WT + (size_t)(drow0 + n) * ldt + k0 + 8 * kc)); }
;     asm volatile("s_waitcnt lgkmcnt(0)" ::: "memory");
; }
.LBB0_2383:
	s_waitcnt vmcnt(0)
	v_pk_mul_f32 v[2:3], v[2:3], v[10:11] op_sel_hi:[1,0]
	v_add_u32_e32 v1, 0x3cf0, v95
	ds_write2_b32 v1, v2, v3 offset1:1
	v_pk_mul_f32 v[2:3], v[4:5], v[10:11] op_sel_hi:[1,0]
	v_add_u32_e32 v1, 0x3cf8, v95
	ds_write2_b32 v1, v2, v3 offset1:1
	s_waitcnt lgkmcnt(0)
	ds_read2_b32 v[8:9], v97 offset1:8
	ds_read2_b32 v[10:11], v97 offset0:65 offset1:73
	ds_read2_b32 v[12:13], v97 offset0:130 offset1:138
	ds_read2_b32 v[14:15], v97 offset0:195 offset1:203
	v_add_u32_e32 v26, 0x400, v97
	s_waitcnt lgkmcnt(3)
	s_waitcnt lgkmcnt(2)
	ds_read2_b32 v[16:17], v26 offset0:4 offset1:12
	ds_read2_b32 v[18:19], v26 offset0:69 offset1:77
	v_cvt_pk_bf16_f32 v4, v8, v10
	s_waitcnt lgkmcnt(3)
	s_waitcnt lgkmcnt(2)
	ds_read2_b32 v[20:21], v26 offset0:134 offset1:142
	ds_read2_b32 v[22:23], v26 offset0:199 offset1:207
	v_cvt_pk_bf16_f32 v5, v12, v14
	s_waitcnt lgkmcnt(3)
	s_waitcnt lgkmcnt(2)
	v_cvt_pk_bf16_f32 v6, v16, v18
	s_waitcnt lgkmcnt(1)
	s_waitcnt lgkmcnt(0)
	s_mov_b32 s7, s13
	v_cvt_pk_bf16_f32 v7, v20, v22
	v_or_b32_e32 v1, s10, v96
	v_lshl_add_u64 v[2:3], s[6:7], 1, v[74:75]
	v_lshlrev_b32_e32 v146, 9, v1
	v_lshl_add_u64 v[24:25], v[2:3], 0, v[146:147]
	global_store_dwordx4 v[24:25], v[4:7], off nt
	s_nop 1
	v_cvt_pk_bf16_f32 v4, v9, v11
	v_cvt_pk_bf16_f32 v5, v13, v15
	v_cvt_pk_bf16_f32 v6, v17, v19
	v_cvt_pk_bf16_f32 v7, v21, v23
	v_or_b32_e32 v1, s10, v98
	v_lshlrev_b32_e32 v146, 9, v1
	ds_read2_b32 v[8:9], v97 offset0:16 offset1:24
	v_lshl_add_u64 v[10:11], v[2:3], 0, v[146:147]
	global_store_dwordx4 v[10:11], v[4:7], off nt
	ds_read2_b32 v[10:11], v97 offset0:81 offset1:89
	ds_read2_b32 v[12:13], v97 offset0:146 offset1:154
	ds_read2_b32 v[14:15], v97 offset0:211 offset1:219
	s_waitcnt lgkmcnt(3)
	s_waitcnt lgkmcnt(2)
	ds_read2_b32 v[16:17], v26 offset0:20 offset1:28
	ds_read2_b32 v[18:19], v26 offset0:85 offset1:93
	v_cvt_pk_bf16_f32 v4, v8, v10
	s_waitcnt lgkmcnt(3)
	s_waitcnt lgkmcnt(2)
	ds_read2_b32 v[20:21], v26 offset0:150 offset1:158
	ds_read2_b32 v[22:23], v26 offset0:215 offset1:223
	v_cvt_pk_bf16_f32 v5, v12, v14
	s_waitcnt lgkmcnt(3)
	s_waitcnt lgkmcnt(2)
	v_cvt_pk_bf16_f32 v6, v16, v18
	s_waitcnt lgkmcnt(1)
	s_waitcnt lgkmcnt(0)
	v_cvt_pk_bf16_f32 v7, v20, v22
	v_or_b32_e32 v1, s10, v99
	v_lshlrev_b32_e32 v146, 9, v1
	v_lshl_add_u64 v[24:25], v[2:3], 0, v[146:147]
	global_store_dwordx4 v[24:25], v[4:7], off nt
	s_nop 1
	v_cvt_pk_bf16_f32 v4, v9, v11
	v_cvt_pk_bf16_f32 v5, v13, v15
	v_cvt_pk_bf16_f32 v6, v17, v19
	v_cvt_pk_bf16_f32 v7, v21, v23
	v_or_b32_e32 v1, s10, v100
	v_lshlrev_b32_e32 v146, 9, v1
	ds_read2_b32 v[8:9], v97 offset0:32 offset1:40
	v_lshl_add_u64 v[10:11], v[2:3], 0, v[146:147]
	global_store_dwordx4 v[10:11], v[4:7], off nt
	ds_read2_b32 v[10:11], v97 offset0:97 offset1:105
	ds_read2_b32 v[12:13], v97 offset0:162 offset1:170
	ds_read2_b32 v[14:15], v97 offset0:227 offset1:235
	s_waitcnt lgkmcnt(3)
	s_waitcnt lgkmcnt(2)
	ds_read2_b32 v[16:17], v26 offset0:36 offset1:44
	ds_read2_b32 v[18:19], v26 offset0:101 offset1:109
	v_cvt_pk_bf16_f32 v4, v8, v10
	s_waitcnt lgkmcnt(3)
	s_waitcnt lgkmcnt(2)
	ds_read2_b32 v[20:21], v26 offset0:166 offset1:174
	ds_read2_b32 v[22:23], v26 offset0:231 offset1:239
	v_cvt_pk_bf16_f32 v5, v12, v14
	s_waitcnt lgkmcnt(3)
	s_waitcnt lgkmcnt(2)
	v_cvt_pk_bf16_f32 v6, v16, v18
	s_waitcnt lgkmcnt(1)
	s_waitcnt lgkmcnt(0)
	v_cvt_pk_bf16_f32 v7, v20, v22
	v_or_b32_e32 v1, s10, v101
	v_lshlrev_b32_e32 v146, 9, v1
	v_lshl_add_u64 v[24:25], v[2:3], 0, v[146:147]
	global_store_dwordx4 v[24:25], v[4:7], off nt
	s_nop 1
	v_cvt_pk_bf16_f32 v4, v9, v11
	v_cvt_pk_bf16_f32 v5, v13, v15
	v_cvt_pk_bf16_f32 v6, v17, v19
	v_cvt_pk_bf16_f32 v7, v21, v23
	v_or_b32_e32 v1, s10, v102
	v_lshlrev_b32_e32 v146, 9, v1
	ds_read2_b32 v[8:9], v97 offset0:48 offset1:56
	v_lshl_add_u64 v[10:11], v[2:3], 0, v[146:147]
	global_store_dwordx4 v[10:11], v[4:7], off nt
	ds_read2_b32 v[10:11], v97 offset0:113 offset1:121
	ds_read2_b32 v[12:13], v97 offset0:178 offset1:186
	ds_read2_b32 v[14:15], v97 offset0:243 offset1:251
	s_waitcnt lgkmcnt(3)
	s_waitcnt lgkmcnt(2)
	ds_read2_b32 v[16:17], v26 offset0:52 offset1:60
	ds_read2_b32 v[18:19], v26 offset0:117 offset1:125
	v_cvt_pk_bf16_f32 v4, v8, v10
	s_waitcnt lgkmcnt(3)
	s_waitcnt lgkmcnt(2)
	ds_read2_b32 v[20:21], v26 offset0:182 offset1:190
	ds_read2_b32 v[22:23], v26 offset0:247 offset1:255
	v_cvt_pk_bf16_f32 v5, v12, v14
	s_waitcnt lgkmcnt(3)
	s_waitcnt lgkmcnt(2)
	v_cvt_pk_bf16_f32 v6, v16, v18
	s_waitcnt lgkmcnt(1)
	s_waitcnt lgkmcnt(0)
	v_cvt_pk_bf16_f32 v7, v20, v22
	v_or_b32_e32 v1, s10, v103
	v_lshlrev_b32_e32 v146, 9, v1
	v_lshl_add_u64 v[24:25], v[2:3], 0, v[146:147]
	global_store_dwordx4 v[24:25], v[4:7], off nt
	s_nop 1
	v_cvt_pk_bf16_f32 v4, v9, v11
	v_cvt_pk_bf16_f32 v5, v13, v15
	v_cvt_pk_bf16_f32 v6, v17, v19
	v_cvt_pk_bf16_f32 v7, v21, v23
	v_or_b32_e32 v1, s10, v104
	v_lshlrev_b32_e32 v146, 9, v1
	v_lshl_add_u64 v[2:3], v[2:3], 0, v[146:147]
	global_store_dwordx4 v[2:3], v[4:7], off nt
	s_waitcnt lgkmcnt(0)

; #define LAS __attribute__((address_space(3)))
; __device__ __forceinline__ unsigned pk2(float lo, float hi) { return f2bf(lo) | (f2bf(hi) << 16); }
; __device__ __forceinline__ void tr_item(const float* W, int ldw, int k0, int n0, bf16* WT, int ldt, int drow0, LAS float* scr, int lane, const float* kscale = nullptr) {
;     ...
;     for (int i = 0; i < 16; ++i) { LAS float* q = wp + (4 * i) * 65; const float ks = kscale ? kscale[k0 + 4 * i + (lane >> 4)] : 1.f; q[0] = v[i].x * ks; q[1] = v[i].y * ks; q[2] = v[i].z * ks; q[3] = v[i].w * ks; }
;     asm volatile("s_waitcnt lgkmcnt(0)" ::: "memory");
;     const int kc = lane & 7;
; #pragma unroll
;     for (int j = 0; j < 8; ++j) { const int n = (lane >> 3) + 8 * j; const LAS float* sp = scr + (8 * kc) * 65 + n;
;         u32x4 o; o.x = pk2(sp[0 * 65], sp[1 * 65]); o.y = pk2(sp[2 * 65], sp[3 * 65]); o.z = pk2(sp[4 * 65], sp[5 * 65]); o.w = pk2(sp[6 * 65], sp[7 * 65]);
;         __builtin_nontemporal_store(o, (u32x4*)(WT + (size_t)(drow0 + n) * ldt + k0 + 8 * kc)); }
;     asm volatile("s_waitcnt lgkmcnt(0)" ::: "memory");
; }
.LBB0_2410:
	s_waitcnt vmcnt(0)
	v_pk_mul_f32 v[2:3], v[2:3], v[10:11] op_sel_hi:[1,0]
	v_add_u32_e32 v1, 0x3cf0, v95
	ds_write2_b32 v1, v2, v3 offset1:1
	v_pk_mul_f32 v[2:3], v[4:5], v[10:11] op_sel_hi:[1,0]
	v_add_u32_e32 v1, 0x3cf8, v95
	ds_write2_b32 v1, v2, v3 offset1:1
	s_waitcnt lgkmcnt(0)
	ds_read2_b32 v[8:9], v97 offset1:8
	ds_read2_b32 v[10:11], v97 offset0:65 offset1:73
	ds_read2_b32 v[12:13], v97 offset0:130 offset1:138
	ds_read2_b32 v[14:15], v97 offset0:195 offset1:203
	v_add_u32_e32 v26, 0x400, v97
	s_waitcnt lgkmcnt(3)
	s_waitcnt lgkmcnt(2)
	ds_read2_b32 v[16:17], v26 offset0:4 offset1:12
	ds_read2_b32 v[18:19], v26 offset0:69 offset1:77
	v_cvt_pk_bf16_f32 v4, v8, v10
	s_waitcnt lgkmcnt(3)
	s_waitcnt lgkmcnt(2)
	ds_read2_b32 v[20:21], v26 offset0:134 offset1:142
	ds_read2_b32 v[22:23], v26 offset0:199 offset1:207
	v_cvt_pk_bf16_f32 v5, v12, v14
	s_waitcnt lgkmcnt(3)
	s_waitcnt lgkmcnt(2)
	v_cvt_pk_bf16_f32 v6, v16, v18
	s_waitcnt lgkmcnt(1)
	v_or_b32_e32 v24, s6, v96
	s_lshl_b32 s12, s10, 1
	s_waitcnt lgkmcnt(0)
	v_ashrrev_i32_e32 v25, 31, v24
	v_lshl_add_u64 v[2:3], v[76:77], 0, s[12:13]
	v_lshlrev_b64 v[24:25], 10, v[24:25]
	v_cvt_pk_bf16_f32 v7, v20, v22
	v_lshl_add_u64 v[24:25], v[2:3], 0, v[24:25]
	global_store_dwordx4 v[24:25], v[4:7], off nt
	s_nop 1
	v_cvt_pk_bf16_f32 v4, v9, v11
	v_cvt_pk_bf16_f32 v5, v13, v15
	v_cvt_pk_bf16_f32 v6, v17, v19
	v_or_b32_e32 v8, s6, v98
	v_ashrrev_i32_e32 v9, 31, v8
	v_lshlrev_b64 v[8:9], 10, v[8:9]
	v_cvt_pk_bf16_f32 v7, v21, v23
	ds_read2_b32 v[10:11], v97 offset0:16 offset1:24
	v_lshl_add_u64 v[8:9], v[2:3], 0, v[8:9]
	global_store_dwordx4 v[8:9], v[4:7], off nt
	ds_read2_b32 v[8:9], v97 offset0:81 offset1:89
	ds_read2_b32 v[12:13], v97 offset0:146 offset1:154
	ds_read2_b32 v[14:15], v97 offset0:211 offset1:219
	s_waitcnt lgkmcnt(3)
	s_waitcnt lgkmcnt(2)
	ds_read2_b32 v[16:17], v26 offset0:20 offset1:28
	ds_read2_b32 v[18:19], v26 offset0:85 offset1:93
	v_cvt_pk_bf16_f32 v4, v10, v8
	s_waitcnt lgkmcnt(3)
	s_waitcnt lgkmcnt(2)
	ds_read2_b32 v[20:21], v26 offset0:150 offset1:158
	ds_read2_b32 v[22:23], v26 offset0:215 offset1:223
	v_cvt_pk_bf16_f32 v5, v12, v14
	s_waitcnt lgkmcnt(3)
	s_waitcnt lgkmcnt(2)
	v_cvt_pk_bf16_f32 v6, v16, v18
	s_waitcnt lgkmcnt(1)
	v_or_b32_e32 v24, s6, v99
	s_waitcnt lgkmcnt(0)
	v_ashrrev_i32_e32 v25, 31, v24
	v_lshlrev_b64 v[24:25], 10, v[24:25]
	v_cvt_pk_bf16_f32 v7, v20, v22
	v_lshl_add_u64 v[24:25], v[2:3], 0, v[24:25]
	global_store_dwordx4 v[24:25], v[4:7], off nt
	s_nop 1
	v_cvt_pk_bf16_f32 v4, v11, v9
	v_cvt_pk_bf16_f32 v5, v13, v15
	v_cvt_pk_bf16_f32 v6, v17, v19
	v_or_b32_e32 v8, s6, v100
	v_ashrrev_i32_e32 v9, 31, v8
	v_lshlrev_b64 v[8:9], 10, v[8:9]
	v_cvt_pk_bf16_f32 v7, v21, v23
	ds_read2_b32 v[10:11], v97 offset0:32 offset1:40
	v_lshl_add_u64 v[8:9], v[2:3], 0, v[8:9]
	global_store_dwordx4 v[8:9], v[4:7], off nt
	ds_read2_b32 v[8:9], v97 offset0:97 offset1:105
	ds_read2_b32 v[12:13], v97 offset0:162 offset1:170
	ds_read2_b32 v[14:15], v97 offset0:227 offset1:235
	s_waitcnt lgkmcnt(3)
	s_waitcnt lgkmcnt(2)
	ds_read2_b32 v[16:17], v26 offset0:36 offset1:44
	ds_read2_b32 v[18:19], v26 offset0:101 offset1:109
	v_cvt_pk_bf16_f32 v4, v10, v8
	s_waitcnt lgkmcnt(3)
	s_waitcnt lgkmcnt(2)
	ds_read2_b32 v[20:21], v26 offset0:166 offset1:174
	ds_read2_b32 v[22:23], v26 offset0:231 offset1:239
	v_cvt_pk_bf16_f32 v5, v12, v14
	s_waitcnt lgkmcnt(3)
	s_waitcnt lgkmcnt(2)
	v_cvt_pk_bf16_f32 v6, v16, v18
	s_waitcnt lgkmcnt(1)
	v_or_b32_e32 v24, s6, v101
	s_waitcnt lgkmcnt(0)
	v_ashrrev_i32_e32 v25, 31, v24
	v_lshlrev_b64 v[24:25], 10, v[24:25]
	v_cvt_pk_bf16_f32 v7, v20, v22
	v_lshl_add_u64 v[24:25], v[2:3], 0, v[24:25]
	global_store_dwordx4 v[24:25], v[4:7], off nt
	s_nop 1
	v_cvt_pk_bf16_f32 v4, v11, v9
	v_cvt_pk_bf16_f32 v5, v13, v15
	v_cvt_pk_bf16_f32 v6, v17, v19
	v_or_b32_e32 v8, s6, v102
	v_ashrrev_i32_e32 v9, 31, v8
	v_lshlrev_b64 v[8:9], 10, v[8:9]
	v_cvt_pk_bf16_f32 v7, v21, v23
	ds_read2_b32 v[10:11], v97 offset0:48 offset1:56
	v_lshl_add_u64 v[8:9], v[2:3], 0, v[8:9]
	global_store_dwordx4 v[8:9], v[4:7], off nt
	ds_read2_b32 v[8:9], v97 offset0:113 offset1:121
	ds_read2_b32 v[12:13], v97 offset0:178 offset1:186
	ds_read2_b32 v[14:15], v97 offset0:243 offset1:251
	s_waitcnt lgkmcnt(3)
	s_waitcnt lgkmcnt(2)
	ds_read2_b32 v[16:17], v26 offset0:52 offset1:60
	ds_read2_b32 v[18:19], v26 offset0:117 offset1:125
	v_cvt_pk_bf16_f32 v4, v10, v8
	s_waitcnt lgkmcnt(3)
	s_waitcnt lgkmcnt(2)
	ds_read2_b32 v[20:21], v26 offset0:182 offset1:190
	ds_read2_b32 v[22:23], v26 offset0:247 offset1:255
	v_cvt_pk_bf16_f32 v5, v12, v14
	s_waitcnt lgkmcnt(3)
	s_waitcnt lgkmcnt(2)
	v_cvt_pk_bf16_f32 v6, v16, v18
	s_waitcnt lgkmcnt(1)
	v_or_b32_e32 v24, s6, v103
	s_waitcnt lgkmcnt(0)
	v_ashrrev_i32_e32 v25, 31, v24
	v_lshlrev_b64 v[24:25], 10, v[24:25]
	v_cvt_pk_bf16_f32 v7, v20, v22
	v_lshl_add_u64 v[24:25], v[2:3], 0, v[24:25]
	global_store_dwordx4 v[24:25], v[4:7], off nt
	s_nop 1
	v_cvt_pk_bf16_f32 v4, v11, v9
	v_cvt_pk_bf16_f32 v5, v13, v15
	v_cvt_pk_bf16_f32 v6, v17, v19
	v_or_b32_e32 v8, s6, v104
	v_ashrrev_i32_e32 v9, 31, v8
	v_lshlrev_b64 v[8:9], 10, v[8:9]
	v_cvt_pk_bf16_f32 v7, v21, v23
	v_lshl_add_u64 v[2:3], v[2:3], 0, v[8:9]
	global_store_dwordx4 v[2:3], v[4:7], off nt
	s_waitcnt lgkmcnt(0)

; #define LAS __attribute__((address_space(3)))
; #define WSW(T, off, l) WSP(T, WS_WSET + (size_t)(l) * WSET_STRIDE + (off))
; __device__ __forceinline__ void tr_item(const float* W, int ldw, int k0, int n0, bf16* WT, int ldt, int drow0, LAS float* scr, int lane, const float* kscale = nullptr) {
;     const float* src = W + (size_t)(k0 + (lane >> 4)) * ldw + n0 + (lane & 15) * 4;
;     f32x4 v[16];
; #pragma unroll
;     for (int i = 0; i < 16; ++i) v[i] = __builtin_nontemporal_load((const f32x4*)(src + (size_t)(4 * i) * ldw));
;     LAS float* wp = scr + (lane >> 4) * 65 + (lane & 15) * 4;
; #pragma unroll
;     for (int i = 0; i < 16; ++i) { LAS float* q = wp + (4 * i) * 65; const float ks = kscale ? kscale[k0 + 4 * i + (lane >> 4)] : 1.f; q[0] = v[i].x * ks; q[1] = v[i].y * ks; q[2] = v[i].z * ks; q[3] = v[i].w * ks; }
;     asm volatile("s_waitcnt lgkmcnt(0)" ::: "memory");
; __device__ __forceinline__ void convert_tile(const Args& a, GAS unsigned char* wsb, int l, int t, LAS float* scr, int lane) {
;     ...
;     if (r < I_IN) { const int kb = r / 45, nb = r - kb * 45; tr_item(INP(7) + (size_t)l * DM * INW, INW, kb * 64, nb * 64, WSW(bf16, W_IN, l), DM, nb * 64, scr, lane); return; }
.LBB0_2412:
	s_andn2_b64 vcc, exec, s[6:7]
	s_cbranch_vccnz .LBB0_2414
	s_mul_i32 s6, s17, 0x2d83
	s_lshr_b32 s8, s6, 19
	s_mul_i32 s6, s8, 0xffffffd3
	s_add_i32 s6, s6, s17
	v_lshl_or_b32 v1, s8, 6, v67
	v_readlane_b32 s10, v253, 6
	s_lshl_b32 s6, s6, 6
	v_mul_u32_u24_e32 v2, 0x2d00, v1
	v_mov_b32_e32 v3, v147
	v_readlane_b32 s11, v253, 7
	s_ashr_i32 s7, s6, 31
	v_lshlrev_b32_e32 v4, 2, v66
	v_lshl_add_u64 v[2:3], s[10:11], 0, v[2:3]
	v_lshl_add_u64 v[2:3], s[6:7], 2, v[2:3]
	v_mov_b32_e32 v5, v147
	v_lshl_add_u64 v[62:63], v[2:3], 0, v[4:5]
	s_mov_b32 s7, 0xb000
	v_add_co_u32_e32 v6, vcc, s7, v62
	s_mov_b32 s7, 0x16000
	s_nop 0
	v_addc_co_u32_e32 v7, vcc, 0, v63, vcc
	v_add_co_u32_e32 v10, vcc, s7, v62
	global_load_dwordx4 v[2:5], v[62:63], off nt
	s_nop 0
	global_load_dwordx4 v[6:9], v[6:7], off offset:1024 nt
	v_addc_co_u32_e32 v11, vcc, 0, v63, vcc
	s_mov_b32 s7, 0x21000
	v_add_co_u32_e32 v14, vcc, s7, v62
	s_mov_b32 s7, 0x2d000
	s_nop 0
	v_addc_co_u32_e32 v15, vcc, 0, v63, vcc
	global_load_dwordx4 v[10:13], v[10:11], off offset:2048 nt
	s_nop 0
	global_load_dwordx4 v[14:17], v[14:15], off offset:3072 nt
	v_add_co_u32_e32 v18, vcc, s7, v62
	s_mov_b32 s7, 0x38000
	s_nop 0
	v_addc_co_u32_e32 v19, vcc, 0, v63, vcc
	v_add_co_u32_e32 v22, vcc, s7, v62
	s_mov_b32 s7, 0x43000
	s_nop 0
	v_addc_co_u32_e32 v23, vcc, 0, v63, vcc
	global_load_dwordx4 v[18:21], v[18:19], off nt
	s_nop 0
	global_load_dwordx4 v[22:25], v[22:23], off offset:1024 nt
	v_add_co_u32_e32 v26, vcc, s7, v62
	s_mov_b32 s7, 0x4e000
	s_nop 0
	v_addc_co_u32_e32 v27, vcc, 0, v63, vcc
	v_add_co_u32_e32 v30, vcc, s7, v62
	s_mov_b32 s7, 0x5a000
	s_nop 0
	v_addc_co_u32_e32 v31, vcc, 0, v63, vcc
	global_load_dwordx4 v[26:29], v[26:27], off offset:2048 nt
	s_nop 0
	global_load_dwordx4 v[30:33], v[30:31], off offset:3072 nt
	v_add_co_u32_e32 v34, vcc, s7, v62
	s_mov_b32 s7, 0x65000
	s_nop 0
	v_addc_co_u32_e32 v35, vcc, 0, v63, vcc
	v_add_co_u32_e32 v38, vcc, s7, v62
	s_mov_b32 s7, 0x70000
	s_nop 0
	v_addc_co_u32_e32 v39, vcc, 0, v63, vcc
	global_load_dwordx4 v[34:37], v[34:35], off nt
	s_nop 0
	global_load_dwordx4 v[38:41], v[38:39], off offset:1024 nt
	v_add_co_u32_e32 v42, vcc, s7, v62
	s_mov_b32 s7, 0x7b000
	s_nop 0
	v_addc_co_u32_e32 v43, vcc, 0, v63, vcc
	v_add_co_u32_e32 v46, vcc, s7, v62
	s_mov_b32 s7, 0x87000
	s_nop 0
	v_addc_co_u32_e32 v47, vcc, 0, v63, vcc
	global_load_dwordx4 v[42:45], v[42:43], off offset:2048 nt
	s_nop 0
	global_load_dwordx4 v[46:49], v[46:47], off offset:3072 nt
	v_add_co_u32_e32 v50, vcc, s7, v62
	s_mov_b32 s7, 0x92000
	s_nop 0
	v_addc_co_u32_e32 v51, vcc, 0, v63, vcc
	v_add_co_u32_e32 v54, vcc, s7, v62
	s_mov_b32 s7, 0x9d000
	s_nop 0
	v_addc_co_u32_e32 v55, vcc, 0, v63, vcc
	global_load_dwordx4 v[50:53], v[50:51], off nt
	s_nop 0
	global_load_dwordx4 v[54:57], v[54:55], off offset:1024 nt
	v_add_co_u32_e32 v58, vcc, s7, v62
	s_mov_b32 s7, 0xa8000
	s_nop 0
	v_addc_co_u32_e32 v59, vcc, 0, v63, vcc
	global_load_dwordx4 v[58:61], v[58:59], off offset:2048 nt
	v_add_co_u32_e32 v62, vcc, s7, v62
	v_add_u32_e32 v1, 0x410, v95
	s_nop 0
	v_addc_co_u32_e32 v63, vcc, 0, v63, vcc
	global_load_dwordx4 v[62:65], v[62:63], off offset:3072 nt
	s_waitcnt vmcnt(15)
	ds_write2_b32 v95, v2, v3 offset1:1
	ds_write2_b32 v95, v4, v5 offset0:2 offset1:3
	s_waitcnt vmcnt(14)
	ds_write2_b32 v1, v6, v7 offset1:1
	v_add_u32_e32 v1, 0x418, v95
	ds_write2_b32 v1, v8, v9 offset1:1
	v_add_u32_e32 v1, 0x820, v95
	s_lshl_b32 s12, s8, 7
	v_lshl_add_u64 v[2:3], v[78:79], 0, s[12:13]
	s_waitcnt vmcnt(13)
	ds_write2_b32 v1, v10, v11 offset1:1
	v_add_u32_e32 v1, 0x828, v95
	ds_write2_b32 v1, v12, v13 offset1:1
	v_add_u32_e32 v1, 0xc30, v95
	s_waitcnt vmcnt(12)
	ds_write2_b32 v1, v14, v15 offset1:1
	v_add_u32_e32 v1, 0xc38, v95
	ds_write2_b32 v1, v16, v17 offset1:1
	v_add_u32_e32 v1, 0x1040, v95
	s_waitcnt vmcnt(11)
	ds_write2_b32 v1, v18, v19 offset1:1
	v_add_u32_e32 v1, 0x1048, v95
	ds_write2_b32 v1, v20, v21 offset1:1
	v_add_u32_e32 v1, 0x1450, v95
	s_waitcnt vmcnt(10)
	ds_write2_b32 v1, v22, v23 offset1:1
	v_add_u32_e32 v1, 0x1458, v95
	ds_write2_b32 v1, v24, v25 offset1:1
	v_add_u32_e32 v1, 0x1860, v95
	v_or_b32_e32 v24, s6, v96
	v_ashrrev_i32_e32 v25, 31, v24
	v_lshlrev_b64 v[24:25], 12, v[24:25]
	s_waitcnt vmcnt(9)
	ds_write2_b32 v1, v26, v27 offset1:1
	v_add_u32_e32 v1, 0x1868, v95
	ds_write2_b32 v1, v28, v29 offset1:1
	v_add_u32_e32 v1, 0x1c70, v95
	s_waitcnt vmcnt(8)
	ds_write2_b32 v1, v30, v31 offset1:1
	v_add_u32_e32 v1, 0x1c78, v95
	ds_write2_b32 v1, v32, v33 offset1:1
	v_add_u32_e32 v1, 0x2080, v95
	v_add_u32_e32 v26, 0x400, v97
	v_lshl_add_u64 v[24:25], v[2:3], 0, v[24:25]
	s_waitcnt vmcnt(7)
	ds_write2_b32 v1, v34, v35 offset1:1
	v_add_u32_e32 v1, 0x2088, v95
	ds_write2_b32 v1, v36, v37 offset1:1
	v_add_u32_e32 v1, 0x2490, v95
	s_waitcnt vmcnt(6)
	ds_write2_b32 v1, v38, v39 offset1:1
	v_add_u32_e32 v1, 0x2498, v95
	ds_write2_b32 v1, v40, v41 offset1:1
	v_add_u32_e32 v1, 0x28a0, v95
	s_waitcnt vmcnt(5)
	ds_write2_b32 v1, v42, v43 offset1:1
	v_add_u32_e32 v1, 0x28a8, v95
	ds_write2_b32 v1, v44, v45 offset1:1
	v_add_u32_e32 v1, 0x2cb0, v95
	s_waitcnt vmcnt(4)
	ds_write2_b32 v1, v46, v47 offset1:1
	v_add_u32_e32 v1, 0x2cb8, v95
	ds_write2_b32 v1, v48, v49 offset1:1
	v_add_u32_e32 v1, 0x30c0, v95
	s_waitcnt vmcnt(3)
; #define LAS __attribute__((address_space(3)))
; __device__ __forceinline__ unsigned pk2(float lo, float hi) { return f2bf(lo) | (f2bf(hi) << 16); }
; __device__ __forceinline__ void tr_item(const float* W, int ldw, int k0, int n0, bf16* WT, int ldt, int drow0, LAS float* scr, int lane, const float* kscale = nullptr) {
;     ...
;     const int kc = lane & 7;
; #pragma unroll
;     for (int j = 0; j < 8; ++j) { const int n = (lane >> 3) + 8 * j; const LAS float* sp = scr + (8 * kc) * 65 + n;
;         u32x4 o; o.x = pk2(sp[0 * 65], sp[1 * 65]); o.y = pk2(sp[2 * 65], sp[3 * 65]); o.z = pk2(sp[4 * 65], sp[5 * 65]); o.w = pk2(sp[6 * 65], sp[7 * 65]);
;         __builtin_nontemporal_store(o, (u32x4*)(WT + (size_t)(drow0 + n) * ldt + k0 + 8 * kc)); }
;     asm volatile("s_waitcnt lgkmcnt(0)" ::: "memory");
; }
	ds_write2_b32 v1, v50, v51 offset1:1
	v_add_u32_e32 v1, 0x30c8, v95
	ds_write2_b32 v1, v52, v53 offset1:1
	v_add_u32_e32 v1, 0x34d0, v95
	s_waitcnt vmcnt(2)
	ds_write2_b32 v1, v54, v55 offset1:1
	v_add_u32_e32 v1, 0x34d8, v95
	ds_write2_b32 v1, v56, v57 offset1:1
	v_add_u32_e32 v1, 0x38e0, v95
	s_waitcnt vmcnt(1)
	ds_write2_b32 v1, v58, v59 offset1:1
	v_add_u32_e32 v1, 0x38e8, v95
	ds_write2_b32 v1, v60, v61 offset1:1
	v_add_u32_e32 v1, 0x3cf0, v95
	s_waitcnt vmcnt(0)
	ds_write2_b32 v1, v62, v63 offset1:1
	v_add_u32_e32 v1, 0x3cf8, v95
	ds_write2_b32 v1, v64, v65 offset1:1
	s_waitcnt lgkmcnt(0)
	ds_read2_b32 v[8:9], v97 offset1:8
	ds_read2_b32 v[10:11], v97 offset0:65 offset1:73
	ds_read2_b32 v[12:13], v97 offset0:130 offset1:138
	ds_read2_b32 v[14:15], v97 offset0:195 offset1:203
	ds_read2_b32 v[16:17], v26 offset0:4 offset1:12
	s_waitcnt lgkmcnt(4)
	s_waitcnt lgkmcnt(3)
	ds_read2_b32 v[18:19], v26 offset0:69 offset1:77
	v_cvt_pk_bf16_f32 v4, v8, v10
	s_waitcnt lgkmcnt(3)
	s_waitcnt lgkmcnt(2)
	ds_read2_b32 v[20:21], v26 offset0:134 offset1:142
	ds_read2_b32 v[22:23], v26 offset0:199 offset1:207
	v_cvt_pk_bf16_f32 v5, v12, v14
	s_waitcnt lgkmcnt(3)
	s_waitcnt lgkmcnt(2)
	v_cvt_pk_bf16_f32 v6, v16, v18
	s_waitcnt lgkmcnt(1)
	s_waitcnt lgkmcnt(0)
	v_cvt_pk_bf16_f32 v7, v20, v22
	global_store_dwordx4 v[24:25], v[4:7], off nt
	s_nop 1
	v_cvt_pk_bf16_f32 v4, v9, v11
	v_cvt_pk_bf16_f32 v5, v13, v15
	v_cvt_pk_bf16_f32 v6, v17, v19
	v_or_b32_e32 v8, s6, v98
	v_ashrrev_i32_e32 v9, 31, v8
	v_lshlrev_b64 v[8:9], 12, v[8:9]
	v_cvt_pk_bf16_f32 v7, v21, v23
	ds_read2_b32 v[10:11], v97 offset0:16 offset1:24
	v_lshl_add_u64 v[8:9], v[2:3], 0, v[8:9]
	global_store_dwordx4 v[8:9], v[4:7], off nt
	ds_read2_b32 v[8:9], v97 offset0:81 offset1:89
	ds_read2_b32 v[12:13], v97 offset0:146 offset1:154
	ds_read2_b32 v[14:15], v97 offset0:211 offset1:219
	s_waitcnt lgkmcnt(3)
	s_waitcnt lgkmcnt(2)
	ds_read2_b32 v[16:17], v26 offset0:20 offset1:28
	ds_read2_b32 v[18:19], v26 offset0:85 offset1:93
	v_cvt_pk_bf16_f32 v4, v10, v8
	s_waitcnt lgkmcnt(3)
	s_waitcnt lgkmcnt(2)
	ds_read2_b32 v[20:21], v26 offset0:150 offset1:158
	ds_read2_b32 v[22:23], v26 offset0:215 offset1:223
	v_cvt_pk_bf16_f32 v5, v12, v14
	s_waitcnt lgkmcnt(3)
	s_waitcnt lgkmcnt(2)
	v_cvt_pk_bf16_f32 v6, v16, v18
	s_waitcnt lgkmcnt(1)
	v_or_b32_e32 v24, s6, v99
	s_waitcnt lgkmcnt(0)
	v_ashrrev_i32_e32 v25, 31, v24
	v_lshlrev_b64 v[24:25], 12, v[24:25]
	v_cvt_pk_bf16_f32 v7, v20, v22
	v_lshl_add_u64 v[24:25], v[2:3], 0, v[24:25]
	global_store_dwordx4 v[24:25], v[4:7], off nt
	s_nop 1
	v_cvt_pk_bf16_f32 v4, v11, v9
	v_cvt_pk_bf16_f32 v5, v13, v15
	v_cvt_pk_bf16_f32 v6, v17, v19
	v_or_b32_e32 v8, s6, v100
	v_ashrrev_i32_e32 v9, 31, v8
	v_lshlrev_b64 v[8:9], 12, v[8:9]
	v_cvt_pk_bf16_f32 v7, v21, v23
	ds_read2_b32 v[10:11], v97 offset0:32 offset1:40
	v_lshl_add_u64 v[8:9], v[2:3], 0, v[8:9]
	global_store_dwordx4 v[8:9], v[4:7], off nt
	ds_read2_b32 v[8:9], v97 offset0:97 offset1:105
	ds_read2_b32 v[12:13], v97 offset0:162 offset1:170
	ds_read2_b32 v[14:15], v97 offset0:227 offset1:235
	s_waitcnt lgkmcnt(3)
	s_waitcnt lgkmcnt(2)
	ds_read2_b32 v[16:17], v26 offset0:36 offset1:44
	ds_read2_b32 v[18:19], v26 offset0:101 offset1:109
	v_cvt_pk_bf16_f32 v4, v10, v8
	s_waitcnt lgkmcnt(3)
	s_waitcnt lgkmcnt(2)
	ds_read2_b32 v[20:21], v26 offset0:166 offset1:174
	ds_read2_b32 v[22:23], v26 offset0:231 offset1:239
	v_cvt_pk_bf16_f32 v5, v12, v14
	s_waitcnt lgkmcnt(3)
	s_waitcnt lgkmcnt(2)
	v_cvt_pk_bf16_f32 v6, v16, v18
	s_waitcnt lgkmcnt(1)
	v_or_b32_e32 v24, s6, v101
	s_waitcnt lgkmcnt(0)
	v_ashrrev_i32_e32 v25, 31, v24
	v_lshlrev_b64 v[24:25], 12, v[24:25]
	v_cvt_pk_bf16_f32 v7, v20, v22
	v_lshl_add_u64 v[24:25], v[2:3], 0, v[24:25]
	global_store_dwordx4 v[24:25], v[4:7], off nt
	s_nop 1
	v_cvt_pk_bf16_f32 v4, v11, v9
	v_cvt_pk_bf16_f32 v5, v13, v15
	v_cvt_pk_bf16_f32 v6, v17, v19
	v_or_b32_e32 v8, s6, v102
	v_ashrrev_i32_e32 v9, 31, v8
	v_lshlrev_b64 v[8:9], 12, v[8:9]
	v_cvt_pk_bf16_f32 v7, v21, v23
	ds_read2_b32 v[10:11], v97 offset0:48 offset1:56
	v_lshl_add_u64 v[8:9], v[2:3], 0, v[8:9]
	global_store_dwordx4 v[8:9], v[4:7], off nt
	ds_read2_b32 v[8:9], v97 offset0:113 offset1:121
	ds_read2_b32 v[12:13], v97 offset0:178 offset1:186
	ds_read2_b32 v[14:15], v97 offset0:243 offset1:251
	s_waitcnt lgkmcnt(3)
	s_waitcnt lgkmcnt(2)
	ds_read2_b32 v[16:17], v26 offset0:52 offset1:60
	ds_read2_b32 v[18:19], v26 offset0:117 offset1:125
	v_cvt_pk_bf16_f32 v4, v10, v8
	s_waitcnt lgkmcnt(3)
	s_waitcnt lgkmcnt(2)
	ds_read2_b32 v[20:21], v26 offset0:182 offset1:190
	ds_read2_b32 v[22:23], v26 offset0:247 offset1:255
	v_cvt_pk_bf16_f32 v5, v12, v14
	s_waitcnt lgkmcnt(3)
	s_waitcnt lgkmcnt(2)
	v_cvt_pk_bf16_f32 v6, v16, v18
	s_waitcnt lgkmcnt(1)
	v_or_b32_e32 v24, s6, v103
	s_waitcnt lgkmcnt(0)
	v_ashrrev_i32_e32 v25, 31, v24
	v_lshlrev_b64 v[24:25], 12, v[24:25]
	v_cvt_pk_bf16_f32 v7, v20, v22
	v_lshl_add_u64 v[24:25], v[2:3], 0, v[24:25]
	global_store_dwordx4 v[24:25], v[4:7], off nt
	s_nop 1
	v_cvt_pk_bf16_f32 v4, v11, v9
	v_cvt_pk_bf16_f32 v5, v13, v15
	v_cvt_pk_bf16_f32 v6, v17, v19
	v_or_b32_e32 v8, s6, v104
	v_ashrrev_i32_e32 v9, 31, v8
	v_lshlrev_b64 v[8:9], 12, v[8:9]
	v_cvt_pk_bf16_f32 v7, v21, v23
	v_lshl_add_u64 v[2:3], v[2:3], 0, v[8:9]
	global_store_dwordx4 v[2:3], v[4:7], off nt
	s_waitcnt lgkmcnt(0)

; #define LAS __attribute__((address_space(3)))
; #define WSW(T, off, l) WSP(T, WS_WSET + (size_t)(l) * WSET_STRIDE + (off))
; __device__ __forceinline__ void tr_item(const float* W, int ldw, int k0, int n0, bf16* WT, int ldt, int drow0, LAS float* scr, int lane, const float* kscale = nullptr) {
;     const float* src = W + (size_t)(k0 + (lane >> 4)) * ldw + n0 + (lane & 15) * 4;
;     f32x4 v[16];
; #pragma unroll
;     for (int i = 0; i < 16; ++i) v[i] = __builtin_nontemporal_load((const f32x4*)(src + (size_t)(4 * i) * ldw));
;     LAS float* wp = scr + (lane >> 4) * 65 + (lane & 15) * 4;
; #pragma unroll
;     for (int i = 0; i < 16; ++i) { LAS float* q = wp + (4 * i) * 65; const float ks = kscale ? kscale[k0 + 4 * i + (lane >> 4)] : 1.f; q[0] = v[i].x * ks; q[1] = v[i].y * ks; q[2] = v[i].z * ks; q[3] = v[i].w * ks; }
;     asm volatile("s_waitcnt lgkmcnt(0)" ::: "memory");
; __device__ __forceinline__ void convert_tile(const Args& a, GAS unsigned char* wsb, int l, int t, LAS float* scr, int lane) {
;     ...
;     if (r < I_OUT) { const int kb = r / 32, nb = r - kb * 32; tr_item(INP(21) + (size_t)l * DM * DM, DM, kb * 64, nb * 64, WSW(bf16, W_OUT, l), DM, nb * 64, scr, lane); return; }
.LBB0_2429:
	s_andn2_b64 vcc, exec, s[6:7]
	s_cbranch_vccnz .LBB0_2431
	s_lshl_b32 s6, s17, 1
	s_and_b32 s6, s6, 0x1fc0
	s_addk_i32 s6, 0xf240
	s_lshl_b32 s7, s17, 6
	v_or_b32_e32 v2, s6, v67
	v_mov_b32_e32 v3, v147
	s_and_b32 s8, s7, 0x7c0
	v_lshlrev_b64 v[2:3], 13, v[2:3]
	v_lshl_add_u64 v[2:3], s[60:61], 0, v[2:3]
	s_lshl_b32 s12, s8, 2
	v_lshl_add_u64 v[2:3], v[2:3], 0, s[12:13]
	v_lshlrev_b32_e32 v4, 2, v66
	v_mov_b32_e32 v5, v147
	v_lshl_add_u64 v[62:63], v[2:3], 0, v[4:5]
	v_add_co_u32_e32 v6, vcc, s83, v62
	s_mov_b32 s7, 0x20000
	s_nop 0
	v_addc_co_u32_e32 v7, vcc, 0, v63, vcc
	v_add_co_u32_e32 v10, vcc, s81, v62
	global_load_dwordx4 v[2:5], v[62:63], off nt
	s_nop 0
	global_load_dwordx4 v[6:9], v[6:7], off nt
	v_addc_co_u32_e32 v11, vcc, 0, v63, vcc
	v_add_co_u32_e32 v14, vcc, s82, v62
	v_add_u32_e32 v1, 0x410, v95
	s_nop 0
	v_addc_co_u32_e32 v15, vcc, 0, v63, vcc
	global_load_dwordx4 v[10:13], v[10:11], off nt
	s_nop 0
	global_load_dwordx4 v[14:17], v[14:15], off nt
	v_add_co_u32_e32 v18, vcc, s7, v62
	s_mov_b32 s7, 0x28000
	s_nop 0
	v_addc_co_u32_e32 v19, vcc, 0, v63, vcc
	v_add_co_u32_e32 v22, vcc, s7, v62
	s_mov_b32 s7, 0x30000
	s_nop 0
	v_addc_co_u32_e32 v23, vcc, 0, v63, vcc
	global_load_dwordx4 v[18:21], v[18:19], off nt
	s_nop 0
	global_load_dwordx4 v[22:25], v[22:23], off nt
	v_add_co_u32_e32 v26, vcc, s7, v62
	s_mov_b32 s7, 0x38000
	s_nop 0
	v_addc_co_u32_e32 v27, vcc, 0, v63, vcc
	v_add_co_u32_e32 v30, vcc, s7, v62
	s_mov_b32 s7, 0x40000
	s_nop 0
	v_addc_co_u32_e32 v31, vcc, 0, v63, vcc
	global_load_dwordx4 v[26:29], v[26:27], off nt
	s_nop 0
	global_load_dwordx4 v[30:33], v[30:31], off nt
	v_add_co_u32_e32 v34, vcc, s7, v62
	s_mov_b32 s7, 0x48000
	s_nop 0
	v_addc_co_u32_e32 v35, vcc, 0, v63, vcc
	v_add_co_u32_e32 v38, vcc, s7, v62
	s_mov_b32 s7, 0x50000
	s_nop 0
	v_addc_co_u32_e32 v39, vcc, 0, v63, vcc
	global_load_dwordx4 v[34:37], v[34:35], off nt
	s_nop 0
	global_load_dwordx4 v[38:41], v[38:39], off nt
	v_add_co_u32_e32 v42, vcc, s7, v62
	s_mov_b32 s7, 0x58000
	s_nop 0
	v_addc_co_u32_e32 v43, vcc, 0, v63, vcc
	v_add_co_u32_e32 v46, vcc, s7, v62
	s_mov_b32 s7, 0x60000
	s_nop 0
	v_addc_co_u32_e32 v47, vcc, 0, v63, vcc
	global_load_dwordx4 v[42:45], v[42:43], off nt
	s_nop 0
	global_load_dwordx4 v[46:49], v[46:47], off nt
	v_add_co_u32_e32 v50, vcc, s7, v62
	s_mov_b32 s7, 0x68000
	s_nop 0
	v_addc_co_u32_e32 v51, vcc, 0, v63, vcc
	v_add_co_u32_e32 v54, vcc, s7, v62
	s_mov_b32 s7, 0x70000
	s_nop 0
	v_addc_co_u32_e32 v55, vcc, 0, v63, vcc
	global_load_dwordx4 v[50:53], v[50:51], off nt
	s_nop 0
	global_load_dwordx4 v[54:57], v[54:55], off nt
	v_add_co_u32_e32 v58, vcc, s7, v62
	s_mov_b32 s7, 0x78000
	s_nop 0
	v_addc_co_u32_e32 v59, vcc, 0, v63, vcc
	global_load_dwordx4 v[58:61], v[58:59], off nt
	v_add_co_u32_e32 v62, vcc, s7, v62
	s_mov_b32 s7, s13
	s_nop 0
	v_addc_co_u32_e32 v63, vcc, 0, v63, vcc
	global_load_dwordx4 v[62:65], v[62:63], off nt
	s_waitcnt vmcnt(15)
	ds_write2_b32 v95, v2, v3 offset1:1
	ds_write2_b32 v95, v4, v5 offset0:2 offset1:3
	s_waitcnt vmcnt(14)
	ds_write2_b32 v1, v6, v7 offset1:1
	v_add_u32_e32 v1, 0x418, v95
	ds_write2_b32 v1, v8, v9 offset1:1
	v_add_u32_e32 v1, 0x820, v95
	v_lshl_add_u64 v[2:3], s[6:7], 1, v[84:85]
	s_waitcnt vmcnt(13)
	ds_write2_b32 v1, v10, v11 offset1:1
	v_add_u32_e32 v1, 0x828, v95
	ds_write2_b32 v1, v12, v13 offset1:1
	v_add_u32_e32 v1, 0xc30, v95
	s_waitcnt vmcnt(12)
	ds_write2_b32 v1, v14, v15 offset1:1
	v_add_u32_e32 v1, 0xc38, v95
	ds_write2_b32 v1, v16, v17 offset1:1
	v_add_u32_e32 v1, 0x1040, v95
	s_waitcnt vmcnt(11)
	ds_write2_b32 v1, v18, v19 offset1:1
	v_add_u32_e32 v1, 0x1048, v95
	ds_write2_b32 v1, v20, v21 offset1:1
	v_add_u32_e32 v1, 0x1450, v95
	s_waitcnt vmcnt(10)
	ds_write2_b32 v1, v22, v23 offset1:1
	v_add_u32_e32 v1, 0x1458, v95
	ds_write2_b32 v1, v24, v25 offset1:1
	v_add_u32_e32 v1, 0x1860, v95
	v_mov_b32_e32 v25, v147
	s_waitcnt vmcnt(9)
	ds_write2_b32 v1, v26, v27 offset1:1
	v_add_u32_e32 v1, 0x1868, v95
	ds_write2_b32 v1, v28, v29 offset1:1
	v_add_u32_e32 v1, 0x1c70, v95
	s_waitcnt vmcnt(8)
	ds_write2_b32 v1, v30, v31 offset1:1
	v_add_u32_e32 v1, 0x1c78, v95
	ds_write2_b32 v1, v32, v33 offset1:1
	v_add_u32_e32 v1, 0x2080, v95
	v_add_u32_e32 v26, 0x400, v97
	s_waitcnt vmcnt(7)
	ds_write2_b32 v1, v34, v35 offset1:1
	v_add_u32_e32 v1, 0x2088, v95
	ds_write2_b32 v1, v36, v37 offset1:1
	v_add_u32_e32 v1, 0x2490, v95
	s_waitcnt vmcnt(6)
	ds_write2_b32 v1, v38, v39 offset1:1
	v_add_u32_e32 v1, 0x2498, v95
	ds_write2_b32 v1, v40, v41 offset1:1
	v_add_u32_e32 v1, 0x28a0, v95
	s_waitcnt vmcnt(5)
	ds_write2_b32 v1, v42, v43 offset1:1
	v_add_u32_e32 v1, 0x28a8, v95
	ds_write2_b32 v1, v44, v45 offset1:1
	v_add_u32_e32 v1, 0x2cb0, v95
	s_waitcnt vmcnt(4)
	ds_write2_b32 v1, v46, v47 offset1:1
	v_add_u32_e32 v1, 0x2cb8, v95
	ds_write2_b32 v1, v48, v49 offset1:1
	v_add_u32_e32 v1, 0x30c0, v95
	s_waitcnt vmcnt(3)
	ds_write2_b32 v1, v50, v51 offset1:1
	v_add_u32_e32 v1, 0x30c8, v95
	ds_write2_b32 v1, v52, v53 offset1:1
	v_add_u32_e32 v1, 0x34d0, v95
	s_waitcnt vmcnt(2)
; #define LAS __attribute__((address_space(3)))
; __device__ __forceinline__ unsigned pk2(float lo, float hi) { return f2bf(lo) | (f2bf(hi) << 16); }
; __device__ __forceinline__ void tr_item(const float* W, int ldw, int k0, int n0, bf16* WT, int ldt, int drow0, LAS float* scr, int lane, const float* kscale = nullptr) {
;     ...
;     const int kc = lane & 7;
; #pragma unroll
;     for (int j = 0; j < 8; ++j) { const int n = (lane >> 3) + 8 * j; const LAS float* sp = scr + (8 * kc) * 65 + n;
;         u32x4 o; o.x = pk2(sp[0 * 65], sp[1 * 65]); o.y = pk2(sp[2 * 65], sp[3 * 65]); o.z = pk2(sp[4 * 65], sp[5 * 65]); o.w = pk2(sp[6 * 65], sp[7 * 65]);
;         __builtin_nontemporal_store(o, (u32x4*)(WT + (size_t)(drow0 + n) * ldt + k0 + 8 * kc)); }
;     asm volatile("s_waitcnt lgkmcnt(0)" ::: "memory");
; }
	ds_write2_b32 v1, v54, v55 offset1:1
	v_add_u32_e32 v1, 0x34d8, v95
	ds_write2_b32 v1, v56, v57 offset1:1
	v_add_u32_e32 v1, 0x38e0, v95
	s_waitcnt vmcnt(1)
	ds_write2_b32 v1, v58, v59 offset1:1
	v_add_u32_e32 v1, 0x38e8, v95
	ds_write2_b32 v1, v60, v61 offset1:1
	v_add_u32_e32 v1, 0x3cf0, v95
	s_waitcnt vmcnt(0)
	ds_write2_b32 v1, v62, v63 offset1:1
	v_add_u32_e32 v1, 0x3cf8, v95
	ds_write2_b32 v1, v64, v65 offset1:1
	s_waitcnt lgkmcnt(0)
	ds_read2_b32 v[8:9], v97 offset1:8
	ds_read2_b32 v[10:11], v97 offset0:65 offset1:73
	ds_read2_b32 v[12:13], v97 offset0:130 offset1:138
	ds_read2_b32 v[14:15], v97 offset0:195 offset1:203
	ds_read2_b32 v[16:17], v26 offset0:4 offset1:12
	s_waitcnt lgkmcnt(4)
	s_waitcnt lgkmcnt(3)
	ds_read2_b32 v[18:19], v26 offset0:69 offset1:77
	v_cvt_pk_bf16_f32 v4, v8, v10
	s_waitcnt lgkmcnt(3)
	s_waitcnt lgkmcnt(2)
	ds_read2_b32 v[20:21], v26 offset0:134 offset1:142
	ds_read2_b32 v[22:23], v26 offset0:199 offset1:207
	v_cvt_pk_bf16_f32 v5, v12, v14
	s_waitcnt lgkmcnt(3)
	s_waitcnt lgkmcnt(2)
	v_cvt_pk_bf16_f32 v6, v16, v18
	s_waitcnt lgkmcnt(1)
	s_waitcnt lgkmcnt(0)
	v_cvt_pk_bf16_f32 v7, v20, v22
	v_or_b32_e32 v1, s8, v96
	v_lshlrev_b32_e32 v24, 12, v1
	v_lshl_add_u64 v[24:25], v[2:3], 0, v[24:25]
	global_store_dwordx4 v[24:25], v[4:7], off nt
	s_nop 1
	v_cvt_pk_bf16_f32 v4, v9, v11
	v_cvt_pk_bf16_f32 v5, v13, v15
	v_cvt_pk_bf16_f32 v6, v17, v19
	v_cvt_pk_bf16_f32 v7, v21, v23
	v_or_b32_e32 v1, s8, v98
	v_lshlrev_b32_e32 v8, 12, v1
	v_mov_b32_e32 v9, v147
	ds_read2_b32 v[10:11], v97 offset0:16 offset1:24
	v_lshl_add_u64 v[8:9], v[2:3], 0, v[8:9]
	global_store_dwordx4 v[8:9], v[4:7], off nt
	ds_read2_b32 v[8:9], v97 offset0:81 offset1:89
	ds_read2_b32 v[12:13], v97 offset0:146 offset1:154
	ds_read2_b32 v[14:15], v97 offset0:211 offset1:219
	s_waitcnt lgkmcnt(3)
	s_waitcnt lgkmcnt(2)
	ds_read2_b32 v[16:17], v26 offset0:20 offset1:28
	ds_read2_b32 v[18:19], v26 offset0:85 offset1:93
	v_cvt_pk_bf16_f32 v4, v10, v8
	s_waitcnt lgkmcnt(3)
	s_waitcnt lgkmcnt(2)
	ds_read2_b32 v[20:21], v26 offset0:150 offset1:158
	ds_read2_b32 v[22:23], v26 offset0:215 offset1:223
	v_cvt_pk_bf16_f32 v5, v12, v14
	s_waitcnt lgkmcnt(3)
	s_waitcnt lgkmcnt(2)
	v_cvt_pk_bf16_f32 v6, v16, v18
	s_waitcnt lgkmcnt(1)
	s_waitcnt lgkmcnt(0)
	v_cvt_pk_bf16_f32 v7, v20, v22
	v_or_b32_e32 v1, s8, v99
	v_lshlrev_b32_e32 v24, 12, v1
	v_mov_b32_e32 v25, v147
	v_lshl_add_u64 v[24:25], v[2:3], 0, v[24:25]
	global_store_dwordx4 v[24:25], v[4:7], off nt
	s_nop 1
	v_cvt_pk_bf16_f32 v4, v11, v9
	v_cvt_pk_bf16_f32 v5, v13, v15
	v_cvt_pk_bf16_f32 v6, v17, v19
	v_cvt_pk_bf16_f32 v7, v21, v23
	v_or_b32_e32 v1, s8, v100
	v_lshlrev_b32_e32 v8, 12, v1
	v_mov_b32_e32 v9, v147
	ds_read2_b32 v[10:11], v97 offset0:32 offset1:40
	v_lshl_add_u64 v[8:9], v[2:3], 0, v[8:9]
	global_store_dwordx4 v[8:9], v[4:7], off nt
	ds_read2_b32 v[8:9], v97 offset0:97 offset1:105
	ds_read2_b32 v[12:13], v97 offset0:162 offset1:170
	ds_read2_b32 v[14:15], v97 offset0:227 offset1:235
	s_waitcnt lgkmcnt(3)
	s_waitcnt lgkmcnt(2)
	ds_read2_b32 v[16:17], v26 offset0:36 offset1:44
	ds_read2_b32 v[18:19], v26 offset0:101 offset1:109
	v_cvt_pk_bf16_f32 v4, v10, v8
	s_waitcnt lgkmcnt(3)
	s_waitcnt lgkmcnt(2)
	ds_read2_b32 v[20:21], v26 offset0:166 offset1:174
	ds_read2_b32 v[22:23], v26 offset0:231 offset1:239
	v_cvt_pk_bf16_f32 v5, v12, v14
	s_waitcnt lgkmcnt(3)
	s_waitcnt lgkmcnt(2)
	v_cvt_pk_bf16_f32 v6, v16, v18
	s_waitcnt lgkmcnt(1)
	s_waitcnt lgkmcnt(0)
	v_cvt_pk_bf16_f32 v7, v20, v22
	v_or_b32_e32 v1, s8, v101
	v_lshlrev_b32_e32 v24, 12, v1
	v_mov_b32_e32 v25, v147
	v_lshl_add_u64 v[24:25], v[2:3], 0, v[24:25]
	global_store_dwordx4 v[24:25], v[4:7], off nt
	s_nop 1
	v_cvt_pk_bf16_f32 v4, v11, v9
	v_cvt_pk_bf16_f32 v5, v13, v15
	v_cvt_pk_bf16_f32 v6, v17, v19
	v_cvt_pk_bf16_f32 v7, v21, v23
	v_or_b32_e32 v1, s8, v102
	v_lshlrev_b32_e32 v8, 12, v1
	v_mov_b32_e32 v9, v147
	ds_read2_b32 v[10:11], v97 offset0:48 offset1:56
	v_lshl_add_u64 v[8:9], v[2:3], 0, v[8:9]
	global_store_dwordx4 v[8:9], v[4:7], off nt
	ds_read2_b32 v[8:9], v97 offset0:113 offset1:121
	ds_read2_b32 v[12:13], v97 offset0:178 offset1:186
	ds_read2_b32 v[14:15], v97 offset0:243 offset1:251
	s_waitcnt lgkmcnt(3)
	s_waitcnt lgkmcnt(2)
	ds_read2_b32 v[16:17], v26 offset0:52 offset1:60
	ds_read2_b32 v[18:19], v26 offset0:117 offset1:125
	v_cvt_pk_bf16_f32 v4, v10, v8
	s_waitcnt lgkmcnt(3)
	s_waitcnt lgkmcnt(2)
	ds_read2_b32 v[20:21], v26 offset0:182 offset1:190
	ds_read2_b32 v[22:23], v26 offset0:247 offset1:255
	v_cvt_pk_bf16_f32 v5, v12, v14
	s_waitcnt lgkmcnt(3)
	s_waitcnt lgkmcnt(2)
	v_cvt_pk_bf16_f32 v6, v16, v18
	s_waitcnt lgkmcnt(1)
	s_waitcnt lgkmcnt(0)
	v_cvt_pk_bf16_f32 v7, v20, v22
	v_or_b32_e32 v1, s8, v103
	v_lshlrev_b32_e32 v24, 12, v1
	v_mov_b32_e32 v25, v147
	v_lshl_add_u64 v[24:25], v[2:3], 0, v[24:25]
	global_store_dwordx4 v[24:25], v[4:7], off nt
	s_nop 1
	v_cvt_pk_bf16_f32 v4, v11, v9
	v_cvt_pk_bf16_f32 v5, v13, v15
	v_cvt_pk_bf16_f32 v6, v17, v19
	v_cvt_pk_bf16_f32 v7, v21, v23
	v_or_b32_e32 v1, s8, v104
	v_lshlrev_b32_e32 v8, 12, v1
	v_mov_b32_e32 v9, v147
	v_lshl_add_u64 v[2:3], v[2:3], 0, v[8:9]
	global_store_dwordx4 v[2:3], v[4:7], off nt
	s_waitcnt lgkmcnt(0)

; #define LAS __attribute__((address_space(3)))
; __device__ __forceinline__ unsigned pk2(float lo, float hi) { return f2bf(lo) | (f2bf(hi) << 16); }
; __device__ __forceinline__ void tr_item(const float* W, int ldw, int k0, int n0, bf16* WT, int ldt, int drow0, LAS float* scr, int lane, const float* kscale = nullptr) {
;     ...
;     for (int i = 0; i < 16; ++i) { LAS float* q = wp + (4 * i) * 65; const float ks = kscale ? kscale[k0 + 4 * i + (lane >> 4)] : 1.f; q[0] = v[i].x * ks; q[1] = v[i].y * ks; q[2] = v[i].z * ks; q[3] = v[i].w * ks; }
;     asm volatile("s_waitcnt lgkmcnt(0)" ::: "memory");
;     const int kc = lane & 7;
; #pragma unroll
;     for (int j = 0; j < 8; ++j) { const int n = (lane >> 3) + 8 * j; const LAS float* sp = scr + (8 * kc) * 65 + n;
;         u32x4 o; o.x = pk2(sp[0 * 65], sp[1 * 65]); o.y = pk2(sp[2 * 65], sp[3 * 65]); o.z = pk2(sp[4 * 65], sp[5 * 65]); o.w = pk2(sp[6 * 65], sp[7 * 65]);
;         __builtin_nontemporal_store(o, (u32x4*)(WT + (size_t)(drow0 + n) * ldt + k0 + 8 * kc)); }
;     asm volatile("s_waitcnt lgkmcnt(0)" ::: "memory");
; }
.LBB0_2457:
	s_waitcnt vmcnt(0)
	v_pk_mul_f32 v[2:3], v[2:3], v[10:11] op_sel_hi:[1,0]
	v_add_u32_e32 v1, 0x3cf0, v95
	ds_write2_b32 v1, v2, v3 offset1:1
	v_pk_mul_f32 v[2:3], v[4:5], v[10:11] op_sel_hi:[1,0]
	v_add_u32_e32 v1, 0x3cf8, v95
	ds_write2_b32 v1, v2, v3 offset1:1
	s_waitcnt lgkmcnt(0)
	ds_read2_b32 v[8:9], v97 offset1:8
	ds_read2_b32 v[10:11], v97 offset0:65 offset1:73
	ds_read2_b32 v[12:13], v97 offset0:130 offset1:138
	ds_read2_b32 v[14:15], v97 offset0:195 offset1:203
	v_add_u32_e32 v26, 0x400, v97
	s_waitcnt lgkmcnt(3)
	s_waitcnt lgkmcnt(2)
	ds_read2_b32 v[16:17], v26 offset0:4 offset1:12
	ds_read2_b32 v[18:19], v26 offset0:69 offset1:77
	v_cvt_pk_bf16_f32 v4, v8, v10
	s_waitcnt lgkmcnt(3)
	s_waitcnt lgkmcnt(2)
	ds_read2_b32 v[20:21], v26 offset0:134 offset1:142
	ds_read2_b32 v[22:23], v26 offset0:199 offset1:207
	v_cvt_pk_bf16_f32 v5, v12, v14
	s_waitcnt lgkmcnt(3)
	s_waitcnt lgkmcnt(2)
	v_cvt_pk_bf16_f32 v6, v16, v18
	s_waitcnt lgkmcnt(1)
	s_waitcnt lgkmcnt(0)
	s_mov_b32 s7, s13
	v_cvt_pk_bf16_f32 v7, v20, v22
	v_or_b32_e32 v1, s10, v96
	v_lshl_add_u64 v[2:3], s[6:7], 1, v[86:87]
	v_lshlrev_b32_e32 v146, 9, v1
	v_lshl_add_u64 v[24:25], v[2:3], 0, v[146:147]
	global_store_dwordx4 v[24:25], v[4:7], off nt
	s_nop 1
	v_cvt_pk_bf16_f32 v4, v9, v11
	v_cvt_pk_bf16_f32 v5, v13, v15
	v_cvt_pk_bf16_f32 v6, v17, v19
	v_cvt_pk_bf16_f32 v7, v21, v23
	v_or_b32_e32 v1, s10, v98
	v_lshlrev_b32_e32 v146, 9, v1
	ds_read2_b32 v[8:9], v97 offset0:16 offset1:24
	v_lshl_add_u64 v[10:11], v[2:3], 0, v[146:147]
	global_store_dwordx4 v[10:11], v[4:7], off nt
	ds_read2_b32 v[10:11], v97 offset0:81 offset1:89
	ds_read2_b32 v[12:13], v97 offset0:146 offset1:154
	ds_read2_b32 v[14:15], v97 offset0:211 offset1:219
	s_waitcnt lgkmcnt(3)
	s_waitcnt lgkmcnt(2)
	ds_read2_b32 v[16:17], v26 offset0:20 offset1:28
	ds_read2_b32 v[18:19], v26 offset0:85 offset1:93
	v_cvt_pk_bf16_f32 v4, v8, v10
	s_waitcnt lgkmcnt(3)
	s_waitcnt lgkmcnt(2)
	ds_read2_b32 v[20:21], v26 offset0:150 offset1:158
	ds_read2_b32 v[22:23], v26 offset0:215 offset1:223
	v_cvt_pk_bf16_f32 v5, v12, v14
	s_waitcnt lgkmcnt(3)
	s_waitcnt lgkmcnt(2)
	v_cvt_pk_bf16_f32 v6, v16, v18
	s_waitcnt lgkmcnt(1)
	s_waitcnt lgkmcnt(0)
	v_cvt_pk_bf16_f32 v7, v20, v22
	v_or_b32_e32 v1, s10, v99
	v_lshlrev_b32_e32 v146, 9, v1
	v_lshl_add_u64 v[24:25], v[2:3], 0, v[146:147]
	global_store_dwordx4 v[24:25], v[4:7], off nt
	s_nop 1
	v_cvt_pk_bf16_f32 v4, v9, v11
	v_cvt_pk_bf16_f32 v5, v13, v15
	v_cvt_pk_bf16_f32 v6, v17, v19
	v_cvt_pk_bf16_f32 v7, v21, v23
	v_or_b32_e32 v1, s10, v100
	v_lshlrev_b32_e32 v146, 9, v1
	ds_read2_b32 v[8:9], v97 offset0:32 offset1:40
	v_lshl_add_u64 v[10:11], v[2:3], 0, v[146:147]
	global_store_dwordx4 v[10:11], v[4:7], off nt
	ds_read2_b32 v[10:11], v97 offset0:97 offset1:105
	ds_read2_b32 v[12:13], v97 offset0:162 offset1:170
	ds_read2_b32 v[14:15], v97 offset0:227 offset1:235
	s_waitcnt lgkmcnt(3)
	s_waitcnt lgkmcnt(2)
	ds_read2_b32 v[16:17], v26 offset0:36 offset1:44
	ds_read2_b32 v[18:19], v26 offset0:101 offset1:109
	v_cvt_pk_bf16_f32 v4, v8, v10
	s_waitcnt lgkmcnt(3)
	s_waitcnt lgkmcnt(2)
	ds_read2_b32 v[20:21], v26 offset0:166 offset1:174
	ds_read2_b32 v[22:23], v26 offset0:231 offset1:239
	v_cvt_pk_bf16_f32 v5, v12, v14
	s_waitcnt lgkmcnt(3)
	s_waitcnt lgkmcnt(2)
	v_cvt_pk_bf16_f32 v6, v16, v18
	s_waitcnt lgkmcnt(1)
	s_waitcnt lgkmcnt(0)
	v_cvt_pk_bf16_f32 v7, v20, v22
	v_or_b32_e32 v1, s10, v101
	v_lshlrev_b32_e32 v146, 9, v1
	v_lshl_add_u64 v[24:25], v[2:3], 0, v[146:147]
	global_store_dwordx4 v[24:25], v[4:7], off nt
	s_nop 1
	v_cvt_pk_bf16_f32 v4, v9, v11
	v_cvt_pk_bf16_f32 v5, v13, v15
	v_cvt_pk_bf16_f32 v6, v17, v19
	v_cvt_pk_bf16_f32 v7, v21, v23
	v_or_b32_e32 v1, s10, v102
	v_lshlrev_b32_e32 v146, 9, v1
	ds_read2_b32 v[8:9], v97 offset0:48 offset1:56
	v_lshl_add_u64 v[10:11], v[2:3], 0, v[146:147]
	global_store_dwordx4 v[10:11], v[4:7], off nt
	ds_read2_b32 v[10:11], v97 offset0:113 offset1:121
	ds_read2_b32 v[12:13], v97 offset0:178 offset1:186
	ds_read2_b32 v[14:15], v97 offset0:243 offset1:251
	s_waitcnt lgkmcnt(3)
	s_waitcnt lgkmcnt(2)
	ds_read2_b32 v[16:17], v26 offset0:52 offset1:60
	ds_read2_b32 v[18:19], v26 offset0:117 offset1:125
	v_cvt_pk_bf16_f32 v4, v8, v10
	s_waitcnt lgkmcnt(3)
	s_waitcnt lgkmcnt(2)
	ds_read2_b32 v[20:21], v26 offset0:182 offset1:190
	ds_read2_b32 v[22:23], v26 offset0:247 offset1:255
	v_cvt_pk_bf16_f32 v5, v12, v14
	s_waitcnt lgkmcnt(3)
	s_waitcnt lgkmcnt(2)
	v_cvt_pk_bf16_f32 v6, v16, v18
	s_waitcnt lgkmcnt(1)
	s_waitcnt lgkmcnt(0)
	v_cvt_pk_bf16_f32 v7, v20, v22
	v_or_b32_e32 v1, s10, v103
	v_lshlrev_b32_e32 v146, 9, v1
	v_lshl_add_u64 v[24:25], v[2:3], 0, v[146:147]
	global_store_dwordx4 v[24:25], v[4:7], off nt
	s_nop 1
	v_cvt_pk_bf16_f32 v4, v9, v11
	v_cvt_pk_bf16_f32 v5, v13, v15
	v_cvt_pk_bf16_f32 v6, v17, v19
	v_cvt_pk_bf16_f32 v7, v21, v23
	v_or_b32_e32 v1, s10, v104
	v_lshlrev_b32_e32 v146, 9, v1
	v_lshl_add_u64 v[2:3], v[2:3], 0, v[146:147]
	global_store_dwordx4 v[2:3], v[4:7], off nt
	s_waitcnt lgkmcnt(0)

; #define LAS __attribute__((address_space(3)))
; __device__ __forceinline__ unsigned pk2(float lo, float hi) { return f2bf(lo) | (f2bf(hi) << 16); }
; __device__ __forceinline__ void tr_item(const float* W, int ldw, int k0, int n0, bf16* WT, int ldt, int drow0, LAS float* scr, int lane, const float* kscale = nullptr) {
;     ...
;     for (int i = 0; i < 16; ++i) { LAS float* q = wp + (4 * i) * 65; const float ks = kscale ? kscale[k0 + 4 * i + (lane >> 4)] : 1.f; q[0] = v[i].x * ks; q[1] = v[i].y * ks; q[2] = v[i].z * ks; q[3] = v[i].w * ks; }
;     asm volatile("s_waitcnt lgkmcnt(0)" ::: "memory");
;     const int kc = lane & 7;
; #pragma unroll
;     for (int j = 0; j < 8; ++j) { const int n = (lane >> 3) + 8 * j; const LAS float* sp = scr + (8 * kc) * 65 + n;
;         u32x4 o; o.x = pk2(sp[0 * 65], sp[1 * 65]); o.y = pk2(sp[2 * 65], sp[3 * 65]); o.z = pk2(sp[4 * 65], sp[5 * 65]); o.w = pk2(sp[6 * 65], sp[7 * 65]);
;         __builtin_nontemporal_store(o, (u32x4*)(WT + (size_t)(drow0 + n) * ldt + k0 + 8 * kc)); }
;     asm volatile("s_waitcnt lgkmcnt(0)" ::: "memory");
; }
.LBB0_2484:
	s_waitcnt vmcnt(0)
	v_pk_mul_f32 v[2:3], v[2:3], v[10:11] op_sel_hi:[1,0]
	v_add_u32_e32 v1, 0x3cf0, v95
	ds_write2_b32 v1, v2, v3 offset1:1
	v_pk_mul_f32 v[2:3], v[4:5], v[10:11] op_sel_hi:[1,0]
	v_add_u32_e32 v1, 0x3cf8, v95
	ds_write2_b32 v1, v2, v3 offset1:1
	s_waitcnt lgkmcnt(0)
	ds_read2_b32 v[8:9], v97 offset1:8
	ds_read2_b32 v[10:11], v97 offset0:65 offset1:73
	ds_read2_b32 v[12:13], v97 offset0:130 offset1:138
	ds_read2_b32 v[14:15], v97 offset0:195 offset1:203
	v_add_u32_e32 v26, 0x400, v97
	s_waitcnt lgkmcnt(3)
	s_waitcnt lgkmcnt(2)
	ds_read2_b32 v[16:17], v26 offset0:4 offset1:12
	ds_read2_b32 v[18:19], v26 offset0:69 offset1:77
	v_cvt_pk_bf16_f32 v4, v8, v10
	s_waitcnt lgkmcnt(3)
	s_waitcnt lgkmcnt(2)
	ds_read2_b32 v[20:21], v26 offset0:134 offset1:142
	ds_read2_b32 v[22:23], v26 offset0:199 offset1:207
	v_cvt_pk_bf16_f32 v5, v12, v14
	s_waitcnt lgkmcnt(3)
	s_waitcnt lgkmcnt(2)
	v_cvt_pk_bf16_f32 v6, v16, v18
	s_waitcnt lgkmcnt(1)
	v_or_b32_e32 v24, s6, v96
	s_lshl_b32 s12, s10, 1
	s_waitcnt lgkmcnt(0)
	v_ashrrev_i32_e32 v25, 31, v24
	v_lshl_add_u64 v[2:3], v[88:89], 0, s[12:13]
	v_lshlrev_b64 v[24:25], 10, v[24:25]
	v_cvt_pk_bf16_f32 v7, v20, v22
	v_lshl_add_u64 v[24:25], v[2:3], 0, v[24:25]
	global_store_dwordx4 v[24:25], v[4:7], off nt
	s_nop 1
	v_cvt_pk_bf16_f32 v4, v9, v11
	v_cvt_pk_bf16_f32 v5, v13, v15
	v_cvt_pk_bf16_f32 v6, v17, v19
	v_or_b32_e32 v8, s6, v98
	v_ashrrev_i32_e32 v9, 31, v8
	v_lshlrev_b64 v[8:9], 10, v[8:9]
	v_cvt_pk_bf16_f32 v7, v21, v23
	ds_read2_b32 v[10:11], v97 offset0:16 offset1:24
	v_lshl_add_u64 v[8:9], v[2:3], 0, v[8:9]
	global_store_dwordx4 v[8:9], v[4:7], off nt
	ds_read2_b32 v[8:9], v97 offset0:81 offset1:89
	ds_read2_b32 v[12:13], v97 offset0:146 offset1:154
	ds_read2_b32 v[14:15], v97 offset0:211 offset1:219
	s_waitcnt lgkmcnt(3)
	s_waitcnt lgkmcnt(2)
	ds_read2_b32 v[16:17], v26 offset0:20 offset1:28
	ds_read2_b32 v[18:19], v26 offset0:85 offset1:93
	v_cvt_pk_bf16_f32 v4, v10, v8
	s_waitcnt lgkmcnt(3)
	s_waitcnt lgkmcnt(2)
	ds_read2_b32 v[20:21], v26 offset0:150 offset1:158
	ds_read2_b32 v[22:23], v26 offset0:215 offset1:223
	v_cvt_pk_bf16_f32 v5, v12, v14
	s_waitcnt lgkmcnt(3)
	s_waitcnt lgkmcnt(2)
	v_cvt_pk_bf16_f32 v6, v16, v18
	s_waitcnt lgkmcnt(1)
	v_or_b32_e32 v24, s6, v99
	s_waitcnt lgkmcnt(0)
	v_ashrrev_i32_e32 v25, 31, v24
	v_lshlrev_b64 v[24:25], 10, v[24:25]
	v_cvt_pk_bf16_f32 v7, v20, v22
	v_lshl_add_u64 v[24:25], v[2:3], 0, v[24:25]
	global_store_dwordx4 v[24:25], v[4:7], off nt
	s_nop 1
	v_cvt_pk_bf16_f32 v4, v11, v9
	v_cvt_pk_bf16_f32 v5, v13, v15
	v_cvt_pk_bf16_f32 v6, v17, v19
	v_or_b32_e32 v8, s6, v100
	v_ashrrev_i32_e32 v9, 31, v8
	v_lshlrev_b64 v[8:9], 10, v[8:9]
	v_cvt_pk_bf16_f32 v7, v21, v23
	ds_read2_b32 v[10:11], v97 offset0:32 offset1:40
	v_lshl_add_u64 v[8:9], v[2:3], 0, v[8:9]
	global_store_dwordx4 v[8:9], v[4:7], off nt
	ds_read2_b32 v[8:9], v97 offset0:97 offset1:105
	ds_read2_b32 v[12:13], v97 offset0:162 offset1:170
	ds_read2_b32 v[14:15], v97 offset0:227 offset1:235
	s_waitcnt lgkmcnt(3)
	s_waitcnt lgkmcnt(2)
	ds_read2_b32 v[16:17], v26 offset0:36 offset1:44
	ds_read2_b32 v[18:19], v26 offset0:101 offset1:109
	v_cvt_pk_bf16_f32 v4, v10, v8
	s_waitcnt lgkmcnt(3)
	s_waitcnt lgkmcnt(2)
	ds_read2_b32 v[20:21], v26 offset0:166 offset1:174
	ds_read2_b32 v[22:23], v26 offset0:231 offset1:239
	v_cvt_pk_bf16_f32 v5, v12, v14
	s_waitcnt lgkmcnt(3)
	s_waitcnt lgkmcnt(2)
	v_cvt_pk_bf16_f32 v6, v16, v18
	s_waitcnt lgkmcnt(1)
	v_or_b32_e32 v24, s6, v101
	s_waitcnt lgkmcnt(0)
	v_ashrrev_i32_e32 v25, 31, v24
	v_lshlrev_b64 v[24:25], 10, v[24:25]
	v_cvt_pk_bf16_f32 v7, v20, v22
	v_lshl_add_u64 v[24:25], v[2:3], 0, v[24:25]
	global_store_dwordx4 v[24:25], v[4:7], off nt
	s_nop 1
	v_cvt_pk_bf16_f32 v4, v11, v9
	v_cvt_pk_bf16_f32 v5, v13, v15
	v_cvt_pk_bf16_f32 v6, v17, v19
	v_or_b32_e32 v8, s6, v102
	v_ashrrev_i32_e32 v9, 31, v8
	v_lshlrev_b64 v[8:9], 10, v[8:9]
	v_cvt_pk_bf16_f32 v7, v21, v23
	ds_read2_b32 v[10:11], v97 offset0:48 offset1:56
	v_lshl_add_u64 v[8:9], v[2:3], 0, v[8:9]
	global_store_dwordx4 v[8:9], v[4:7], off nt
	ds_read2_b32 v[8:9], v97 offset0:113 offset1:121
	ds_read2_b32 v[12:13], v97 offset0:178 offset1:186
	ds_read2_b32 v[14:15], v97 offset0:243 offset1:251
	s_waitcnt lgkmcnt(3)
	s_waitcnt lgkmcnt(2)
	ds_read2_b32 v[16:17], v26 offset0:52 offset1:60
	ds_read2_b32 v[18:19], v26 offset0:117 offset1:125
	v_cvt_pk_bf16_f32 v4, v10, v8
	s_waitcnt lgkmcnt(3)
	s_waitcnt lgkmcnt(2)
	ds_read2_b32 v[20:21], v26 offset0:182 offset1:190
	ds_read2_b32 v[22:23], v26 offset0:247 offset1:255
	v_cvt_pk_bf16_f32 v5, v12, v14
	s_waitcnt lgkmcnt(3)
	s_waitcnt lgkmcnt(2)
	v_cvt_pk_bf16_f32 v6, v16, v18
	s_waitcnt lgkmcnt(1)
	v_or_b32_e32 v24, s6, v103
	s_waitcnt lgkmcnt(0)
	v_ashrrev_i32_e32 v25, 31, v24
	v_lshlrev_b64 v[24:25], 10, v[24:25]
	v_cvt_pk_bf16_f32 v7, v20, v22
	v_lshl_add_u64 v[24:25], v[2:3], 0, v[24:25]
	global_store_dwordx4 v[24:25], v[4:7], off nt
	s_nop 1
	v_cvt_pk_bf16_f32 v4, v11, v9
	v_cvt_pk_bf16_f32 v5, v13, v15
	v_cvt_pk_bf16_f32 v6, v17, v19
	v_or_b32_e32 v8, s6, v104
	v_ashrrev_i32_e32 v9, 31, v8
	v_lshlrev_b64 v[8:9], 10, v[8:9]
	v_cvt_pk_bf16_f32 v7, v21, v23
	v_lshl_add_u64 v[2:3], v[2:3], 0, v[8:9]
	global_store_dwordx4 v[2:3], v[4:7], off nt
	s_waitcnt lgkmcnt(0)

; #define LAS __attribute__((address_space(3)))
; #define WSW(T, off, l) WSP(T, WS_WSET + (size_t)(l) * WSET_STRIDE + (off))
; __device__ __forceinline__ void tr_item(const float* W, int ldw, int k0, int n0, bf16* WT, int ldt, int drow0, LAS float* scr, int lane, const float* kscale = nullptr) {
;     const float* src = W + (size_t)(k0 + (lane >> 4)) * ldw + n0 + (lane & 15) * 4;
;     f32x4 v[16];
; #pragma unroll
;     for (int i = 0; i < 16; ++i) v[i] = __builtin_nontemporal_load((const f32x4*)(src + (size_t)(4 * i) * ldw));
;     LAS float* wp = scr + (lane >> 4) * 65 + (lane & 15) * 4;
; #pragma unroll
;     for (int i = 0; i < 16; ++i) { LAS float* q = wp + (4 * i) * 65; const float ks = kscale ? kscale[k0 + 4 * i + (lane >> 4)] : 1.f; q[0] = v[i].x * ks; q[1] = v[i].y * ks; q[2] = v[i].z * ks; q[3] = v[i].w * ks; }
;     asm volatile("s_waitcnt lgkmcnt(0)" ::: "memory");
; __device__ __forceinline__ void convert_tile(const Args& a, GAS unsigned char* wsb, int l, int t, LAS float* scr, int lane) {
;     ...
;     if (r < I_IN) { const int kb = r / 45, nb = r - kb * 45; tr_item(INP(7) + (size_t)l * DM * INW, INW, kb * 64, nb * 64, WSW(bf16, W_IN, l), DM, nb * 64, scr, lane); return; }
.LBB0_2486:
	s_andn2_b64 vcc, exec, s[6:7]
	s_cbranch_vccnz .LBB0_2331
	s_mul_hi_i32 s6, s17, 0xb60b60b7
	s_add_i32 s6, s6, s17
	s_lshr_b32 s7, s6, 31
	s_ashr_i32 s6, s6, 5
	s_add_i32 s6, s6, s7
	s_mul_i32 s7, s6, 0xffffffd3
	v_readlane_b32 s40, v253, 52
	s_add_i32 s7, s7, s17
	s_lshl_b32 s8, s6, 6
	v_readlane_b32 s54, v254, 2
	v_readlane_b32 s55, v254, 3
	s_lshl_b32 s6, s7, 6
	v_or_b32_e32 v1, s8, v67
	v_mov_b64_e32 v[2:3], s[54:55]
	s_movk_i32 s7, 0x2d00
	v_mad_i64_i32 v[2:3], s[10:11], v1, s7, v[2:3]
	s_ashr_i32 s7, s6, 31
	v_lshl_add_u64 v[2:3], s[6:7], 2, v[2:3]
	v_lshlrev_b32_e32 v4, 2, v66
	v_mov_b32_e32 v5, v147
	v_lshl_add_u64 v[62:63], v[2:3], 0, v[4:5]
	s_mov_b32 s7, 0xb000
	v_add_co_u32_e32 v6, vcc, s7, v62
	s_mov_b32 s7, 0x16000
	s_nop 0
	v_addc_co_u32_e32 v7, vcc, 0, v63, vcc
	v_add_co_u32_e32 v10, vcc, s7, v62
	global_load_dwordx4 v[2:5], v[62:63], off nt
	s_nop 0
	global_load_dwordx4 v[6:9], v[6:7], off offset:1024 nt
	v_addc_co_u32_e32 v11, vcc, 0, v63, vcc
	s_mov_b32 s7, 0x21000
	v_add_co_u32_e32 v14, vcc, s7, v62
	s_mov_b32 s7, 0x2d000
	s_nop 0
	v_addc_co_u32_e32 v15, vcc, 0, v63, vcc
	global_load_dwordx4 v[10:13], v[10:11], off offset:2048 nt
	s_nop 0
	global_load_dwordx4 v[14:17], v[14:15], off offset:3072 nt
	v_add_co_u32_e32 v18, vcc, s7, v62
	s_mov_b32 s7, 0x38000
	s_nop 0
	v_addc_co_u32_e32 v19, vcc, 0, v63, vcc
	v_add_co_u32_e32 v22, vcc, s7, v62
	s_mov_b32 s7, 0x43000
	s_nop 0
	v_addc_co_u32_e32 v23, vcc, 0, v63, vcc
	global_load_dwordx4 v[18:21], v[18:19], off nt
	s_nop 0
	global_load_dwordx4 v[22:25], v[22:23], off offset:1024 nt
	v_add_co_u32_e32 v26, vcc, s7, v62
	s_mov_b32 s7, 0x4e000
	s_nop 0
	v_addc_co_u32_e32 v27, vcc, 0, v63, vcc
	v_add_co_u32_e32 v30, vcc, s7, v62
	s_mov_b32 s7, 0x5a000
	s_nop 0
	v_addc_co_u32_e32 v31, vcc, 0, v63, vcc
	global_load_dwordx4 v[26:29], v[26:27], off offset:2048 nt
	s_nop 0
	global_load_dwordx4 v[30:33], v[30:31], off offset:3072 nt
	v_add_co_u32_e32 v34, vcc, s7, v62
	s_mov_b32 s7, 0x65000
	s_nop 0
	v_addc_co_u32_e32 v35, vcc, 0, v63, vcc
	v_add_co_u32_e32 v38, vcc, s7, v62
	s_mov_b32 s7, 0x70000
	s_nop 0
	v_addc_co_u32_e32 v39, vcc, 0, v63, vcc
	global_load_dwordx4 v[34:37], v[34:35], off nt
	s_nop 0
	global_load_dwordx4 v[38:41], v[38:39], off offset:1024 nt
	v_add_co_u32_e32 v42, vcc, s7, v62
	s_mov_b32 s7, 0x7b000
	s_nop 0
	v_addc_co_u32_e32 v43, vcc, 0, v63, vcc
	v_add_co_u32_e32 v46, vcc, s7, v62
	s_mov_b32 s7, 0x87000
	s_nop 0
	v_addc_co_u32_e32 v47, vcc, 0, v63, vcc
	global_load_dwordx4 v[42:45], v[42:43], off offset:2048 nt
	s_nop 0
	global_load_dwordx4 v[46:49], v[46:47], off offset:3072 nt
	v_add_co_u32_e32 v50, vcc, s7, v62
	s_mov_b32 s7, 0x92000
	s_nop 0
	v_addc_co_u32_e32 v51, vcc, 0, v63, vcc
	global_load_dwordx4 v[50:53], v[50:51], off nt
	v_add_co_u32_e32 v54, vcc, s7, v62
	s_mov_b32 s7, 0x9d000
	s_nop 0
	v_addc_co_u32_e32 v55, vcc, 0, v63, vcc
	global_load_dwordx4 v[54:57], v[54:55], off offset:1024 nt
	v_add_co_u32_e32 v58, vcc, s7, v62
	s_mov_b32 s7, 0xa8000
	s_nop 0
	v_addc_co_u32_e32 v59, vcc, 0, v63, vcc
	global_load_dwordx4 v[58:61], v[58:59], off offset:2048 nt
	v_add_co_u32_e32 v62, vcc, s7, v62
	v_add_u32_e32 v1, 0x410, v95
	s_nop 0
	v_addc_co_u32_e32 v63, vcc, 0, v63, vcc
	global_load_dwordx4 v[62:65], v[62:63], off offset:3072 nt
	s_waitcnt vmcnt(15)
	ds_write2_b32 v95, v2, v3 offset1:1
	ds_write2_b32 v95, v4, v5 offset0:2 offset1:3
	s_waitcnt vmcnt(14)
	ds_write2_b32 v1, v6, v7 offset1:1
	v_add_u32_e32 v1, 0x418, v95
	ds_write2_b32 v1, v8, v9 offset1:1
	v_add_u32_e32 v1, 0x820, v95
	s_ashr_i32 s9, s8, 31
	v_lshl_add_u64 v[2:3], s[8:9], 1, v[90:91]
	v_readlane_b32 s48, v253, 60
	v_readlane_b32 s49, v253, 61
	s_waitcnt vmcnt(13)
	ds_write2_b32 v1, v10, v11 offset1:1
	v_add_u32_e32 v1, 0x828, v95
	ds_write2_b32 v1, v12, v13 offset1:1
	v_add_u32_e32 v1, 0xc30, v95
	s_waitcnt vmcnt(12)
	ds_write2_b32 v1, v14, v15 offset1:1
	v_add_u32_e32 v1, 0xc38, v95
	ds_write2_b32 v1, v16, v17 offset1:1
	v_add_u32_e32 v1, 0x1040, v95
	v_readlane_b32 s50, v253, 62
	v_readlane_b32 s51, v253, 63
	v_readlane_b32 s52, v254, 0
	s_waitcnt vmcnt(11)
	ds_write2_b32 v1, v18, v19 offset1:1
	v_add_u32_e32 v1, 0x1048, v95
	ds_write2_b32 v1, v20, v21 offset1:1
	v_add_u32_e32 v1, 0x1450, v95
	s_waitcnt vmcnt(10)
	ds_write2_b32 v1, v22, v23 offset1:1
	v_add_u32_e32 v1, 0x1458, v95
	ds_write2_b32 v1, v24, v25 offset1:1
	v_add_u32_e32 v1, 0x1860, v95
	v_or_b32_e32 v24, s6, v96
	v_ashrrev_i32_e32 v25, 31, v24
	v_lshlrev_b64 v[24:25], 12, v[24:25]
	s_waitcnt vmcnt(9)
	ds_write2_b32 v1, v26, v27 offset1:1
	v_add_u32_e32 v1, 0x1868, v95
	ds_write2_b32 v1, v28, v29 offset1:1
	v_add_u32_e32 v1, 0x1c70, v95
	s_waitcnt vmcnt(8)
	ds_write2_b32 v1, v30, v31 offset1:1
	v_add_u32_e32 v1, 0x1c78, v95
	ds_write2_b32 v1, v32, v33 offset1:1
	v_add_u32_e32 v1, 0x2080, v95
	v_add_u32_e32 v26, 0x400, v97
	v_lshl_add_u64 v[24:25], v[2:3], 0, v[24:25]
	v_readlane_b32 s53, v254, 1
	s_waitcnt vmcnt(7)
	ds_write2_b32 v1, v34, v35 offset1:1
	v_add_u32_e32 v1, 0x2088, v95
	ds_write2_b32 v1, v36, v37 offset1:1
	v_add_u32_e32 v1, 0x2490, v95
	s_waitcnt vmcnt(6)
	ds_write2_b32 v1, v38, v39 offset1:1
	v_add_u32_e32 v1, 0x2498, v95
	ds_write2_b32 v1, v40, v41 offset1:1
	v_add_u32_e32 v1, 0x28a0, v95
	v_readlane_b32 s48, v254, 35
	v_readlane_b32 s49, v254, 36
	v_readlane_b32 s50, v254, 37
	s_waitcnt vmcnt(5)
	ds_write2_b32 v1, v42, v43 offset1:1
	v_add_u32_e32 v1, 0x28a8, v95
	ds_write2_b32 v1, v44, v45 offset1:1
	v_add_u32_e32 v1, 0x2cb0, v95
	s_waitcnt vmcnt(4)
	ds_write2_b32 v1, v46, v47 offset1:1
	v_add_u32_e32 v1, 0x2cb8, v95
	ds_write2_b32 v1, v48, v49 offset1:1
	v_add_u32_e32 v1, 0x30c0, v95
	s_waitcnt vmcnt(3)
; #define LAS __attribute__((address_space(3)))
; __device__ __forceinline__ unsigned pk2(float lo, float hi) { return f2bf(lo) | (f2bf(hi) << 16); }
; __device__ __forceinline__ void tr_item(const float* W, int ldw, int k0, int n0, bf16* WT, int ldt, int drow0, LAS float* scr, int lane, const float* kscale = nullptr) {
;     ...
;     const int kc = lane & 7;
; #pragma unroll
;     for (int j = 0; j < 8; ++j) { const int n = (lane >> 3) + 8 * j; const LAS float* sp = scr + (8 * kc) * 65 + n;
;         u32x4 o; o.x = pk2(sp[0 * 65], sp[1 * 65]); o.y = pk2(sp[2 * 65], sp[3 * 65]); o.z = pk2(sp[4 * 65], sp[5 * 65]); o.w = pk2(sp[6 * 65], sp[7 * 65]);
;         __builtin_nontemporal_store(o, (u32x4*)(WT + (size_t)(drow0 + n) * ldt + k0 + 8 * kc)); }
;     asm volatile("s_waitcnt lgkmcnt(0)" ::: "memory");
; }
	ds_write2_b32 v1, v50, v51 offset1:1
	v_add_u32_e32 v1, 0x30c8, v95
	ds_write2_b32 v1, v52, v53 offset1:1
	v_add_u32_e32 v1, 0x34d0, v95
	v_readlane_b32 s51, v254, 38
	s_waitcnt vmcnt(2)
	ds_write2_b32 v1, v54, v55 offset1:1
	v_add_u32_e32 v1, 0x34d8, v95
	ds_write2_b32 v1, v56, v57 offset1:1
	v_add_u32_e32 v1, 0x38e0, v95
	v_readlane_b32 s52, v254, 39
	v_readlane_b32 s53, v254, 40
	s_waitcnt vmcnt(1)
	ds_write2_b32 v1, v58, v59 offset1:1
	v_add_u32_e32 v1, 0x38e8, v95
	ds_write2_b32 v1, v60, v61 offset1:1
	v_add_u32_e32 v1, 0x3cf0, v95
	v_readlane_b32 s54, v254, 41
	v_readlane_b32 s55, v254, 42
	s_waitcnt vmcnt(0)
	ds_write2_b32 v1, v62, v63 offset1:1
	v_add_u32_e32 v1, 0x3cf8, v95
	ds_write2_b32 v1, v64, v65 offset1:1
	s_waitcnt lgkmcnt(0)
	ds_read2_b32 v[8:9], v97 offset1:8
	ds_read2_b32 v[10:11], v97 offset0:65 offset1:73
	ds_read2_b32 v[12:13], v97 offset0:130 offset1:138
	ds_read2_b32 v[14:15], v97 offset0:195 offset1:203
	ds_read2_b32 v[16:17], v26 offset0:4 offset1:12
	s_waitcnt lgkmcnt(4)
	s_waitcnt lgkmcnt(3)
	ds_read2_b32 v[18:19], v26 offset0:69 offset1:77
	v_cvt_pk_bf16_f32 v4, v8, v10
	s_waitcnt lgkmcnt(3)
	s_waitcnt lgkmcnt(2)
	ds_read2_b32 v[20:21], v26 offset0:134 offset1:142
	ds_read2_b32 v[22:23], v26 offset0:199 offset1:207
	v_cvt_pk_bf16_f32 v5, v12, v14
	s_waitcnt lgkmcnt(3)
	s_waitcnt lgkmcnt(2)
	v_cvt_pk_bf16_f32 v6, v16, v18
	s_waitcnt lgkmcnt(1)
	s_waitcnt lgkmcnt(0)
	v_cvt_pk_bf16_f32 v7, v20, v22
	global_store_dwordx4 v[24:25], v[4:7], off nt
	s_nop 1
	v_cvt_pk_bf16_f32 v4, v9, v11
	v_cvt_pk_bf16_f32 v5, v13, v15
	v_cvt_pk_bf16_f32 v6, v17, v19
	v_or_b32_e32 v8, s6, v98
	v_ashrrev_i32_e32 v9, 31, v8
	v_lshlrev_b64 v[8:9], 12, v[8:9]
	v_cvt_pk_bf16_f32 v7, v21, v23
	ds_read2_b32 v[10:11], v97 offset0:16 offset1:24
	v_lshl_add_u64 v[8:9], v[2:3], 0, v[8:9]
	global_store_dwordx4 v[8:9], v[4:7], off nt
	ds_read2_b32 v[8:9], v97 offset0:81 offset1:89
	ds_read2_b32 v[12:13], v97 offset0:146 offset1:154
	ds_read2_b32 v[14:15], v97 offset0:211 offset1:219
	s_waitcnt lgkmcnt(3)
	s_waitcnt lgkmcnt(2)
	ds_read2_b32 v[16:17], v26 offset0:20 offset1:28
	ds_read2_b32 v[18:19], v26 offset0:85 offset1:93
	v_cvt_pk_bf16_f32 v4, v10, v8
	s_waitcnt lgkmcnt(3)
	s_waitcnt lgkmcnt(2)
	ds_read2_b32 v[20:21], v26 offset0:150 offset1:158
	ds_read2_b32 v[22:23], v26 offset0:215 offset1:223
	v_cvt_pk_bf16_f32 v5, v12, v14
	s_waitcnt lgkmcnt(3)
	s_waitcnt lgkmcnt(2)
	v_cvt_pk_bf16_f32 v6, v16, v18
	s_waitcnt lgkmcnt(1)
	v_or_b32_e32 v24, s6, v99
	s_waitcnt lgkmcnt(0)
	v_ashrrev_i32_e32 v25, 31, v24
	v_lshlrev_b64 v[24:25], 12, v[24:25]
	v_cvt_pk_bf16_f32 v7, v20, v22
	v_lshl_add_u64 v[24:25], v[2:3], 0, v[24:25]
	global_store_dwordx4 v[24:25], v[4:7], off nt
	s_nop 1
	v_cvt_pk_bf16_f32 v4, v11, v9
	v_cvt_pk_bf16_f32 v5, v13, v15
	v_cvt_pk_bf16_f32 v6, v17, v19
	v_or_b32_e32 v8, s6, v100
	v_ashrrev_i32_e32 v9, 31, v8
	v_lshlrev_b64 v[8:9], 12, v[8:9]
	v_cvt_pk_bf16_f32 v7, v21, v23
	ds_read2_b32 v[10:11], v97 offset0:32 offset1:40
	v_lshl_add_u64 v[8:9], v[2:3], 0, v[8:9]
	global_store_dwordx4 v[8:9], v[4:7], off nt
	ds_read2_b32 v[8:9], v97 offset0:97 offset1:105
	ds_read2_b32 v[12:13], v97 offset0:162 offset1:170
	ds_read2_b32 v[14:15], v97 offset0:227 offset1:235
	s_waitcnt lgkmcnt(3)
	s_waitcnt lgkmcnt(2)
	ds_read2_b32 v[16:17], v26 offset0:36 offset1:44
	ds_read2_b32 v[18:19], v26 offset0:101 offset1:109
	v_cvt_pk_bf16_f32 v4, v10, v8
	s_waitcnt lgkmcnt(3)
	s_waitcnt lgkmcnt(2)
	ds_read2_b32 v[20:21], v26 offset0:166 offset1:174
	ds_read2_b32 v[22:23], v26 offset0:231 offset1:239
	v_cvt_pk_bf16_f32 v5, v12, v14
	s_waitcnt lgkmcnt(3)
	s_waitcnt lgkmcnt(2)
	v_cvt_pk_bf16_f32 v6, v16, v18
	s_waitcnt lgkmcnt(1)
	v_or_b32_e32 v24, s6, v101
	s_waitcnt lgkmcnt(0)
	v_ashrrev_i32_e32 v25, 31, v24
	v_lshlrev_b64 v[24:25], 12, v[24:25]
	v_cvt_pk_bf16_f32 v7, v20, v22
	v_lshl_add_u64 v[24:25], v[2:3], 0, v[24:25]
	global_store_dwordx4 v[24:25], v[4:7], off nt
	s_nop 1
	v_cvt_pk_bf16_f32 v4, v11, v9
	v_cvt_pk_bf16_f32 v5, v13, v15
	v_cvt_pk_bf16_f32 v6, v17, v19
	v_or_b32_e32 v8, s6, v102
	v_ashrrev_i32_e32 v9, 31, v8
	v_lshlrev_b64 v[8:9], 12, v[8:9]
	v_cvt_pk_bf16_f32 v7, v21, v23
	ds_read2_b32 v[10:11], v97 offset0:48 offset1:56
	v_lshl_add_u64 v[8:9], v[2:3], 0, v[8:9]
	global_store_dwordx4 v[8:9], v[4:7], off nt
	ds_read2_b32 v[8:9], v97 offset0:113 offset1:121
	ds_read2_b32 v[12:13], v97 offset0:178 offset1:186
	ds_read2_b32 v[14:15], v97 offset0:243 offset1:251
	s_waitcnt lgkmcnt(3)
	s_waitcnt lgkmcnt(2)
	ds_read2_b32 v[16:17], v26 offset0:52 offset1:60
	ds_read2_b32 v[18:19], v26 offset0:117 offset1:125
	v_cvt_pk_bf16_f32 v4, v10, v8
	s_waitcnt lgkmcnt(3)
	s_waitcnt lgkmcnt(2)
	ds_read2_b32 v[20:21], v26 offset0:182 offset1:190
	ds_read2_b32 v[22:23], v26 offset0:247 offset1:255
	v_cvt_pk_bf16_f32 v5, v12, v14
	s_waitcnt lgkmcnt(3)
	s_waitcnt lgkmcnt(2)
	v_cvt_pk_bf16_f32 v6, v16, v18
	s_waitcnt lgkmcnt(1)
	v_or_b32_e32 v24, s6, v103
	s_waitcnt lgkmcnt(0)
	v_ashrrev_i32_e32 v25, 31, v24
	v_lshlrev_b64 v[24:25], 12, v[24:25]
	v_cvt_pk_bf16_f32 v7, v20, v22
	v_lshl_add_u64 v[24:25], v[2:3], 0, v[24:25]
	global_store_dwordx4 v[24:25], v[4:7], off nt
	s_nop 1
	v_cvt_pk_bf16_f32 v4, v11, v9
	v_cvt_pk_bf16_f32 v5, v13, v15
	v_cvt_pk_bf16_f32 v6, v17, v19
	v_or_b32_e32 v8, s6, v104
	v_ashrrev_i32_e32 v9, 31, v8
	v_lshlrev_b64 v[8:9], 12, v[8:9]
	v_cvt_pk_bf16_f32 v7, v21, v23
	v_lshl_add_u64 v[2:3], v[2:3], 0, v[8:9]
	global_store_dwordx4 v[2:3], v[4:7], off nt
	s_waitcnt lgkmcnt(0)
	v_readlane_b32 s58, v254, 45
	v_readlane_b32 s59, v254, 46
	v_readlane_b32 s60, v254, 47
	v_readlane_b32 s61, v254, 48
	v_readlane_b32 s62, v254, 49
	v_readlane_b32 s63, v254, 50
	v_readlane_b32 s41, v253, 53
	v_readlane_b32 s42, v253, 54
	v_readlane_b32 s43, v253, 55
	v_readlane_b32 s44, v253, 56
	v_readlane_b32 s45, v253, 57
	v_readlane_b32 s46, v253, 58
	v_readlane_b32 s47, v253, 59
	v_readlane_b32 s56, v254, 43
	v_readlane_b32 s57, v254, 44
	s_branch .LBB0_2331

; __device__ __forceinline__ unsigned pk2(float lo, float hi) { return f2bf(lo) | (f2bf(hi) << 16); }
; __device__ __forceinline__ float dot4(f32x4 a, f32x4 b) { return (a.x * b.x + a.y * b.y) + (a.z * b.z + a.w * b.w); }
; __device__ __forceinline__ void phase_combine(const Args& a, const Ctx& c0, int l, bool last_in) {
;     ...
;         for (int j = 0; j < 4; ++j) { const int idx = (lane + 64 * j) * 8; const u32x4 xw = *(const u32x4*)(XM + (size_t)row * DM + idx);
;             xv[j][0] = (f32x4){bflo(xw.x), bfhi(xw.x), bflo(xw.y), bfhi(xw.y)}; xv[j][1] = (f32x4){bflo(xw.z), bfhi(xw.z), bflo(xw.w), bfhi(xw.w)};
;     ...
;         for (int j = 0; j < 4; ++j) { const int idx = (lane + 64 * j) * 8;
; #pragma unroll
;             for (int hlf = 0; hlf < 2; ++hlf) { xv[j][hlf] = xv[j][hlf] + gv[j][hlf] * acc[j][hlf]; ssn += dot4(xv[j][hlf], xv[j][hlf]); }
;             if (last) { *(f32x4*)(out + (size_t)row * DM + idx) = xv[j][0]; *(f32x4*)(out + (size_t)row * DM + idx + 4) = xv[j][1]; }
;             else { u32x4 w; w.x = pk2(xv[j][0].x, xv[j][0].y); w.y = pk2(xv[j][0].z, xv[j][0].w); w.z = pk2(xv[j][1].x, xv[j][1].y); w.w = pk2(xv[j][1].z, xv[j][1].w); *(u32x4*)(x1o + (size_t)row * DM + idx) = w; } }
.LBB0_2734:
	s_add_u32 s20, s27, s14
	s_addc_u32 s21, s31, s15
	s_lshl_b64 s[2:3], s[10:11], 13
	v_readlane_b32 s44, v254, 21
	v_readlane_b32 s22, v254, 59
	v_lshlrev_b32_e32 v50, 16, v46
	v_and_b32_e32 v51, 0xffff0000, v46
	v_lshlrev_b32_e32 v46, 16, v47
	v_and_b32_e32 v47, 0xffff0000, v47
	v_lshlrev_b32_e32 v52, 16, v48
	v_and_b32_e32 v53, 0xffff0000, v48
	v_lshlrev_b32_e32 v48, 16, v49
	v_and_b32_e32 v49, 0xffff0000, v49
	v_readlane_b32 s45, v254, 22
	s_add_u32 s18, s44, s2
	v_readlane_b32 s23, v254, 60
	s_addc_u32 s19, s45, s3
	v_pk_fma_f32 v[40:41], v[40:41], v[102:103], v[46:47]
	v_pk_fma_f32 v[38:39], v[38:39], v[100:101], v[50:51]
	v_pk_fma_f32 v[36:37], v[36:37], v[98:99], v[48:49]
	v_pk_fma_f32 v[34:35], v[34:35], v[96:97], v[52:53]
	s_mov_b64 s[2:3], -1
	s_and_b64 vcc, exec, s[22:23]
	v_lshlrev_b32_e32 v46, 1, v56
	v_readlane_b32 s46, v254, 23
	v_readlane_b32 s47, v254, 24
	s_cbranch_vccz .LBB0_2736
	v_cvt_pk_bf16_f32 v48, v38, v39
	v_cvt_pk_bf16_f32 v49, v40, v41
	v_cvt_pk_bf16_f32 v50, v34, v35
	v_cvt_pk_bf16_f32 v51, v36, v37
	global_store_dwordx4 v46, v[48:51], s[20:21]
	s_mov_b64 s[2:3], 0

; __device__ __forceinline__ unsigned pk2(float lo, float hi) { return f2bf(lo) | (f2bf(hi) << 16); }
; __device__ __forceinline__ float dot4(f32x4 a, f32x4 b) { return (a.x * b.x + a.y * b.y) + (a.z * b.z + a.w * b.w); }
; __device__ __forceinline__ void phase_combine(const Args& a, const Ctx& c0, int l, bool last_in) {
;     ...
;         for (int j = 0; j < 4; ++j) { const int idx = (lane + 64 * j) * 8; const u32x4 xw = *(const u32x4*)(XM + (size_t)row * DM + idx);
;             xv[j][0] = (f32x4){bflo(xw.x), bfhi(xw.x), bflo(xw.y), bfhi(xw.y)}; xv[j][1] = (f32x4){bflo(xw.z), bfhi(xw.z), bflo(xw.w), bfhi(xw.w)};
;     ...
;         for (int j = 0; j < 4; ++j) { const int idx = (lane + 64 * j) * 8;
; #pragma unroll
;             for (int hlf = 0; hlf < 2; ++hlf) { xv[j][hlf] = xv[j][hlf] + gv[j][hlf] * acc[j][hlf]; ssn += dot4(xv[j][hlf], xv[j][hlf]); }
;             if (last) { *(f32x4*)(out + (size_t)row * DM + idx) = xv[j][0]; *(f32x4*)(out + (size_t)row * DM + idx + 4) = xv[j][1]; }
;             else { u32x4 w; w.x = pk2(xv[j][0].x, xv[j][0].y); w.y = pk2(xv[j][0].z, xv[j][0].w); w.z = pk2(xv[j][1].x, xv[j][1].y); w.w = pk2(xv[j][1].z, xv[j][1].w); *(u32x4*)(x1o + (size_t)row * DM + idx) = w; } }
.LBB0_2738:
	v_readlane_b32 s22, v254, 59
	v_readlane_b32 s23, v254, 60
	v_lshlrev_b32_e32 v48, 16, v42
	v_and_b32_e32 v49, 0xffff0000, v42
	v_lshlrev_b32_e32 v42, 16, v43
	v_and_b32_e32 v43, 0xffff0000, v43
	v_lshlrev_b32_e32 v50, 16, v44
	v_and_b32_e32 v51, 0xffff0000, v44
	v_lshlrev_b32_e32 v44, 16, v45
	v_and_b32_e32 v45, 0xffff0000, v45
	v_cndmask_b32_e64 v1, 0, 1, s[22:23]
	v_pk_fma_f32 v[32:33], v[32:33], v[94:95], v[42:43]
	v_pk_fma_f32 v[30:31], v[30:31], v[92:93], v[48:49]
	v_pk_fma_f32 v[24:25], v[24:25], v[90:91], v[44:45]
	v_pk_fma_f32 v[22:23], v[22:23], v[88:89], v[50:51]
	v_cmp_ne_u32_e64 s[2:3], 1, v1
	s_andn2_b64 vcc, exec, s[22:23]
	s_mov_b64 s[22:23], -1
	s_cbranch_vccnz .LBB0_2740
	v_cvt_pk_bf16_f32 v42, v30, v31
	v_cvt_pk_bf16_f32 v43, v32, v33
	v_cvt_pk_bf16_f32 v44, v22, v23
	v_cvt_pk_bf16_f32 v45, v24, v25
	s_mov_b64 s[22:23], 0
	global_store_dwordx4 v46, v[42:45], s[20:21] offset:1024

; __device__ __forceinline__ unsigned pk2(float lo, float hi) { return f2bf(lo) | (f2bf(hi) << 16); }
; __device__ __forceinline__ float dot4(f32x4 a, f32x4 b) { return (a.x * b.x + a.y * b.y) + (a.z * b.z + a.w * b.w); }
; __device__ __forceinline__ void phase_combine(const Args& a, const Ctx& c0, int l, bool last_in) {
;     ...
;         for (int j = 0; j < 4; ++j) { const int idx = (lane + 64 * j) * 8; const u32x4 xw = *(const u32x4*)(XM + (size_t)row * DM + idx);
;             xv[j][0] = (f32x4){bflo(xw.x), bfhi(xw.x), bflo(xw.y), bfhi(xw.y)}; xv[j][1] = (f32x4){bflo(xw.z), bfhi(xw.z), bflo(xw.w), bfhi(xw.w)};
;     ...
;         for (int j = 0; j < 4; ++j) { const int idx = (lane + 64 * j) * 8;
; #pragma unroll
;             for (int hlf = 0; hlf < 2; ++hlf) { xv[j][hlf] = xv[j][hlf] + gv[j][hlf] * acc[j][hlf]; ssn += dot4(xv[j][hlf], xv[j][hlf]); }
;             if (last) { *(f32x4*)(out + (size_t)row * DM + idx) = xv[j][0]; *(f32x4*)(out + (size_t)row * DM + idx + 4) = xv[j][1]; }
;             else { u32x4 w; w.x = pk2(xv[j][0].x, xv[j][0].y); w.y = pk2(xv[j][0].z, xv[j][0].w); w.z = pk2(xv[j][1].x, xv[j][1].y); w.w = pk2(xv[j][1].z, xv[j][1].w); *(u32x4*)(x1o + (size_t)row * DM + idx) = w; } }
.LBB0_2742:
	v_lshlrev_b32_e32 v42, 16, v26
	v_and_b32_e32 v43, 0xffff0000, v26
	v_lshlrev_b32_e32 v26, 16, v27
	v_and_b32_e32 v27, 0xffff0000, v27
	v_lshlrev_b32_e32 v44, 16, v28
	v_and_b32_e32 v45, 0xffff0000, v28
	v_lshlrev_b32_e32 v28, 16, v29
	v_and_b32_e32 v29, 0xffff0000, v29
	v_pk_fma_f32 v[16:17], v[16:17], v[86:87], v[26:27]
	v_pk_fma_f32 v[14:15], v[14:15], v[84:85], v[42:43]
	v_pk_fma_f32 v[12:13], v[12:13], v[82:83], v[28:29]
	v_pk_fma_f32 v[10:11], v[10:11], v[80:81], v[44:45]
	s_and_b64 vcc, exec, s[2:3]
	s_mov_b64 s[22:23], -1
	s_cbranch_vccnz .LBB0_2744
	v_cvt_pk_bf16_f32 v26, v14, v15
	v_cvt_pk_bf16_f32 v27, v16, v17
	v_cvt_pk_bf16_f32 v28, v10, v11
	v_cvt_pk_bf16_f32 v29, v12, v13
	s_mov_b64 s[22:23], 0
	global_store_dwordx4 v46, v[26:29], s[20:21] offset:2048

; __device__ __forceinline__ unsigned pk2(float lo, float hi) { return f2bf(lo) | (f2bf(hi) << 16); }
; __device__ __forceinline__ float dot4(f32x4 a, f32x4 b) { return (a.x * b.x + a.y * b.y) + (a.z * b.z + a.w * b.w); }
; __device__ __forceinline__ void phase_combine(const Args& a, const Ctx& c0, int l, bool last_in) {
;     ...
;         for (int j = 0; j < 4; ++j) { const int idx = (lane + 64 * j) * 8; const u32x4 xw = *(const u32x4*)(XM + (size_t)row * DM + idx);
;             xv[j][0] = (f32x4){bflo(xw.x), bfhi(xw.x), bflo(xw.y), bfhi(xw.y)}; xv[j][1] = (f32x4){bflo(xw.z), bfhi(xw.z), bflo(xw.w), bfhi(xw.w)};
;     ...
;         for (int j = 0; j < 4; ++j) { const int idx = (lane + 64 * j) * 8;
; #pragma unroll
;             for (int hlf = 0; hlf < 2; ++hlf) { xv[j][hlf] = xv[j][hlf] + gv[j][hlf] * acc[j][hlf]; ssn += dot4(xv[j][hlf], xv[j][hlf]); }
;             if (last) { *(f32x4*)(out + (size_t)row * DM + idx) = xv[j][0]; *(f32x4*)(out + (size_t)row * DM + idx + 4) = xv[j][1]; }
;             else { u32x4 w; w.x = pk2(xv[j][0].x, xv[j][0].y); w.y = pk2(xv[j][0].z, xv[j][0].w); w.z = pk2(xv[j][1].x, xv[j][1].y); w.w = pk2(xv[j][1].z, xv[j][1].w); *(u32x4*)(x1o + (size_t)row * DM + idx) = w; } }
.LBB0_2746:
	v_lshlrev_b32_e32 v26, 16, v18
	v_and_b32_e32 v27, 0xffff0000, v18
	v_lshlrev_b32_e32 v18, 16, v19
	v_and_b32_e32 v19, 0xffff0000, v19
	v_lshlrev_b32_e32 v28, 16, v20
	v_and_b32_e32 v29, 0xffff0000, v20
	v_lshlrev_b32_e32 v20, 16, v21
	v_and_b32_e32 v21, 0xffff0000, v21
	v_pk_fma_f32 v[8:9], v[8:9], v[78:79], v[18:19]
	v_pk_fma_f32 v[6:7], v[6:7], v[76:77], v[26:27]
	v_pk_fma_f32 v[4:5], v[4:5], v[74:75], v[20:21]
	v_pk_fma_f32 v[2:3], v[2:3], v[72:73], v[28:29]
	s_and_b64 vcc, exec, s[2:3]
	s_mov_b64 s[22:23], -1
	s_cbranch_vccnz .LBB0_2749
	v_cvt_pk_bf16_f32 v18, v6, v7
	v_cvt_pk_bf16_f32 v19, v8, v9
	v_cvt_pk_bf16_f32 v20, v2, v3
	v_cvt_pk_bf16_f32 v21, v4, v5
	global_store_dwordx4 v46, v[18:21], s[20:21] offset:3072
	s_cbranch_execz .LBB0_2750

; __device__ __forceinline__ void phase_combine(const Args& a, const Ctx& c0, int l, bool last_in) {
;     ...
;         if (!last) {
;             const float* mv1 = modv + (size_t)5 * NMODW + (size_t)mb * NMODW; const float* g1n = INP(6) + (size_t)(l + 1) * DM;
;             const float rstd = rsqrtf(wave_sum(ssn) * (1.f / DM) + EPS); bf16* hrow = WSP(bf16, WS_H) + (size_t)row * DM;
; #pragma unroll
;             for (int j = 0; j < 4; ++j) { const int idx = (lane + 64 * j) * 8; u32x4 w;
; #pragma unroll
;                 for (int hlf = 0; hlf < 2; ++hlf) { const int ix = idx + hlf * 4; const f32x4 gsv = *(const f32x4*)(g1n + ix) * (1.f + *(const f32x4*)(mv1 + DM + ix)), shv = *(const f32x4*)(mv1 + ix);
.LBB0_2751:
	v_mul_f32_e32 v1, v39, v39
	v_mul_f32_e32 v18, v41, v41
	v_fmac_f32_e32 v1, v38, v38
	v_fmac_f32_e32 v18, v40, v40
	v_add_f32_e32 v1, v1, v18
	v_mul_f32_e32 v18, v35, v35
	v_mul_f32_e32 v19, v37, v37
	v_fmac_f32_e32 v18, v34, v34
	v_fmac_f32_e32 v19, v36, v36
	v_add_f32_e32 v18, v18, v19
	v_add_f32_e32 v1, v18, v1
	v_mul_f32_e32 v18, v31, v31
	v_mul_f32_e32 v19, v33, v33
	v_fmac_f32_e32 v18, v30, v30
	v_fmac_f32_e32 v19, v32, v32
	v_add_f32_e32 v18, v18, v19
	v_add_f32_e32 v1, v18, v1
	v_mul_f32_e32 v18, v23, v23
	v_mul_f32_e32 v19, v25, v25
	v_fmac_f32_e32 v18, v22, v22
	v_fmac_f32_e32 v19, v24, v24
	v_add_f32_e32 v18, v18, v19
	v_add_f32_e32 v1, v18, v1
	v_mul_f32_e32 v18, v15, v15
	v_mul_f32_e32 v19, v17, v17
	v_fmac_f32_e32 v18, v14, v14
	v_fmac_f32_e32 v19, v16, v16
	v_add_f32_e32 v18, v18, v19
	v_add_f32_e32 v1, v18, v1
	v_mul_f32_e32 v18, v11, v11
	v_mul_f32_e32 v19, v13, v13
	v_fmac_f32_e32 v18, v10, v10
	v_fmac_f32_e32 v19, v12, v12
	v_add_f32_e32 v18, v18, v19
	v_add_f32_e32 v1, v18, v1
	v_mul_f32_e32 v18, v7, v7
	v_mul_f32_e32 v19, v9, v9
	v_fmac_f32_e32 v18, v6, v6
	v_fmac_f32_e32 v19, v8, v8
	v_add_f32_e32 v18, v18, v19
	v_add_f32_e32 v1, v18, v1
	v_mul_f32_e32 v18, v3, v3
	v_mul_f32_e32 v19, v5, v5
	v_fmac_f32_e32 v18, v2, v2
	v_fmac_f32_e32 v19, v4, v4
	v_add_f32_e32 v18, v18, v19
	v_add_f32_e32 v1, v18, v1
	v_xor_b32_e32 v18, 1, v210
	v_cmp_lt_i32_e32 vcc, v18, v215
	s_add_u32 s2, s36, s16
	s_addc_u32 s3, s40, s17
	v_cndmask_b32_e32 v18, v210, v18, vcc
	v_lshlrev_b32_e32 v18, 2, v18
	ds_bpermute_b32 v18, v18, v1
	s_add_u32 s16, s2, 0x2000
	s_addc_u32 s17, s3, 0
	s_waitcnt lgkmcnt(0)
	v_add_f32_e32 v1, v1, v18
	v_xor_b32_e32 v18, 2, v210
	v_cmp_lt_i32_e32 vcc, v18, v215
	s_nop 1
	v_cndmask_b32_e32 v18, v210, v18, vcc
	v_lshlrev_b32_e32 v18, 2, v18
	ds_bpermute_b32 v18, v18, v1
	s_waitcnt lgkmcnt(0)
	v_add_f32_e32 v1, v1, v18
	v_xor_b32_e32 v18, 4, v210
	v_cmp_lt_i32_e32 vcc, v18, v215
	s_nop 1
	v_cndmask_b32_e32 v18, v210, v18, vcc
	v_lshlrev_b32_e32 v18, 2, v18
	ds_bpermute_b32 v18, v18, v1
	s_waitcnt lgkmcnt(0)
	v_add_f32_e32 v1, v1, v18
	v_xor_b32_e32 v18, 8, v210
	v_cmp_lt_i32_e32 vcc, v18, v215
	s_nop 1
	v_cndmask_b32_e32 v18, v210, v18, vcc
	v_lshlrev_b32_e32 v18, 2, v18
	ds_bpermute_b32 v18, v18, v1
	v_cmp_lt_i32_e32 vcc, v220, v215
	s_waitcnt lgkmcnt(0)
	v_add_f32_e32 v1, v1, v18
	v_cndmask_b32_e32 v18, v210, v220, vcc
	v_lshlrev_b32_e32 v18, 2, v18
	ds_bpermute_b32 v18, v18, v1
	v_cmp_lt_i32_e32 vcc, v221, v215
	s_waitcnt lgkmcnt(0)
	v_add_f32_e32 v1, v1, v18
	v_cndmask_b32_e32 v18, v210, v221, vcc
	v_lshlrev_b32_e32 v18, 2, v18
	ds_bpermute_b32 v18, v18, v1
	s_waitcnt lgkmcnt(0)
	v_add_f32_e32 v1, v1, v18
	v_fmamk_f32 v1, v1, 0x3a000000, v180
	v_cmp_gt_f32_e32 vcc, s79, v1
	v_mul_f32_e32 v18, 0x4b800000, v1
	s_nop 0
	v_cndmask_b32_e32 v1, v1, v18, vcc
	v_rsq_f32_e32 v1, v1
	s_nop 0
	v_mul_f32_e32 v18, 0x45800000, v1
	v_cndmask_b32_e32 v72, v1, v18, vcc
	global_load_dwordx4 v[18:21], v57, s[2:3] offset:16
	global_load_dwordx4 v[46:49], v57, s[2:3]
	global_load_dwordx4 v[26:29], v[60:61], off offset:16
	global_load_dwordx4 v[50:53], v[60:61], off
	global_load_dwordx4 v[42:45], v57, s[16:17] offset:16
	global_load_dwordx4 v[74:77], v57, s[16:17]
	v_pk_mul_f32 v[38:39], v[38:39], v[72:73] op_sel_hi:[1,0]
	v_pk_mul_f32 v[40:41], v[40:41], v[72:73] op_sel_hi:[1,0]
	v_pk_mul_f32 v[34:35], v[34:35], v[72:73] op_sel_hi:[1,0]
	v_pk_mul_f32 v[36:37], v[36:37], v[72:73] op_sel_hi:[1,0]
	v_pk_mul_f32 v[30:31], v[30:31], v[72:73] op_sel_hi:[1,0]
	v_pk_mul_f32 v[32:33], v[32:33], v[72:73] op_sel_hi:[1,0]
	v_pk_mul_f32 v[22:23], v[22:23], v[72:73] op_sel_hi:[1,0]
	v_pk_mul_f32 v[24:25], v[24:25], v[72:73] op_sel_hi:[1,0]
	v_pk_mul_f32 v[14:15], v[14:15], v[72:73] op_sel_hi:[1,0]
	v_pk_mul_f32 v[16:17], v[16:17], v[72:73] op_sel_hi:[1,0]
	v_pk_mul_f32 v[10:11], v[10:11], v[72:73] op_sel_hi:[1,0]
	v_pk_mul_f32 v[12:13], v[12:13], v[72:73] op_sel_hi:[1,0]
	v_pk_mul_f32 v[6:7], v[6:7], v[72:73] op_sel_hi:[1,0]
	v_pk_mul_f32 v[8:9], v[8:9], v[72:73] op_sel_hi:[1,0]
	v_pk_mul_f32 v[2:3], v[2:3], v[72:73] op_sel_hi:[1,0]
	v_pk_mul_f32 v[4:5], v[4:5], v[72:73] op_sel_hi:[1,0]
	s_waitcnt vmcnt(1)
	v_pk_add_f32 v[42:43], v[42:43], 1.0 op_sel_hi:[1,0]
	s_waitcnt vmcnt(0)
; __device__ __forceinline__ unsigned pk2(float lo, float hi) { return f2bf(lo) | (f2bf(hi) << 16); }
; __device__ __forceinline__ void phase_combine(const Args& a, const Ctx& c0, int l, bool last_in) {
;     ...
;             const float* mv1 = modv + (size_t)5 * NMODW + (size_t)mb * NMODW; const float* g1n = INP(6) + (size_t)(l + 1) * DM;
;             const float rstd = rsqrtf(wave_sum(ssn) * (1.f / DM) + EPS); bf16* hrow = WSP(bf16, WS_H) + (size_t)row * DM;
; #pragma unroll
;             for (int j = 0; j < 4; ++j) { const int idx = (lane + 64 * j) * 8; u32x4 w;
; #pragma unroll
;                 for (int hlf = 0; hlf < 2; ++hlf) { const int ix = idx + hlf * 4; const f32x4 gsv = *(const f32x4*)(g1n + ix) * (1.f + *(const f32x4*)(mv1 + DM + ix)), shv = *(const f32x4*)(mv1 + ix);
;                     const f32x4 o = (xv[j][hlf] * rstd) * gsv + shv;
;                     if (hlf == 0) { w.x = pk2(o.x, o.y); w.y = pk2(o.z, o.w); } else { w.z = pk2(o.x, o.y); w.w = pk2(o.z, o.w); } }
;                 *(u32x4*)(hrow + idx) = w; } }
	v_pk_add_f32 v[74:75], v[74:75], 1.0 op_sel_hi:[1,0]
	v_pk_add_f32 v[76:77], v[76:77], 1.0 op_sel_hi:[1,0]
	v_pk_mul_f32 v[50:51], v[50:51], v[74:75]
	v_pk_mul_f32 v[52:53], v[52:53], v[76:77]
	v_pk_fma_f32 v[38:39], v[50:51], v[38:39], v[46:47]
	v_pk_fma_f32 v[40:41], v[52:53], v[40:41], v[48:49]
	v_bfe_u32 v1, v38, 16, 1
	v_add3_u32 v1, v38, v1, s37
	v_bfe_u32 v38, v39, 16, 1
	v_lshrrev_b32_e32 v1, 16, v1
	v_add3_u32 v38, v39, v38, s37
	v_and_or_b32 v38, v38, s33, v1
	v_pk_mul_f32 v[26:27], v[26:27], v[42:43]
	v_pk_fma_f32 v[18:19], v[26:27], v[34:35], v[18:19]
	v_cvt_pk_bf16_f32 v39, v40, v41
	v_bfe_u32 v1, v19, 16, 1
	v_pk_add_f32 v[40:41], v[44:45], 1.0 op_sel_hi:[1,0]
	v_add3_u32 v1, v19, v1, s37
	v_bfe_u32 v19, v18, 16, 1
	v_pk_mul_f32 v[28:29], v[28:29], v[40:41]
	v_add3_u32 v18, v18, v19, s37
	v_pk_fma_f32 v[20:21], v[28:29], v[36:37], v[20:21]
	v_lshrrev_b32_e32 v18, 16, v18
	v_and_or_b32 v40, v1, s33, v18
	v_cvt_pk_bf16_f32 v41, v20, v21
	v_lshl_add_u64 v[18:19], v[70:71], 0, s[14:15]
	global_store_dwordx4 v[18:19], v[38:41], off
	global_load_dwordx4 v[26:29], v57, s[2:3] offset:2064
	global_load_dwordx4 v[34:37], v57, s[2:3] offset:2048
	s_nop 0
	global_load_dwordx4 v[38:41], v[62:63], off offset:16
	global_load_dwordx4 v[42:45], v[62:63], off
	global_load_dwordx4 v[46:49], v104, s[16:17] offset:16
	global_load_dwordx4 v[50:53], v104, s[16:17]
	s_waitcnt vmcnt(0)
	v_pk_add_f32 v[20:21], v[52:53], 1.0 op_sel_hi:[1,0]
	v_pk_add_f32 v[50:51], v[50:51], 1.0 op_sel_hi:[1,0]
	v_pk_mul_f32 v[20:21], v[44:45], v[20:21]
	v_pk_mul_f32 v[42:43], v[42:43], v[50:51]
	v_pk_fma_f32 v[32:33], v[20:21], v[32:33], v[36:37]
	v_pk_fma_f32 v[20:21], v[42:43], v[30:31], v[34:35]
	v_pk_add_f32 v[30:31], v[48:49], 1.0 op_sel_hi:[1,0]
	v_bfe_u32 v1, v20, 16, 1
	v_add3_u32 v1, v20, v1, s37
	v_bfe_u32 v20, v21, 16, 1
	v_lshrrev_b32_e32 v1, 16, v1
	v_add3_u32 v20, v21, v20, s37
	v_and_or_b32 v20, v20, s33, v1
	v_bfe_u32 v1, v32, 16, 1
	v_bfe_u32 v21, v33, 16, 1
	v_add3_u32 v1, v32, v1, s37
	v_add3_u32 v21, v33, v21, s37
	v_pk_add_f32 v[32:33], v[46:47], 1.0 op_sel_hi:[1,0]
	v_lshrrev_b32_e32 v1, 16, v1
	v_pk_mul_f32 v[32:33], v[38:39], v[32:33]
	v_and_or_b32 v21, v21, s33, v1
	v_pk_fma_f32 v[22:23], v[22:23], v[32:33], v[26:27]
	v_pk_mul_f32 v[30:31], v[40:41], v[30:31]
	v_bfe_u32 v1, v23, 16, 1
	v_add3_u32 v1, v23, v1, s37
	v_bfe_u32 v23, v22, 16, 1
	v_pk_fma_f32 v[24:25], v[24:25], v[30:31], v[28:29]
	v_add3_u32 v22, v22, v23, s37
	v_lshrrev_b32_e32 v22, 16, v22
	v_and_or_b32 v22, v1, s33, v22
	v_cvt_pk_bf16_f32 v23, v24, v25
	global_store_dwordx4 v[18:19], v[20:23], off offset:1024
	global_load_dwordx4 v[20:23], v105, s[2:3] offset:16
	s_nop 0
	global_load_dwordx4 v[24:27], v105, s[2:3]
	global_load_dwordx4 v[28:31], v[64:65], off offset:16
	global_load_dwordx4 v[32:35], v[64:65], off
	global_load_dwordx4 v[36:39], v105, s[16:17] offset:16
	global_load_dwordx4 v[40:43], v105, s[16:17]
	s_waitcnt vmcnt(0)
	v_pk_add_f32 v[40:41], v[40:41], 1.0 op_sel_hi:[1,0]
	s_nop 0
	v_pk_mul_f32 v[32:33], v[32:33], v[40:41]
	v_pk_add_f32 v[42:43], v[42:43], 1.0 op_sel_hi:[1,0]
	v_pk_fma_f32 v[14:15], v[14:15], v[32:33], v[24:25]
	v_pk_mul_f32 v[34:35], v[34:35], v[42:43]
	v_bfe_u32 v1, v14, 16, 1
	v_add3_u32 v1, v14, v1, s37
	v_bfe_u32 v14, v15, 16, 1
	v_pk_fma_f32 v[16:17], v[16:17], v[34:35], v[26:27]
	v_lshrrev_b32_e32 v1, 16, v1
	v_add3_u32 v14, v15, v14, s37
	v_and_or_b32 v14, v14, s33, v1
	v_pk_add_f32 v[24:25], v[36:37], 1.0 op_sel_hi:[1,0]
	v_pk_mul_f32 v[24:25], v[28:29], v[24:25]
	v_pk_fma_f32 v[10:11], v[10:11], v[24:25], v[20:21]
	v_cvt_pk_bf16_f32 v15, v16, v17
	v_bfe_u32 v1, v11, 16, 1
	v_pk_add_f32 v[16:17], v[38:39], 1.0 op_sel_hi:[1,0]
	v_add3_u32 v1, v11, v1, s37
	v_bfe_u32 v11, v10, 16, 1
	v_pk_mul_f32 v[16:17], v[30:31], v[16:17]
	v_add3_u32 v10, v10, v11, s37
	v_pk_fma_f32 v[12:13], v[12:13], v[16:17], v[22:23]
	v_lshrrev_b32_e32 v10, 16, v10
	v_and_or_b32 v16, v1, s33, v10
	v_cvt_pk_bf16_f32 v17, v12, v13
	global_store_dwordx4 v[18:19], v[14:17], off offset:2048
	global_load_dwordx4 v[10:13], v106, s[2:3] offset:16
	s_nop 0
	global_load_dwordx4 v[14:17], v106, s[2:3]
	global_load_dwordx4 v[20:23], v[66:67], off offset:16
	global_load_dwordx4 v[24:27], v[66:67], off
	global_load_dwordx4 v[28:31], v106, s[16:17] offset:16
	global_load_dwordx4 v[32:35], v106, s[16:17]
	s_waitcnt vmcnt(0)
	v_pk_add_f32 v[32:33], v[32:33], 1.0 op_sel_hi:[1,0]
	s_nop 0
	v_pk_mul_f32 v[24:25], v[24:25], v[32:33]
	v_pk_add_f32 v[34:35], v[34:35], 1.0 op_sel_hi:[1,0]
	v_pk_fma_f32 v[6:7], v[6:7], v[24:25], v[14:15]
	v_pk_mul_f32 v[26:27], v[26:27], v[34:35]
	v_bfe_u32 v1, v6, 16, 1
	v_add3_u32 v1, v6, v1, s37
	v_bfe_u32 v6, v7, 16, 1
	v_pk_fma_f32 v[8:9], v[8:9], v[26:27], v[16:17]
	v_lshrrev_b32_e32 v1, 16, v1
	v_add3_u32 v6, v7, v6, s37
	v_and_or_b32 v6, v6, s33, v1
	v_pk_add_f32 v[14:15], v[28:29], 1.0 op_sel_hi:[1,0]
	v_pk_mul_f32 v[14:15], v[20:21], v[14:15]
	v_pk_fma_f32 v[2:3], v[2:3], v[14:15], v[10:11]
	v_cvt_pk_bf16_f32 v7, v8, v9
	v_bfe_u32 v1, v3, 16, 1
	v_pk_add_f32 v[8:9], v[30:31], 1.0 op_sel_hi:[1,0]
	v_add3_u32 v1, v3, v1, s37
	v_bfe_u32 v3, v2, 16, 1
	v_pk_mul_f32 v[8:9], v[22:23], v[8:9]
	v_add3_u32 v2, v2, v3, s37
	v_pk_fma_f32 v[4:5], v[4:5], v[8:9], v[12:13]
	v_lshrrev_b32_e32 v2, 16, v2
	v_and_or_b32 v8, v1, s33, v2
	v_cvt_pk_bf16_f32 v9, v4, v5
	global_store_dwordx4 v[18:19], v[6:9], off offset:3072
	s_branch .LBB0_2727

; #define LAS __attribute__((address_space(3)))
; #define WSW(T, off, l) WSP(T, WS_WSET + (size_t)(l) * WSET_STRIDE + (off))
; __device__ __forceinline__ void tr_item(const float* W, int ldw, int k0, int n0, bf16* WT, int ldt, int drow0, LAS float* scr, int lane, const float* kscale = nullptr) {
;     const float* src = W + (size_t)(k0 + (lane >> 4)) * ldw + n0 + (lane & 15) * 4;
;     f32x4 v[16];
; #pragma unroll
;     for (int i = 0; i < 16; ++i) v[i] = __builtin_nontemporal_load((const f32x4*)(src + (size_t)(4 * i) * ldw));
;     LAS float* wp = scr + (lane >> 4) * 65 + (lane & 15) * 4;
; #pragma unroll
;     for (int i = 0; i < 16; ++i) { LAS float* q = wp + (4 * i) * 65; const float ks = kscale ? kscale[k0 + 4 * i + (lane >> 4)] : 1.f; q[0] = v[i].x * ks; q[1] = v[i].y * ks; q[2] = v[i].z * ks; q[3] = v[i].w * ks; }
; __device__ __forceinline__ void convert_tile(const Args& a, GAS unsigned char* wsb, int l, int t, LAS float* scr, int lane) {
;     ...
;     if (r < I_OUT) { const int kb = r / 32, nb = r - kb * 32; tr_item(INP(21) + (size_t)l * DM * DM, DM, kb * 64, nb * 64, WSW(bf16, W_OUT, l), DM, nb * 64, scr, lane); return; }
.LBB0_2782:
	s_andn2_b64 vcc, exec, s[8:9]
	s_cbranch_vccnz .LBB0_2784
	s_lshl_b32 s8, s18, 1
	s_and_b32 s8, s8, 0x1fc0
	s_addk_i32 s8, 0xf240
	s_lshl_b32 s9, s18, 6
	v_or_b32_e32 v2, s8, v67
	v_mov_b32_e32 v3, v147
	v_readlane_b32 s14, v252, 60
	s_and_b32 s10, s9, 0x7c0
	v_lshlrev_b64 v[2:3], 13, v[2:3]
	v_readlane_b32 s15, v252, 61
	s_lshl_b32 s12, s10, 2
	v_lshlrev_b32_e32 v4, 2, v66
	v_lshl_add_u64 v[2:3], s[14:15], 0, v[2:3]
	v_lshl_add_u64 v[2:3], v[2:3], 0, s[12:13]
	v_mov_b32_e32 v5, v147
	v_lshl_add_u64 v[62:63], v[2:3], 0, v[4:5]
	v_add_co_u32_e32 v6, vcc, s83, v62
	s_mov_b32 s9, 0x20000
	s_nop 0
	v_addc_co_u32_e32 v7, vcc, 0, v63, vcc
	v_add_co_u32_e32 v10, vcc, s81, v62
	global_load_dwordx4 v[2:5], v[62:63], off nt
	s_nop 0
	global_load_dwordx4 v[6:9], v[6:7], off nt
	v_addc_co_u32_e32 v11, vcc, 0, v63, vcc
	v_add_co_u32_e32 v14, vcc, s82, v62
	v_add_u32_e32 v1, 0x410, v95
	s_nop 0
	v_addc_co_u32_e32 v15, vcc, 0, v63, vcc
	global_load_dwordx4 v[10:13], v[10:11], off nt
	s_nop 0
	global_load_dwordx4 v[14:17], v[14:15], off nt
	v_add_co_u32_e32 v18, vcc, s9, v62
	s_mov_b32 s9, 0x28000
	s_nop 0
	v_addc_co_u32_e32 v19, vcc, 0, v63, vcc
	v_add_co_u32_e32 v22, vcc, s9, v62
	s_mov_b32 s9, 0x30000
	s_nop 0
	v_addc_co_u32_e32 v23, vcc, 0, v63, vcc
	global_load_dwordx4 v[18:21], v[18:19], off nt
	s_nop 0
	global_load_dwordx4 v[22:25], v[22:23], off nt
	v_add_co_u32_e32 v26, vcc, s9, v62
	s_mov_b32 s9, 0x38000
	s_nop 0
	v_addc_co_u32_e32 v27, vcc, 0, v63, vcc
	v_add_co_u32_e32 v30, vcc, s9, v62
	s_mov_b32 s9, 0x40000
	s_nop 0
	v_addc_co_u32_e32 v31, vcc, 0, v63, vcc
	global_load_dwordx4 v[26:29], v[26:27], off nt
	s_nop 0
	global_load_dwordx4 v[30:33], v[30:31], off nt
	v_add_co_u32_e32 v34, vcc, s9, v62
	s_mov_b32 s9, 0x48000
	s_nop 0
	v_addc_co_u32_e32 v35, vcc, 0, v63, vcc
	v_add_co_u32_e32 v38, vcc, s9, v62
	s_mov_b32 s9, 0x50000
	s_nop 0
	v_addc_co_u32_e32 v39, vcc, 0, v63, vcc
	global_load_dwordx4 v[34:37], v[34:35], off nt
	s_nop 0
	global_load_dwordx4 v[38:41], v[38:39], off nt
	v_add_co_u32_e32 v42, vcc, s9, v62
	s_mov_b32 s9, 0x58000
	s_nop 0
	v_addc_co_u32_e32 v43, vcc, 0, v63, vcc
	v_add_co_u32_e32 v46, vcc, s9, v62
	s_mov_b32 s9, 0x60000
	s_nop 0
	v_addc_co_u32_e32 v47, vcc, 0, v63, vcc
	global_load_dwordx4 v[42:45], v[42:43], off nt
	s_nop 0
	global_load_dwordx4 v[46:49], v[46:47], off nt
	v_add_co_u32_e32 v50, vcc, s9, v62
	s_mov_b32 s9, 0x68000
	s_nop 0
	v_addc_co_u32_e32 v51, vcc, 0, v63, vcc
	v_add_co_u32_e32 v54, vcc, s9, v62
	s_mov_b32 s9, 0x70000
	s_nop 0
	v_addc_co_u32_e32 v55, vcc, 0, v63, vcc
	global_load_dwordx4 v[50:53], v[50:51], off nt
	s_nop 0
	global_load_dwordx4 v[54:57], v[54:55], off nt
	v_add_co_u32_e32 v58, vcc, s9, v62
	s_mov_b32 s9, 0x78000
	s_nop 0
	v_addc_co_u32_e32 v59, vcc, 0, v63, vcc
	global_load_dwordx4 v[58:61], v[58:59], off nt
	v_add_co_u32_e32 v62, vcc, s9, v62
	s_mov_b32 s9, s13
	s_nop 0
	v_addc_co_u32_e32 v63, vcc, 0, v63, vcc
	global_load_dwordx4 v[62:65], v[62:63], off nt
	s_waitcnt vmcnt(15)
	ds_write2_b32 v95, v2, v3 offset1:1
	ds_write2_b32 v95, v4, v5 offset0:2 offset1:3
	s_waitcnt vmcnt(14)
	ds_write2_b32 v1, v6, v7 offset1:1
	v_add_u32_e32 v1, 0x418, v95
	ds_write2_b32 v1, v8, v9 offset1:1
	v_add_u32_e32 v1, 0x820, v95
	v_lshl_add_u64 v[2:3], s[8:9], 1, v[72:73]
	s_waitcnt vmcnt(13)
	ds_write2_b32 v1, v10, v11 offset1:1
	v_add_u32_e32 v1, 0x828, v95
	ds_write2_b32 v1, v12, v13 offset1:1
	v_add_u32_e32 v1, 0xc30, v95
	s_waitcnt vmcnt(12)
	ds_write2_b32 v1, v14, v15 offset1:1
	v_add_u32_e32 v1, 0xc38, v95
	ds_write2_b32 v1, v16, v17 offset1:1
	v_add_u32_e32 v1, 0x1040, v95
	s_waitcnt vmcnt(11)
	ds_write2_b32 v1, v18, v19 offset1:1
	v_add_u32_e32 v1, 0x1048, v95
	ds_write2_b32 v1, v20, v21 offset1:1
	v_add_u32_e32 v1, 0x1450, v95
	s_waitcnt vmcnt(10)
	ds_write2_b32 v1, v22, v23 offset1:1
	v_add_u32_e32 v1, 0x1458, v95
	ds_write2_b32 v1, v24, v25 offset1:1
	v_add_u32_e32 v1, 0x1860, v95
	v_mov_b32_e32 v25, v147
	s_waitcnt vmcnt(9)
	ds_write2_b32 v1, v26, v27 offset1:1
	v_add_u32_e32 v1, 0x1868, v95
	ds_write2_b32 v1, v28, v29 offset1:1
	v_add_u32_e32 v1, 0x1c70, v95
	s_waitcnt vmcnt(8)
	ds_write2_b32 v1, v30, v31 offset1:1
	v_add_u32_e32 v1, 0x1c78, v95
	ds_write2_b32 v1, v32, v33 offset1:1
	v_add_u32_e32 v1, 0x2080, v95
	v_add_u32_e32 v26, 0x400, v97
	s_waitcnt vmcnt(7)
	ds_write2_b32 v1, v34, v35 offset1:1
	v_add_u32_e32 v1, 0x2088, v95
	ds_write2_b32 v1, v36, v37 offset1:1
	v_add_u32_e32 v1, 0x2490, v95
	s_waitcnt vmcnt(6)
	ds_write2_b32 v1, v38, v39 offset1:1
	v_add_u32_e32 v1, 0x2498, v95
	ds_write2_b32 v1, v40, v41 offset1:1
	v_add_u32_e32 v1, 0x28a0, v95
	s_waitcnt vmcnt(5)
	ds_write2_b32 v1, v42, v43 offset1:1
	v_add_u32_e32 v1, 0x28a8, v95
	ds_write2_b32 v1, v44, v45 offset1:1
	v_add_u32_e32 v1, 0x2cb0, v95
	s_waitcnt vmcnt(4)
	ds_write2_b32 v1, v46, v47 offset1:1
	v_add_u32_e32 v1, 0x2cb8, v95
	ds_write2_b32 v1, v48, v49 offset1:1
	v_add_u32_e32 v1, 0x30c0, v95
	s_waitcnt vmcnt(3)
	ds_write2_b32 v1, v50, v51 offset1:1
	v_add_u32_e32 v1, 0x30c8, v95
	ds_write2_b32 v1, v52, v53 offset1:1
	v_add_u32_e32 v1, 0x34d0, v95
	s_waitcnt vmcnt(2)
; #define LAS __attribute__((address_space(3)))
; __device__ __forceinline__ unsigned pk2(float lo, float hi) { return f2bf(lo) | (f2bf(hi) << 16); }
; __device__ __forceinline__ void tr_item(const float* W, int ldw, int k0, int n0, bf16* WT, int ldt, int drow0, LAS float* scr, int lane, const float* kscale = nullptr) {
;     ...
;     for (int i = 0; i < 16; ++i) { LAS float* q = wp + (4 * i) * 65; const float ks = kscale ? kscale[k0 + 4 * i + (lane >> 4)] : 1.f; q[0] = v[i].x * ks; q[1] = v[i].y * ks; q[2] = v[i].z * ks; q[3] = v[i].w * ks; }
;     asm volatile("s_waitcnt lgkmcnt(0)" ::: "memory");
;     const int kc = lane & 7;
; #pragma unroll
;     for (int j = 0; j < 8; ++j) { const int n = (lane >> 3) + 8 * j; const LAS float* sp = scr + (8 * kc) * 65 + n;
;         u32x4 o; o.x = pk2(sp[0 * 65], sp[1 * 65]); o.y = pk2(sp[2 * 65], sp[3 * 65]); o.z = pk2(sp[4 * 65], sp[5 * 65]); o.w = pk2(sp[6 * 65], sp[7 * 65]);
;         __builtin_nontemporal_store(o, (u32x4*)(WT + (size_t)(drow0 + n) * ldt + k0 + 8 * kc)); }
;     asm volatile("s_waitcnt lgkmcnt(0)" ::: "memory");
	ds_write2_b32 v1, v54, v55 offset1:1
	v_add_u32_e32 v1, 0x34d8, v95
	ds_write2_b32 v1, v56, v57 offset1:1
	v_add_u32_e32 v1, 0x38e0, v95
	s_waitcnt vmcnt(1)
	ds_write2_b32 v1, v58, v59 offset1:1
	v_add_u32_e32 v1, 0x38e8, v95
	ds_write2_b32 v1, v60, v61 offset1:1
	v_add_u32_e32 v1, 0x3cf0, v95
	s_waitcnt vmcnt(0)
	ds_write2_b32 v1, v62, v63 offset1:1
	v_add_u32_e32 v1, 0x3cf8, v95
	ds_write2_b32 v1, v64, v65 offset1:1
	s_waitcnt lgkmcnt(0)
	ds_read2_b32 v[8:9], v97 offset1:8
	ds_read2_b32 v[10:11], v97 offset0:65 offset1:73
	ds_read2_b32 v[12:13], v97 offset0:130 offset1:138
	ds_read2_b32 v[14:15], v97 offset0:195 offset1:203
	ds_read2_b32 v[16:17], v26 offset0:4 offset1:12
	s_waitcnt lgkmcnt(4)
	s_waitcnt lgkmcnt(3)
	ds_read2_b32 v[18:19], v26 offset0:69 offset1:77
	v_cvt_pk_bf16_f32 v4, v8, v10
	s_waitcnt lgkmcnt(3)
	s_waitcnt lgkmcnt(2)
	ds_read2_b32 v[20:21], v26 offset0:134 offset1:142
	ds_read2_b32 v[22:23], v26 offset0:199 offset1:207
	v_cvt_pk_bf16_f32 v5, v12, v14
	s_waitcnt lgkmcnt(3)
	s_waitcnt lgkmcnt(2)
	v_cvt_pk_bf16_f32 v6, v16, v18
	s_waitcnt lgkmcnt(1)
	s_waitcnt lgkmcnt(0)
	v_cvt_pk_bf16_f32 v7, v20, v22
	v_or_b32_e32 v1, s10, v96
	v_lshlrev_b32_e32 v24, 12, v1
	v_lshl_add_u64 v[24:25], v[2:3], 0, v[24:25]
	global_store_dwordx4 v[24:25], v[4:7], off nt
	s_nop 1
	v_cvt_pk_bf16_f32 v4, v9, v11
	v_cvt_pk_bf16_f32 v5, v13, v15
	v_cvt_pk_bf16_f32 v6, v17, v19
	v_cvt_pk_bf16_f32 v7, v21, v23
	v_or_b32_e32 v1, s10, v98
	v_lshlrev_b32_e32 v8, 12, v1
	v_mov_b32_e32 v9, v147
	ds_read2_b32 v[10:11], v97 offset0:16 offset1:24
	v_lshl_add_u64 v[8:9], v[2:3], 0, v[8:9]
	global_store_dwordx4 v[8:9], v[4:7], off nt
	ds_read2_b32 v[8:9], v97 offset0:81 offset1:89
	ds_read2_b32 v[12:13], v97 offset0:146 offset1:154
	ds_read2_b32 v[14:15], v97 offset0:211 offset1:219
	s_waitcnt lgkmcnt(3)
	s_waitcnt lgkmcnt(2)
	ds_read2_b32 v[16:17], v26 offset0:20 offset1:28
	ds_read2_b32 v[18:19], v26 offset0:85 offset1:93
	v_cvt_pk_bf16_f32 v4, v10, v8
	s_waitcnt lgkmcnt(3)
	s_waitcnt lgkmcnt(2)
	ds_read2_b32 v[20:21], v26 offset0:150 offset1:158
	ds_read2_b32 v[22:23], v26 offset0:215 offset1:223
	v_cvt_pk_bf16_f32 v5, v12, v14
	s_waitcnt lgkmcnt(3)
	s_waitcnt lgkmcnt(2)
	v_cvt_pk_bf16_f32 v6, v16, v18
	s_waitcnt lgkmcnt(1)
	s_waitcnt lgkmcnt(0)
	v_cvt_pk_bf16_f32 v7, v20, v22
	v_or_b32_e32 v1, s10, v99
	v_lshlrev_b32_e32 v24, 12, v1
	v_mov_b32_e32 v25, v147
	v_lshl_add_u64 v[24:25], v[2:3], 0, v[24:25]
	global_store_dwordx4 v[24:25], v[4:7], off nt
	s_nop 1
	v_cvt_pk_bf16_f32 v4, v11, v9
	v_cvt_pk_bf16_f32 v5, v13, v15
	v_cvt_pk_bf16_f32 v6, v17, v19
	v_cvt_pk_bf16_f32 v7, v21, v23
	v_or_b32_e32 v1, s10, v100
	v_lshlrev_b32_e32 v8, 12, v1
	v_mov_b32_e32 v9, v147
	ds_read2_b32 v[10:11], v97 offset0:32 offset1:40
	v_lshl_add_u64 v[8:9], v[2:3], 0, v[8:9]
	global_store_dwordx4 v[8:9], v[4:7], off nt
	ds_read2_b32 v[8:9], v97 offset0:97 offset1:105
	ds_read2_b32 v[12:13], v97 offset0:162 offset1:170
	ds_read2_b32 v[14:15], v97 offset0:227 offset1:235
	s_waitcnt lgkmcnt(3)
	s_waitcnt lgkmcnt(2)
	ds_read2_b32 v[16:17], v26 offset0:36 offset1:44
	ds_read2_b32 v[18:19], v26 offset0:101 offset1:109
	v_cvt_pk_bf16_f32 v4, v10, v8
	s_waitcnt lgkmcnt(3)
	s_waitcnt lgkmcnt(2)
	ds_read2_b32 v[20:21], v26 offset0:166 offset1:174
	ds_read2_b32 v[22:23], v26 offset0:231 offset1:239
	v_cvt_pk_bf16_f32 v5, v12, v14
	s_waitcnt lgkmcnt(3)
	s_waitcnt lgkmcnt(2)
	v_cvt_pk_bf16_f32 v6, v16, v18
	s_waitcnt lgkmcnt(1)
	s_waitcnt lgkmcnt(0)
	v_cvt_pk_bf16_f32 v7, v20, v22
	v_or_b32_e32 v1, s10, v101
	v_lshlrev_b32_e32 v24, 12, v1
	v_mov_b32_e32 v25, v147
	v_lshl_add_u64 v[24:25], v[2:3], 0, v[24:25]
	global_store_dwordx4 v[24:25], v[4:7], off nt
	s_nop 1
	v_cvt_pk_bf16_f32 v4, v11, v9
	v_cvt_pk_bf16_f32 v5, v13, v15
	v_cvt_pk_bf16_f32 v6, v17, v19
	v_cvt_pk_bf16_f32 v7, v21, v23
	v_or_b32_e32 v1, s10, v102
	v_lshlrev_b32_e32 v8, 12, v1
	v_mov_b32_e32 v9, v147
	ds_read2_b32 v[10:11], v97 offset0:48 offset1:56
	v_lshl_add_u64 v[8:9], v[2:3], 0, v[8:9]
	global_store_dwordx4 v[8:9], v[4:7], off nt
	ds_read2_b32 v[8:9], v97 offset0:113 offset1:121
	ds_read2_b32 v[12:13], v97 offset0:178 offset1:186
	ds_read2_b32 v[14:15], v97 offset0:243 offset1:251
	s_waitcnt lgkmcnt(3)
	s_waitcnt lgkmcnt(2)
	ds_read2_b32 v[16:17], v26 offset0:52 offset1:60
	ds_read2_b32 v[18:19], v26 offset0:117 offset1:125
	v_cvt_pk_bf16_f32 v4, v10, v8
	s_waitcnt lgkmcnt(3)
	s_waitcnt lgkmcnt(2)
	ds_read2_b32 v[20:21], v26 offset0:182 offset1:190
	ds_read2_b32 v[22:23], v26 offset0:247 offset1:255
	v_cvt_pk_bf16_f32 v5, v12, v14
	s_waitcnt lgkmcnt(3)
	s_waitcnt lgkmcnt(2)
	v_cvt_pk_bf16_f32 v6, v16, v18
	s_waitcnt lgkmcnt(1)
	s_waitcnt lgkmcnt(0)
	v_cvt_pk_bf16_f32 v7, v20, v22
	v_or_b32_e32 v1, s10, v103
	v_lshlrev_b32_e32 v24, 12, v1
	v_mov_b32_e32 v25, v147
	v_lshl_add_u64 v[24:25], v[2:3], 0, v[24:25]
	global_store_dwordx4 v[24:25], v[4:7], off nt
	s_nop 1
	v_cvt_pk_bf16_f32 v4, v11, v9
	v_cvt_pk_bf16_f32 v5, v13, v15
	v_cvt_pk_bf16_f32 v6, v17, v19
	v_cvt_pk_bf16_f32 v7, v21, v23
	v_or_b32_e32 v1, s10, v104
	v_lshlrev_b32_e32 v8, 12, v1
	v_mov_b32_e32 v9, v147
	v_lshl_add_u64 v[2:3], v[2:3], 0, v[8:9]
	global_store_dwordx4 v[2:3], v[4:7], off nt
	s_waitcnt lgkmcnt(0)

; #define LAS __attribute__((address_space(3)))
; __device__ __forceinline__ unsigned pk2(float lo, float hi) { return f2bf(lo) | (f2bf(hi) << 16); }
; __device__ __forceinline__ void tr_item(const float* W, int ldw, int k0, int n0, bf16* WT, int ldt, int drow0, LAS float* scr, int lane, const float* kscale = nullptr) {
;     ...
;     for (int i = 0; i < 16; ++i) { LAS float* q = wp + (4 * i) * 65; const float ks = kscale ? kscale[k0 + 4 * i + (lane >> 4)] : 1.f; q[0] = v[i].x * ks; q[1] = v[i].y * ks; q[2] = v[i].z * ks; q[3] = v[i].w * ks; }
;     asm volatile("s_waitcnt lgkmcnt(0)" ::: "memory");
;     const int kc = lane & 7;
; #pragma unroll
;     for (int j = 0; j < 8; ++j) { const int n = (lane >> 3) + 8 * j; const LAS float* sp = scr + (8 * kc) * 65 + n;
;         u32x4 o; o.x = pk2(sp[0 * 65], sp[1 * 65]); o.y = pk2(sp[2 * 65], sp[3 * 65]); o.z = pk2(sp[4 * 65], sp[5 * 65]); o.w = pk2(sp[6 * 65], sp[7 * 65]);
;         __builtin_nontemporal_store(o, (u32x4*)(WT + (size_t)(drow0 + n) * ldt + k0 + 8 * kc)); }
;     asm volatile("s_waitcnt lgkmcnt(0)" ::: "memory");
.LBB0_2810:
	s_waitcnt vmcnt(0)
	v_pk_mul_f32 v[2:3], v[2:3], v[10:11] op_sel_hi:[1,0]
	v_add_u32_e32 v1, 0x3cf0, v95
	ds_write2_b32 v1, v2, v3 offset1:1
	v_pk_mul_f32 v[2:3], v[4:5], v[10:11] op_sel_hi:[1,0]
	v_add_u32_e32 v1, 0x3cf8, v95
	ds_write2_b32 v1, v2, v3 offset1:1
	s_waitcnt lgkmcnt(0)
	ds_read2_b32 v[8:9], v97 offset1:8
	ds_read2_b32 v[10:11], v97 offset0:65 offset1:73
	ds_read2_b32 v[12:13], v97 offset0:130 offset1:138
	ds_read2_b32 v[14:15], v97 offset0:195 offset1:203
	v_add_u32_e32 v26, 0x400, v97
	s_waitcnt lgkmcnt(3)
	s_waitcnt lgkmcnt(2)
	ds_read2_b32 v[16:17], v26 offset0:4 offset1:12
	ds_read2_b32 v[18:19], v26 offset0:69 offset1:77
	v_cvt_pk_bf16_f32 v4, v8, v10
	s_waitcnt lgkmcnt(3)
	s_waitcnt lgkmcnt(2)
	ds_read2_b32 v[20:21], v26 offset0:134 offset1:142
	ds_read2_b32 v[22:23], v26 offset0:199 offset1:207
	v_cvt_pk_bf16_f32 v5, v12, v14
	s_waitcnt lgkmcnt(3)
	s_waitcnt lgkmcnt(2)
	v_cvt_pk_bf16_f32 v6, v16, v18
	s_waitcnt lgkmcnt(1)
	s_waitcnt lgkmcnt(0)
	s_mov_b32 s9, s13
	v_cvt_pk_bf16_f32 v7, v20, v22
	v_or_b32_e32 v1, s14, v96
	v_lshl_add_u64 v[2:3], s[8:9], 1, v[74:75]
	v_lshlrev_b32_e32 v146, 9, v1
	v_lshl_add_u64 v[24:25], v[2:3], 0, v[146:147]
	global_store_dwordx4 v[24:25], v[4:7], off nt
	s_nop 1
	v_cvt_pk_bf16_f32 v4, v9, v11
	v_cvt_pk_bf16_f32 v5, v13, v15
	v_cvt_pk_bf16_f32 v6, v17, v19
	v_cvt_pk_bf16_f32 v7, v21, v23
	v_or_b32_e32 v1, s14, v98
	v_lshlrev_b32_e32 v146, 9, v1
	ds_read2_b32 v[8:9], v97 offset0:16 offset1:24
	v_lshl_add_u64 v[10:11], v[2:3], 0, v[146:147]
	global_store_dwordx4 v[10:11], v[4:7], off nt
	ds_read2_b32 v[10:11], v97 offset0:81 offset1:89
	ds_read2_b32 v[12:13], v97 offset0:146 offset1:154
	ds_read2_b32 v[14:15], v97 offset0:211 offset1:219
	s_waitcnt lgkmcnt(3)
	s_waitcnt lgkmcnt(2)
	ds_read2_b32 v[16:17], v26 offset0:20 offset1:28
	ds_read2_b32 v[18:19], v26 offset0:85 offset1:93
	v_cvt_pk_bf16_f32 v4, v8, v10
	s_waitcnt lgkmcnt(3)
	s_waitcnt lgkmcnt(2)
	ds_read2_b32 v[20:21], v26 offset0:150 offset1:158
	ds_read2_b32 v[22:23], v26 offset0:215 offset1:223
	v_cvt_pk_bf16_f32 v5, v12, v14
	s_waitcnt lgkmcnt(3)
	s_waitcnt lgkmcnt(2)
	v_cvt_pk_bf16_f32 v6, v16, v18
	s_waitcnt lgkmcnt(1)
	s_waitcnt lgkmcnt(0)
	v_cvt_pk_bf16_f32 v7, v20, v22
	v_or_b32_e32 v1, s14, v99
	v_lshlrev_b32_e32 v146, 9, v1
	v_lshl_add_u64 v[24:25], v[2:3], 0, v[146:147]
	global_store_dwordx4 v[24:25], v[4:7], off nt
	s_nop 1
	v_cvt_pk_bf16_f32 v4, v9, v11
	v_cvt_pk_bf16_f32 v5, v13, v15
	v_cvt_pk_bf16_f32 v6, v17, v19
	v_cvt_pk_bf16_f32 v7, v21, v23
	v_or_b32_e32 v1, s14, v100
	v_lshlrev_b32_e32 v146, 9, v1
	ds_read2_b32 v[8:9], v97 offset0:32 offset1:40
	v_lshl_add_u64 v[10:11], v[2:3], 0, v[146:147]
	global_store_dwordx4 v[10:11], v[4:7], off nt
	ds_read2_b32 v[10:11], v97 offset0:97 offset1:105
	ds_read2_b32 v[12:13], v97 offset0:162 offset1:170
	ds_read2_b32 v[14:15], v97 offset0:227 offset1:235
	s_waitcnt lgkmcnt(3)
	s_waitcnt lgkmcnt(2)
	ds_read2_b32 v[16:17], v26 offset0:36 offset1:44
	ds_read2_b32 v[18:19], v26 offset0:101 offset1:109
	v_cvt_pk_bf16_f32 v4, v8, v10
	s_waitcnt lgkmcnt(3)
	s_waitcnt lgkmcnt(2)
	ds_read2_b32 v[20:21], v26 offset0:166 offset1:174
	ds_read2_b32 v[22:23], v26 offset0:231 offset1:239
	v_cvt_pk_bf16_f32 v5, v12, v14
	s_waitcnt lgkmcnt(3)
	s_waitcnt lgkmcnt(2)
	v_cvt_pk_bf16_f32 v6, v16, v18
	s_waitcnt lgkmcnt(1)
	s_waitcnt lgkmcnt(0)
	v_cvt_pk_bf16_f32 v7, v20, v22
	v_or_b32_e32 v1, s14, v101
	v_lshlrev_b32_e32 v146, 9, v1
	v_lshl_add_u64 v[24:25], v[2:3], 0, v[146:147]
	global_store_dwordx4 v[24:25], v[4:7], off nt
	s_nop 1
	v_cvt_pk_bf16_f32 v4, v9, v11
	v_cvt_pk_bf16_f32 v5, v13, v15
	v_cvt_pk_bf16_f32 v6, v17, v19
	v_cvt_pk_bf16_f32 v7, v21, v23
	v_or_b32_e32 v1, s14, v102
	v_lshlrev_b32_e32 v146, 9, v1
	ds_read2_b32 v[8:9], v97 offset0:48 offset1:56
	v_lshl_add_u64 v[10:11], v[2:3], 0, v[146:147]
	global_store_dwordx4 v[10:11], v[4:7], off nt
	ds_read2_b32 v[10:11], v97 offset0:113 offset1:121
	ds_read2_b32 v[12:13], v97 offset0:178 offset1:186
	ds_read2_b32 v[14:15], v97 offset0:243 offset1:251
	s_waitcnt lgkmcnt(3)
	s_waitcnt lgkmcnt(2)
	ds_read2_b32 v[16:17], v26 offset0:52 offset1:60
	ds_read2_b32 v[18:19], v26 offset0:117 offset1:125
	v_cvt_pk_bf16_f32 v4, v8, v10
	s_waitcnt lgkmcnt(3)
	s_waitcnt lgkmcnt(2)
	ds_read2_b32 v[20:21], v26 offset0:182 offset1:190
	ds_read2_b32 v[22:23], v26 offset0:247 offset1:255
	v_cvt_pk_bf16_f32 v5, v12, v14
	s_waitcnt lgkmcnt(3)
	s_waitcnt lgkmcnt(2)
	v_cvt_pk_bf16_f32 v6, v16, v18
	s_waitcnt lgkmcnt(1)
	s_waitcnt lgkmcnt(0)
	v_cvt_pk_bf16_f32 v7, v20, v22
	v_or_b32_e32 v1, s14, v103
	v_lshlrev_b32_e32 v146, 9, v1
	v_lshl_add_u64 v[24:25], v[2:3], 0, v[146:147]
	global_store_dwordx4 v[24:25], v[4:7], off nt
	s_nop 1
	v_cvt_pk_bf16_f32 v4, v9, v11
	v_cvt_pk_bf16_f32 v5, v13, v15
	v_cvt_pk_bf16_f32 v6, v17, v19
	v_cvt_pk_bf16_f32 v7, v21, v23
	v_or_b32_e32 v1, s14, v104
	v_lshlrev_b32_e32 v146, 9, v1
	v_lshl_add_u64 v[2:3], v[2:3], 0, v[146:147]
	global_store_dwordx4 v[2:3], v[4:7], off nt
	s_waitcnt lgkmcnt(0)

; #define LAS __attribute__((address_space(3)))
; __device__ __forceinline__ unsigned pk2(float lo, float hi) { return f2bf(lo) | (f2bf(hi) << 16); }
; __device__ __forceinline__ void tr_item(const float* W, int ldw, int k0, int n0, bf16* WT, int ldt, int drow0, LAS float* scr, int lane, const float* kscale = nullptr) {
;     ...
;     for (int i = 0; i < 16; ++i) { LAS float* q = wp + (4 * i) * 65; const float ks = kscale ? kscale[k0 + 4 * i + (lane >> 4)] : 1.f; q[0] = v[i].x * ks; q[1] = v[i].y * ks; q[2] = v[i].z * ks; q[3] = v[i].w * ks; }
;     asm volatile("s_waitcnt lgkmcnt(0)" ::: "memory");
;     const int kc = lane & 7;
; #pragma unroll
;     for (int j = 0; j < 8; ++j) { const int n = (lane >> 3) + 8 * j; const LAS float* sp = scr + (8 * kc) * 65 + n;
;         u32x4 o; o.x = pk2(sp[0 * 65], sp[1 * 65]); o.y = pk2(sp[2 * 65], sp[3 * 65]); o.z = pk2(sp[4 * 65], sp[5 * 65]); o.w = pk2(sp[6 * 65], sp[7 * 65]);
;         __builtin_nontemporal_store(o, (u32x4*)(WT + (size_t)(drow0 + n) * ldt + k0 + 8 * kc)); }
;     asm volatile("s_waitcnt lgkmcnt(0)" ::: "memory");
.LBB0_2837:
	s_waitcnt vmcnt(0)
	v_pk_mul_f32 v[2:3], v[2:3], v[10:11] op_sel_hi:[1,0]
	v_add_u32_e32 v1, 0x3cf0, v95
	ds_write2_b32 v1, v2, v3 offset1:1
	v_pk_mul_f32 v[2:3], v[4:5], v[10:11] op_sel_hi:[1,0]
	v_add_u32_e32 v1, 0x3cf8, v95
	ds_write2_b32 v1, v2, v3 offset1:1
	s_waitcnt lgkmcnt(0)
	ds_read2_b32 v[8:9], v97 offset1:8
	ds_read2_b32 v[10:11], v97 offset0:65 offset1:73
	ds_read2_b32 v[12:13], v97 offset0:130 offset1:138
	ds_read2_b32 v[14:15], v97 offset0:195 offset1:203
	v_add_u32_e32 v26, 0x400, v97
	s_waitcnt lgkmcnt(3)
	s_waitcnt lgkmcnt(2)
	ds_read2_b32 v[16:17], v26 offset0:4 offset1:12
	ds_read2_b32 v[18:19], v26 offset0:69 offset1:77
	v_cvt_pk_bf16_f32 v4, v8, v10
	s_waitcnt lgkmcnt(3)
	s_waitcnt lgkmcnt(2)
	ds_read2_b32 v[20:21], v26 offset0:134 offset1:142
	ds_read2_b32 v[22:23], v26 offset0:199 offset1:207
	v_cvt_pk_bf16_f32 v5, v12, v14
	s_waitcnt lgkmcnt(3)
	s_waitcnt lgkmcnt(2)
	v_cvt_pk_bf16_f32 v6, v16, v18
	s_waitcnt lgkmcnt(1)
	v_or_b32_e32 v24, s8, v96
	s_lshl_b32 s12, s12, 1
	s_waitcnt lgkmcnt(0)
	v_ashrrev_i32_e32 v25, 31, v24
	v_lshl_add_u64 v[2:3], v[76:77], 0, s[12:13]
	v_lshlrev_b64 v[24:25], 10, v[24:25]
	v_cvt_pk_bf16_f32 v7, v20, v22
	v_lshl_add_u64 v[24:25], v[2:3], 0, v[24:25]
	global_store_dwordx4 v[24:25], v[4:7], off nt
	s_nop 1
	v_cvt_pk_bf16_f32 v4, v9, v11
	v_cvt_pk_bf16_f32 v5, v13, v15
	v_cvt_pk_bf16_f32 v6, v17, v19
	v_or_b32_e32 v8, s8, v98
	v_ashrrev_i32_e32 v9, 31, v8
	v_lshlrev_b64 v[8:9], 10, v[8:9]
	v_cvt_pk_bf16_f32 v7, v21, v23
	ds_read2_b32 v[10:11], v97 offset0:16 offset1:24
	v_lshl_add_u64 v[8:9], v[2:3], 0, v[8:9]
	global_store_dwordx4 v[8:9], v[4:7], off nt
	ds_read2_b32 v[8:9], v97 offset0:81 offset1:89
	ds_read2_b32 v[12:13], v97 offset0:146 offset1:154
	ds_read2_b32 v[14:15], v97 offset0:211 offset1:219
	s_waitcnt lgkmcnt(3)
	s_waitcnt lgkmcnt(2)
	ds_read2_b32 v[16:17], v26 offset0:20 offset1:28
	ds_read2_b32 v[18:19], v26 offset0:85 offset1:93
	v_cvt_pk_bf16_f32 v4, v10, v8
	s_waitcnt lgkmcnt(3)
	s_waitcnt lgkmcnt(2)
	ds_read2_b32 v[20:21], v26 offset0:150 offset1:158
	ds_read2_b32 v[22:23], v26 offset0:215 offset1:223
	v_cvt_pk_bf16_f32 v5, v12, v14
	s_waitcnt lgkmcnt(3)
	s_waitcnt lgkmcnt(2)
	v_cvt_pk_bf16_f32 v6, v16, v18
	s_waitcnt lgkmcnt(1)
	v_or_b32_e32 v24, s8, v99
	s_waitcnt lgkmcnt(0)
	v_ashrrev_i32_e32 v25, 31, v24
	v_lshlrev_b64 v[24:25], 10, v[24:25]
	v_cvt_pk_bf16_f32 v7, v20, v22
	v_lshl_add_u64 v[24:25], v[2:3], 0, v[24:25]
	global_store_dwordx4 v[24:25], v[4:7], off nt
	s_nop 1
	v_cvt_pk_bf16_f32 v4, v11, v9
	v_cvt_pk_bf16_f32 v5, v13, v15
	v_cvt_pk_bf16_f32 v6, v17, v19
	v_or_b32_e32 v8, s8, v100
	v_ashrrev_i32_e32 v9, 31, v8
	v_lshlrev_b64 v[8:9], 10, v[8:9]
	v_cvt_pk_bf16_f32 v7, v21, v23
	ds_read2_b32 v[10:11], v97 offset0:32 offset1:40
	v_lshl_add_u64 v[8:9], v[2:3], 0, v[8:9]
	global_store_dwordx4 v[8:9], v[4:7], off nt
	ds_read2_b32 v[8:9], v97 offset0:97 offset1:105
	ds_read2_b32 v[12:13], v97 offset0:162 offset1:170
	ds_read2_b32 v[14:15], v97 offset0:227 offset1:235
	s_waitcnt lgkmcnt(3)
	s_waitcnt lgkmcnt(2)
	ds_read2_b32 v[16:17], v26 offset0:36 offset1:44
	ds_read2_b32 v[18:19], v26 offset0:101 offset1:109
	v_cvt_pk_bf16_f32 v4, v10, v8
	s_waitcnt lgkmcnt(3)
	s_waitcnt lgkmcnt(2)
	ds_read2_b32 v[20:21], v26 offset0:166 offset1:174
	ds_read2_b32 v[22:23], v26 offset0:231 offset1:239
	v_cvt_pk_bf16_f32 v5, v12, v14
	s_waitcnt lgkmcnt(3)
	s_waitcnt lgkmcnt(2)
	v_cvt_pk_bf16_f32 v6, v16, v18
	s_waitcnt lgkmcnt(1)
	v_or_b32_e32 v24, s8, v101
	s_waitcnt lgkmcnt(0)
	v_ashrrev_i32_e32 v25, 31, v24
	v_lshlrev_b64 v[24:25], 10, v[24:25]
	v_cvt_pk_bf16_f32 v7, v20, v22
	v_lshl_add_u64 v[24:25], v[2:3], 0, v[24:25]
	global_store_dwordx4 v[24:25], v[4:7], off nt
	s_nop 1
	v_cvt_pk_bf16_f32 v4, v11, v9
	v_cvt_pk_bf16_f32 v5, v13, v15
	v_cvt_pk_bf16_f32 v6, v17, v19
	v_or_b32_e32 v8, s8, v102
	v_ashrrev_i32_e32 v9, 31, v8
	v_lshlrev_b64 v[8:9], 10, v[8:9]
	v_cvt_pk_bf16_f32 v7, v21, v23
	ds_read2_b32 v[10:11], v97 offset0:48 offset1:56
	v_lshl_add_u64 v[8:9], v[2:3], 0, v[8:9]
	global_store_dwordx4 v[8:9], v[4:7], off nt
	ds_read2_b32 v[8:9], v97 offset0:113 offset1:121
	ds_read2_b32 v[12:13], v97 offset0:178 offset1:186
	ds_read2_b32 v[14:15], v97 offset0:243 offset1:251
	s_waitcnt lgkmcnt(3)
	s_waitcnt lgkmcnt(2)
	ds_read2_b32 v[16:17], v26 offset0:52 offset1:60
	ds_read2_b32 v[18:19], v26 offset0:117 offset1:125
	v_cvt_pk_bf16_f32 v4, v10, v8
	s_waitcnt lgkmcnt(3)
	s_waitcnt lgkmcnt(2)
	ds_read2_b32 v[20:21], v26 offset0:182 offset1:190
	ds_read2_b32 v[22:23], v26 offset0:247 offset1:255
	v_cvt_pk_bf16_f32 v5, v12, v14
	s_waitcnt lgkmcnt(3)
	s_waitcnt lgkmcnt(2)
	v_cvt_pk_bf16_f32 v6, v16, v18
	s_waitcnt lgkmcnt(1)
	v_or_b32_e32 v24, s8, v103
	s_waitcnt lgkmcnt(0)
	v_ashrrev_i32_e32 v25, 31, v24
	v_lshlrev_b64 v[24:25], 10, v[24:25]
	v_cvt_pk_bf16_f32 v7, v20, v22
	v_lshl_add_u64 v[24:25], v[2:3], 0, v[24:25]
	global_store_dwordx4 v[24:25], v[4:7], off nt
	s_nop 1
	v_cvt_pk_bf16_f32 v4, v11, v9
	v_cvt_pk_bf16_f32 v5, v13, v15
	v_cvt_pk_bf16_f32 v6, v17, v19
	v_or_b32_e32 v8, s8, v104
	v_ashrrev_i32_e32 v9, 31, v8
	v_lshlrev_b64 v[8:9], 10, v[8:9]
	v_cvt_pk_bf16_f32 v7, v21, v23
	v_lshl_add_u64 v[2:3], v[2:3], 0, v[8:9]
	global_store_dwordx4 v[2:3], v[4:7], off nt
	s_waitcnt lgkmcnt(0)

; #define LAS __attribute__((address_space(3)))
; #define WSW(T, off, l) WSP(T, WS_WSET + (size_t)(l) * WSET_STRIDE + (off))
; __device__ __forceinline__ void tr_item(const float* W, int ldw, int k0, int n0, bf16* WT, int ldt, int drow0, LAS float* scr, int lane, const float* kscale = nullptr) {
;     const float* src = W + (size_t)(k0 + (lane >> 4)) * ldw + n0 + (lane & 15) * 4;
;     f32x4 v[16];
; #pragma unroll
;     for (int i = 0; i < 16; ++i) v[i] = __builtin_nontemporal_load((const f32x4*)(src + (size_t)(4 * i) * ldw));
;     LAS float* wp = scr + (lane >> 4) * 65 + (lane & 15) * 4;
; #pragma unroll
;     for (int i = 0; i < 16; ++i) { LAS float* q = wp + (4 * i) * 65; const float ks = kscale ? kscale[k0 + 4 * i + (lane >> 4)] : 1.f; q[0] = v[i].x * ks; q[1] = v[i].y * ks; q[2] = v[i].z * ks; q[3] = v[i].w * ks; }
; __device__ __forceinline__ void convert_tile(const Args& a, GAS unsigned char* wsb, int l, int t, LAS float* scr, int lane) {
;     ...
;     if (r < I_IN) { const int kb = r / 45, nb = r - kb * 45; tr_item(INP(7) + (size_t)l * DM * INW, INW, kb * 64, nb * 64, WSW(bf16, W_IN, l), DM, nb * 64, scr, lane); return; }
.LBB0_2839:
	s_andn2_b64 vcc, exec, s[8:9]
	s_cbranch_vccnz .LBB0_2841
	s_mul_i32 s8, s18, 0x2d83
	s_lshr_b32 s10, s8, 19
	s_mul_i32 s8, s10, 0xffffffd3
	s_add_i32 s8, s8, s18
	v_lshl_or_b32 v1, s10, 6, v67
	v_readlane_b32 s14, v253, 6
	s_lshl_b32 s8, s8, 6
	v_mul_u32_u24_e32 v2, 0x2d00, v1
	v_mov_b32_e32 v3, v147
	v_readlane_b32 s15, v253, 7
	s_ashr_i32 s9, s8, 31
	v_lshlrev_b32_e32 v4, 2, v66
	v_lshl_add_u64 v[2:3], s[14:15], 0, v[2:3]
	v_lshl_add_u64 v[2:3], s[8:9], 2, v[2:3]
	v_mov_b32_e32 v5, v147
	v_lshl_add_u64 v[62:63], v[2:3], 0, v[4:5]
	s_mov_b32 s9, 0xb000
	v_add_co_u32_e32 v6, vcc, s9, v62
	s_mov_b32 s9, 0x16000
	s_nop 0
	v_addc_co_u32_e32 v7, vcc, 0, v63, vcc
	v_add_co_u32_e32 v10, vcc, s9, v62
	global_load_dwordx4 v[2:5], v[62:63], off nt
	s_nop 0
	global_load_dwordx4 v[6:9], v[6:7], off offset:1024 nt
	v_addc_co_u32_e32 v11, vcc, 0, v63, vcc
	s_mov_b32 s9, 0x21000
	v_add_co_u32_e32 v14, vcc, s9, v62
	s_mov_b32 s9, 0x2d000
	s_nop 0
	v_addc_co_u32_e32 v15, vcc, 0, v63, vcc
	global_load_dwordx4 v[10:13], v[10:11], off offset:2048 nt
	s_nop 0
	global_load_dwordx4 v[14:17], v[14:15], off offset:3072 nt
	v_add_co_u32_e32 v18, vcc, s9, v62
	s_mov_b32 s9, 0x38000
	s_nop 0
	v_addc_co_u32_e32 v19, vcc, 0, v63, vcc
	v_add_co_u32_e32 v22, vcc, s9, v62
	s_mov_b32 s9, 0x43000
	s_nop 0
	v_addc_co_u32_e32 v23, vcc, 0, v63, vcc
	global_load_dwordx4 v[18:21], v[18:19], off nt
	s_nop 0
	global_load_dwordx4 v[22:25], v[22:23], off offset:1024 nt
	v_add_co_u32_e32 v26, vcc, s9, v62
	s_mov_b32 s9, 0x4e000
	s_nop 0
	v_addc_co_u32_e32 v27, vcc, 0, v63, vcc
	v_add_co_u32_e32 v30, vcc, s9, v62
	s_mov_b32 s9, 0x5a000
	s_nop 0
	v_addc_co_u32_e32 v31, vcc, 0, v63, vcc
	global_load_dwordx4 v[26:29], v[26:27], off offset:2048 nt
	s_nop 0
	global_load_dwordx4 v[30:33], v[30:31], off offset:3072 nt
	v_add_co_u32_e32 v34, vcc, s9, v62
	s_mov_b32 s9, 0x65000
	s_nop 0
	v_addc_co_u32_e32 v35, vcc, 0, v63, vcc
	v_add_co_u32_e32 v38, vcc, s9, v62
	s_mov_b32 s9, 0x70000
	s_nop 0
	v_addc_co_u32_e32 v39, vcc, 0, v63, vcc
	global_load_dwordx4 v[34:37], v[34:35], off nt
	s_nop 0
	global_load_dwordx4 v[38:41], v[38:39], off offset:1024 nt
	v_add_co_u32_e32 v42, vcc, s9, v62
	s_mov_b32 s9, 0x7b000
	s_nop 0
	v_addc_co_u32_e32 v43, vcc, 0, v63, vcc
	v_add_co_u32_e32 v46, vcc, s9, v62
	s_mov_b32 s9, 0x87000
	s_nop 0
	v_addc_co_u32_e32 v47, vcc, 0, v63, vcc
	global_load_dwordx4 v[42:45], v[42:43], off offset:2048 nt
	s_nop 0
	global_load_dwordx4 v[46:49], v[46:47], off offset:3072 nt
	v_add_co_u32_e32 v50, vcc, s9, v62
	s_mov_b32 s9, 0x92000
	s_nop 0
	v_addc_co_u32_e32 v51, vcc, 0, v63, vcc
	v_add_co_u32_e32 v54, vcc, s9, v62
	s_mov_b32 s9, 0x9d000
	s_nop 0
	v_addc_co_u32_e32 v55, vcc, 0, v63, vcc
	global_load_dwordx4 v[50:53], v[50:51], off nt
	s_nop 0
	global_load_dwordx4 v[54:57], v[54:55], off offset:1024 nt
	v_add_co_u32_e32 v58, vcc, s9, v62
	s_mov_b32 s9, 0xa8000
	s_nop 0
	v_addc_co_u32_e32 v59, vcc, 0, v63, vcc
	global_load_dwordx4 v[58:61], v[58:59], off offset:2048 nt
	v_add_co_u32_e32 v62, vcc, s9, v62
	v_add_u32_e32 v1, 0x410, v95
	s_nop 0
	v_addc_co_u32_e32 v63, vcc, 0, v63, vcc
	global_load_dwordx4 v[62:65], v[62:63], off offset:3072 nt
	s_waitcnt vmcnt(15)
	ds_write2_b32 v95, v2, v3 offset1:1
	ds_write2_b32 v95, v4, v5 offset0:2 offset1:3
	s_waitcnt vmcnt(14)
	ds_write2_b32 v1, v6, v7 offset1:1
	v_add_u32_e32 v1, 0x418, v95
	ds_write2_b32 v1, v8, v9 offset1:1
	v_add_u32_e32 v1, 0x820, v95
	s_lshl_b32 s12, s10, 7
	v_lshl_add_u64 v[2:3], v[78:79], 0, s[12:13]
	s_waitcnt vmcnt(13)
	ds_write2_b32 v1, v10, v11 offset1:1
	v_add_u32_e32 v1, 0x828, v95
	ds_write2_b32 v1, v12, v13 offset1:1
	v_add_u32_e32 v1, 0xc30, v95
	s_waitcnt vmcnt(12)
	ds_write2_b32 v1, v14, v15 offset1:1
	v_add_u32_e32 v1, 0xc38, v95
	ds_write2_b32 v1, v16, v17 offset1:1
	v_add_u32_e32 v1, 0x1040, v95
	s_waitcnt vmcnt(11)
	ds_write2_b32 v1, v18, v19 offset1:1
	v_add_u32_e32 v1, 0x1048, v95
	ds_write2_b32 v1, v20, v21 offset1:1
	v_add_u32_e32 v1, 0x1450, v95
	s_waitcnt vmcnt(10)
	ds_write2_b32 v1, v22, v23 offset1:1
	v_add_u32_e32 v1, 0x1458, v95
	ds_write2_b32 v1, v24, v25 offset1:1
	v_add_u32_e32 v1, 0x1860, v95
	v_or_b32_e32 v24, s8, v96
	v_ashrrev_i32_e32 v25, 31, v24
	v_lshlrev_b64 v[24:25], 12, v[24:25]
	s_waitcnt vmcnt(9)
	ds_write2_b32 v1, v26, v27 offset1:1
	v_add_u32_e32 v1, 0x1868, v95
	ds_write2_b32 v1, v28, v29 offset1:1
	v_add_u32_e32 v1, 0x1c70, v95
	s_waitcnt vmcnt(8)
	ds_write2_b32 v1, v30, v31 offset1:1
	v_add_u32_e32 v1, 0x1c78, v95
	ds_write2_b32 v1, v32, v33 offset1:1
	v_add_u32_e32 v1, 0x2080, v95
	v_add_u32_e32 v26, 0x400, v97
	v_lshl_add_u64 v[24:25], v[2:3], 0, v[24:25]
	s_waitcnt vmcnt(7)
	ds_write2_b32 v1, v34, v35 offset1:1
	v_add_u32_e32 v1, 0x2088, v95
	ds_write2_b32 v1, v36, v37 offset1:1
	v_add_u32_e32 v1, 0x2490, v95
	s_waitcnt vmcnt(6)
	ds_write2_b32 v1, v38, v39 offset1:1
	v_add_u32_e32 v1, 0x2498, v95
	ds_write2_b32 v1, v40, v41 offset1:1
	v_add_u32_e32 v1, 0x28a0, v95
	s_waitcnt vmcnt(5)
	ds_write2_b32 v1, v42, v43 offset1:1
	v_add_u32_e32 v1, 0x28a8, v95
	ds_write2_b32 v1, v44, v45 offset1:1
	v_add_u32_e32 v1, 0x2cb0, v95
	s_waitcnt vmcnt(4)
	ds_write2_b32 v1, v46, v47 offset1:1
	v_add_u32_e32 v1, 0x2cb8, v95
	ds_write2_b32 v1, v48, v49 offset1:1
	v_add_u32_e32 v1, 0x30c0, v95
	s_waitcnt vmcnt(3)
; #define LAS __attribute__((address_space(3)))
; __device__ __forceinline__ unsigned pk2(float lo, float hi) { return f2bf(lo) | (f2bf(hi) << 16); }
; __device__ __forceinline__ void tr_item(const float* W, int ldw, int k0, int n0, bf16* WT, int ldt, int drow0, LAS float* scr, int lane, const float* kscale = nullptr) {
;     ...
;     for (int i = 0; i < 16; ++i) { LAS float* q = wp + (4 * i) * 65; const float ks = kscale ? kscale[k0 + 4 * i + (lane >> 4)] : 1.f; q[0] = v[i].x * ks; q[1] = v[i].y * ks; q[2] = v[i].z * ks; q[3] = v[i].w * ks; }
;     asm volatile("s_waitcnt lgkmcnt(0)" ::: "memory");
;     const int kc = lane & 7;
; #pragma unroll
;     for (int j = 0; j < 8; ++j) { const int n = (lane >> 3) + 8 * j; const LAS float* sp = scr + (8 * kc) * 65 + n;
;         u32x4 o; o.x = pk2(sp[0 * 65], sp[1 * 65]); o.y = pk2(sp[2 * 65], sp[3 * 65]); o.z = pk2(sp[4 * 65], sp[5 * 65]); o.w = pk2(sp[6 * 65], sp[7 * 65]);
;         __builtin_nontemporal_store(o, (u32x4*)(WT + (size_t)(drow0 + n) * ldt + k0 + 8 * kc)); }
;     asm volatile("s_waitcnt lgkmcnt(0)" ::: "memory");
	ds_write2_b32 v1, v50, v51 offset1:1
	v_add_u32_e32 v1, 0x30c8, v95
	ds_write2_b32 v1, v52, v53 offset1:1
	v_add_u32_e32 v1, 0x34d0, v95
	s_waitcnt vmcnt(2)
	ds_write2_b32 v1, v54, v55 offset1:1
	v_add_u32_e32 v1, 0x34d8, v95
	ds_write2_b32 v1, v56, v57 offset1:1
	v_add_u32_e32 v1, 0x38e0, v95
	s_waitcnt vmcnt(1)
	ds_write2_b32 v1, v58, v59 offset1:1
	v_add_u32_e32 v1, 0x38e8, v95
	ds_write2_b32 v1, v60, v61 offset1:1
	v_add_u32_e32 v1, 0x3cf0, v95
	s_waitcnt vmcnt(0)
	ds_write2_b32 v1, v62, v63 offset1:1
	v_add_u32_e32 v1, 0x3cf8, v95
	ds_write2_b32 v1, v64, v65 offset1:1
	s_waitcnt lgkmcnt(0)
	ds_read2_b32 v[8:9], v97 offset1:8
	ds_read2_b32 v[10:11], v97 offset0:65 offset1:73
	ds_read2_b32 v[12:13], v97 offset0:130 offset1:138
	ds_read2_b32 v[14:15], v97 offset0:195 offset1:203
	ds_read2_b32 v[16:17], v26 offset0:4 offset1:12
	s_waitcnt lgkmcnt(4)
	s_waitcnt lgkmcnt(3)
	ds_read2_b32 v[18:19], v26 offset0:69 offset1:77
	v_cvt_pk_bf16_f32 v4, v8, v10
	s_waitcnt lgkmcnt(3)
	s_waitcnt lgkmcnt(2)
	ds_read2_b32 v[20:21], v26 offset0:134 offset1:142
	ds_read2_b32 v[22:23], v26 offset0:199 offset1:207
	v_cvt_pk_bf16_f32 v5, v12, v14
	s_waitcnt lgkmcnt(3)
	s_waitcnt lgkmcnt(2)
	v_cvt_pk_bf16_f32 v6, v16, v18
	s_waitcnt lgkmcnt(1)
	s_waitcnt lgkmcnt(0)
	v_cvt_pk_bf16_f32 v7, v20, v22
	global_store_dwordx4 v[24:25], v[4:7], off nt
	s_nop 1
	v_cvt_pk_bf16_f32 v4, v9, v11
	v_cvt_pk_bf16_f32 v5, v13, v15
	v_cvt_pk_bf16_f32 v6, v17, v19
	v_or_b32_e32 v8, s8, v98
	v_ashrrev_i32_e32 v9, 31, v8
	v_lshlrev_b64 v[8:9], 12, v[8:9]
	v_cvt_pk_bf16_f32 v7, v21, v23
	ds_read2_b32 v[10:11], v97 offset0:16 offset1:24
	v_lshl_add_u64 v[8:9], v[2:3], 0, v[8:9]
	global_store_dwordx4 v[8:9], v[4:7], off nt
	ds_read2_b32 v[8:9], v97 offset0:81 offset1:89
	ds_read2_b32 v[12:13], v97 offset0:146 offset1:154
	ds_read2_b32 v[14:15], v97 offset0:211 offset1:219
	s_waitcnt lgkmcnt(3)
	s_waitcnt lgkmcnt(2)
	ds_read2_b32 v[16:17], v26 offset0:20 offset1:28
	ds_read2_b32 v[18:19], v26 offset0:85 offset1:93
	v_cvt_pk_bf16_f32 v4, v10, v8
	s_waitcnt lgkmcnt(3)
	s_waitcnt lgkmcnt(2)
	ds_read2_b32 v[20:21], v26 offset0:150 offset1:158
	ds_read2_b32 v[22:23], v26 offset0:215 offset1:223
	v_cvt_pk_bf16_f32 v5, v12, v14
	s_waitcnt lgkmcnt(3)
	s_waitcnt lgkmcnt(2)
	v_cvt_pk_bf16_f32 v6, v16, v18
	s_waitcnt lgkmcnt(1)
	v_or_b32_e32 v24, s8, v99
	s_waitcnt lgkmcnt(0)
	v_ashrrev_i32_e32 v25, 31, v24
	v_lshlrev_b64 v[24:25], 12, v[24:25]
	v_cvt_pk_bf16_f32 v7, v20, v22
	v_lshl_add_u64 v[24:25], v[2:3], 0, v[24:25]
	global_store_dwordx4 v[24:25], v[4:7], off nt
	s_nop 1
	v_cvt_pk_bf16_f32 v4, v11, v9
	v_cvt_pk_bf16_f32 v5, v13, v15
	v_cvt_pk_bf16_f32 v6, v17, v19
	v_or_b32_e32 v8, s8, v100
	v_ashrrev_i32_e32 v9, 31, v8
	v_lshlrev_b64 v[8:9], 12, v[8:9]
	v_cvt_pk_bf16_f32 v7, v21, v23
	ds_read2_b32 v[10:11], v97 offset0:32 offset1:40
	v_lshl_add_u64 v[8:9], v[2:3], 0, v[8:9]
	global_store_dwordx4 v[8:9], v[4:7], off nt
	ds_read2_b32 v[8:9], v97 offset0:97 offset1:105
	ds_read2_b32 v[12:13], v97 offset0:162 offset1:170
	ds_read2_b32 v[14:15], v97 offset0:227 offset1:235
	s_waitcnt lgkmcnt(3)
	s_waitcnt lgkmcnt(2)
	ds_read2_b32 v[16:17], v26 offset0:36 offset1:44
	ds_read2_b32 v[18:19], v26 offset0:101 offset1:109
	v_cvt_pk_bf16_f32 v4, v10, v8
	s_waitcnt lgkmcnt(3)
	s_waitcnt lgkmcnt(2)
	ds_read2_b32 v[20:21], v26 offset0:166 offset1:174
	ds_read2_b32 v[22:23], v26 offset0:231 offset1:239
	v_cvt_pk_bf16_f32 v5, v12, v14
	s_waitcnt lgkmcnt(3)
	s_waitcnt lgkmcnt(2)
	v_cvt_pk_bf16_f32 v6, v16, v18
	s_waitcnt lgkmcnt(1)
	v_or_b32_e32 v24, s8, v101
	s_waitcnt lgkmcnt(0)
	v_ashrrev_i32_e32 v25, 31, v24
	v_lshlrev_b64 v[24:25], 12, v[24:25]
	v_cvt_pk_bf16_f32 v7, v20, v22
	v_lshl_add_u64 v[24:25], v[2:3], 0, v[24:25]
	global_store_dwordx4 v[24:25], v[4:7], off nt
	s_nop 1
	v_cvt_pk_bf16_f32 v4, v11, v9
	v_cvt_pk_bf16_f32 v5, v13, v15
	v_cvt_pk_bf16_f32 v6, v17, v19
	v_or_b32_e32 v8, s8, v102
	v_ashrrev_i32_e32 v9, 31, v8
	v_lshlrev_b64 v[8:9], 12, v[8:9]
	v_cvt_pk_bf16_f32 v7, v21, v23
	ds_read2_b32 v[10:11], v97 offset0:48 offset1:56
	v_lshl_add_u64 v[8:9], v[2:3], 0, v[8:9]
	global_store_dwordx4 v[8:9], v[4:7], off nt
	ds_read2_b32 v[8:9], v97 offset0:113 offset1:121
	ds_read2_b32 v[12:13], v97 offset0:178 offset1:186
	ds_read2_b32 v[14:15], v97 offset0:243 offset1:251
	s_waitcnt lgkmcnt(3)
	s_waitcnt lgkmcnt(2)
	ds_read2_b32 v[16:17], v26 offset0:52 offset1:60
	ds_read2_b32 v[18:19], v26 offset0:117 offset1:125
	v_cvt_pk_bf16_f32 v4, v10, v8
	s_waitcnt lgkmcnt(3)
	s_waitcnt lgkmcnt(2)
	ds_read2_b32 v[20:21], v26 offset0:182 offset1:190
	ds_read2_b32 v[22:23], v26 offset0:247 offset1:255
	v_cvt_pk_bf16_f32 v5, v12, v14
	s_waitcnt lgkmcnt(3)
	s_waitcnt lgkmcnt(2)
	v_cvt_pk_bf16_f32 v6, v16, v18
	s_waitcnt lgkmcnt(1)
	v_or_b32_e32 v24, s8, v103
	s_waitcnt lgkmcnt(0)
	v_ashrrev_i32_e32 v25, 31, v24
	v_lshlrev_b64 v[24:25], 12, v[24:25]
	v_cvt_pk_bf16_f32 v7, v20, v22
	v_lshl_add_u64 v[24:25], v[2:3], 0, v[24:25]
	global_store_dwordx4 v[24:25], v[4:7], off nt
	s_nop 1
	v_cvt_pk_bf16_f32 v4, v11, v9
	v_cvt_pk_bf16_f32 v5, v13, v15
	v_cvt_pk_bf16_f32 v6, v17, v19
	v_or_b32_e32 v8, s8, v104
	v_ashrrev_i32_e32 v9, 31, v8
	v_lshlrev_b64 v[8:9], 12, v[8:9]
	v_cvt_pk_bf16_f32 v7, v21, v23
	v_lshl_add_u64 v[2:3], v[2:3], 0, v[8:9]
	global_store_dwordx4 v[2:3], v[4:7], off nt
	s_waitcnt lgkmcnt(0)

; #define LAS __attribute__((address_space(3)))
; #define WSW(T, off, l) WSP(T, WS_WSET + (size_t)(l) * WSET_STRIDE + (off))
; __device__ __forceinline__ void tr_item(const float* W, int ldw, int k0, int n0, bf16* WT, int ldt, int drow0, LAS float* scr, int lane, const float* kscale = nullptr) {
;     const float* src = W + (size_t)(k0 + (lane >> 4)) * ldw + n0 + (lane & 15) * 4;
;     f32x4 v[16];
; #pragma unroll
;     for (int i = 0; i < 16; ++i) v[i] = __builtin_nontemporal_load((const f32x4*)(src + (size_t)(4 * i) * ldw));
;     LAS float* wp = scr + (lane >> 4) * 65 + (lane & 15) * 4;
; #pragma unroll
;     for (int i = 0; i < 16; ++i) { LAS float* q = wp + (4 * i) * 65; const float ks = kscale ? kscale[k0 + 4 * i + (lane >> 4)] : 1.f; q[0] = v[i].x * ks; q[1] = v[i].y * ks; q[2] = v[i].z * ks; q[3] = v[i].w * ks; }
; __device__ __forceinline__ void convert_tile(const Args& a, GAS unsigned char* wsb, int l, int t, LAS float* scr, int lane) {
;     ...
;     if (r < I_OUT) { const int kb = r / 32, nb = r - kb * 32; tr_item(INP(21) + (size_t)l * DM * DM, DM, kb * 64, nb * 64, WSW(bf16, W_OUT, l), DM, nb * 64, scr, lane); return; }
.LBB0_2856:
	s_andn2_b64 vcc, exec, s[8:9]
	s_cbranch_vccnz .LBB0_2858
	s_lshl_b32 s8, s18, 1
	s_and_b32 s8, s8, 0x1fc0
	s_addk_i32 s8, 0xf240
	s_lshl_b32 s9, s18, 6
	v_or_b32_e32 v2, s8, v67
	v_mov_b32_e32 v3, v147
	s_and_b32 s10, s9, 0x7c0
	v_lshlrev_b64 v[2:3], 13, v[2:3]
	v_lshl_add_u64 v[2:3], s[60:61], 0, v[2:3]
	s_lshl_b32 s12, s10, 2
	v_lshl_add_u64 v[2:3], v[2:3], 0, s[12:13]
	v_lshlrev_b32_e32 v4, 2, v66
	v_mov_b32_e32 v5, v147
	v_lshl_add_u64 v[62:63], v[2:3], 0, v[4:5]
	v_add_co_u32_e32 v6, vcc, s83, v62
	s_mov_b32 s9, 0x20000
	s_nop 0
	v_addc_co_u32_e32 v7, vcc, 0, v63, vcc
	v_add_co_u32_e32 v10, vcc, s81, v62
	global_load_dwordx4 v[2:5], v[62:63], off nt
	s_nop 0
	global_load_dwordx4 v[6:9], v[6:7], off nt
	v_addc_co_u32_e32 v11, vcc, 0, v63, vcc
	v_add_co_u32_e32 v14, vcc, s82, v62
	v_add_u32_e32 v1, 0x410, v95
	s_nop 0
	v_addc_co_u32_e32 v15, vcc, 0, v63, vcc
	global_load_dwordx4 v[10:13], v[10:11], off nt
	s_nop 0
	global_load_dwordx4 v[14:17], v[14:15], off nt
	v_add_co_u32_e32 v18, vcc, s9, v62
	s_mov_b32 s9, 0x28000
	s_nop 0
	v_addc_co_u32_e32 v19, vcc, 0, v63, vcc
	v_add_co_u32_e32 v22, vcc, s9, v62
	s_mov_b32 s9, 0x30000
	s_nop 0
	v_addc_co_u32_e32 v23, vcc, 0, v63, vcc
	global_load_dwordx4 v[18:21], v[18:19], off nt
	s_nop 0
	global_load_dwordx4 v[22:25], v[22:23], off nt
	v_add_co_u32_e32 v26, vcc, s9, v62
	s_mov_b32 s9, 0x38000
	s_nop 0
	v_addc_co_u32_e32 v27, vcc, 0, v63, vcc
	v_add_co_u32_e32 v30, vcc, s9, v62
	s_mov_b32 s9, 0x40000
	s_nop 0
	v_addc_co_u32_e32 v31, vcc, 0, v63, vcc
	global_load_dwordx4 v[26:29], v[26:27], off nt
	s_nop 0
	global_load_dwordx4 v[30:33], v[30:31], off nt
	v_add_co_u32_e32 v34, vcc, s9, v62
	s_mov_b32 s9, 0x48000
	s_nop 0
	v_addc_co_u32_e32 v35, vcc, 0, v63, vcc
	v_add_co_u32_e32 v38, vcc, s9, v62
	s_mov_b32 s9, 0x50000
	s_nop 0
	v_addc_co_u32_e32 v39, vcc, 0, v63, vcc
	global_load_dwordx4 v[34:37], v[34:35], off nt
	s_nop 0
	global_load_dwordx4 v[38:41], v[38:39], off nt
	v_add_co_u32_e32 v42, vcc, s9, v62
	s_mov_b32 s9, 0x58000
	s_nop 0
	v_addc_co_u32_e32 v43, vcc, 0, v63, vcc
	v_add_co_u32_e32 v46, vcc, s9, v62
	s_mov_b32 s9, 0x60000
	s_nop 0
	v_addc_co_u32_e32 v47, vcc, 0, v63, vcc
	global_load_dwordx4 v[42:45], v[42:43], off nt
	s_nop 0
	global_load_dwordx4 v[46:49], v[46:47], off nt
	v_add_co_u32_e32 v50, vcc, s9, v62
	s_mov_b32 s9, 0x68000
	s_nop 0
	v_addc_co_u32_e32 v51, vcc, 0, v63, vcc
	v_add_co_u32_e32 v54, vcc, s9, v62
	s_mov_b32 s9, 0x70000
	s_nop 0
	v_addc_co_u32_e32 v55, vcc, 0, v63, vcc
	global_load_dwordx4 v[50:53], v[50:51], off nt
	s_nop 0
	global_load_dwordx4 v[54:57], v[54:55], off nt
	v_add_co_u32_e32 v58, vcc, s9, v62
	s_mov_b32 s9, 0x78000
	s_nop 0
	v_addc_co_u32_e32 v59, vcc, 0, v63, vcc
	global_load_dwordx4 v[58:61], v[58:59], off nt
	v_add_co_u32_e32 v62, vcc, s9, v62
	s_mov_b32 s9, s13
	s_nop 0
	v_addc_co_u32_e32 v63, vcc, 0, v63, vcc
	global_load_dwordx4 v[62:65], v[62:63], off nt
	s_waitcnt vmcnt(15)
	ds_write2_b32 v95, v2, v3 offset1:1
	ds_write2_b32 v95, v4, v5 offset0:2 offset1:3
	s_waitcnt vmcnt(14)
	ds_write2_b32 v1, v6, v7 offset1:1
	v_add_u32_e32 v1, 0x418, v95
	ds_write2_b32 v1, v8, v9 offset1:1
	v_add_u32_e32 v1, 0x820, v95
	v_lshl_add_u64 v[2:3], s[8:9], 1, v[84:85]
	s_waitcnt vmcnt(13)
	ds_write2_b32 v1, v10, v11 offset1:1
	v_add_u32_e32 v1, 0x828, v95
	ds_write2_b32 v1, v12, v13 offset1:1
	v_add_u32_e32 v1, 0xc30, v95
	s_waitcnt vmcnt(12)
	ds_write2_b32 v1, v14, v15 offset1:1
	v_add_u32_e32 v1, 0xc38, v95
	ds_write2_b32 v1, v16, v17 offset1:1
	v_add_u32_e32 v1, 0x1040, v95
	s_waitcnt vmcnt(11)
	ds_write2_b32 v1, v18, v19 offset1:1
	v_add_u32_e32 v1, 0x1048, v95
	ds_write2_b32 v1, v20, v21 offset1:1
	v_add_u32_e32 v1, 0x1450, v95
	s_waitcnt vmcnt(10)
	ds_write2_b32 v1, v22, v23 offset1:1
	v_add_u32_e32 v1, 0x1458, v95
	ds_write2_b32 v1, v24, v25 offset1:1
	v_add_u32_e32 v1, 0x1860, v95
	v_mov_b32_e32 v25, v147
	s_waitcnt vmcnt(9)
	ds_write2_b32 v1, v26, v27 offset1:1
	v_add_u32_e32 v1, 0x1868, v95
	ds_write2_b32 v1, v28, v29 offset1:1
	v_add_u32_e32 v1, 0x1c70, v95
	s_waitcnt vmcnt(8)
	ds_write2_b32 v1, v30, v31 offset1:1
	v_add_u32_e32 v1, 0x1c78, v95
	ds_write2_b32 v1, v32, v33 offset1:1
	v_add_u32_e32 v1, 0x2080, v95
	v_add_u32_e32 v26, 0x400, v97
	s_waitcnt vmcnt(7)
	ds_write2_b32 v1, v34, v35 offset1:1
	v_add_u32_e32 v1, 0x2088, v95
	ds_write2_b32 v1, v36, v37 offset1:1
	v_add_u32_e32 v1, 0x2490, v95
	s_waitcnt vmcnt(6)
	ds_write2_b32 v1, v38, v39 offset1:1
	v_add_u32_e32 v1, 0x2498, v95
	ds_write2_b32 v1, v40, v41 offset1:1
	v_add_u32_e32 v1, 0x28a0, v95
	s_waitcnt vmcnt(5)
	ds_write2_b32 v1, v42, v43 offset1:1
	v_add_u32_e32 v1, 0x28a8, v95
	ds_write2_b32 v1, v44, v45 offset1:1
	v_add_u32_e32 v1, 0x2cb0, v95
	s_waitcnt vmcnt(4)
	ds_write2_b32 v1, v46, v47 offset1:1
	v_add_u32_e32 v1, 0x2cb8, v95
	ds_write2_b32 v1, v48, v49 offset1:1
	v_add_u32_e32 v1, 0x30c0, v95
	s_waitcnt vmcnt(3)
	ds_write2_b32 v1, v50, v51 offset1:1
	v_add_u32_e32 v1, 0x30c8, v95
	ds_write2_b32 v1, v52, v53 offset1:1
	v_add_u32_e32 v1, 0x34d0, v95
	s_waitcnt vmcnt(2)
	ds_write2_b32 v1, v54, v55 offset1:1
	v_add_u32_e32 v1, 0x34d8, v95
	ds_write2_b32 v1, v56, v57 offset1:1
	v_add_u32_e32 v1, 0x38e0, v95
	s_waitcnt vmcnt(1)
; #define LAS __attribute__((address_space(3)))
; __device__ __forceinline__ unsigned pk2(float lo, float hi) { return f2bf(lo) | (f2bf(hi) << 16); }
; __device__ __forceinline__ void tr_item(const float* W, int ldw, int k0, int n0, bf16* WT, int ldt, int drow0, LAS float* scr, int lane, const float* kscale = nullptr) {
;     ...
;     for (int i = 0; i < 16; ++i) { LAS float* q = wp + (4 * i) * 65; const float ks = kscale ? kscale[k0 + 4 * i + (lane >> 4)] : 1.f; q[0] = v[i].x * ks; q[1] = v[i].y * ks; q[2] = v[i].z * ks; q[3] = v[i].w * ks; }
;     asm volatile("s_waitcnt lgkmcnt(0)" ::: "memory");
;     const int kc = lane & 7;
; #pragma unroll
;     for (int j = 0; j < 8; ++j) { const int n = (lane >> 3) + 8 * j; const LAS float* sp = scr + (8 * kc) * 65 + n;
;         u32x4 o; o.x = pk2(sp[0 * 65], sp[1 * 65]); o.y = pk2(sp[2 * 65], sp[3 * 65]); o.z = pk2(sp[4 * 65], sp[5 * 65]); o.w = pk2(sp[6 * 65], sp[7 * 65]);
;         __builtin_nontemporal_store(o, (u32x4*)(WT + (size_t)(drow0 + n) * ldt + k0 + 8 * kc)); }
;     asm volatile("s_waitcnt lgkmcnt(0)" ::: "memory");
	ds_write2_b32 v1, v58, v59 offset1:1
	v_add_u32_e32 v1, 0x38e8, v95
	ds_write2_b32 v1, v60, v61 offset1:1
	v_add_u32_e32 v1, 0x3cf0, v95
	s_waitcnt vmcnt(0)
	ds_write2_b32 v1, v62, v63 offset1:1
	v_add_u32_e32 v1, 0x3cf8, v95
	ds_write2_b32 v1, v64, v65 offset1:1
	s_waitcnt lgkmcnt(0)
	ds_read2_b32 v[8:9], v97 offset1:8
	ds_read2_b32 v[10:11], v97 offset0:65 offset1:73
	ds_read2_b32 v[12:13], v97 offset0:130 offset1:138
	ds_read2_b32 v[14:15], v97 offset0:195 offset1:203
	ds_read2_b32 v[16:17], v26 offset0:4 offset1:12
	s_waitcnt lgkmcnt(4)
	s_waitcnt lgkmcnt(3)
	ds_read2_b32 v[18:19], v26 offset0:69 offset1:77
	v_cvt_pk_bf16_f32 v4, v8, v10
	s_waitcnt lgkmcnt(3)
	s_waitcnt lgkmcnt(2)
	ds_read2_b32 v[20:21], v26 offset0:134 offset1:142
	ds_read2_b32 v[22:23], v26 offset0:199 offset1:207
	v_cvt_pk_bf16_f32 v5, v12, v14
	s_waitcnt lgkmcnt(3)
	s_waitcnt lgkmcnt(2)
	v_cvt_pk_bf16_f32 v6, v16, v18
	s_waitcnt lgkmcnt(1)
	s_waitcnt lgkmcnt(0)
	v_cvt_pk_bf16_f32 v7, v20, v22
	v_or_b32_e32 v1, s10, v96
	v_lshlrev_b32_e32 v24, 12, v1
	v_lshl_add_u64 v[24:25], v[2:3], 0, v[24:25]
	global_store_dwordx4 v[24:25], v[4:7], off nt
	s_nop 1
	v_cvt_pk_bf16_f32 v4, v9, v11
	v_cvt_pk_bf16_f32 v5, v13, v15
	v_cvt_pk_bf16_f32 v6, v17, v19
	v_cvt_pk_bf16_f32 v7, v21, v23
	v_or_b32_e32 v1, s10, v98
	v_lshlrev_b32_e32 v8, 12, v1
	v_mov_b32_e32 v9, v147
	ds_read2_b32 v[10:11], v97 offset0:16 offset1:24
	v_lshl_add_u64 v[8:9], v[2:3], 0, v[8:9]
	global_store_dwordx4 v[8:9], v[4:7], off nt
	ds_read2_b32 v[8:9], v97 offset0:81 offset1:89
	ds_read2_b32 v[12:13], v97 offset0:146 offset1:154
	ds_read2_b32 v[14:15], v97 offset0:211 offset1:219
	s_waitcnt lgkmcnt(3)
	s_waitcnt lgkmcnt(2)
	ds_read2_b32 v[16:17], v26 offset0:20 offset1:28
	ds_read2_b32 v[18:19], v26 offset0:85 offset1:93
	v_cvt_pk_bf16_f32 v4, v10, v8
	s_waitcnt lgkmcnt(3)
	s_waitcnt lgkmcnt(2)
	ds_read2_b32 v[20:21], v26 offset0:150 offset1:158
	ds_read2_b32 v[22:23], v26 offset0:215 offset1:223
	v_cvt_pk_bf16_f32 v5, v12, v14
	s_waitcnt lgkmcnt(3)
	s_waitcnt lgkmcnt(2)
	v_cvt_pk_bf16_f32 v6, v16, v18
	s_waitcnt lgkmcnt(1)
	s_waitcnt lgkmcnt(0)
	v_cvt_pk_bf16_f32 v7, v20, v22
	v_or_b32_e32 v1, s10, v99
	v_lshlrev_b32_e32 v24, 12, v1
	v_mov_b32_e32 v25, v147
	v_lshl_add_u64 v[24:25], v[2:3], 0, v[24:25]
	global_store_dwordx4 v[24:25], v[4:7], off nt
	s_nop 1
	v_cvt_pk_bf16_f32 v4, v11, v9
	v_cvt_pk_bf16_f32 v5, v13, v15
	v_cvt_pk_bf16_f32 v6, v17, v19
	v_cvt_pk_bf16_f32 v7, v21, v23
	v_or_b32_e32 v1, s10, v100
	v_lshlrev_b32_e32 v8, 12, v1
	v_mov_b32_e32 v9, v147
	ds_read2_b32 v[10:11], v97 offset0:32 offset1:40
	v_lshl_add_u64 v[8:9], v[2:3], 0, v[8:9]
	global_store_dwordx4 v[8:9], v[4:7], off nt
	ds_read2_b32 v[8:9], v97 offset0:97 offset1:105
	ds_read2_b32 v[12:13], v97 offset0:162 offset1:170
	ds_read2_b32 v[14:15], v97 offset0:227 offset1:235
	s_waitcnt lgkmcnt(3)
	s_waitcnt lgkmcnt(2)
	ds_read2_b32 v[16:17], v26 offset0:36 offset1:44
	ds_read2_b32 v[18:19], v26 offset0:101 offset1:109
	v_cvt_pk_bf16_f32 v4, v10, v8
	s_waitcnt lgkmcnt(3)
	s_waitcnt lgkmcnt(2)
	ds_read2_b32 v[20:21], v26 offset0:166 offset1:174
	ds_read2_b32 v[22:23], v26 offset0:231 offset1:239
	v_cvt_pk_bf16_f32 v5, v12, v14
	s_waitcnt lgkmcnt(3)
	s_waitcnt lgkmcnt(2)
	v_cvt_pk_bf16_f32 v6, v16, v18
	s_waitcnt lgkmcnt(1)
	s_waitcnt lgkmcnt(0)
	v_cvt_pk_bf16_f32 v7, v20, v22
	v_or_b32_e32 v1, s10, v101
	v_lshlrev_b32_e32 v24, 12, v1
	v_mov_b32_e32 v25, v147
	v_lshl_add_u64 v[24:25], v[2:3], 0, v[24:25]
	global_store_dwordx4 v[24:25], v[4:7], off nt
	s_nop 1
	v_cvt_pk_bf16_f32 v4, v11, v9
	v_cvt_pk_bf16_f32 v5, v13, v15
	v_cvt_pk_bf16_f32 v6, v17, v19
	v_cvt_pk_bf16_f32 v7, v21, v23
	v_or_b32_e32 v1, s10, v102
	v_lshlrev_b32_e32 v8, 12, v1
	v_mov_b32_e32 v9, v147
	ds_read2_b32 v[10:11], v97 offset0:48 offset1:56
	v_lshl_add_u64 v[8:9], v[2:3], 0, v[8:9]
	global_store_dwordx4 v[8:9], v[4:7], off nt
	ds_read2_b32 v[8:9], v97 offset0:113 offset1:121
	ds_read2_b32 v[12:13], v97 offset0:178 offset1:186
	ds_read2_b32 v[14:15], v97 offset0:243 offset1:251
	s_waitcnt lgkmcnt(3)
	s_waitcnt lgkmcnt(2)
	ds_read2_b32 v[16:17], v26 offset0:52 offset1:60
	ds_read2_b32 v[18:19], v26 offset0:117 offset1:125
	v_cvt_pk_bf16_f32 v4, v10, v8
	s_waitcnt lgkmcnt(3)
	s_waitcnt lgkmcnt(2)
	ds_read2_b32 v[20:21], v26 offset0:182 offset1:190
	ds_read2_b32 v[22:23], v26 offset0:247 offset1:255
	v_cvt_pk_bf16_f32 v5, v12, v14
	s_waitcnt lgkmcnt(3)
	s_waitcnt lgkmcnt(2)
	v_cvt_pk_bf16_f32 v6, v16, v18
	s_waitcnt lgkmcnt(1)
	s_waitcnt lgkmcnt(0)
	v_cvt_pk_bf16_f32 v7, v20, v22
	v_or_b32_e32 v1, s10, v103
	v_lshlrev_b32_e32 v24, 12, v1
	v_mov_b32_e32 v25, v147
	v_lshl_add_u64 v[24:25], v[2:3], 0, v[24:25]
	global_store_dwordx4 v[24:25], v[4:7], off nt
	s_nop 1
	v_cvt_pk_bf16_f32 v4, v11, v9
	v_cvt_pk_bf16_f32 v5, v13, v15
	v_cvt_pk_bf16_f32 v6, v17, v19
	v_cvt_pk_bf16_f32 v7, v21, v23
	v_or_b32_e32 v1, s10, v104
	v_lshlrev_b32_e32 v8, 12, v1
	v_mov_b32_e32 v9, v147
	v_lshl_add_u64 v[2:3], v[2:3], 0, v[8:9]
	global_store_dwordx4 v[2:3], v[4:7], off nt
	s_waitcnt lgkmcnt(0)

; #define LAS __attribute__((address_space(3)))
; __device__ __forceinline__ unsigned pk2(float lo, float hi) { return f2bf(lo) | (f2bf(hi) << 16); }
; __device__ __forceinline__ void tr_item(const float* W, int ldw, int k0, int n0, bf16* WT, int ldt, int drow0, LAS float* scr, int lane, const float* kscale = nullptr) {
;     ...
;     for (int i = 0; i < 16; ++i) { LAS float* q = wp + (4 * i) * 65; const float ks = kscale ? kscale[k0 + 4 * i + (lane >> 4)] : 1.f; q[0] = v[i].x * ks; q[1] = v[i].y * ks; q[2] = v[i].z * ks; q[3] = v[i].w * ks; }
;     asm volatile("s_waitcnt lgkmcnt(0)" ::: "memory");
;     const int kc = lane & 7;
; #pragma unroll
;     for (int j = 0; j < 8; ++j) { const int n = (lane >> 3) + 8 * j; const LAS float* sp = scr + (8 * kc) * 65 + n;
;         u32x4 o; o.x = pk2(sp[0 * 65], sp[1 * 65]); o.y = pk2(sp[2 * 65], sp[3 * 65]); o.z = pk2(sp[4 * 65], sp[5 * 65]); o.w = pk2(sp[6 * 65], sp[7 * 65]);
;         __builtin_nontemporal_store(o, (u32x4*)(WT + (size_t)(drow0 + n) * ldt + k0 + 8 * kc)); }
;     asm volatile("s_waitcnt lgkmcnt(0)" ::: "memory");
.LBB0_2884:
	s_waitcnt vmcnt(0)
	v_pk_mul_f32 v[2:3], v[2:3], v[10:11] op_sel_hi:[1,0]
	v_add_u32_e32 v1, 0x3cf0, v95
	ds_write2_b32 v1, v2, v3 offset1:1
	v_pk_mul_f32 v[2:3], v[4:5], v[10:11] op_sel_hi:[1,0]
	v_add_u32_e32 v1, 0x3cf8, v95
	ds_write2_b32 v1, v2, v3 offset1:1
	s_waitcnt lgkmcnt(0)
	ds_read2_b32 v[8:9], v97 offset1:8
	ds_read2_b32 v[10:11], v97 offset0:65 offset1:73
	ds_read2_b32 v[12:13], v97 offset0:130 offset1:138
	ds_read2_b32 v[14:15], v97 offset0:195 offset1:203
	v_add_u32_e32 v26, 0x400, v97
	s_waitcnt lgkmcnt(3)
	s_waitcnt lgkmcnt(2)
	ds_read2_b32 v[16:17], v26 offset0:4 offset1:12
	ds_read2_b32 v[18:19], v26 offset0:69 offset1:77
	v_cvt_pk_bf16_f32 v4, v8, v10
	s_waitcnt lgkmcnt(3)
	s_waitcnt lgkmcnt(2)
	ds_read2_b32 v[20:21], v26 offset0:134 offset1:142
	ds_read2_b32 v[22:23], v26 offset0:199 offset1:207
	v_cvt_pk_bf16_f32 v5, v12, v14
	s_waitcnt lgkmcnt(3)
	s_waitcnt lgkmcnt(2)
	v_cvt_pk_bf16_f32 v6, v16, v18
	s_waitcnt lgkmcnt(1)
	s_waitcnt lgkmcnt(0)
	s_mov_b32 s9, s13
	v_cvt_pk_bf16_f32 v7, v20, v22
	v_or_b32_e32 v1, s14, v96
	v_lshl_add_u64 v[2:3], s[8:9], 1, v[86:87]
	v_lshlrev_b32_e32 v146, 9, v1
	v_lshl_add_u64 v[24:25], v[2:3], 0, v[146:147]
	global_store_dwordx4 v[24:25], v[4:7], off nt
	s_nop 1
	v_cvt_pk_bf16_f32 v4, v9, v11
	v_cvt_pk_bf16_f32 v5, v13, v15
	v_cvt_pk_bf16_f32 v6, v17, v19
	v_cvt_pk_bf16_f32 v7, v21, v23
	v_or_b32_e32 v1, s14, v98
	v_lshlrev_b32_e32 v146, 9, v1
	ds_read2_b32 v[8:9], v97 offset0:16 offset1:24
	v_lshl_add_u64 v[10:11], v[2:3], 0, v[146:147]
	global_store_dwordx4 v[10:11], v[4:7], off nt
	ds_read2_b32 v[10:11], v97 offset0:81 offset1:89
	ds_read2_b32 v[12:13], v97 offset0:146 offset1:154
	ds_read2_b32 v[14:15], v97 offset0:211 offset1:219
	s_waitcnt lgkmcnt(3)
	s_waitcnt lgkmcnt(2)
	ds_read2_b32 v[16:17], v26 offset0:20 offset1:28
	ds_read2_b32 v[18:19], v26 offset0:85 offset1:93
	v_cvt_pk_bf16_f32 v4, v8, v10
	s_waitcnt lgkmcnt(3)
	s_waitcnt lgkmcnt(2)
	ds_read2_b32 v[20:21], v26 offset0:150 offset1:158
	ds_read2_b32 v[22:23], v26 offset0:215 offset1:223
	v_cvt_pk_bf16_f32 v5, v12, v14
	s_waitcnt lgkmcnt(3)
	s_waitcnt lgkmcnt(2)
	v_cvt_pk_bf16_f32 v6, v16, v18
	s_waitcnt lgkmcnt(1)
	s_waitcnt lgkmcnt(0)
	v_cvt_pk_bf16_f32 v7, v20, v22
	v_or_b32_e32 v1, s14, v99
	v_lshlrev_b32_e32 v146, 9, v1
	v_lshl_add_u64 v[24:25], v[2:3], 0, v[146:147]
	global_store_dwordx4 v[24:25], v[4:7], off nt
	s_nop 1
	v_cvt_pk_bf16_f32 v4, v9, v11
	v_cvt_pk_bf16_f32 v5, v13, v15
	v_cvt_pk_bf16_f32 v6, v17, v19
	v_cvt_pk_bf16_f32 v7, v21, v23
	v_or_b32_e32 v1, s14, v100
	v_lshlrev_b32_e32 v146, 9, v1
	ds_read2_b32 v[8:9], v97 offset0:32 offset1:40
	v_lshl_add_u64 v[10:11], v[2:3], 0, v[146:147]
	global_store_dwordx4 v[10:11], v[4:7], off nt
	ds_read2_b32 v[10:11], v97 offset0:97 offset1:105
	ds_read2_b32 v[12:13], v97 offset0:162 offset1:170
	ds_read2_b32 v[14:15], v97 offset0:227 offset1:235
	s_waitcnt lgkmcnt(3)
	s_waitcnt lgkmcnt(2)
	ds_read2_b32 v[16:17], v26 offset0:36 offset1:44
	ds_read2_b32 v[18:19], v26 offset0:101 offset1:109
	v_cvt_pk_bf16_f32 v4, v8, v10
	s_waitcnt lgkmcnt(3)
	s_waitcnt lgkmcnt(2)
	ds_read2_b32 v[20:21], v26 offset0:166 offset1:174
	ds_read2_b32 v[22:23], v26 offset0:231 offset1:239
	v_cvt_pk_bf16_f32 v5, v12, v14
	s_waitcnt lgkmcnt(3)
	s_waitcnt lgkmcnt(2)
	v_cvt_pk_bf16_f32 v6, v16, v18
	s_waitcnt lgkmcnt(1)
	s_waitcnt lgkmcnt(0)
	v_cvt_pk_bf16_f32 v7, v20, v22
	v_or_b32_e32 v1, s14, v101
	v_lshlrev_b32_e32 v146, 9, v1
	v_lshl_add_u64 v[24:25], v[2:3], 0, v[146:147]
	global_store_dwordx4 v[24:25], v[4:7], off nt
	s_nop 1
	v_cvt_pk_bf16_f32 v4, v9, v11
	v_cvt_pk_bf16_f32 v5, v13, v15
	v_cvt_pk_bf16_f32 v6, v17, v19
	v_cvt_pk_bf16_f32 v7, v21, v23
	v_or_b32_e32 v1, s14, v102
	v_lshlrev_b32_e32 v146, 9, v1
	ds_read2_b32 v[8:9], v97 offset0:48 offset1:56
	v_lshl_add_u64 v[10:11], v[2:3], 0, v[146:147]
	global_store_dwordx4 v[10:11], v[4:7], off nt
	ds_read2_b32 v[10:11], v97 offset0:113 offset1:121
	ds_read2_b32 v[12:13], v97 offset0:178 offset1:186
	ds_read2_b32 v[14:15], v97 offset0:243 offset1:251
	s_waitcnt lgkmcnt(3)
	s_waitcnt lgkmcnt(2)
	ds_read2_b32 v[16:17], v26 offset0:52 offset1:60
	ds_read2_b32 v[18:19], v26 offset0:117 offset1:125
	v_cvt_pk_bf16_f32 v4, v8, v10
	s_waitcnt lgkmcnt(3)
	s_waitcnt lgkmcnt(2)
	ds_read2_b32 v[20:21], v26 offset0:182 offset1:190
	ds_read2_b32 v[22:23], v26 offset0:247 offset1:255
	v_cvt_pk_bf16_f32 v5, v12, v14
	s_waitcnt lgkmcnt(3)
	s_waitcnt lgkmcnt(2)
	v_cvt_pk_bf16_f32 v6, v16, v18
	s_waitcnt lgkmcnt(1)
	s_waitcnt lgkmcnt(0)
	v_cvt_pk_bf16_f32 v7, v20, v22
	v_or_b32_e32 v1, s14, v103
	v_lshlrev_b32_e32 v146, 9, v1
	v_lshl_add_u64 v[24:25], v[2:3], 0, v[146:147]
	global_store_dwordx4 v[24:25], v[4:7], off nt
	s_nop 1
	v_cvt_pk_bf16_f32 v4, v9, v11
	v_cvt_pk_bf16_f32 v5, v13, v15
	v_cvt_pk_bf16_f32 v6, v17, v19
	v_cvt_pk_bf16_f32 v7, v21, v23
	v_or_b32_e32 v1, s14, v104
	v_lshlrev_b32_e32 v146, 9, v1
	v_lshl_add_u64 v[2:3], v[2:3], 0, v[146:147]
	global_store_dwordx4 v[2:3], v[4:7], off nt
	s_waitcnt lgkmcnt(0)

; #define LAS __attribute__((address_space(3)))
; __device__ __forceinline__ unsigned pk2(float lo, float hi) { return f2bf(lo) | (f2bf(hi) << 16); }
; __device__ __forceinline__ void tr_item(const float* W, int ldw, int k0, int n0, bf16* WT, int ldt, int drow0, LAS float* scr, int lane, const float* kscale = nullptr) {
;     ...
;     for (int i = 0; i < 16; ++i) { LAS float* q = wp + (4 * i) * 65; const float ks = kscale ? kscale[k0 + 4 * i + (lane >> 4)] : 1.f; q[0] = v[i].x * ks; q[1] = v[i].y * ks; q[2] = v[i].z * ks; q[3] = v[i].w * ks; }
;     asm volatile("s_waitcnt lgkmcnt(0)" ::: "memory");
;     const int kc = lane & 7;
; #pragma unroll
;     for (int j = 0; j < 8; ++j) { const int n = (lane >> 3) + 8 * j; const LAS float* sp = scr + (8 * kc) * 65 + n;
;         u32x4 o; o.x = pk2(sp[0 * 65], sp[1 * 65]); o.y = pk2(sp[2 * 65], sp[3 * 65]); o.z = pk2(sp[4 * 65], sp[5 * 65]); o.w = pk2(sp[6 * 65], sp[7 * 65]);
;         __builtin_nontemporal_store(o, (u32x4*)(WT + (size_t)(drow0 + n) * ldt + k0 + 8 * kc)); }
;     asm volatile("s_waitcnt lgkmcnt(0)" ::: "memory");
.LBB0_2911:
	s_waitcnt vmcnt(0)
	v_pk_mul_f32 v[2:3], v[2:3], v[10:11] op_sel_hi:[1,0]
	v_add_u32_e32 v1, 0x3cf0, v95
	ds_write2_b32 v1, v2, v3 offset1:1
	v_pk_mul_f32 v[2:3], v[4:5], v[10:11] op_sel_hi:[1,0]
	v_add_u32_e32 v1, 0x3cf8, v95
	ds_write2_b32 v1, v2, v3 offset1:1
	s_waitcnt lgkmcnt(0)
	ds_read2_b32 v[8:9], v97 offset1:8
	ds_read2_b32 v[10:11], v97 offset0:65 offset1:73
	ds_read2_b32 v[12:13], v97 offset0:130 offset1:138
	ds_read2_b32 v[14:15], v97 offset0:195 offset1:203
	v_add_u32_e32 v26, 0x400, v97
	s_waitcnt lgkmcnt(3)
	s_waitcnt lgkmcnt(2)
	ds_read2_b32 v[16:17], v26 offset0:4 offset1:12
	ds_read2_b32 v[18:19], v26 offset0:69 offset1:77
	v_cvt_pk_bf16_f32 v4, v8, v10
	s_waitcnt lgkmcnt(3)
	s_waitcnt lgkmcnt(2)
	ds_read2_b32 v[20:21], v26 offset0:134 offset1:142
	ds_read2_b32 v[22:23], v26 offset0:199 offset1:207
	v_cvt_pk_bf16_f32 v5, v12, v14
	s_waitcnt lgkmcnt(3)
	s_waitcnt lgkmcnt(2)
	v_cvt_pk_bf16_f32 v6, v16, v18
	s_waitcnt lgkmcnt(1)
	v_or_b32_e32 v24, s8, v96
	s_lshl_b32 s12, s12, 1
	s_waitcnt lgkmcnt(0)
	v_ashrrev_i32_e32 v25, 31, v24
	v_lshl_add_u64 v[2:3], v[88:89], 0, s[12:13]
	v_lshlrev_b64 v[24:25], 10, v[24:25]
	v_cvt_pk_bf16_f32 v7, v20, v22
	v_lshl_add_u64 v[24:25], v[2:3], 0, v[24:25]
	global_store_dwordx4 v[24:25], v[4:7], off nt
	s_nop 1
	v_cvt_pk_bf16_f32 v4, v9, v11
	v_cvt_pk_bf16_f32 v5, v13, v15
	v_cvt_pk_bf16_f32 v6, v17, v19
	v_or_b32_e32 v8, s8, v98
	v_ashrrev_i32_e32 v9, 31, v8
	v_lshlrev_b64 v[8:9], 10, v[8:9]
	v_cvt_pk_bf16_f32 v7, v21, v23
	ds_read2_b32 v[10:11], v97 offset0:16 offset1:24
	v_lshl_add_u64 v[8:9], v[2:3], 0, v[8:9]
	global_store_dwordx4 v[8:9], v[4:7], off nt
	ds_read2_b32 v[8:9], v97 offset0:81 offset1:89
	ds_read2_b32 v[12:13], v97 offset0:146 offset1:154
	ds_read2_b32 v[14:15], v97 offset0:211 offset1:219
	s_waitcnt lgkmcnt(3)
	s_waitcnt lgkmcnt(2)
	ds_read2_b32 v[16:17], v26 offset0:20 offset1:28
	ds_read2_b32 v[18:19], v26 offset0:85 offset1:93
	v_cvt_pk_bf16_f32 v4, v10, v8
	s_waitcnt lgkmcnt(3)
	s_waitcnt lgkmcnt(2)
	ds_read2_b32 v[20:21], v26 offset0:150 offset1:158
	ds_read2_b32 v[22:23], v26 offset0:215 offset1:223
	v_cvt_pk_bf16_f32 v5, v12, v14
	s_waitcnt lgkmcnt(3)
	s_waitcnt lgkmcnt(2)
	v_cvt_pk_bf16_f32 v6, v16, v18
	s_waitcnt lgkmcnt(1)
	v_or_b32_e32 v24, s8, v99
	s_waitcnt lgkmcnt(0)
	v_ashrrev_i32_e32 v25, 31, v24
	v_lshlrev_b64 v[24:25], 10, v[24:25]
	v_cvt_pk_bf16_f32 v7, v20, v22
	v_lshl_add_u64 v[24:25], v[2:3], 0, v[24:25]
	global_store_dwordx4 v[24:25], v[4:7], off nt
	s_nop 1
	v_cvt_pk_bf16_f32 v4, v11, v9
	v_cvt_pk_bf16_f32 v5, v13, v15
	v_cvt_pk_bf16_f32 v6, v17, v19
	v_or_b32_e32 v8, s8, v100
	v_ashrrev_i32_e32 v9, 31, v8
	v_lshlrev_b64 v[8:9], 10, v[8:9]
	v_cvt_pk_bf16_f32 v7, v21, v23
	ds_read2_b32 v[10:11], v97 offset0:32 offset1:40
	v_lshl_add_u64 v[8:9], v[2:3], 0, v[8:9]
	global_store_dwordx4 v[8:9], v[4:7], off nt
	ds_read2_b32 v[8:9], v97 offset0:97 offset1:105
	ds_read2_b32 v[12:13], v97 offset0:162 offset1:170
	ds_read2_b32 v[14:15], v97 offset0:227 offset1:235
	s_waitcnt lgkmcnt(3)
	s_waitcnt lgkmcnt(2)
	ds_read2_b32 v[16:17], v26 offset0:36 offset1:44
	ds_read2_b32 v[18:19], v26 offset0:101 offset1:109
	v_cvt_pk_bf16_f32 v4, v10, v8
	s_waitcnt lgkmcnt(3)
	s_waitcnt lgkmcnt(2)
	ds_read2_b32 v[20:21], v26 offset0:166 offset1:174
	ds_read2_b32 v[22:23], v26 offset0:231 offset1:239
	v_cvt_pk_bf16_f32 v5, v12, v14
	s_waitcnt lgkmcnt(3)
	s_waitcnt lgkmcnt(2)
	v_cvt_pk_bf16_f32 v6, v16, v18
	s_waitcnt lgkmcnt(1)
	v_or_b32_e32 v24, s8, v101
	s_waitcnt lgkmcnt(0)
	v_ashrrev_i32_e32 v25, 31, v24
	v_lshlrev_b64 v[24:25], 10, v[24:25]
	v_cvt_pk_bf16_f32 v7, v20, v22
	v_lshl_add_u64 v[24:25], v[2:3], 0, v[24:25]
	global_store_dwordx4 v[24:25], v[4:7], off nt
	s_nop 1
	v_cvt_pk_bf16_f32 v4, v11, v9
	v_cvt_pk_bf16_f32 v5, v13, v15
	v_cvt_pk_bf16_f32 v6, v17, v19
	v_or_b32_e32 v8, s8, v102
	v_ashrrev_i32_e32 v9, 31, v8
	v_lshlrev_b64 v[8:9], 10, v[8:9]
	v_cvt_pk_bf16_f32 v7, v21, v23
	ds_read2_b32 v[10:11], v97 offset0:48 offset1:56
	v_lshl_add_u64 v[8:9], v[2:3], 0, v[8:9]
	global_store_dwordx4 v[8:9], v[4:7], off nt
	ds_read2_b32 v[8:9], v97 offset0:113 offset1:121
	ds_read2_b32 v[12:13], v97 offset0:178 offset1:186
	ds_read2_b32 v[14:15], v97 offset0:243 offset1:251
	s_waitcnt lgkmcnt(3)
	s_waitcnt lgkmcnt(2)
	ds_read2_b32 v[16:17], v26 offset0:52 offset1:60
	ds_read2_b32 v[18:19], v26 offset0:117 offset1:125
	v_cvt_pk_bf16_f32 v4, v10, v8
	s_waitcnt lgkmcnt(3)
	s_waitcnt lgkmcnt(2)
	ds_read2_b32 v[20:21], v26 offset0:182 offset1:190
	ds_read2_b32 v[22:23], v26 offset0:247 offset1:255
	v_cvt_pk_bf16_f32 v5, v12, v14
	s_waitcnt lgkmcnt(3)
	s_waitcnt lgkmcnt(2)
	v_cvt_pk_bf16_f32 v6, v16, v18
	s_waitcnt lgkmcnt(1)
	v_or_b32_e32 v24, s8, v103
	s_waitcnt lgkmcnt(0)
	v_ashrrev_i32_e32 v25, 31, v24
	v_lshlrev_b64 v[24:25], 10, v[24:25]
	v_cvt_pk_bf16_f32 v7, v20, v22
	v_lshl_add_u64 v[24:25], v[2:3], 0, v[24:25]
	global_store_dwordx4 v[24:25], v[4:7], off nt
	s_nop 1
	v_cvt_pk_bf16_f32 v4, v11, v9
	v_cvt_pk_bf16_f32 v5, v13, v15
	v_cvt_pk_bf16_f32 v6, v17, v19
	v_or_b32_e32 v8, s8, v104
	v_ashrrev_i32_e32 v9, 31, v8
	v_lshlrev_b64 v[8:9], 10, v[8:9]
	v_cvt_pk_bf16_f32 v7, v21, v23
	v_lshl_add_u64 v[2:3], v[2:3], 0, v[8:9]
	global_store_dwordx4 v[2:3], v[4:7], off nt
	s_waitcnt lgkmcnt(0)

; #define LAS __attribute__((address_space(3)))
; #define WSW(T, off, l) WSP(T, WS_WSET + (size_t)(l) * WSET_STRIDE + (off))
; __device__ __forceinline__ void tr_item(const float* W, int ldw, int k0, int n0, bf16* WT, int ldt, int drow0, LAS float* scr, int lane, const float* kscale = nullptr) {
;     const float* src = W + (size_t)(k0 + (lane >> 4)) * ldw + n0 + (lane & 15) * 4;
;     f32x4 v[16];
; #pragma unroll
;     for (int i = 0; i < 16; ++i) v[i] = __builtin_nontemporal_load((const f32x4*)(src + (size_t)(4 * i) * ldw));
;     LAS float* wp = scr + (lane >> 4) * 65 + (lane & 15) * 4;
; #pragma unroll
;     for (int i = 0; i < 16; ++i) { LAS float* q = wp + (4 * i) * 65; const float ks = kscale ? kscale[k0 + 4 * i + (lane >> 4)] : 1.f; q[0] = v[i].x * ks; q[1] = v[i].y * ks; q[2] = v[i].z * ks; q[3] = v[i].w * ks; }
; __device__ __forceinline__ void convert_tile(const Args& a, GAS unsigned char* wsb, int l, int t, LAS float* scr, int lane) {
;     ...
;     if (r < I_IN) { const int kb = r / 45, nb = r - kb * 45; tr_item(INP(7) + (size_t)l * DM * INW, INW, kb * 64, nb * 64, WSW(bf16, W_IN, l), DM, nb * 64, scr, lane); return; }
.LBB0_2913:
	s_andn2_b64 vcc, exec, s[8:9]
	s_cbranch_vccnz .LBB0_2758
	s_mul_hi_i32 s8, s18, 0xb60b60b7
	s_add_i32 s8, s8, s18
	s_lshr_b32 s9, s8, 31
	s_ashr_i32 s8, s8, 5
	s_add_i32 s8, s8, s9
	s_mul_i32 s9, s8, 0xffffffd3
	v_readlane_b32 s40, v253, 52
	s_add_i32 s9, s9, s18
	s_lshl_b32 s10, s8, 6
	v_readlane_b32 s54, v254, 2
	v_readlane_b32 s55, v254, 3
	s_lshl_b32 s8, s9, 6
	v_or_b32_e32 v1, s10, v67
	v_mov_b64_e32 v[2:3], s[54:55]
	s_movk_i32 s9, 0x2d00
	v_mad_i64_i32 v[2:3], s[14:15], v1, s9, v[2:3]
	s_ashr_i32 s9, s8, 31
	v_lshl_add_u64 v[2:3], s[8:9], 2, v[2:3]
	v_lshlrev_b32_e32 v4, 2, v66
	v_mov_b32_e32 v5, v147
	v_lshl_add_u64 v[62:63], v[2:3], 0, v[4:5]
	s_mov_b32 s9, 0xb000
	v_add_co_u32_e32 v6, vcc, s9, v62
	s_mov_b32 s9, 0x16000
	s_nop 0
	v_addc_co_u32_e32 v7, vcc, 0, v63, vcc
	v_add_co_u32_e32 v10, vcc, s9, v62
	global_load_dwordx4 v[2:5], v[62:63], off nt
	s_nop 0
	global_load_dwordx4 v[6:9], v[6:7], off offset:1024 nt
	v_addc_co_u32_e32 v11, vcc, 0, v63, vcc
	s_mov_b32 s9, 0x21000
	v_add_co_u32_e32 v14, vcc, s9, v62
	s_mov_b32 s9, 0x2d000
	s_nop 0
	v_addc_co_u32_e32 v15, vcc, 0, v63, vcc
	global_load_dwordx4 v[10:13], v[10:11], off offset:2048 nt
	s_nop 0
	global_load_dwordx4 v[14:17], v[14:15], off offset:3072 nt
	v_add_co_u32_e32 v18, vcc, s9, v62
	s_mov_b32 s9, 0x38000
	s_nop 0
	v_addc_co_u32_e32 v19, vcc, 0, v63, vcc
	v_add_co_u32_e32 v22, vcc, s9, v62
	s_mov_b32 s9, 0x43000
	s_nop 0
	v_addc_co_u32_e32 v23, vcc, 0, v63, vcc
	global_load_dwordx4 v[18:21], v[18:19], off nt
	s_nop 0
	global_load_dwordx4 v[22:25], v[22:23], off offset:1024 nt
	v_add_co_u32_e32 v26, vcc, s9, v62
	s_mov_b32 s9, 0x4e000
	s_nop 0
	v_addc_co_u32_e32 v27, vcc, 0, v63, vcc
	v_add_co_u32_e32 v30, vcc, s9, v62
	s_mov_b32 s9, 0x5a000
	s_nop 0
	v_addc_co_u32_e32 v31, vcc, 0, v63, vcc
	global_load_dwordx4 v[26:29], v[26:27], off offset:2048 nt
	s_nop 0
	global_load_dwordx4 v[30:33], v[30:31], off offset:3072 nt
	v_add_co_u32_e32 v34, vcc, s9, v62
	s_mov_b32 s9, 0x65000
	s_nop 0
	v_addc_co_u32_e32 v35, vcc, 0, v63, vcc
	v_add_co_u32_e32 v38, vcc, s9, v62
	s_mov_b32 s9, 0x70000
	s_nop 0
	v_addc_co_u32_e32 v39, vcc, 0, v63, vcc
	global_load_dwordx4 v[34:37], v[34:35], off nt
	s_nop 0
	global_load_dwordx4 v[38:41], v[38:39], off offset:1024 nt
	v_add_co_u32_e32 v42, vcc, s9, v62
	s_mov_b32 s9, 0x7b000
	s_nop 0
	v_addc_co_u32_e32 v43, vcc, 0, v63, vcc
	v_add_co_u32_e32 v46, vcc, s9, v62
	s_mov_b32 s9, 0x87000
	s_nop 0
	v_addc_co_u32_e32 v47, vcc, 0, v63, vcc
	global_load_dwordx4 v[42:45], v[42:43], off offset:2048 nt
	s_nop 0
	global_load_dwordx4 v[46:49], v[46:47], off offset:3072 nt
	v_add_co_u32_e32 v50, vcc, s9, v62
	s_mov_b32 s9, 0x92000
	s_nop 0
	v_addc_co_u32_e32 v51, vcc, 0, v63, vcc
	global_load_dwordx4 v[50:53], v[50:51], off nt
	v_add_co_u32_e32 v54, vcc, s9, v62
	s_mov_b32 s9, 0x9d000
	s_nop 0
	v_addc_co_u32_e32 v55, vcc, 0, v63, vcc
	global_load_dwordx4 v[54:57], v[54:55], off offset:1024 nt
	v_add_co_u32_e32 v58, vcc, s9, v62
	s_mov_b32 s9, 0xa8000
	s_nop 0
	v_addc_co_u32_e32 v59, vcc, 0, v63, vcc
	global_load_dwordx4 v[58:61], v[58:59], off offset:2048 nt
	v_add_co_u32_e32 v62, vcc, s9, v62
	v_add_u32_e32 v1, 0x410, v95
	s_nop 0
	v_addc_co_u32_e32 v63, vcc, 0, v63, vcc
	global_load_dwordx4 v[62:65], v[62:63], off offset:3072 nt
	s_waitcnt vmcnt(15)
	ds_write2_b32 v95, v2, v3 offset1:1
	ds_write2_b32 v95, v4, v5 offset0:2 offset1:3
	s_waitcnt vmcnt(14)
	ds_write2_b32 v1, v6, v7 offset1:1
	v_add_u32_e32 v1, 0x418, v95
	ds_write2_b32 v1, v8, v9 offset1:1
	v_add_u32_e32 v1, 0x820, v95
	s_ashr_i32 s11, s10, 31
	v_lshl_add_u64 v[2:3], s[10:11], 1, v[90:91]
	v_readlane_b32 s48, v253, 60
	v_readlane_b32 s49, v253, 61
	s_waitcnt vmcnt(13)
	ds_write2_b32 v1, v10, v11 offset1:1
	v_add_u32_e32 v1, 0x828, v95
	ds_write2_b32 v1, v12, v13 offset1:1
	v_add_u32_e32 v1, 0xc30, v95
	s_waitcnt vmcnt(12)
	ds_write2_b32 v1, v14, v15 offset1:1
	v_add_u32_e32 v1, 0xc38, v95
	ds_write2_b32 v1, v16, v17 offset1:1
	v_add_u32_e32 v1, 0x1040, v95
	v_readlane_b32 s50, v253, 62
	v_readlane_b32 s51, v253, 63
	v_readlane_b32 s52, v254, 0
	s_waitcnt vmcnt(11)
	ds_write2_b32 v1, v18, v19 offset1:1
	v_add_u32_e32 v1, 0x1048, v95
	ds_write2_b32 v1, v20, v21 offset1:1
	v_add_u32_e32 v1, 0x1450, v95
	s_waitcnt vmcnt(10)
	ds_write2_b32 v1, v22, v23 offset1:1
	v_add_u32_e32 v1, 0x1458, v95
	ds_write2_b32 v1, v24, v25 offset1:1
	v_add_u32_e32 v1, 0x1860, v95
	v_or_b32_e32 v24, s8, v96
	v_ashrrev_i32_e32 v25, 31, v24
	v_lshlrev_b64 v[24:25], 12, v[24:25]
	s_waitcnt vmcnt(9)
	ds_write2_b32 v1, v26, v27 offset1:1
	v_add_u32_e32 v1, 0x1868, v95
	ds_write2_b32 v1, v28, v29 offset1:1
	v_add_u32_e32 v1, 0x1c70, v95
	s_waitcnt vmcnt(8)
	ds_write2_b32 v1, v30, v31 offset1:1
	v_add_u32_e32 v1, 0x1c78, v95
	ds_write2_b32 v1, v32, v33 offset1:1
	v_add_u32_e32 v1, 0x2080, v95
	v_add_u32_e32 v26, 0x400, v97
	v_lshl_add_u64 v[24:25], v[2:3], 0, v[24:25]
	v_readlane_b32 s53, v254, 1
	s_waitcnt vmcnt(7)
	ds_write2_b32 v1, v34, v35 offset1:1
	v_add_u32_e32 v1, 0x2088, v95
	ds_write2_b32 v1, v36, v37 offset1:1
	v_add_u32_e32 v1, 0x2490, v95
	s_waitcnt vmcnt(6)
	ds_write2_b32 v1, v38, v39 offset1:1
	v_add_u32_e32 v1, 0x2498, v95
	ds_write2_b32 v1, v40, v41 offset1:1
	v_add_u32_e32 v1, 0x28a0, v95
	v_readlane_b32 s48, v254, 35
	v_readlane_b32 s49, v254, 36
	v_readlane_b32 s50, v254, 37
	s_waitcnt vmcnt(5)
	ds_write2_b32 v1, v42, v43 offset1:1
	v_add_u32_e32 v1, 0x28a8, v95
	ds_write2_b32 v1, v44, v45 offset1:1
	v_add_u32_e32 v1, 0x2cb0, v95
	s_waitcnt vmcnt(4)
	ds_write2_b32 v1, v46, v47 offset1:1
	v_add_u32_e32 v1, 0x2cb8, v95
	ds_write2_b32 v1, v48, v49 offset1:1
	v_add_u32_e32 v1, 0x30c0, v95
	s_waitcnt vmcnt(3)
; #define LAS __attribute__((address_space(3)))
; __device__ __forceinline__ unsigned pk2(float lo, float hi) { return f2bf(lo) | (f2bf(hi) << 16); }
; __device__ __forceinline__ void tr_item(const float* W, int ldw, int k0, int n0, bf16* WT, int ldt, int drow0, LAS float* scr, int lane, const float* kscale = nullptr) {
;     ...
;     for (int i = 0; i < 16; ++i) { LAS float* q = wp + (4 * i) * 65; const float ks = kscale ? kscale[k0 + 4 * i + (lane >> 4)] : 1.f; q[0] = v[i].x * ks; q[1] = v[i].y * ks; q[2] = v[i].z * ks; q[3] = v[i].w * ks; }
;     asm volatile("s_waitcnt lgkmcnt(0)" ::: "memory");
;     const int kc = lane & 7;
; #pragma unroll
;     for (int j = 0; j < 8; ++j) { const int n = (lane >> 3) + 8 * j; const LAS float* sp = scr + (8 * kc) * 65 + n;
;         u32x4 o; o.x = pk2(sp[0 * 65], sp[1 * 65]); o.y = pk2(sp[2 * 65], sp[3 * 65]); o.z = pk2(sp[4 * 65], sp[5 * 65]); o.w = pk2(sp[6 * 65], sp[7 * 65]);
;         __builtin_nontemporal_store(o, (u32x4*)(WT + (size_t)(drow0 + n) * ldt + k0 + 8 * kc)); }
;     asm volatile("s_waitcnt lgkmcnt(0)" ::: "memory");
	ds_write2_b32 v1, v50, v51 offset1:1
	v_add_u32_e32 v1, 0x30c8, v95
	ds_write2_b32 v1, v52, v53 offset1:1
	v_add_u32_e32 v1, 0x34d0, v95
	v_readlane_b32 s51, v254, 38
	s_waitcnt vmcnt(2)
	ds_write2_b32 v1, v54, v55 offset1:1
	v_add_u32_e32 v1, 0x34d8, v95
	ds_write2_b32 v1, v56, v57 offset1:1
	v_add_u32_e32 v1, 0x38e0, v95
	v_readlane_b32 s52, v254, 39
	v_readlane_b32 s53, v254, 40
	s_waitcnt vmcnt(1)
	ds_write2_b32 v1, v58, v59 offset1:1
	v_add_u32_e32 v1, 0x38e8, v95
	ds_write2_b32 v1, v60, v61 offset1:1
	v_add_u32_e32 v1, 0x3cf0, v95
	v_readlane_b32 s54, v254, 41
	v_readlane_b32 s55, v254, 42
	s_waitcnt vmcnt(0)
	ds_write2_b32 v1, v62, v63 offset1:1
	v_add_u32_e32 v1, 0x3cf8, v95
	ds_write2_b32 v1, v64, v65 offset1:1
	s_waitcnt lgkmcnt(0)
	ds_read2_b32 v[8:9], v97 offset1:8
	ds_read2_b32 v[10:11], v97 offset0:65 offset1:73
	ds_read2_b32 v[12:13], v97 offset0:130 offset1:138
	ds_read2_b32 v[14:15], v97 offset0:195 offset1:203
	ds_read2_b32 v[16:17], v26 offset0:4 offset1:12
	s_waitcnt lgkmcnt(4)
	s_waitcnt lgkmcnt(3)
	ds_read2_b32 v[18:19], v26 offset0:69 offset1:77
	v_cvt_pk_bf16_f32 v4, v8, v10
	s_waitcnt lgkmcnt(3)
	s_waitcnt lgkmcnt(2)
	ds_read2_b32 v[20:21], v26 offset0:134 offset1:142
	ds_read2_b32 v[22:23], v26 offset0:199 offset1:207
	v_cvt_pk_bf16_f32 v5, v12, v14
	s_waitcnt lgkmcnt(3)
	s_waitcnt lgkmcnt(2)
	v_cvt_pk_bf16_f32 v6, v16, v18
	s_waitcnt lgkmcnt(1)
	s_waitcnt lgkmcnt(0)
	v_cvt_pk_bf16_f32 v7, v20, v22
	global_store_dwordx4 v[24:25], v[4:7], off nt
	s_nop 1
	v_cvt_pk_bf16_f32 v4, v9, v11
	v_cvt_pk_bf16_f32 v5, v13, v15
	v_cvt_pk_bf16_f32 v6, v17, v19
	v_or_b32_e32 v8, s8, v98
	v_ashrrev_i32_e32 v9, 31, v8
	v_lshlrev_b64 v[8:9], 12, v[8:9]
	v_cvt_pk_bf16_f32 v7, v21, v23
	ds_read2_b32 v[10:11], v97 offset0:16 offset1:24
	v_lshl_add_u64 v[8:9], v[2:3], 0, v[8:9]
	global_store_dwordx4 v[8:9], v[4:7], off nt
	ds_read2_b32 v[8:9], v97 offset0:81 offset1:89
	ds_read2_b32 v[12:13], v97 offset0:146 offset1:154
	ds_read2_b32 v[14:15], v97 offset0:211 offset1:219
	s_waitcnt lgkmcnt(3)
	s_waitcnt lgkmcnt(2)
	ds_read2_b32 v[16:17], v26 offset0:20 offset1:28
	ds_read2_b32 v[18:19], v26 offset0:85 offset1:93
	v_cvt_pk_bf16_f32 v4, v10, v8
	s_waitcnt lgkmcnt(3)
	s_waitcnt lgkmcnt(2)
	ds_read2_b32 v[20:21], v26 offset0:150 offset1:158
	ds_read2_b32 v[22:23], v26 offset0:215 offset1:223
	v_cvt_pk_bf16_f32 v5, v12, v14
	s_waitcnt lgkmcnt(3)
	s_waitcnt lgkmcnt(2)
	v_cvt_pk_bf16_f32 v6, v16, v18
	s_waitcnt lgkmcnt(1)
	v_or_b32_e32 v24, s8, v99
	s_waitcnt lgkmcnt(0)
	v_ashrrev_i32_e32 v25, 31, v24
	v_lshlrev_b64 v[24:25], 12, v[24:25]
	v_cvt_pk_bf16_f32 v7, v20, v22
	v_lshl_add_u64 v[24:25], v[2:3], 0, v[24:25]
	global_store_dwordx4 v[24:25], v[4:7], off nt
	s_nop 1
	v_cvt_pk_bf16_f32 v4, v11, v9
	v_cvt_pk_bf16_f32 v5, v13, v15
	v_cvt_pk_bf16_f32 v6, v17, v19
	v_or_b32_e32 v8, s8, v100
	v_ashrrev_i32_e32 v9, 31, v8
	v_lshlrev_b64 v[8:9], 12, v[8:9]
	v_cvt_pk_bf16_f32 v7, v21, v23
	ds_read2_b32 v[10:11], v97 offset0:32 offset1:40
	v_lshl_add_u64 v[8:9], v[2:3], 0, v[8:9]
	global_store_dwordx4 v[8:9], v[4:7], off nt
	ds_read2_b32 v[8:9], v97 offset0:97 offset1:105
	ds_read2_b32 v[12:13], v97 offset0:162 offset1:170
	ds_read2_b32 v[14:15], v97 offset0:227 offset1:235
	s_waitcnt lgkmcnt(3)
	s_waitcnt lgkmcnt(2)
	ds_read2_b32 v[16:17], v26 offset0:36 offset1:44
	ds_read2_b32 v[18:19], v26 offset0:101 offset1:109
	v_cvt_pk_bf16_f32 v4, v10, v8
	s_waitcnt lgkmcnt(3)
	s_waitcnt lgkmcnt(2)
	ds_read2_b32 v[20:21], v26 offset0:166 offset1:174
	ds_read2_b32 v[22:23], v26 offset0:231 offset1:239
	v_cvt_pk_bf16_f32 v5, v12, v14
	s_waitcnt lgkmcnt(3)
	s_waitcnt lgkmcnt(2)
	v_cvt_pk_bf16_f32 v6, v16, v18
	s_waitcnt lgkmcnt(1)
	v_or_b32_e32 v24, s8, v101
	s_waitcnt lgkmcnt(0)
	v_ashrrev_i32_e32 v25, 31, v24
	v_lshlrev_b64 v[24:25], 12, v[24:25]
	v_cvt_pk_bf16_f32 v7, v20, v22
	v_lshl_add_u64 v[24:25], v[2:3], 0, v[24:25]
	global_store_dwordx4 v[24:25], v[4:7], off nt
	s_nop 1
	v_cvt_pk_bf16_f32 v4, v11, v9
	v_cvt_pk_bf16_f32 v5, v13, v15
	v_cvt_pk_bf16_f32 v6, v17, v19
	v_or_b32_e32 v8, s8, v102
	v_ashrrev_i32_e32 v9, 31, v8
	v_lshlrev_b64 v[8:9], 12, v[8:9]
	v_cvt_pk_bf16_f32 v7, v21, v23
	ds_read2_b32 v[10:11], v97 offset0:48 offset1:56
	v_lshl_add_u64 v[8:9], v[2:3], 0, v[8:9]
	global_store_dwordx4 v[8:9], v[4:7], off nt
	ds_read2_b32 v[8:9], v97 offset0:113 offset1:121
	ds_read2_b32 v[12:13], v97 offset0:178 offset1:186
	ds_read2_b32 v[14:15], v97 offset0:243 offset1:251
	s_waitcnt lgkmcnt(3)
	s_waitcnt lgkmcnt(2)
	ds_read2_b32 v[16:17], v26 offset0:52 offset1:60
	ds_read2_b32 v[18:19], v26 offset0:117 offset1:125
	v_cvt_pk_bf16_f32 v4, v10, v8
	s_waitcnt lgkmcnt(3)
	s_waitcnt lgkmcnt(2)
	ds_read2_b32 v[20:21], v26 offset0:182 offset1:190
	ds_read2_b32 v[22:23], v26 offset0:247 offset1:255
	v_cvt_pk_bf16_f32 v5, v12, v14
	s_waitcnt lgkmcnt(3)
	s_waitcnt lgkmcnt(2)
	v_cvt_pk_bf16_f32 v6, v16, v18
	s_waitcnt lgkmcnt(1)
	v_or_b32_e32 v24, s8, v103
	s_waitcnt lgkmcnt(0)
	v_ashrrev_i32_e32 v25, 31, v24
	v_lshlrev_b64 v[24:25], 12, v[24:25]
	v_cvt_pk_bf16_f32 v7, v20, v22
	v_lshl_add_u64 v[24:25], v[2:3], 0, v[24:25]
	global_store_dwordx4 v[24:25], v[4:7], off nt
	s_nop 1
	v_cvt_pk_bf16_f32 v4, v11, v9
	v_cvt_pk_bf16_f32 v5, v13, v15
	v_cvt_pk_bf16_f32 v6, v17, v19
	v_or_b32_e32 v8, s8, v104
	v_ashrrev_i32_e32 v9, 31, v8
	v_lshlrev_b64 v[8:9], 12, v[8:9]
	v_cvt_pk_bf16_f32 v7, v21, v23
	v_lshl_add_u64 v[2:3], v[2:3], 0, v[8:9]
	global_store_dwordx4 v[2:3], v[4:7], off nt
	s_waitcnt lgkmcnt(0)
	v_readlane_b32 s58, v254, 45
	v_readlane_b32 s59, v254, 46
	v_readlane_b32 s60, v254, 47
	v_readlane_b32 s61, v254, 48
	v_readlane_b32 s62, v254, 49
	v_readlane_b32 s63, v254, 50
	v_readlane_b32 s41, v253, 53
	v_readlane_b32 s42, v253, 54
	v_readlane_b32 s43, v253, 55
	v_readlane_b32 s44, v253, 56
	v_readlane_b32 s45, v253, 57
	v_readlane_b32 s46, v253, 58
	v_readlane_b32 s47, v253, 59
	v_readlane_b32 s56, v254, 43
	v_readlane_b32 s57, v254, 44
	s_branch .LBB0_2758
